# v97: remaining load-phase address VALU (first-level adds, G5 row selects) moved into the preceding MFMA block of the same wave
# baseline (speedup 1.0000x reference)
; #define PG8_STAGE_A(b, h, ptr, NX) do { if constexpr (Sched::GATHER) { unsigned gs_[2]; gs_[0] = ((NX) && last_) ? gN[h][0] : gA[h][0]; gs_[1] = ((NX) && last_) ? gN[h][1] : gA[h][1]; PG8_STAGE(PG8_SA(b, h), ptr, gs_); } \
;         else PG8_STAGE(PG8_SA(b, h), (ptr) + ((h) ? hstep : (size_t)0), voffA); } while (0)
; #define PG8_STAGE(bufoff, gbase, voff) do { _Pragma("unroll") for (int _i = 0; _i < 2; ++_i) \
;         __builtin_amdgcn_global_load_lds((const unsigned*)((const char*)(gbase) + (voff)[_i]), (PG8_LAS unsigned*)(lds + (bufoff) + ldsw + _i * 8192), 16, 0, 0); } while (0)
; #define PG8_LDA(dst, b, h) do { _Pragma("unroll") for (int m = 0; m < 4; ++m) _Pragma("unroll") for (int k = 0; k < 2; ++k) dst[m][k] = *(const PG8_LAS bf16x8*)(lds + PG8_SA(b, h) + aoff + m * 2048 + k * 1024); } while (0)
; #define PG8_LDB(dst, b, h) do { _Pragma("unroll") for (int n = 0; n < 2; ++n) _Pragma("unroll") for (int k = 0; k < 2; ++k) dst[n][k] = *(const PG8_LAS bf16x8*)(lds + PG8_SB(b, h) + boff + n * 2048 + k * 1024); } while (0)
; #define PG8_WAIT_V(n) asm volatile("s_waitcnt vmcnt(" #n ")" ::: "memory")
; #define PG8_WAIT_L(n) asm volatile("s_waitcnt lgkmcnt(" #n ")" ::: "memory")
; template <class Epi, class Sched, bool ALIGN_EPI = false, bool SP2 = false>
; __device__ __forceinline__ void gemm_phase(PG8_LAS unsigned char* lds, const Gemm g, const Sched& S, const Epi& E, const bool skip_epi = false) {
;     ...
;         for (int t = 0; t < nt; t += 2) {
;             const bool last = (t == nt - 2); last_ = last && has_next;
;             const char* a1 = cA + (size_t)(t + 1) * kstep;
;             const char* a2 = last ? nA : cA + (size_t)(t + 2) * kstep; const char* b2 = last ? nB : cB + (size_t)(t + 2) * kstep;
;             const char* a3 = a2 + kstep; const char* b3 = b2 + kstep;
;             if (last && has_next) S.a_ready(nxt);
;             if constexpr (SP2) {
;             PG8_LDB(B0, 0, 0); PG8_LDB(B1, 0, 1); PG8_SCHED; PG8_LDA(At, 0, 0); PG8_STAGE_A(1, 1, a1, false);
;             PG8_WAIT_V(8); PG8_WAIT_L(0); PG8_BAR; PG8_MMA(0, 0, At, B0); PG8_MMA(0, 1, At, B1); PG8_BAR; PG8_SCHED;
;             PG8_LDA(At, 0, 1); PG8_STAGE(PG8_SB(0, 0), b2, voffB); PG8_STAGE(PG8_SB(0, 1), b2 + hstep, voffB); PG8_STAGE_A(0, 0, a2, true);
;             PG8_WAIT_V(8); PG8_WAIT_L(0); PG8_BAR; PG8_MMA(1, 0, At, B0); PG8_MMA(1, 1, At, B1); PG8_BAR; PG8_SCHED;
.LBB0_252:
	s_ashr_i32 s17, s16, 31
	s_lshl_b64 s[18:19], s[16:17], 19
	s_add_u32 s18, s86, s18
	s_addc_u32 s19, s87, s19
	s_and_b64 s[20:21], s[4:5], exec
	s_cselect_b32 s17, s19, s25
	s_cselect_b32 s56, s18, s24
	s_ashr_i32 s15, s14, 31
	s_lshl_b64 s[20:21], s[14:15], 19
	v_readlane_b32 s28, v254, 36
	v_readlane_b32 s29, v254, 37
	s_add_u32 s20, s28, s20
	s_addc_u32 s21, s29, s21
	s_and_b64 s[28:29], s[4:5], exec
	s_cselect_b32 s15, s21, s27
	s_cselect_b32 s57, s20, s26
	s_add_u32 s24, s24, 0x40080
	s_addc_u32 s25, s25, 0
	s_add_u32 s58, s26, 0x100
	s_addc_u32 s59, s27, 0
	s_mov_b32 s60, -2
	s_waitcnt vmcnt(0)
	ds_read_b128 v[148:151], v170
	ds_read_b128 v[152:155], v170 offset:1024
	ds_read_b128 v[156:159], v170 offset:2048
	ds_read_b128 v[160:163], v170 offset:3072
	ds_read_b128 v[176:179], v171
	ds_read_b128 v[180:183], v171 offset:1024
	ds_read_b128 v[184:187], v171 offset:2048
	ds_read_b128 v[188:191], v171 offset:3072
	s_add_u32 s26, s24, 0xfffc0080
	s_addc_u32 s27, s25, -1
	s_cmp_eq_u32 s60, 12
	s_cselect_b32 s29, s17, s27
	s_cselect_b32 s28, s56, s26
	s_cselect_b32 s27, s15, s59
	s_cselect_b32 s26, s57, s58
	s_add_i32 m0, s23, 0xc000
	ds_read_b128 v[192:195], v172
	ds_read_b128 v[196:199], v172 offset:1024
	ds_read_b128 v[200:203], v172 offset:2048
	ds_read_b128 v[204:207], v172 offset:3072
	ds_read_b128 v[208:211], v172 offset:4096
	ds_read_b128 v[212:215], v172 offset:5120
	ds_read_b128 v[216:219], v172 offset:6144
	ds_read_b128 v[220:223], v172 offset:7168
	global_load_lds_dwordx4 v140, s[24:25]
	s_add_i32 m0, s23, 0xe000
	s_nop 0
	global_load_lds_dwordx4 v142, s[24:25]
	s_waitcnt vmcnt(8)
	s_waitcnt lgkmcnt(0)
	s_barrier
	s_setprio 3
	s_waitcnt lgkmcnt(0)
	v_mfma_f32_16x16x32_bf16 v[126:129], v[148:151], v[192:195], 0
	v_mfma_f32_16x16x32_bf16 v[122:125], v[156:159], v[192:195], 0
	v_mfma_f32_16x16x32_bf16 v[114:117], v[148:151], v[200:203], 0
	v_mfma_f32_16x16x32_bf16 v[106:109], v[156:159], v[200:203], 0
	v_lshl_add_u64 v[164:165], s[26:27], 0, v[134:135]
	v_mfma_f32_16x16x32_bf16 v[98:101], v[148:151], v[208:211], 0
	v_mfma_f32_16x16x32_bf16 v[90:93], v[156:159], v[208:211], 0
	v_lshl_add_u64 v[224:225], s[26:27], 0, v[130:131]
	v_mfma_f32_16x16x32_bf16 v[82:85], v[148:151], v[216:219], 0
	v_mfma_f32_16x16x32_bf16 v[74:77], v[156:159], v[216:219], 0
	v_lshl_add_u64 v[230:231], s[28:29], 0, v[132:133]
	v_mfma_f32_16x16x32_bf16 v[126:129], v[152:155], v[196:199], v[126:129]
	v_mfma_f32_16x16x32_bf16 v[122:125], v[160:163], v[196:199], v[122:125]
	v_lshl_add_u64 v[226:227], s[28:29], 0, v[136:137]
	v_mfma_f32_16x16x32_bf16 v[114:117], v[152:155], v[204:207], v[114:117]
	v_mfma_f32_16x16x32_bf16 v[106:109], v[160:163], v[204:207], v[106:109]
	v_mfma_f32_16x16x32_bf16 v[98:101], v[152:155], v[212:215], v[98:101]
	v_mfma_f32_16x16x32_bf16 v[90:93], v[160:163], v[212:215], v[90:93]
	v_mfma_f32_16x16x32_bf16 v[82:85], v[152:155], v[220:223], v[82:85]
	v_mfma_f32_16x16x32_bf16 v[74:77], v[160:163], v[220:223], v[74:77]
	s_setprio 0
	s_setprio 3
	v_mfma_f32_16x16x32_bf16 v[118:121], v[176:179], v[192:195], 0
	v_mfma_f32_16x16x32_bf16 v[110:113], v[184:187], v[192:195], 0
	v_mfma_f32_16x16x32_bf16 v[102:105], v[176:179], v[200:203], 0
	v_mfma_f32_16x16x32_bf16 v[94:97], v[184:187], v[200:203], 0
	v_mfma_f32_16x16x32_bf16 v[86:89], v[176:179], v[208:211], 0
	v_mfma_f32_16x16x32_bf16 v[78:81], v[184:187], v[208:211], 0
	v_mfma_f32_16x16x32_bf16 v[70:73], v[176:179], v[216:219], 0
	v_mfma_f32_16x16x32_bf16 v[66:69], v[184:187], v[216:219], 0
	v_mfma_f32_16x16x32_bf16 v[118:121], v[180:183], v[196:199], v[118:121]
	v_mfma_f32_16x16x32_bf16 v[110:113], v[188:191], v[196:199], v[110:113]
	v_mfma_f32_16x16x32_bf16 v[102:105], v[180:183], v[204:207], v[102:105]
	v_mfma_f32_16x16x32_bf16 v[94:97], v[188:191], v[204:207], v[94:97]
	v_mfma_f32_16x16x32_bf16 v[86:89], v[180:183], v[212:215], v[86:89]
	v_mfma_f32_16x16x32_bf16 v[78:81], v[188:191], v[212:215], v[78:81]
	v_mfma_f32_16x16x32_bf16 v[70:73], v[180:183], v[220:223], v[70:73]
	v_mfma_f32_16x16x32_bf16 v[66:69], v[188:191], v[220:223], v[66:69]
	s_setprio 0
	s_barrier
	s_add_i32 s61, s46, s2
	s_mov_b32 m0, s61
	ds_read_b128 v[192:195], v172 offset:16384
	ds_read_b128 v[196:199], v172 offset:17408
	ds_read_b128 v[200:203], v172 offset:18432
	ds_read_b128 v[204:207], v172 offset:19456
	ds_read_b128 v[208:211], v172 offset:20480
	ds_read_b128 v[212:215], v172 offset:21504
	ds_read_b128 v[216:219], v172 offset:22528
	ds_read_b128 v[220:223], v172 offset:23552
	global_load_lds_dwordx4 v[164:165], off
	s_add_i32 m0, s61, 0x2000
	s_add_u32 s62, s26, 0x40000
	s_addc_u32 s63, s27, 0
	s_add_i32 s61, s47, s2
	global_load_lds_dwordx4 v[224:225], off
	s_mov_b32 m0, s61
	s_nop 0
	global_load_lds_dwordx4 v134, s[62:63]
	s_add_i32 m0, s61, 0x2000
	s_nop 0
	global_load_lds_dwordx4 v130, s[62:63]
	s_mov_b32 m0, s23
	s_nop 0
	global_load_lds_dwordx4 v[226:227], off
	s_mov_b32 m0, s31
	s_nop 0
	global_load_lds_dwordx4 v[230:231], off
	s_waitcnt vmcnt(8)
	s_waitcnt lgkmcnt(0)
	s_barrier
; #define PG8_STAGE_A(b, h, ptr, NX) do { if constexpr (Sched::GATHER) { unsigned gs_[2]; gs_[0] = ((NX) && last_) ? gN[h][0] : gA[h][0]; gs_[1] = ((NX) && last_) ? gN[h][1] : gA[h][1]; PG8_STAGE(PG8_SA(b, h), ptr, gs_); } \
;         else PG8_STAGE(PG8_SA(b, h), (ptr) + ((h) ? hstep : (size_t)0), voffA); } while (0)
; #define PG8_STAGE(bufoff, gbase, voff) do { _Pragma("unroll") for (int _i = 0; _i < 2; ++_i) \
;         __builtin_amdgcn_global_load_lds((const unsigned*)((const char*)(gbase) + (voff)[_i]), (PG8_LAS unsigned*)(lds + (bufoff) + ldsw + _i * 8192), 16, 0, 0); } while (0)
; #define PG8_LDA(dst, b, h) do { _Pragma("unroll") for (int m = 0; m < 4; ++m) _Pragma("unroll") for (int k = 0; k < 2; ++k) dst[m][k] = *(const PG8_LAS bf16x8*)(lds + PG8_SA(b, h) + aoff + m * 2048 + k * 1024); } while (0)
; #define PG8_LDB(dst, b, h) do { _Pragma("unroll") for (int n = 0; n < 2; ++n) _Pragma("unroll") for (int k = 0; k < 2; ++k) dst[n][k] = *(const PG8_LAS bf16x8*)(lds + PG8_SB(b, h) + boff + n * 2048 + k * 1024); } while (0)
; #define PG8_MMA(ai, bj, At, Bt) do { __builtin_amdgcn_s_setprio(1); _Pragma("unroll") for (int m = 0; m < 4; ++m) _Pragma("unroll") for (int n = 0; n < 2; ++n) _Pragma("unroll") for (int k = 0; k < 2; ++k) \
;         acc[ai][bj][m][n] = __builtin_amdgcn_mfma_f32_16x16x32_bf16(Bt[n][k], At[m][k], acc[ai][bj][m][n], 0, 0, 0); __builtin_amdgcn_s_setprio(0); } while (0)
; #define PG8_WAIT_V(n) asm volatile("s_waitcnt vmcnt(" #n ")" ::: "memory")
; #define PG8_BAR __builtin_amdgcn_s_barrier()
; template <class Epi, class Sched, bool ALIGN_EPI = false, bool SP2 = false>
; __device__ __forceinline__ void gemm_phase(PG8_LAS unsigned char* lds, const Gemm g, const Sched& S, const Epi& E, const bool skip_epi = false) {
;     ...
;             PG8_WAIT_V(8); PG8_WAIT_L(0); PG8_BAR; PG8_MMA(0, 0, At, B0); PG8_MMA(0, 1, At, B1); PG8_BAR; PG8_SCHED;
;             PG8_LDA(At, 0, 1); PG8_STAGE(PG8_SB(0, 0), b2, voffB); PG8_STAGE(PG8_SB(0, 1), b2 + hstep, voffB); PG8_STAGE_A(0, 0, a2, true);
;             PG8_WAIT_V(8); PG8_WAIT_L(0); PG8_BAR; PG8_MMA(1, 0, At, B0); PG8_MMA(1, 1, At, B1); PG8_BAR; PG8_SCHED;
;             PG8_LDB(B0, 1, 0); PG8_LDB(B1, 1, 1); PG8_SCHED; PG8_LDA(At, 1, 0); PG8_STAGE_A(0, 1, a2, true);
;             PG8_WAIT_V(8); PG8_WAIT_L(0); PG8_BAR; PG8_MMA(0, 0, At, B0); PG8_MMA(0, 1, At, B1); PG8_BAR; PG8_SCHED;
	s_setprio 3
	s_waitcnt lgkmcnt(0)
	v_mfma_f32_16x16x32_bf16 v[62:65], v[148:151], v[192:195], 0
	v_mfma_f32_16x16x32_bf16 v[58:61], v[156:159], v[192:195], 0
	v_mfma_f32_16x16x32_bf16 v[50:53], v[148:151], v[200:203], 0
	v_mfma_f32_16x16x32_bf16 v[42:45], v[156:159], v[200:203], 0
	v_mfma_f32_16x16x32_bf16 v[34:37], v[148:151], v[208:211], 0
	v_mfma_f32_16x16x32_bf16 v[26:29], v[156:159], v[208:211], 0
	v_mfma_f32_16x16x32_bf16 v[18:21], v[148:151], v[216:219], 0
	v_mfma_f32_16x16x32_bf16 v[10:13], v[156:159], v[216:219], 0
	v_mfma_f32_16x16x32_bf16 v[62:65], v[152:155], v[196:199], v[62:65]
	v_mfma_f32_16x16x32_bf16 v[58:61], v[160:163], v[196:199], v[58:61]
	v_mfma_f32_16x16x32_bf16 v[50:53], v[152:155], v[204:207], v[50:53]
	v_mfma_f32_16x16x32_bf16 v[42:45], v[160:163], v[204:207], v[42:45]
	v_mfma_f32_16x16x32_bf16 v[34:37], v[152:155], v[212:215], v[34:37]
	v_mfma_f32_16x16x32_bf16 v[26:29], v[160:163], v[212:215], v[26:29]
	v_mfma_f32_16x16x32_bf16 v[18:21], v[152:155], v[220:223], v[18:21]
	v_mfma_f32_16x16x32_bf16 v[10:13], v[160:163], v[220:223], v[10:13]
	s_setprio 0
	s_setprio 3
	v_mfma_f32_16x16x32_bf16 v[54:57], v[176:179], v[192:195], 0
	v_mfma_f32_16x16x32_bf16 v[46:49], v[184:187], v[192:195], 0
	v_mfma_f32_16x16x32_bf16 v[38:41], v[176:179], v[200:203], 0
	v_mfma_f32_16x16x32_bf16 v[30:33], v[184:187], v[200:203], 0
	v_mfma_f32_16x16x32_bf16 v[22:25], v[176:179], v[208:211], 0
	v_mfma_f32_16x16x32_bf16 v[14:17], v[184:187], v[208:211], 0
	v_mfma_f32_16x16x32_bf16 v[6:9], v[176:179], v[216:219], 0
	v_mfma_f32_16x16x32_bf16 v[2:5], v[184:187], v[216:219], 0
	v_mfma_f32_16x16x32_bf16 v[54:57], v[180:183], v[196:199], v[54:57]
	v_mfma_f32_16x16x32_bf16 v[46:49], v[188:191], v[196:199], v[46:49]
	v_mfma_f32_16x16x32_bf16 v[38:41], v[180:183], v[204:207], v[38:41]
	v_mfma_f32_16x16x32_bf16 v[30:33], v[188:191], v[204:207], v[30:33]
	v_mfma_f32_16x16x32_bf16 v[22:25], v[180:183], v[212:215], v[22:25]
	v_mfma_f32_16x16x32_bf16 v[14:17], v[188:191], v[212:215], v[14:17]
	v_mfma_f32_16x16x32_bf16 v[6:9], v[180:183], v[220:223], v[6:9]
	v_mfma_f32_16x16x32_bf16 v[2:5], v[188:191], v[220:223], v[2:5]
	s_setprio 0
	s_barrier
	s_add_i32 s61, 0, 0x18000
	s_add_i32 s62, 0, 0x1c000
	v_add_u32_e32 v160, s61, v1
	v_add_u32_e32 v188, s62, v1
	ds_read_b128 v[148:151], v160
	ds_read_b128 v[152:155], v160 offset:1024
	ds_read_b128 v[156:159], v160 offset:2048
	ds_read_b128 v[160:163], v160 offset:3072
	ds_read_b128 v[176:179], v188
	ds_read_b128 v[180:183], v188 offset:1024
	ds_read_b128 v[184:187], v188 offset:2048
	ds_read_b128 v[188:191], v188 offset:3072
	s_add_u32 s28, s28, 0x40000
	s_addc_u32 s29, s29, 0
	s_mov_b32 m0, s34
	ds_read_b128 v[192:195], v172 offset:32768
	ds_read_b128 v[196:199], v172 offset:33792
	ds_read_b128 v[200:203], v172 offset:34816
	ds_read_b128 v[204:207], v172 offset:35840
	ds_read_b128 v[208:211], v172 offset:36864
	ds_read_b128 v[212:215], v172 offset:37888
	ds_read_b128 v[216:219], v172 offset:38912
	ds_read_b128 v[220:223], v172 offset:39936
	global_load_lds_dwordx4 v136, s[28:29]
	s_mov_b32 m0, s35
	s_nop 0
	global_load_lds_dwordx4 v132, s[28:29]
	s_waitcnt vmcnt(8)
	s_waitcnt lgkmcnt(0)
	s_barrier
	s_setprio 3
	s_waitcnt lgkmcnt(0)
	v_mfma_f32_16x16x32_bf16 v[126:129], v[148:151], v[192:195], v[126:129]
	v_mfma_f32_16x16x32_bf16 v[122:125], v[156:159], v[192:195], v[122:125]
	v_mfma_f32_16x16x32_bf16 v[114:117], v[148:151], v[200:203], v[114:117]
	v_mfma_f32_16x16x32_bf16 v[106:109], v[156:159], v[200:203], v[106:109]
	v_mfma_f32_16x16x32_bf16 v[98:101], v[148:151], v[208:211], v[98:101]
	v_mfma_f32_16x16x32_bf16 v[90:93], v[156:159], v[208:211], v[90:93]
	v_mfma_f32_16x16x32_bf16 v[82:85], v[148:151], v[216:219], v[82:85]
	v_mfma_f32_16x16x32_bf16 v[74:77], v[156:159], v[216:219], v[74:77]
	v_mfma_f32_16x16x32_bf16 v[126:129], v[152:155], v[196:199], v[126:129]
	v_mfma_f32_16x16x32_bf16 v[122:125], v[160:163], v[196:199], v[122:125]
	v_mfma_f32_16x16x32_bf16 v[114:117], v[152:155], v[204:207], v[114:117]
	v_mfma_f32_16x16x32_bf16 v[106:109], v[160:163], v[204:207], v[106:109]
	v_mfma_f32_16x16x32_bf16 v[98:101], v[152:155], v[212:215], v[98:101]
	v_mfma_f32_16x16x32_bf16 v[90:93], v[160:163], v[212:215], v[90:93]
	v_mfma_f32_16x16x32_bf16 v[82:85], v[152:155], v[220:223], v[82:85]
	v_mfma_f32_16x16x32_bf16 v[74:77], v[160:163], v[220:223], v[74:77]
	s_setprio 0
	s_setprio 3
	v_mfma_f32_16x16x32_bf16 v[118:121], v[176:179], v[192:195], v[118:121]
	v_mfma_f32_16x16x32_bf16 v[110:113], v[184:187], v[192:195], v[110:113]
	v_mfma_f32_16x16x32_bf16 v[102:105], v[176:179], v[200:203], v[102:105]
	v_mfma_f32_16x16x32_bf16 v[94:97], v[184:187], v[200:203], v[94:97]
	v_mfma_f32_16x16x32_bf16 v[86:89], v[176:179], v[208:211], v[86:89]
	v_mfma_f32_16x16x32_bf16 v[78:81], v[184:187], v[208:211], v[78:81]
	v_mfma_f32_16x16x32_bf16 v[70:73], v[176:179], v[216:219], v[70:73]
	v_mfma_f32_16x16x32_bf16 v[66:69], v[184:187], v[216:219], v[66:69]
	v_mfma_f32_16x16x32_bf16 v[118:121], v[180:183], v[196:199], v[118:121]
	v_mfma_f32_16x16x32_bf16 v[110:113], v[188:191], v[196:199], v[110:113]
	v_mfma_f32_16x16x32_bf16 v[102:105], v[180:183], v[204:207], v[102:105]
	v_mfma_f32_16x16x32_bf16 v[94:97], v[188:191], v[204:207], v[94:97]
	v_mfma_f32_16x16x32_bf16 v[86:89], v[180:183], v[212:215], v[86:89]
	v_mfma_f32_16x16x32_bf16 v[78:81], v[188:191], v[212:215], v[78:81]
	v_mfma_f32_16x16x32_bf16 v[70:73], v[180:183], v[220:223], v[70:73]
	v_mfma_f32_16x16x32_bf16 v[66:69], v[188:191], v[220:223], v[66:69]
	s_setprio 0
	s_barrier
; #define PG8_STAGE_A(b, h, ptr, NX) do { if constexpr (Sched::GATHER) { unsigned gs_[2]; gs_[0] = ((NX) && last_) ? gN[h][0] : gA[h][0]; gs_[1] = ((NX) && last_) ? gN[h][1] : gA[h][1]; PG8_STAGE(PG8_SA(b, h), ptr, gs_); } \
;         else PG8_STAGE(PG8_SA(b, h), (ptr) + ((h) ? hstep : (size_t)0), voffA); } while (0)
; #define PG8_STAGE(bufoff, gbase, voff) do { _Pragma("unroll") for (int _i = 0; _i < 2; ++_i) \
;         __builtin_amdgcn_global_load_lds((const unsigned*)((const char*)(gbase) + (voff)[_i]), (PG8_LAS unsigned*)(lds + (bufoff) + ldsw + _i * 8192), 16, 0, 0); } while (0)
; #define PG8_WAIT_V(n) asm volatile("s_waitcnt vmcnt(" #n ")" ::: "memory")
; #define PG8_BAR __builtin_amdgcn_s_barrier()
; template <class Epi, class Sched, bool ALIGN_EPI = false, bool SP2 = false>
; __device__ __forceinline__ void gemm_phase(PG8_LAS unsigned char* lds, const Gemm g, const Sched& S, const Epi& E, const bool skip_epi = false) {
;     ...
;         for (int t = 0; t < nt; t += 2) {
;             const bool last = (t == nt - 2); last_ = last && has_next;
;             const char* a1 = cA + (size_t)(t + 1) * kstep;
;             const char* a2 = last ? nA : cA + (size_t)(t + 2) * kstep; const char* b2 = last ? nB : cB + (size_t)(t + 2) * kstep;
;             const char* a3 = a2 + kstep; const char* b3 = b2 + kstep;
;             if (last && has_next) S.a_ready(nxt);
;             if constexpr (SP2) {
;             PG8_LDB(B0, 0, 0); PG8_LDB(B1, 0, 1); PG8_SCHED; PG8_LDA(At, 0, 0); PG8_STAGE_A(1, 1, a1, false);
;             PG8_WAIT_V(8); PG8_WAIT_L(0); PG8_BAR; PG8_MMA(0, 0, At, B0); PG8_MMA(0, 1, At, B1); PG8_BAR; PG8_SCHED;
;             PG8_LDA(At, 0, 1); PG8_STAGE(PG8_SB(0, 0), b2, voffB); PG8_STAGE(PG8_SB(0, 1), b2 + hstep, voffB); PG8_STAGE_A(0, 0, a2, true);
;             PG8_WAIT_V(8); PG8_WAIT_L(0); PG8_BAR; PG8_MMA(1, 0, At, B0); PG8_MMA(1, 1, At, B1); PG8_BAR; PG8_SCHED;
;             PG8_LDB(B0, 1, 0); PG8_LDB(B1, 1, 1); PG8_SCHED; PG8_LDA(At, 1, 0); PG8_STAGE_A(0, 1, a2, true);
;             PG8_WAIT_V(8); PG8_WAIT_L(0); PG8_BAR; PG8_MMA(0, 0, At, B0); PG8_MMA(0, 1, At, B1); PG8_BAR; PG8_SCHED;
;             PG8_LDA(At, 1, 1); PG8_STAGE(PG8_SB(1, 0), b3, voffB); PG8_STAGE(PG8_SB(1, 1), b3 + hstep, voffB); PG8_STAGE_A(1, 0, a3, true);
;             PG8_WAIT_V(8); PG8_WAIT_L(0); PG8_BAR; PG8_MMA(1, 0, At, B0); PG8_MMA(1, 1, At, B1); PG8_BAR; PG8_SCHED;
	s_add_i32 s28, s61, s2
	s_add_i32 m0, s28, 0xffffff80
	ds_read_b128 v[192:195], v172 offset:49152
	ds_read_b128 v[196:199], v172 offset:50176
	ds_read_b128 v[200:203], v172 offset:51200
	ds_read_b128 v[204:207], v172 offset:52224
	ds_read_b128 v[208:211], v172 offset:53248
	ds_read_b128 v[212:215], v172 offset:54272
	ds_read_b128 v[216:219], v172 offset:55296
	ds_read_b128 v[220:223], v172 offset:56320
	global_load_lds_dwordx4 v[164:165], off offset:128
	s_add_i32 m0, s28, 0x1f80
	s_add_u32 s26, s26, 0x40080
	s_addc_u32 s27, s27, 0
	s_add_i32 s28, s62, s2
	global_load_lds_dwordx4 v[224:225], off offset:128
	s_mov_b32 m0, s28
	s_nop 0
	global_load_lds_dwordx4 v134, s[26:27]
	s_add_i32 m0, s28, 0x2000
	s_nop 0
	global_load_lds_dwordx4 v130, s[26:27]
	s_add_i32 m0, s37, 0xffffff80
	s_nop 0
	global_load_lds_dwordx4 v[226:227], off offset:128
	s_add_i32 m0, s38, 0xffffff80
	s_nop 0
	global_load_lds_dwordx4 v[230:231], off offset:128
	s_waitcnt vmcnt(8)
	s_waitcnt lgkmcnt(0)
	s_barrier
	s_setprio 3
	s_waitcnt lgkmcnt(0)
	v_mfma_f32_16x16x32_bf16 v[62:65], v[148:151], v[192:195], v[62:65]
	v_mfma_f32_16x16x32_bf16 v[58:61], v[156:159], v[192:195], v[58:61]
	v_mfma_f32_16x16x32_bf16 v[50:53], v[148:151], v[200:203], v[50:53]
	v_mfma_f32_16x16x32_bf16 v[42:45], v[156:159], v[200:203], v[42:45]
	v_mfma_f32_16x16x32_bf16 v[34:37], v[148:151], v[208:211], v[34:37]
	v_mfma_f32_16x16x32_bf16 v[26:29], v[156:159], v[208:211], v[26:29]
	v_mfma_f32_16x16x32_bf16 v[18:21], v[148:151], v[216:219], v[18:21]
	v_mfma_f32_16x16x32_bf16 v[10:13], v[156:159], v[216:219], v[10:13]
	v_mfma_f32_16x16x32_bf16 v[62:65], v[152:155], v[196:199], v[62:65]
	v_mfma_f32_16x16x32_bf16 v[58:61], v[160:163], v[196:199], v[58:61]
	v_mfma_f32_16x16x32_bf16 v[50:53], v[152:155], v[204:207], v[50:53]
	v_mfma_f32_16x16x32_bf16 v[42:45], v[160:163], v[204:207], v[42:45]
	v_mfma_f32_16x16x32_bf16 v[34:37], v[152:155], v[212:215], v[34:37]
	v_mfma_f32_16x16x32_bf16 v[26:29], v[160:163], v[212:215], v[26:29]
	v_mfma_f32_16x16x32_bf16 v[18:21], v[152:155], v[220:223], v[18:21]
	v_mfma_f32_16x16x32_bf16 v[10:13], v[160:163], v[220:223], v[10:13]
	s_setprio 0
	s_setprio 3
	v_mfma_f32_16x16x32_bf16 v[54:57], v[176:179], v[192:195], v[54:57]
	v_mfma_f32_16x16x32_bf16 v[46:49], v[184:187], v[192:195], v[46:49]
	v_mfma_f32_16x16x32_bf16 v[38:41], v[176:179], v[200:203], v[38:41]
	v_mfma_f32_16x16x32_bf16 v[30:33], v[184:187], v[200:203], v[30:33]
	v_mfma_f32_16x16x32_bf16 v[22:25], v[176:179], v[208:211], v[22:25]
	v_mfma_f32_16x16x32_bf16 v[14:17], v[184:187], v[208:211], v[14:17]
	v_mfma_f32_16x16x32_bf16 v[6:9], v[176:179], v[216:219], v[6:9]
	v_mfma_f32_16x16x32_bf16 v[2:5], v[184:187], v[216:219], v[2:5]
	v_mfma_f32_16x16x32_bf16 v[54:57], v[180:183], v[196:199], v[54:57]
	v_mfma_f32_16x16x32_bf16 v[46:49], v[188:191], v[196:199], v[46:49]
	v_mfma_f32_16x16x32_bf16 v[38:41], v[180:183], v[204:207], v[38:41]
	v_mfma_f32_16x16x32_bf16 v[30:33], v[188:191], v[204:207], v[30:33]
	v_mfma_f32_16x16x32_bf16 v[22:25], v[180:183], v[212:215], v[22:25]
	v_mfma_f32_16x16x32_bf16 v[14:17], v[188:191], v[212:215], v[14:17]
	v_mfma_f32_16x16x32_bf16 v[6:9], v[180:183], v[220:223], v[6:9]
	v_mfma_f32_16x16x32_bf16 v[2:5], v[188:191], v[220:223], v[2:5]
	s_setprio 0
	s_barrier
	s_add_i32 s60, s60, 2
	s_add_u32 s24, s24, 0x100
	s_addc_u32 s25, s25, 0
	s_add_u32 s58, s58, 0x100
	s_addc_u32 s59, s59, 0
	s_cmp_gt_u32 s60, 13
.LBB0_253:
	ds_read_b128 v[148:151], v170
	ds_read_b128 v[152:155], v170 offset:1024
	ds_read_b128 v[156:159], v170 offset:2048
	ds_read_b128 v[160:163], v170 offset:3072
	ds_read_b128 v[176:179], v171
	ds_read_b128 v[180:183], v171 offset:1024
	ds_read_b128 v[184:187], v171 offset:2048
	ds_read_b128 v[188:191], v171 offset:3072
	s_add_u32 s26, s24, 0xfffc0080
	s_addc_u32 s27, s25, -1
	s_cmp_eq_u32 s60, 12
	s_cselect_b32 s29, s17, s27
	s_cselect_b32 s28, s56, s26
	s_cselect_b32 s27, s15, s59
	s_cselect_b32 s26, s57, s58
	s_add_i32 m0, s23, 0xc000
	ds_read_b128 v[192:195], v172
	ds_read_b128 v[196:199], v172 offset:1024
	ds_read_b128 v[200:203], v172 offset:2048
	ds_read_b128 v[204:207], v172 offset:3072
	ds_read_b128 v[208:211], v172 offset:4096
	ds_read_b128 v[212:215], v172 offset:5120
	ds_read_b128 v[216:219], v172 offset:6144
	ds_read_b128 v[220:223], v172 offset:7168
	global_load_lds_dwordx4 v140, s[24:25]
	s_add_i32 m0, s23, 0xe000
	s_nop 0
	global_load_lds_dwordx4 v142, s[24:25]
	s_waitcnt vmcnt(8)
	s_waitcnt lgkmcnt(0)
	s_barrier
; #define PG8_STAGE_A(b, h, ptr, NX) do { if constexpr (Sched::GATHER) { unsigned gs_[2]; gs_[0] = ((NX) && last_) ? gN[h][0] : gA[h][0]; gs_[1] = ((NX) && last_) ? gN[h][1] : gA[h][1]; PG8_STAGE(PG8_SA(b, h), ptr, gs_); } \
;         else PG8_STAGE(PG8_SA(b, h), (ptr) + ((h) ? hstep : (size_t)0), voffA); } while (0)
; #define PG8_STAGE(bufoff, gbase, voff) do { _Pragma("unroll") for (int _i = 0; _i < 2; ++_i) \
;         __builtin_amdgcn_global_load_lds((const unsigned*)((const char*)(gbase) + (voff)[_i]), (PG8_LAS unsigned*)(lds + (bufoff) + ldsw + _i * 8192), 16, 0, 0); } while (0)
; #define PG8_LDA(dst, b, h) do { _Pragma("unroll") for (int m = 0; m < 4; ++m) _Pragma("unroll") for (int k = 0; k < 2; ++k) dst[m][k] = *(const PG8_LAS bf16x8*)(lds + PG8_SA(b, h) + aoff + m * 2048 + k * 1024); } while (0)
; #define PG8_LDB(dst, b, h) do { _Pragma("unroll") for (int n = 0; n < 2; ++n) _Pragma("unroll") for (int k = 0; k < 2; ++k) dst[n][k] = *(const PG8_LAS bf16x8*)(lds + PG8_SB(b, h) + boff + n * 2048 + k * 1024); } while (0)
; #define PG8_MMA(ai, bj, At, Bt) do { __builtin_amdgcn_s_setprio(1); _Pragma("unroll") for (int m = 0; m < 4; ++m) _Pragma("unroll") for (int n = 0; n < 2; ++n) _Pragma("unroll") for (int k = 0; k < 2; ++k) \
;         acc[ai][bj][m][n] = __builtin_amdgcn_mfma_f32_16x16x32_bf16(Bt[n][k], At[m][k], acc[ai][bj][m][n], 0, 0, 0); __builtin_amdgcn_s_setprio(0); } while (0)
; #define PG8_WAIT_V(n) asm volatile("s_waitcnt vmcnt(" #n ")" ::: "memory")
; #define PG8_WAIT_L(n) asm volatile("s_waitcnt lgkmcnt(" #n ")" ::: "memory")
; #define PG8_BAR __builtin_amdgcn_s_barrier()
; #define PG8_SCHED __builtin_amdgcn_sched_barrier(0)
; template <class Epi, class Sched, bool ALIGN_EPI = false, bool SP2 = false>
; __device__ __forceinline__ void gemm_phase(PG8_LAS unsigned char* lds, const Gemm g, const Sched& S, const Epi& E, const bool skip_epi = false) {
;     ...
;             PG8_LDB(B0, 0, 0); PG8_LDB(B1, 0, 1); PG8_SCHED; PG8_LDA(At, 0, 0); PG8_STAGE_A(1, 1, a1, false);
;             PG8_WAIT_V(8); PG8_WAIT_L(0); PG8_BAR; PG8_MMA(0, 0, At, B0); PG8_MMA(0, 1, At, B1); PG8_BAR; PG8_SCHED;
;             PG8_LDA(At, 0, 1); PG8_STAGE(PG8_SB(0, 0), b2, voffB); PG8_STAGE(PG8_SB(0, 1), b2 + hstep, voffB); PG8_STAGE_A(0, 0, a2, true);
;             PG8_WAIT_V(8); PG8_WAIT_L(0); PG8_BAR; PG8_MMA(1, 0, At, B0); PG8_MMA(1, 1, At, B1); PG8_BAR; PG8_SCHED;
	s_setprio 3
	s_waitcnt lgkmcnt(0)
	v_mfma_f32_16x16x32_bf16 v[126:129], v[148:151], v[192:195], v[126:129]
	v_mfma_f32_16x16x32_bf16 v[122:125], v[156:159], v[192:195], v[122:125]
	v_mfma_f32_16x16x32_bf16 v[114:117], v[148:151], v[200:203], v[114:117]
	v_mfma_f32_16x16x32_bf16 v[106:109], v[156:159], v[200:203], v[106:109]
	v_lshl_add_u64 v[164:165], s[26:27], 0, v[134:135]
	v_mfma_f32_16x16x32_bf16 v[98:101], v[148:151], v[208:211], v[98:101]
	v_mfma_f32_16x16x32_bf16 v[90:93], v[156:159], v[208:211], v[90:93]
	v_lshl_add_u64 v[224:225], s[26:27], 0, v[130:131]
	v_mfma_f32_16x16x32_bf16 v[82:85], v[148:151], v[216:219], v[82:85]
	v_mfma_f32_16x16x32_bf16 v[74:77], v[156:159], v[216:219], v[74:77]
	v_lshl_add_u64 v[230:231], s[28:29], 0, v[132:133]
	v_mfma_f32_16x16x32_bf16 v[126:129], v[152:155], v[196:199], v[126:129]
	v_mfma_f32_16x16x32_bf16 v[122:125], v[160:163], v[196:199], v[122:125]
	v_lshl_add_u64 v[226:227], s[28:29], 0, v[136:137]
	v_mfma_f32_16x16x32_bf16 v[114:117], v[152:155], v[204:207], v[114:117]
	v_mfma_f32_16x16x32_bf16 v[106:109], v[160:163], v[204:207], v[106:109]
	v_mfma_f32_16x16x32_bf16 v[98:101], v[152:155], v[212:215], v[98:101]
	v_mfma_f32_16x16x32_bf16 v[90:93], v[160:163], v[212:215], v[90:93]
	v_mfma_f32_16x16x32_bf16 v[82:85], v[152:155], v[220:223], v[82:85]
	v_mfma_f32_16x16x32_bf16 v[74:77], v[160:163], v[220:223], v[74:77]
	s_setprio 0
	s_setprio 3
	v_mfma_f32_16x16x32_bf16 v[118:121], v[176:179], v[192:195], v[118:121]
	v_mfma_f32_16x16x32_bf16 v[110:113], v[184:187], v[192:195], v[110:113]
	v_mfma_f32_16x16x32_bf16 v[102:105], v[176:179], v[200:203], v[102:105]
	v_mfma_f32_16x16x32_bf16 v[94:97], v[184:187], v[200:203], v[94:97]
	v_mfma_f32_16x16x32_bf16 v[86:89], v[176:179], v[208:211], v[86:89]
	v_mfma_f32_16x16x32_bf16 v[78:81], v[184:187], v[208:211], v[78:81]
	v_mfma_f32_16x16x32_bf16 v[70:73], v[176:179], v[216:219], v[70:73]
	v_mfma_f32_16x16x32_bf16 v[66:69], v[184:187], v[216:219], v[66:69]
	v_mfma_f32_16x16x32_bf16 v[118:121], v[180:183], v[196:199], v[118:121]
	v_mfma_f32_16x16x32_bf16 v[110:113], v[188:191], v[196:199], v[110:113]
	v_mfma_f32_16x16x32_bf16 v[102:105], v[180:183], v[204:207], v[102:105]
	v_mfma_f32_16x16x32_bf16 v[94:97], v[188:191], v[204:207], v[94:97]
	v_mfma_f32_16x16x32_bf16 v[86:89], v[180:183], v[212:215], v[86:89]
	v_mfma_f32_16x16x32_bf16 v[78:81], v[188:191], v[212:215], v[78:81]
	v_mfma_f32_16x16x32_bf16 v[70:73], v[180:183], v[220:223], v[70:73]
	v_mfma_f32_16x16x32_bf16 v[66:69], v[188:191], v[220:223], v[66:69]
	s_setprio 0
	s_barrier
	s_add_i32 s61, s46, s2
	s_mov_b32 m0, s61
	ds_read_b128 v[192:195], v172 offset:16384
	ds_read_b128 v[196:199], v172 offset:17408
	ds_read_b128 v[200:203], v172 offset:18432
	ds_read_b128 v[204:207], v172 offset:19456
	ds_read_b128 v[208:211], v172 offset:20480
	ds_read_b128 v[212:215], v172 offset:21504
	ds_read_b128 v[216:219], v172 offset:22528
	ds_read_b128 v[220:223], v172 offset:23552
	global_load_lds_dwordx4 v[164:165], off
	s_add_i32 m0, s61, 0x2000
	s_add_u32 s62, s26, 0x40000
	s_addc_u32 s63, s27, 0
	s_add_i32 s61, s47, s2
	global_load_lds_dwordx4 v[224:225], off
	s_mov_b32 m0, s61
	s_nop 0
	global_load_lds_dwordx4 v134, s[62:63]
	s_add_i32 m0, s61, 0x2000
	s_nop 0
	global_load_lds_dwordx4 v130, s[62:63]
	s_mov_b32 m0, s23
	s_nop 0
	global_load_lds_dwordx4 v[226:227], off
	s_mov_b32 m0, s31
	s_nop 0
	global_load_lds_dwordx4 v[230:231], off
	s_waitcnt vmcnt(8)
	s_waitcnt lgkmcnt(0)
	s_barrier
	s_setprio 3
	s_waitcnt lgkmcnt(0)
	v_mfma_f32_16x16x32_bf16 v[62:65], v[148:151], v[192:195], v[62:65]
	v_mfma_f32_16x16x32_bf16 v[58:61], v[156:159], v[192:195], v[58:61]
	v_mfma_f32_16x16x32_bf16 v[50:53], v[148:151], v[200:203], v[50:53]
	v_mfma_f32_16x16x32_bf16 v[42:45], v[156:159], v[200:203], v[42:45]
	v_mfma_f32_16x16x32_bf16 v[34:37], v[148:151], v[208:211], v[34:37]
	v_mfma_f32_16x16x32_bf16 v[26:29], v[156:159], v[208:211], v[26:29]
	v_mfma_f32_16x16x32_bf16 v[18:21], v[148:151], v[216:219], v[18:21]
	v_mfma_f32_16x16x32_bf16 v[10:13], v[156:159], v[216:219], v[10:13]
	v_mfma_f32_16x16x32_bf16 v[62:65], v[152:155], v[196:199], v[62:65]
	v_mfma_f32_16x16x32_bf16 v[58:61], v[160:163], v[196:199], v[58:61]
	v_mfma_f32_16x16x32_bf16 v[50:53], v[152:155], v[204:207], v[50:53]
	v_mfma_f32_16x16x32_bf16 v[42:45], v[160:163], v[204:207], v[42:45]
	v_mfma_f32_16x16x32_bf16 v[34:37], v[152:155], v[212:215], v[34:37]
	v_mfma_f32_16x16x32_bf16 v[26:29], v[160:163], v[212:215], v[26:29]
	v_mfma_f32_16x16x32_bf16 v[18:21], v[152:155], v[220:223], v[18:21]
	v_mfma_f32_16x16x32_bf16 v[10:13], v[160:163], v[220:223], v[10:13]
	s_setprio 0
	s_setprio 3
	v_mfma_f32_16x16x32_bf16 v[54:57], v[176:179], v[192:195], v[54:57]
	v_mfma_f32_16x16x32_bf16 v[46:49], v[184:187], v[192:195], v[46:49]
	v_mfma_f32_16x16x32_bf16 v[38:41], v[176:179], v[200:203], v[38:41]
	v_mfma_f32_16x16x32_bf16 v[30:33], v[184:187], v[200:203], v[30:33]
	v_mfma_f32_16x16x32_bf16 v[22:25], v[176:179], v[208:211], v[22:25]
	v_mfma_f32_16x16x32_bf16 v[14:17], v[184:187], v[208:211], v[14:17]
	v_mfma_f32_16x16x32_bf16 v[6:9], v[176:179], v[216:219], v[6:9]
	v_mfma_f32_16x16x32_bf16 v[2:5], v[184:187], v[216:219], v[2:5]
	v_mfma_f32_16x16x32_bf16 v[54:57], v[180:183], v[196:199], v[54:57]
	v_mfma_f32_16x16x32_bf16 v[46:49], v[188:191], v[196:199], v[46:49]
	v_mfma_f32_16x16x32_bf16 v[38:41], v[180:183], v[204:207], v[38:41]
	v_mfma_f32_16x16x32_bf16 v[30:33], v[188:191], v[204:207], v[30:33]
	v_mfma_f32_16x16x32_bf16 v[22:25], v[180:183], v[212:215], v[22:25]
	v_mfma_f32_16x16x32_bf16 v[14:17], v[188:191], v[212:215], v[14:17]
	v_mfma_f32_16x16x32_bf16 v[6:9], v[180:183], v[220:223], v[6:9]
	v_mfma_f32_16x16x32_bf16 v[2:5], v[188:191], v[220:223], v[2:5]
	s_setprio 0
	s_barrier
; #define PG8_STAGE_A(b, h, ptr, NX) do { if constexpr (Sched::GATHER) { unsigned gs_[2]; gs_[0] = ((NX) && last_) ? gN[h][0] : gA[h][0]; gs_[1] = ((NX) && last_) ? gN[h][1] : gA[h][1]; PG8_STAGE(PG8_SA(b, h), ptr, gs_); } \
;         else PG8_STAGE(PG8_SA(b, h), (ptr) + ((h) ? hstep : (size_t)0), voffA); } while (0)
; #define PG8_LDA(dst, b, h) do { _Pragma("unroll") for (int m = 0; m < 4; ++m) _Pragma("unroll") for (int k = 0; k < 2; ++k) dst[m][k] = *(const PG8_LAS bf16x8*)(lds + PG8_SA(b, h) + aoff + m * 2048 + k * 1024); } while (0)
; #define PG8_LDB(dst, b, h) do { _Pragma("unroll") for (int n = 0; n < 2; ++n) _Pragma("unroll") for (int k = 0; k < 2; ++k) dst[n][k] = *(const PG8_LAS bf16x8*)(lds + PG8_SB(b, h) + boff + n * 2048 + k * 1024); } while (0)
; #define PG8_MMA(ai, bj, At, Bt) do { __builtin_amdgcn_s_setprio(1); _Pragma("unroll") for (int m = 0; m < 4; ++m) _Pragma("unroll") for (int n = 0; n < 2; ++n) _Pragma("unroll") for (int k = 0; k < 2; ++k) \
;         acc[ai][bj][m][n] = __builtin_amdgcn_mfma_f32_16x16x32_bf16(Bt[n][k], At[m][k], acc[ai][bj][m][n], 0, 0, 0); __builtin_amdgcn_s_setprio(0); } while (0)
; #define PG8_WAIT_V(n) asm volatile("s_waitcnt vmcnt(" #n ")" ::: "memory")
; #define PG8_WAIT_L(n) asm volatile("s_waitcnt lgkmcnt(" #n ")" ::: "memory")
; #define PG8_BAR __builtin_amdgcn_s_barrier()
; #define PG8_SCHED __builtin_amdgcn_sched_barrier(0)
; template <class Epi, class Sched, bool ALIGN_EPI = false, bool SP2 = false>
; __device__ __forceinline__ void gemm_phase(PG8_LAS unsigned char* lds, const Gemm g, const Sched& S, const Epi& E, const bool skip_epi = false) {
;     ...
;             PG8_LDB(B0, 1, 0); PG8_LDB(B1, 1, 1); PG8_SCHED; PG8_LDA(At, 1, 0); PG8_STAGE_A(0, 1, a2, true);
;             PG8_WAIT_V(8); PG8_WAIT_L(0); PG8_BAR; PG8_MMA(0, 0, At, B0); PG8_MMA(0, 1, At, B1); PG8_BAR; PG8_SCHED;
	s_add_i32 s61, 0, 0x18000
	s_add_i32 s62, 0, 0x1c000
	v_add_u32_e32 v160, s61, v1
	v_add_u32_e32 v188, s62, v1
	ds_read_b128 v[148:151], v160
	ds_read_b128 v[152:155], v160 offset:1024
	ds_read_b128 v[156:159], v160 offset:2048
	ds_read_b128 v[160:163], v160 offset:3072
	ds_read_b128 v[176:179], v188
	ds_read_b128 v[180:183], v188 offset:1024
	ds_read_b128 v[184:187], v188 offset:2048
	ds_read_b128 v[188:191], v188 offset:3072
	s_add_u32 s28, s28, 0x40000
	s_addc_u32 s29, s29, 0
	s_mov_b32 m0, s34
	ds_read_b128 v[192:195], v172 offset:32768
	ds_read_b128 v[196:199], v172 offset:33792
	ds_read_b128 v[200:203], v172 offset:34816
	ds_read_b128 v[204:207], v172 offset:35840
	ds_read_b128 v[208:211], v172 offset:36864
	ds_read_b128 v[212:215], v172 offset:37888
	ds_read_b128 v[216:219], v172 offset:38912
	ds_read_b128 v[220:223], v172 offset:39936
	global_load_lds_dwordx4 v136, s[28:29]
	s_mov_b32 m0, s35
	s_nop 0
	global_load_lds_dwordx4 v132, s[28:29]
	s_waitcnt vmcnt(8)
	s_waitcnt lgkmcnt(0)
	s_barrier
	s_setprio 3
	s_waitcnt lgkmcnt(0)
	v_mfma_f32_16x16x32_bf16 v[126:129], v[148:151], v[192:195], v[126:129]
	v_mfma_f32_16x16x32_bf16 v[122:125], v[156:159], v[192:195], v[122:125]
	v_mfma_f32_16x16x32_bf16 v[114:117], v[148:151], v[200:203], v[114:117]
	v_mfma_f32_16x16x32_bf16 v[106:109], v[156:159], v[200:203], v[106:109]
	v_mfma_f32_16x16x32_bf16 v[98:101], v[148:151], v[208:211], v[98:101]
	v_mfma_f32_16x16x32_bf16 v[90:93], v[156:159], v[208:211], v[90:93]
	v_mfma_f32_16x16x32_bf16 v[82:85], v[148:151], v[216:219], v[82:85]
	v_mfma_f32_16x16x32_bf16 v[74:77], v[156:159], v[216:219], v[74:77]
	v_mfma_f32_16x16x32_bf16 v[126:129], v[152:155], v[196:199], v[126:129]
	v_mfma_f32_16x16x32_bf16 v[122:125], v[160:163], v[196:199], v[122:125]
	v_mfma_f32_16x16x32_bf16 v[114:117], v[152:155], v[204:207], v[114:117]
	v_mfma_f32_16x16x32_bf16 v[106:109], v[160:163], v[204:207], v[106:109]
	v_mfma_f32_16x16x32_bf16 v[98:101], v[152:155], v[212:215], v[98:101]
	v_mfma_f32_16x16x32_bf16 v[90:93], v[160:163], v[212:215], v[90:93]
	v_mfma_f32_16x16x32_bf16 v[82:85], v[152:155], v[220:223], v[82:85]
	v_mfma_f32_16x16x32_bf16 v[74:77], v[160:163], v[220:223], v[74:77]
	s_setprio 0
	s_setprio 3
	v_mfma_f32_16x16x32_bf16 v[118:121], v[176:179], v[192:195], v[118:121]
	v_mfma_f32_16x16x32_bf16 v[110:113], v[184:187], v[192:195], v[110:113]
	v_mfma_f32_16x16x32_bf16 v[102:105], v[176:179], v[200:203], v[102:105]
	v_mfma_f32_16x16x32_bf16 v[94:97], v[184:187], v[200:203], v[94:97]
	v_mfma_f32_16x16x32_bf16 v[86:89], v[176:179], v[208:211], v[86:89]
	v_mfma_f32_16x16x32_bf16 v[78:81], v[184:187], v[208:211], v[78:81]
	v_mfma_f32_16x16x32_bf16 v[70:73], v[176:179], v[216:219], v[70:73]
	v_mfma_f32_16x16x32_bf16 v[66:69], v[184:187], v[216:219], v[66:69]
	v_mfma_f32_16x16x32_bf16 v[118:121], v[180:183], v[196:199], v[118:121]
	v_mfma_f32_16x16x32_bf16 v[110:113], v[188:191], v[196:199], v[110:113]
	v_mfma_f32_16x16x32_bf16 v[102:105], v[180:183], v[204:207], v[102:105]
	v_mfma_f32_16x16x32_bf16 v[94:97], v[188:191], v[204:207], v[94:97]
	v_mfma_f32_16x16x32_bf16 v[86:89], v[180:183], v[212:215], v[86:89]
	v_mfma_f32_16x16x32_bf16 v[78:81], v[188:191], v[212:215], v[78:81]
	v_mfma_f32_16x16x32_bf16 v[70:73], v[180:183], v[220:223], v[70:73]
	v_mfma_f32_16x16x32_bf16 v[66:69], v[188:191], v[220:223], v[66:69]
	s_setprio 0
	s_barrier
; #define PG8_STAGE_A(b, h, ptr, NX) do { if constexpr (Sched::GATHER) { unsigned gs_[2]; gs_[0] = ((NX) && last_) ? gN[h][0] : gA[h][0]; gs_[1] = ((NX) && last_) ? gN[h][1] : gA[h][1]; PG8_STAGE(PG8_SA(b, h), ptr, gs_); } \
;         else PG8_STAGE(PG8_SA(b, h), (ptr) + ((h) ? hstep : (size_t)0), voffA); } while (0)
; #define PG8_STAGE(bufoff, gbase, voff) do { _Pragma("unroll") for (int _i = 0; _i < 2; ++_i) \
;         __builtin_amdgcn_global_load_lds((const unsigned*)((const char*)(gbase) + (voff)[_i]), (PG8_LAS unsigned*)(lds + (bufoff) + ldsw + _i * 8192), 16, 0, 0); } while (0)
; #define PG8_LDA(dst, b, h) do { _Pragma("unroll") for (int m = 0; m < 4; ++m) _Pragma("unroll") for (int k = 0; k < 2; ++k) dst[m][k] = *(const PG8_LAS bf16x8*)(lds + PG8_SA(b, h) + aoff + m * 2048 + k * 1024); } while (0)
; #define PG8_MMA(ai, bj, At, Bt) do { __builtin_amdgcn_s_setprio(1); _Pragma("unroll") for (int m = 0; m < 4; ++m) _Pragma("unroll") for (int n = 0; n < 2; ++n) _Pragma("unroll") for (int k = 0; k < 2; ++k) \
;         acc[ai][bj][m][n] = __builtin_amdgcn_mfma_f32_16x16x32_bf16(Bt[n][k], At[m][k], acc[ai][bj][m][n], 0, 0, 0); __builtin_amdgcn_s_setprio(0); } while (0)
; #define PG8_WAIT_V(n) asm volatile("s_waitcnt vmcnt(" #n ")" ::: "memory")
; #define PG8_WAIT_L(n) asm volatile("s_waitcnt lgkmcnt(" #n ")" ::: "memory")
; #define PG8_BAR __builtin_amdgcn_s_barrier()
; __device__ __forceinline__ void rstd8(const float* SS, int rowb, int lane, float (&rs)[2][4]) {
;     f32x4 p[2][4];
; #pragma unroll
;     for (int ai = 0; ai < 2; ++ai)
; #pragma unroll
;         for (int m = 0; m < 4; ++m) p[ai][m] = *(const f32x4*)(SS + (size_t)(rowb + HALF * ai + 16 * m + (lane >> 2)) * 16 + 4 * (lane & 3));
;     asm volatile("" : "+v"(p[0][0]), "+v"(p[0][1]), "+v"(p[0][2]), "+v"(p[0][3]), "+v"(p[1][0]), "+v"(p[1][1]), "+v"(p[1][2]), "+v"(p[1][3]));
; template <class Epi, class Sched, bool ALIGN_EPI = false, bool SP2 = false>
; __device__ __forceinline__ void gemm_phase(PG8_LAS unsigned char* lds, const Gemm g, const Sched& S, const Epi& E, const bool skip_epi = false) {
;     ...
;             PG8_LDA(At, 1, 1); PG8_STAGE(PG8_SB(1, 0), b3, voffB); PG8_STAGE(PG8_SB(1, 1), b3 + hstep, voffB); PG8_STAGE_A(1, 0, a3, true);
;             PG8_WAIT_V(8); PG8_WAIT_L(0); PG8_BAR; PG8_MMA(1, 0, At, B0); PG8_MMA(1, 1, At, B1); PG8_BAR; PG8_SCHED;
	s_add_i32 s28, s61, s2
	s_add_i32 m0, s28, 0xffffff80
	ds_read_b128 v[192:195], v172 offset:49152
	ds_read_b128 v[196:199], v172 offset:50176
	ds_read_b128 v[200:203], v172 offset:51200
	ds_read_b128 v[204:207], v172 offset:52224
	ds_read_b128 v[208:211], v172 offset:53248
	ds_read_b128 v[212:215], v172 offset:54272
	ds_read_b128 v[216:219], v172 offset:55296
	ds_read_b128 v[220:223], v172 offset:56320
	global_load_lds_dwordx4 v[164:165], off offset:128
	s_add_i32 m0, s28, 0x1f80
	s_add_u32 s26, s26, 0x40080
	s_addc_u32 s27, s27, 0
	s_add_i32 s28, s62, s2
	global_load_lds_dwordx4 v[224:225], off offset:128
	s_mov_b32 m0, s28
	s_nop 0
	global_load_lds_dwordx4 v134, s[26:27]
	s_add_i32 m0, s28, 0x2000
	s_nop 0
	global_load_lds_dwordx4 v130, s[26:27]
	s_add_i32 m0, s37, 0xffffff80
	s_nop 0
	global_load_lds_dwordx4 v[226:227], off offset:128
	s_add_i32 m0, s38, 0xffffff80
	s_nop 0
	global_load_lds_dwordx4 v[230:231], off offset:128
	s_waitcnt vmcnt(8)
	s_waitcnt lgkmcnt(0)
	s_barrier
	s_setprio 3
	s_waitcnt lgkmcnt(0)
	v_mfma_f32_16x16x32_bf16 v[62:65], v[148:151], v[192:195], v[62:65]
	v_mfma_f32_16x16x32_bf16 v[58:61], v[156:159], v[192:195], v[58:61]
	v_mfma_f32_16x16x32_bf16 v[50:53], v[148:151], v[200:203], v[50:53]
	v_mfma_f32_16x16x32_bf16 v[42:45], v[156:159], v[200:203], v[42:45]
	v_mfma_f32_16x16x32_bf16 v[34:37], v[148:151], v[208:211], v[34:37]
	v_mfma_f32_16x16x32_bf16 v[26:29], v[156:159], v[208:211], v[26:29]
	v_mfma_f32_16x16x32_bf16 v[18:21], v[148:151], v[216:219], v[18:21]
	v_mfma_f32_16x16x32_bf16 v[10:13], v[156:159], v[216:219], v[10:13]
	v_mfma_f32_16x16x32_bf16 v[62:65], v[152:155], v[196:199], v[62:65]
	v_mfma_f32_16x16x32_bf16 v[58:61], v[160:163], v[196:199], v[58:61]
	v_mfma_f32_16x16x32_bf16 v[50:53], v[152:155], v[204:207], v[50:53]
	v_mfma_f32_16x16x32_bf16 v[42:45], v[160:163], v[204:207], v[42:45]
	v_mfma_f32_16x16x32_bf16 v[34:37], v[152:155], v[212:215], v[34:37]
	v_mfma_f32_16x16x32_bf16 v[26:29], v[160:163], v[212:215], v[26:29]
	v_mfma_f32_16x16x32_bf16 v[18:21], v[152:155], v[220:223], v[18:21]
	v_mfma_f32_16x16x32_bf16 v[10:13], v[160:163], v[220:223], v[10:13]
	s_setprio 0
	s_setprio 3
	v_mfma_f32_16x16x32_bf16 v[54:57], v[176:179], v[192:195], v[54:57]
	v_mfma_f32_16x16x32_bf16 v[46:49], v[184:187], v[192:195], v[46:49]
	v_mfma_f32_16x16x32_bf16 v[38:41], v[176:179], v[200:203], v[38:41]
	v_mfma_f32_16x16x32_bf16 v[30:33], v[184:187], v[200:203], v[30:33]
	v_mfma_f32_16x16x32_bf16 v[22:25], v[176:179], v[208:211], v[22:25]
	v_mfma_f32_16x16x32_bf16 v[14:17], v[184:187], v[208:211], v[14:17]
	v_mfma_f32_16x16x32_bf16 v[6:9], v[176:179], v[216:219], v[6:9]
	v_mfma_f32_16x16x32_bf16 v[2:5], v[184:187], v[216:219], v[2:5]
	v_mfma_f32_16x16x32_bf16 v[54:57], v[180:183], v[196:199], v[54:57]
	v_mfma_f32_16x16x32_bf16 v[46:49], v[188:191], v[196:199], v[46:49]
	v_mfma_f32_16x16x32_bf16 v[38:41], v[180:183], v[204:207], v[38:41]
	v_mfma_f32_16x16x32_bf16 v[30:33], v[188:191], v[204:207], v[30:33]
	v_mfma_f32_16x16x32_bf16 v[22:25], v[180:183], v[212:215], v[22:25]
	v_mfma_f32_16x16x32_bf16 v[14:17], v[188:191], v[212:215], v[14:17]
	v_mfma_f32_16x16x32_bf16 v[6:9], v[180:183], v[220:223], v[6:9]
	v_mfma_f32_16x16x32_bf16 v[2:5], v[188:191], v[220:223], v[2:5]
	s_setprio 0
	s_barrier
	s_add_i32 s60, s60, 2
	s_add_u32 s24, s24, 0x100
	s_addc_u32 s25, s25, 0
	s_add_u32 s58, s58, 0x100
	s_addc_u32 s59, s59, 0
	s_cmp_gt_u32 s60, 13
	s_cbranch_scc0 .LBB0_253
	v_lshl_add_u32 v164, s22, 8, v167
	v_ashrrev_i32_e32 v165, 31, v164
	v_lshlrev_b64 v[148:149], 6, v[164:165]
	v_lshl_add_u64 v[148:149], v[138:139], 0, v[148:149]
	v_add_co_u32_e32 v150, vcc, 0x2000, v148
	v_addc_co_u32_e32 v151, vcc, 0, v149, vcc
	global_load_dwordx4 v[176:179], v[148:149], off
	global_load_dwordx4 v[180:183], v[148:149], off offset:1024
	global_load_dwordx4 v[184:187], v[148:149], off offset:2048
	global_load_dwordx4 v[188:191], v[148:149], off offset:3072
	global_load_dwordx4 v[192:195], v[150:151], off
	global_load_dwordx4 v[196:199], v[150:151], off offset:1024
	global_load_dwordx4 v[200:203], v[150:151], off offset:2048
	global_load_dwordx4 v[204:207], v[150:151], off offset:3072
	s_and_b64 vcc, exec, s[12:13]
	s_cbranch_vccz .LBB0_256
	s_barrier

; #define PG8_STAGE_A(b, h, ptr, NX) do { if constexpr (Sched::GATHER) { unsigned gs_[2]; gs_[0] = ((NX) && last_) ? gN[h][0] : gA[h][0]; gs_[1] = ((NX) && last_) ? gN[h][1] : gA[h][1]; PG8_STAGE(PG8_SA(b, h), ptr, gs_); } \
;         else PG8_STAGE(PG8_SA(b, h), (ptr) + ((h) ? hstep : (size_t)0), voffA); } while (0)
; #define PG8_STAGE(bufoff, gbase, voff) do { _Pragma("unroll") for (int _i = 0; _i < 2; ++_i) \
;         __builtin_amdgcn_global_load_lds((const unsigned*)((const char*)(gbase) + (voff)[_i]), (PG8_LAS unsigned*)(lds + (bufoff) + ldsw + _i * 8192), 16, 0, 0); } while (0)
; #define PG8_LDA(dst, b, h) do { _Pragma("unroll") for (int m = 0; m < 4; ++m) _Pragma("unroll") for (int k = 0; k < 2; ++k) dst[m][k] = *(const PG8_LAS bf16x8*)(lds + PG8_SA(b, h) + aoff + m * 2048 + k * 1024); } while (0)
; #define PG8_LDB(dst, b, h) do { _Pragma("unroll") for (int n = 0; n < 2; ++n) _Pragma("unroll") for (int k = 0; k < 2; ++k) dst[n][k] = *(const PG8_LAS bf16x8*)(lds + PG8_SB(b, h) + boff + n * 2048 + k * 1024); } while (0)
; #define PG8_WAIT_V(n) asm volatile("s_waitcnt vmcnt(" #n ")" ::: "memory")
; #define PG8_WAIT_L(n) asm volatile("s_waitcnt lgkmcnt(" #n ")" ::: "memory")
; template <class Epi, class Sched, bool ALIGN_EPI = false, bool SP2 = false>
; __device__ __forceinline__ void gemm_phase(PG8_LAS unsigned char* lds, const Gemm g, const Sched& S, const Epi& E, const bool skip_epi = false) {
;     ...
;         for (int t = 0; t < nt; t += 2) {
;             const bool last = (t == nt - 2); last_ = last && has_next;
;             const char* a1 = cA + (size_t)(t + 1) * kstep;
;             const char* a2 = last ? nA : cA + (size_t)(t + 2) * kstep; const char* b2 = last ? nB : cB + (size_t)(t + 2) * kstep;
;             const char* a3 = a2 + kstep; const char* b3 = b2 + kstep;
;             if (last && has_next) S.a_ready(nxt);
;             if constexpr (SP2) {
;             PG8_LDB(B0, 0, 0); PG8_LDB(B1, 0, 1); PG8_SCHED; PG8_LDA(At, 0, 0); PG8_STAGE_A(1, 1, a1, false);
;             PG8_WAIT_V(8); PG8_WAIT_L(0); PG8_BAR; PG8_MMA(0, 0, At, B0); PG8_MMA(0, 1, At, B1); PG8_BAR; PG8_SCHED;
;             PG8_LDA(At, 0, 1); PG8_STAGE(PG8_SB(0, 0), b2, voffB); PG8_STAGE(PG8_SB(0, 1), b2 + hstep, voffB); PG8_STAGE_A(0, 0, a2, true);
;             PG8_WAIT_V(8); PG8_WAIT_L(0); PG8_BAR; PG8_MMA(1, 0, At, B0); PG8_MMA(1, 1, At, B1); PG8_BAR; PG8_SCHED;
.LBB0_633:
	s_ashr_i32 s19, s18, 31
	s_lshl_b64 s[20:21], s[18:19], 19
	s_add_u32 s20, s46, s20
	s_addc_u32 s21, s47, s21
	s_and_b64 s[22:23], s[6:7], exec
	s_cselect_b32 s19, s21, s27
	s_cselect_b32 s25, s20, s26
	s_ashr_i32 s17, s16, 31
	s_lshl_b64 s[22:23], s[16:17], 19
	v_readlane_b32 s17, v254, 40
	s_add_u32 s22, s17, s22
	v_readlane_b32 s17, v254, 41
	s_addc_u32 s23, s17, s23
	s_and_b64 s[30:31], s[6:7], exec
	s_cselect_b32 s17, s23, s29
	s_cselect_b32 s60, s22, s28
	s_add_u32 s26, s26, 0x40080
	s_addc_u32 s27, s27, 0
	s_add_u32 s61, s28, 0x100
	s_addc_u32 s62, s29, 0
	s_mov_b32 s63, -2
	s_waitcnt lgkmcnt(0)
	ds_read_b128 v[98:101], v234
	ds_read_b128 v[110:113], v234 offset:1024
	ds_read_b128 v[122:125], v234 offset:2048
	ds_read_b128 v[126:129], v234 offset:3072
	ds_read_b128 v[138:141], v235
	ds_read_b128 v[142:145], v235 offset:1024
	ds_read_b128 v[146:149], v235 offset:2048
	ds_read_b128 v[150:153], v235 offset:3072
	s_add_u32 s28, s26, 0xfffc0080
	s_addc_u32 s29, s27, -1
	s_cmp_eq_u32 s63, 12
	s_cselect_b32 s31, s19, s29
	s_cselect_b32 s30, s25, s28
	s_cselect_b32 s29, s17, s62
	s_cselect_b32 s28, s60, s61
	s_add_i32 m0, s3, 0xc000
	ds_read_b128 v[154:157], v236
	ds_read_b128 v[166:169], v236 offset:1024
	ds_read_b128 v[170:173], v236 offset:2048
	ds_read_b128 v[174:177], v236 offset:3072
	ds_read_b128 v[178:181], v236 offset:4096
	ds_read_b128 v[182:185], v236 offset:5120
	ds_read_b128 v[186:189], v236 offset:6144
	ds_read_b128 v[206:209], v236 offset:7168
	global_load_lds_dwordx4 v198, s[26:27]
	s_add_i32 m0, s3, 0xe000
	s_nop 0
	global_load_lds_dwordx4 v200, s[26:27]
	s_waitcnt vmcnt(8)
	s_waitcnt lgkmcnt(0)
	s_barrier
	s_setprio 3
	s_waitcnt lgkmcnt(0)
	v_mfma_f32_16x16x32_bf16 v[162:165], v[98:101], v[154:157], 0
	v_mfma_f32_16x16x32_bf16 v[158:161], v[122:125], v[154:157], 0
	v_mfma_f32_16x16x32_bf16 v[118:121], v[98:101], v[170:173], 0
	v_mfma_f32_16x16x32_bf16 v[114:117], v[122:125], v[170:173], 0
	v_lshl_add_u64 v[210:211], s[28:29], 0, v[192:193]
	v_mfma_f32_16x16x32_bf16 v[94:97], v[98:101], v[178:181], 0
	v_mfma_f32_16x16x32_bf16 v[90:93], v[122:125], v[178:181], 0
	v_lshl_add_u64 v[212:213], s[28:29], 0, v[196:197]
	v_mfma_f32_16x16x32_bf16 v[78:81], v[98:101], v[186:189], 0
	v_mfma_f32_16x16x32_bf16 v[74:77], v[122:125], v[186:189], 0
	v_lshl_add_u64 v[216:217], s[30:31], 0, v[194:195]
	v_mfma_f32_16x16x32_bf16 v[162:165], v[110:113], v[166:169], v[162:165]
	v_mfma_f32_16x16x32_bf16 v[158:161], v[126:129], v[166:169], v[158:161]
	v_lshl_add_u64 v[214:215], s[30:31], 0, v[190:191]
	v_mfma_f32_16x16x32_bf16 v[118:121], v[110:113], v[174:177], v[118:121]
	v_mfma_f32_16x16x32_bf16 v[114:117], v[126:129], v[174:177], v[114:117]
	v_mfma_f32_16x16x32_bf16 v[94:97], v[110:113], v[182:185], v[94:97]
	v_mfma_f32_16x16x32_bf16 v[90:93], v[126:129], v[182:185], v[90:93]
	v_mfma_f32_16x16x32_bf16 v[78:81], v[110:113], v[206:209], v[78:81]
	v_mfma_f32_16x16x32_bf16 v[74:77], v[126:129], v[206:209], v[74:77]
	s_setprio 0
	s_setprio 3
	v_mfma_f32_16x16x32_bf16 v[134:137], v[138:141], v[154:157], 0
	v_mfma_f32_16x16x32_bf16 v[130:133], v[146:149], v[154:157], 0
	v_mfma_f32_16x16x32_bf16 v[106:109], v[138:141], v[170:173], 0
	v_mfma_f32_16x16x32_bf16 v[102:105], v[146:149], v[170:173], 0
	v_mfma_f32_16x16x32_bf16 v[86:89], v[138:141], v[178:181], 0
	v_mfma_f32_16x16x32_bf16 v[82:85], v[146:149], v[178:181], 0
	v_mfma_f32_16x16x32_bf16 v[70:73], v[138:141], v[186:189], 0
	v_mfma_f32_16x16x32_bf16 v[66:69], v[146:149], v[186:189], 0
	v_mfma_f32_16x16x32_bf16 v[134:137], v[142:145], v[166:169], v[134:137]
	v_mfma_f32_16x16x32_bf16 v[130:133], v[150:153], v[166:169], v[130:133]
	v_mfma_f32_16x16x32_bf16 v[106:109], v[142:145], v[174:177], v[106:109]
	v_mfma_f32_16x16x32_bf16 v[102:105], v[150:153], v[174:177], v[102:105]
	v_mfma_f32_16x16x32_bf16 v[86:89], v[142:145], v[182:185], v[86:89]
	v_mfma_f32_16x16x32_bf16 v[82:85], v[150:153], v[182:185], v[82:85]
	v_mfma_f32_16x16x32_bf16 v[70:73], v[142:145], v[206:209], v[70:73]
	v_mfma_f32_16x16x32_bf16 v[66:69], v[150:153], v[206:209], v[66:69]
	s_setprio 0
	s_barrier
	s_add_i32 s64, s57, s2
	s_mov_b32 m0, s64
	ds_read_b128 v[154:157], v236 offset:16384
	ds_read_b128 v[166:169], v236 offset:17408
	ds_read_b128 v[170:173], v236 offset:18432
	ds_read_b128 v[174:177], v236 offset:19456
	ds_read_b128 v[178:181], v236 offset:20480
	ds_read_b128 v[182:185], v236 offset:21504
	ds_read_b128 v[186:189], v236 offset:22528
	ds_read_b128 v[206:209], v236 offset:23552
	global_load_lds_dwordx4 v[210:211], off
	s_add_i32 m0, s64, 0x2000
	s_add_u32 s64, s28, 0x40000
	s_addc_u32 s65, s29, 0
	s_add_i32 s66, s58, s2
	global_load_lds_dwordx4 v[212:213], off
	s_mov_b32 m0, s66
	s_nop 0
	global_load_lds_dwordx4 v192, s[64:65]
	s_add_i32 m0, s66, 0x2000
	s_nop 0
	global_load_lds_dwordx4 v196, s[64:65]
	s_mov_b32 m0, s3
	s_nop 0
	global_load_lds_dwordx4 v[214:215], off
	s_mov_b32 m0, s34
	s_nop 0
	global_load_lds_dwordx4 v[216:217], off
	s_waitcnt vmcnt(8)
	s_waitcnt lgkmcnt(0)
	s_barrier
; #define PG8_STAGE_A(b, h, ptr, NX) do { if constexpr (Sched::GATHER) { unsigned gs_[2]; gs_[0] = ((NX) && last_) ? gN[h][0] : gA[h][0]; gs_[1] = ((NX) && last_) ? gN[h][1] : gA[h][1]; PG8_STAGE(PG8_SA(b, h), ptr, gs_); } \
;         else PG8_STAGE(PG8_SA(b, h), (ptr) + ((h) ? hstep : (size_t)0), voffA); } while (0)
; #define PG8_STAGE(bufoff, gbase, voff) do { _Pragma("unroll") for (int _i = 0; _i < 2; ++_i) \
;         __builtin_amdgcn_global_load_lds((const unsigned*)((const char*)(gbase) + (voff)[_i]), (PG8_LAS unsigned*)(lds + (bufoff) + ldsw + _i * 8192), 16, 0, 0); } while (0)
; #define PG8_LDA(dst, b, h) do { _Pragma("unroll") for (int m = 0; m < 4; ++m) _Pragma("unroll") for (int k = 0; k < 2; ++k) dst[m][k] = *(const PG8_LAS bf16x8*)(lds + PG8_SA(b, h) + aoff + m * 2048 + k * 1024); } while (0)
; #define PG8_LDB(dst, b, h) do { _Pragma("unroll") for (int n = 0; n < 2; ++n) _Pragma("unroll") for (int k = 0; k < 2; ++k) dst[n][k] = *(const PG8_LAS bf16x8*)(lds + PG8_SB(b, h) + boff + n * 2048 + k * 1024); } while (0)
; #define PG8_MMA(ai, bj, At, Bt) do { __builtin_amdgcn_s_setprio(1); _Pragma("unroll") for (int m = 0; m < 4; ++m) _Pragma("unroll") for (int n = 0; n < 2; ++n) _Pragma("unroll") for (int k = 0; k < 2; ++k) \
;         acc[ai][bj][m][n] = __builtin_amdgcn_mfma_f32_16x16x32_bf16(Bt[n][k], At[m][k], acc[ai][bj][m][n], 0, 0, 0); __builtin_amdgcn_s_setprio(0); } while (0)
; #define PG8_WAIT_V(n) asm volatile("s_waitcnt vmcnt(" #n ")" ::: "memory")
; #define PG8_BAR __builtin_amdgcn_s_barrier()
; template <class Epi, class Sched, bool ALIGN_EPI = false, bool SP2 = false>
; __device__ __forceinline__ void gemm_phase(PG8_LAS unsigned char* lds, const Gemm g, const Sched& S, const Epi& E, const bool skip_epi = false) {
;     ...
;             PG8_WAIT_V(8); PG8_WAIT_L(0); PG8_BAR; PG8_MMA(0, 0, At, B0); PG8_MMA(0, 1, At, B1); PG8_BAR; PG8_SCHED;
;             PG8_LDA(At, 0, 1); PG8_STAGE(PG8_SB(0, 0), b2, voffB); PG8_STAGE(PG8_SB(0, 1), b2 + hstep, voffB); PG8_STAGE_A(0, 0, a2, true);
;             PG8_WAIT_V(8); PG8_WAIT_L(0); PG8_BAR; PG8_MMA(1, 0, At, B0); PG8_MMA(1, 1, At, B1); PG8_BAR; PG8_SCHED;
;             PG8_LDB(B0, 1, 0); PG8_LDB(B1, 1, 1); PG8_SCHED; PG8_LDA(At, 1, 0); PG8_STAGE_A(0, 1, a2, true);
;             PG8_WAIT_V(8); PG8_WAIT_L(0); PG8_BAR; PG8_MMA(0, 0, At, B0); PG8_MMA(0, 1, At, B1); PG8_BAR; PG8_SCHED;
	s_setprio 3
	s_waitcnt lgkmcnt(0)
	v_mfma_f32_16x16x32_bf16 v[62:65], v[98:101], v[154:157], 0
	v_mfma_f32_16x16x32_bf16 v[58:61], v[122:125], v[154:157], 0
	v_mfma_f32_16x16x32_bf16 v[46:49], v[98:101], v[170:173], 0
	v_mfma_f32_16x16x32_bf16 v[42:45], v[122:125], v[170:173], 0
	v_mfma_f32_16x16x32_bf16 v[30:33], v[98:101], v[178:181], 0
	v_mfma_f32_16x16x32_bf16 v[26:29], v[122:125], v[178:181], 0
	v_mfma_f32_16x16x32_bf16 v[14:17], v[98:101], v[186:189], 0
	v_mfma_f32_16x16x32_bf16 v[10:13], v[122:125], v[186:189], 0
	v_mfma_f32_16x16x32_bf16 v[62:65], v[110:113], v[166:169], v[62:65]
	v_mfma_f32_16x16x32_bf16 v[58:61], v[126:129], v[166:169], v[58:61]
	v_mfma_f32_16x16x32_bf16 v[46:49], v[110:113], v[174:177], v[46:49]
	v_mfma_f32_16x16x32_bf16 v[42:45], v[126:129], v[174:177], v[42:45]
	v_mfma_f32_16x16x32_bf16 v[30:33], v[110:113], v[182:185], v[30:33]
	v_mfma_f32_16x16x32_bf16 v[26:29], v[126:129], v[182:185], v[26:29]
	v_mfma_f32_16x16x32_bf16 v[14:17], v[110:113], v[206:209], v[14:17]
	v_mfma_f32_16x16x32_bf16 v[10:13], v[126:129], v[206:209], v[10:13]
	s_setprio 0
	s_setprio 3
	v_mfma_f32_16x16x32_bf16 v[54:57], v[138:141], v[154:157], 0
	v_mfma_f32_16x16x32_bf16 v[50:53], v[146:149], v[154:157], 0
	v_mfma_f32_16x16x32_bf16 v[38:41], v[138:141], v[170:173], 0
	v_mfma_f32_16x16x32_bf16 v[34:37], v[146:149], v[170:173], 0
	v_mfma_f32_16x16x32_bf16 v[22:25], v[138:141], v[178:181], 0
	v_mfma_f32_16x16x32_bf16 v[18:21], v[146:149], v[178:181], 0
	v_mfma_f32_16x16x32_bf16 v[6:9], v[138:141], v[186:189], 0
	v_mfma_f32_16x16x32_bf16 v[2:5], v[146:149], v[186:189], 0
	v_mfma_f32_16x16x32_bf16 v[54:57], v[142:145], v[166:169], v[54:57]
	v_mfma_f32_16x16x32_bf16 v[50:53], v[150:153], v[166:169], v[50:53]
	v_mfma_f32_16x16x32_bf16 v[38:41], v[142:145], v[174:177], v[38:41]
	v_mfma_f32_16x16x32_bf16 v[34:37], v[150:153], v[174:177], v[34:37]
	v_mfma_f32_16x16x32_bf16 v[22:25], v[142:145], v[182:185], v[22:25]
	v_mfma_f32_16x16x32_bf16 v[18:21], v[150:153], v[182:185], v[18:21]
	v_mfma_f32_16x16x32_bf16 v[6:9], v[142:145], v[206:209], v[6:9]
	v_mfma_f32_16x16x32_bf16 v[2:5], v[150:153], v[206:209], v[2:5]
	s_setprio 0
	s_barrier
	s_add_i32 s64, 0, 0x18000
	s_add_i32 s65, 0, 0x1c000
	v_add_u32_e32 v126, s64, v229
	v_add_u32_e32 v150, s65, v229
	ds_read_b128 v[98:101], v126
	ds_read_b128 v[110:113], v126 offset:1024
	ds_read_b128 v[122:125], v126 offset:2048
	ds_read_b128 v[126:129], v126 offset:3072
	ds_read_b128 v[138:141], v150
	ds_read_b128 v[142:145], v150 offset:1024
	ds_read_b128 v[146:149], v150 offset:2048
	ds_read_b128 v[150:153], v150 offset:3072
	s_add_u32 s30, s30, 0x40000
	s_addc_u32 s31, s31, 0
	s_mov_b32 m0, s35
	ds_read_b128 v[154:157], v236 offset:32768
	ds_read_b128 v[166:169], v236 offset:33792
	ds_read_b128 v[170:173], v236 offset:34816
	ds_read_b128 v[174:177], v236 offset:35840
	ds_read_b128 v[178:181], v236 offset:36864
	ds_read_b128 v[182:185], v236 offset:37888
	ds_read_b128 v[186:189], v236 offset:38912
	ds_read_b128 v[206:209], v236 offset:39936
	global_load_lds_dwordx4 v190, s[30:31]
	s_mov_b32 m0, s36
	s_nop 0
	global_load_lds_dwordx4 v194, s[30:31]
	s_waitcnt vmcnt(8)
	s_waitcnt lgkmcnt(0)
	s_barrier
	s_setprio 3
	s_waitcnt lgkmcnt(0)
	v_mfma_f32_16x16x32_bf16 v[162:165], v[98:101], v[154:157], v[162:165]
	v_mfma_f32_16x16x32_bf16 v[158:161], v[122:125], v[154:157], v[158:161]
	v_mfma_f32_16x16x32_bf16 v[118:121], v[98:101], v[170:173], v[118:121]
	v_mfma_f32_16x16x32_bf16 v[114:117], v[122:125], v[170:173], v[114:117]
	v_mfma_f32_16x16x32_bf16 v[94:97], v[98:101], v[178:181], v[94:97]
	v_mfma_f32_16x16x32_bf16 v[90:93], v[122:125], v[178:181], v[90:93]
	v_mfma_f32_16x16x32_bf16 v[78:81], v[98:101], v[186:189], v[78:81]
	v_mfma_f32_16x16x32_bf16 v[74:77], v[122:125], v[186:189], v[74:77]
	v_mfma_f32_16x16x32_bf16 v[162:165], v[110:113], v[166:169], v[162:165]
	v_mfma_f32_16x16x32_bf16 v[158:161], v[126:129], v[166:169], v[158:161]
	v_mfma_f32_16x16x32_bf16 v[118:121], v[110:113], v[174:177], v[118:121]
	v_mfma_f32_16x16x32_bf16 v[114:117], v[126:129], v[174:177], v[114:117]
	v_mfma_f32_16x16x32_bf16 v[94:97], v[110:113], v[182:185], v[94:97]
	v_mfma_f32_16x16x32_bf16 v[90:93], v[126:129], v[182:185], v[90:93]
	v_mfma_f32_16x16x32_bf16 v[78:81], v[110:113], v[206:209], v[78:81]
	v_mfma_f32_16x16x32_bf16 v[74:77], v[126:129], v[206:209], v[74:77]
	s_setprio 0
	s_setprio 3
	v_mfma_f32_16x16x32_bf16 v[134:137], v[138:141], v[154:157], v[134:137]
	v_mfma_f32_16x16x32_bf16 v[130:133], v[146:149], v[154:157], v[130:133]
	v_mfma_f32_16x16x32_bf16 v[106:109], v[138:141], v[170:173], v[106:109]
	v_mfma_f32_16x16x32_bf16 v[102:105], v[146:149], v[170:173], v[102:105]
	v_mfma_f32_16x16x32_bf16 v[86:89], v[138:141], v[178:181], v[86:89]
	v_mfma_f32_16x16x32_bf16 v[82:85], v[146:149], v[178:181], v[82:85]
	v_mfma_f32_16x16x32_bf16 v[70:73], v[138:141], v[186:189], v[70:73]
	v_mfma_f32_16x16x32_bf16 v[66:69], v[146:149], v[186:189], v[66:69]
	v_mfma_f32_16x16x32_bf16 v[134:137], v[142:145], v[166:169], v[134:137]
	v_mfma_f32_16x16x32_bf16 v[130:133], v[150:153], v[166:169], v[130:133]
	v_mfma_f32_16x16x32_bf16 v[106:109], v[142:145], v[174:177], v[106:109]
	v_mfma_f32_16x16x32_bf16 v[102:105], v[150:153], v[174:177], v[102:105]
	v_mfma_f32_16x16x32_bf16 v[86:89], v[142:145], v[182:185], v[86:89]
	v_mfma_f32_16x16x32_bf16 v[82:85], v[150:153], v[182:185], v[82:85]
	v_mfma_f32_16x16x32_bf16 v[70:73], v[142:145], v[206:209], v[70:73]
	v_mfma_f32_16x16x32_bf16 v[66:69], v[150:153], v[206:209], v[66:69]
	s_setprio 0
	s_barrier
; #define PG8_STAGE_A(b, h, ptr, NX) do { if constexpr (Sched::GATHER) { unsigned gs_[2]; gs_[0] = ((NX) && last_) ? gN[h][0] : gA[h][0]; gs_[1] = ((NX) && last_) ? gN[h][1] : gA[h][1]; PG8_STAGE(PG8_SA(b, h), ptr, gs_); } \
;         else PG8_STAGE(PG8_SA(b, h), (ptr) + ((h) ? hstep : (size_t)0), voffA); } while (0)
; #define PG8_STAGE(bufoff, gbase, voff) do { _Pragma("unroll") for (int _i = 0; _i < 2; ++_i) \
;         __builtin_amdgcn_global_load_lds((const unsigned*)((const char*)(gbase) + (voff)[_i]), (PG8_LAS unsigned*)(lds + (bufoff) + ldsw + _i * 8192), 16, 0, 0); } while (0)
; #define PG8_WAIT_V(n) asm volatile("s_waitcnt vmcnt(" #n ")" ::: "memory")
; #define PG8_BAR __builtin_amdgcn_s_barrier()
; template <class Epi, class Sched, bool ALIGN_EPI = false, bool SP2 = false>
; __device__ __forceinline__ void gemm_phase(PG8_LAS unsigned char* lds, const Gemm g, const Sched& S, const Epi& E, const bool skip_epi = false) {
;     ...
;         for (int t = 0; t < nt; t += 2) {
;             const bool last = (t == nt - 2); last_ = last && has_next;
;             const char* a1 = cA + (size_t)(t + 1) * kstep;
;             const char* a2 = last ? nA : cA + (size_t)(t + 2) * kstep; const char* b2 = last ? nB : cB + (size_t)(t + 2) * kstep;
;             const char* a3 = a2 + kstep; const char* b3 = b2 + kstep;
;             if (last && has_next) S.a_ready(nxt);
;             if constexpr (SP2) {
;             PG8_LDB(B0, 0, 0); PG8_LDB(B1, 0, 1); PG8_SCHED; PG8_LDA(At, 0, 0); PG8_STAGE_A(1, 1, a1, false);
;             PG8_WAIT_V(8); PG8_WAIT_L(0); PG8_BAR; PG8_MMA(0, 0, At, B0); PG8_MMA(0, 1, At, B1); PG8_BAR; PG8_SCHED;
;             PG8_LDA(At, 0, 1); PG8_STAGE(PG8_SB(0, 0), b2, voffB); PG8_STAGE(PG8_SB(0, 1), b2 + hstep, voffB); PG8_STAGE_A(0, 0, a2, true);
;             PG8_WAIT_V(8); PG8_WAIT_L(0); PG8_BAR; PG8_MMA(1, 0, At, B0); PG8_MMA(1, 1, At, B1); PG8_BAR; PG8_SCHED;
;             PG8_LDB(B0, 1, 0); PG8_LDB(B1, 1, 1); PG8_SCHED; PG8_LDA(At, 1, 0); PG8_STAGE_A(0, 1, a2, true);
;             PG8_WAIT_V(8); PG8_WAIT_L(0); PG8_BAR; PG8_MMA(0, 0, At, B0); PG8_MMA(0, 1, At, B1); PG8_BAR; PG8_SCHED;
;             PG8_LDA(At, 1, 1); PG8_STAGE(PG8_SB(1, 0), b3, voffB); PG8_STAGE(PG8_SB(1, 1), b3 + hstep, voffB); PG8_STAGE_A(1, 0, a3, true);
;             PG8_WAIT_V(8); PG8_WAIT_L(0); PG8_BAR; PG8_MMA(1, 0, At, B0); PG8_MMA(1, 1, At, B1); PG8_BAR; PG8_SCHED;
	s_add_i32 s30, s64, s2
	s_add_i32 m0, s30, 0xffffff80
	ds_read_b128 v[154:157], v236 offset:49152
	ds_read_b128 v[166:169], v236 offset:50176
	ds_read_b128 v[170:173], v236 offset:51200
	ds_read_b128 v[174:177], v236 offset:52224
	ds_read_b128 v[178:181], v236 offset:53248
	ds_read_b128 v[182:185], v236 offset:54272
	ds_read_b128 v[186:189], v236 offset:55296
	ds_read_b128 v[206:209], v236 offset:56320
	global_load_lds_dwordx4 v[210:211], off offset:128
	s_add_i32 m0, s30, 0x1f80
	s_add_u32 s28, s28, 0x40080
	s_addc_u32 s29, s29, 0
	s_add_i32 s30, s65, s2
	global_load_lds_dwordx4 v[212:213], off offset:128
	s_mov_b32 m0, s30
	s_nop 0
	global_load_lds_dwordx4 v192, s[28:29]
	s_add_i32 m0, s30, 0x2000
	s_nop 0
	global_load_lds_dwordx4 v196, s[28:29]
	s_add_i32 m0, s39, 0xffffff80
	s_nop 0
	global_load_lds_dwordx4 v[214:215], off offset:128
	s_add_i32 m0, s48, 0xffffff80
	s_nop 0
	global_load_lds_dwordx4 v[216:217], off offset:128
	s_waitcnt vmcnt(8)
	s_waitcnt lgkmcnt(0)
	s_barrier
	s_setprio 3
	s_waitcnt lgkmcnt(0)
	v_mfma_f32_16x16x32_bf16 v[62:65], v[98:101], v[154:157], v[62:65]
	v_mfma_f32_16x16x32_bf16 v[58:61], v[122:125], v[154:157], v[58:61]
	v_mfma_f32_16x16x32_bf16 v[46:49], v[98:101], v[170:173], v[46:49]
	v_mfma_f32_16x16x32_bf16 v[42:45], v[122:125], v[170:173], v[42:45]
	v_mfma_f32_16x16x32_bf16 v[30:33], v[98:101], v[178:181], v[30:33]
	v_mfma_f32_16x16x32_bf16 v[26:29], v[122:125], v[178:181], v[26:29]
	v_mfma_f32_16x16x32_bf16 v[14:17], v[98:101], v[186:189], v[14:17]
	v_mfma_f32_16x16x32_bf16 v[10:13], v[122:125], v[186:189], v[10:13]
	v_mfma_f32_16x16x32_bf16 v[62:65], v[110:113], v[166:169], v[62:65]
	v_mfma_f32_16x16x32_bf16 v[58:61], v[126:129], v[166:169], v[58:61]
	v_mfma_f32_16x16x32_bf16 v[46:49], v[110:113], v[174:177], v[46:49]
	v_mfma_f32_16x16x32_bf16 v[42:45], v[126:129], v[174:177], v[42:45]
	v_mfma_f32_16x16x32_bf16 v[30:33], v[110:113], v[182:185], v[30:33]
	v_mfma_f32_16x16x32_bf16 v[26:29], v[126:129], v[182:185], v[26:29]
	v_mfma_f32_16x16x32_bf16 v[14:17], v[110:113], v[206:209], v[14:17]
	v_mfma_f32_16x16x32_bf16 v[10:13], v[126:129], v[206:209], v[10:13]
	s_setprio 0
	s_setprio 3
	v_mfma_f32_16x16x32_bf16 v[54:57], v[138:141], v[154:157], v[54:57]
	v_mfma_f32_16x16x32_bf16 v[50:53], v[146:149], v[154:157], v[50:53]
	v_mfma_f32_16x16x32_bf16 v[38:41], v[138:141], v[170:173], v[38:41]
	v_mfma_f32_16x16x32_bf16 v[34:37], v[146:149], v[170:173], v[34:37]
	v_mfma_f32_16x16x32_bf16 v[22:25], v[138:141], v[178:181], v[22:25]
	v_mfma_f32_16x16x32_bf16 v[18:21], v[146:149], v[178:181], v[18:21]
	v_mfma_f32_16x16x32_bf16 v[6:9], v[138:141], v[186:189], v[6:9]
	v_mfma_f32_16x16x32_bf16 v[2:5], v[146:149], v[186:189], v[2:5]
	v_mfma_f32_16x16x32_bf16 v[54:57], v[142:145], v[166:169], v[54:57]
	v_mfma_f32_16x16x32_bf16 v[50:53], v[150:153], v[166:169], v[50:53]
	v_mfma_f32_16x16x32_bf16 v[38:41], v[142:145], v[174:177], v[38:41]
	v_mfma_f32_16x16x32_bf16 v[34:37], v[150:153], v[174:177], v[34:37]
	v_mfma_f32_16x16x32_bf16 v[22:25], v[142:145], v[182:185], v[22:25]
	v_mfma_f32_16x16x32_bf16 v[18:21], v[150:153], v[182:185], v[18:21]
	v_mfma_f32_16x16x32_bf16 v[6:9], v[142:145], v[206:209], v[6:9]
	v_mfma_f32_16x16x32_bf16 v[2:5], v[150:153], v[206:209], v[2:5]
	s_setprio 0
	s_barrier
	s_add_i32 s63, s63, 2
	s_add_u32 s26, s26, 0x100
	s_addc_u32 s27, s27, 0
	s_add_u32 s61, s61, 0x100
	s_addc_u32 s62, s62, 0
	s_cmp_gt_u32 s63, 13
.LBB0_634:
	ds_read_b128 v[98:101], v234
	ds_read_b128 v[110:113], v234 offset:1024
	ds_read_b128 v[122:125], v234 offset:2048
	ds_read_b128 v[126:129], v234 offset:3072
	ds_read_b128 v[138:141], v235
	ds_read_b128 v[142:145], v235 offset:1024
	ds_read_b128 v[146:149], v235 offset:2048
	ds_read_b128 v[150:153], v235 offset:3072
	s_add_u32 s28, s26, 0xfffc0080
	s_addc_u32 s29, s27, -1
	s_cmp_eq_u32 s63, 12
	s_cselect_b32 s31, s19, s29
	s_cselect_b32 s30, s25, s28
	s_cselect_b32 s29, s17, s62
	s_cselect_b32 s28, s60, s61
	s_add_i32 m0, s3, 0xc000
	ds_read_b128 v[154:157], v236
	ds_read_b128 v[166:169], v236 offset:1024
	ds_read_b128 v[170:173], v236 offset:2048
	ds_read_b128 v[174:177], v236 offset:3072
	ds_read_b128 v[178:181], v236 offset:4096
	ds_read_b128 v[182:185], v236 offset:5120
	ds_read_b128 v[186:189], v236 offset:6144
	ds_read_b128 v[206:209], v236 offset:7168
	global_load_lds_dwordx4 v198, s[26:27]
	s_add_i32 m0, s3, 0xe000
	s_nop 0
	global_load_lds_dwordx4 v200, s[26:27]
	s_waitcnt vmcnt(8)
	s_waitcnt lgkmcnt(0)
	s_barrier
; #define PG8_STAGE_A(b, h, ptr, NX) do { if constexpr (Sched::GATHER) { unsigned gs_[2]; gs_[0] = ((NX) && last_) ? gN[h][0] : gA[h][0]; gs_[1] = ((NX) && last_) ? gN[h][1] : gA[h][1]; PG8_STAGE(PG8_SA(b, h), ptr, gs_); } \
;         else PG8_STAGE(PG8_SA(b, h), (ptr) + ((h) ? hstep : (size_t)0), voffA); } while (0)
; #define PG8_STAGE(bufoff, gbase, voff) do { _Pragma("unroll") for (int _i = 0; _i < 2; ++_i) \
;         __builtin_amdgcn_global_load_lds((const unsigned*)((const char*)(gbase) + (voff)[_i]), (PG8_LAS unsigned*)(lds + (bufoff) + ldsw + _i * 8192), 16, 0, 0); } while (0)
; #define PG8_LDA(dst, b, h) do { _Pragma("unroll") for (int m = 0; m < 4; ++m) _Pragma("unroll") for (int k = 0; k < 2; ++k) dst[m][k] = *(const PG8_LAS bf16x8*)(lds + PG8_SA(b, h) + aoff + m * 2048 + k * 1024); } while (0)
; #define PG8_LDB(dst, b, h) do { _Pragma("unroll") for (int n = 0; n < 2; ++n) _Pragma("unroll") for (int k = 0; k < 2; ++k) dst[n][k] = *(const PG8_LAS bf16x8*)(lds + PG8_SB(b, h) + boff + n * 2048 + k * 1024); } while (0)
; #define PG8_MMA(ai, bj, At, Bt) do { __builtin_amdgcn_s_setprio(1); _Pragma("unroll") for (int m = 0; m < 4; ++m) _Pragma("unroll") for (int n = 0; n < 2; ++n) _Pragma("unroll") for (int k = 0; k < 2; ++k) \
;         acc[ai][bj][m][n] = __builtin_amdgcn_mfma_f32_16x16x32_bf16(Bt[n][k], At[m][k], acc[ai][bj][m][n], 0, 0, 0); __builtin_amdgcn_s_setprio(0); } while (0)
; #define PG8_WAIT_V(n) asm volatile("s_waitcnt vmcnt(" #n ")" ::: "memory")
; #define PG8_WAIT_L(n) asm volatile("s_waitcnt lgkmcnt(" #n ")" ::: "memory")
; #define PG8_BAR __builtin_amdgcn_s_barrier()
; #define PG8_SCHED __builtin_amdgcn_sched_barrier(0)
; template <class Epi, class Sched, bool ALIGN_EPI = false, bool SP2 = false>
; __device__ __forceinline__ void gemm_phase(PG8_LAS unsigned char* lds, const Gemm g, const Sched& S, const Epi& E, const bool skip_epi = false) {
;     ...
;             PG8_LDB(B0, 0, 0); PG8_LDB(B1, 0, 1); PG8_SCHED; PG8_LDA(At, 0, 0); PG8_STAGE_A(1, 1, a1, false);
;             PG8_WAIT_V(8); PG8_WAIT_L(0); PG8_BAR; PG8_MMA(0, 0, At, B0); PG8_MMA(0, 1, At, B1); PG8_BAR; PG8_SCHED;
;             PG8_LDA(At, 0, 1); PG8_STAGE(PG8_SB(0, 0), b2, voffB); PG8_STAGE(PG8_SB(0, 1), b2 + hstep, voffB); PG8_STAGE_A(0, 0, a2, true);
;             PG8_WAIT_V(8); PG8_WAIT_L(0); PG8_BAR; PG8_MMA(1, 0, At, B0); PG8_MMA(1, 1, At, B1); PG8_BAR; PG8_SCHED;
	s_setprio 3
	s_waitcnt lgkmcnt(0)
	v_mfma_f32_16x16x32_bf16 v[162:165], v[98:101], v[154:157], v[162:165]
	v_mfma_f32_16x16x32_bf16 v[158:161], v[122:125], v[154:157], v[158:161]
	v_mfma_f32_16x16x32_bf16 v[118:121], v[98:101], v[170:173], v[118:121]
	v_mfma_f32_16x16x32_bf16 v[114:117], v[122:125], v[170:173], v[114:117]
	v_lshl_add_u64 v[210:211], s[28:29], 0, v[192:193]
	v_mfma_f32_16x16x32_bf16 v[94:97], v[98:101], v[178:181], v[94:97]
	v_mfma_f32_16x16x32_bf16 v[90:93], v[122:125], v[178:181], v[90:93]
	v_lshl_add_u64 v[212:213], s[28:29], 0, v[196:197]
	v_mfma_f32_16x16x32_bf16 v[78:81], v[98:101], v[186:189], v[78:81]
	v_mfma_f32_16x16x32_bf16 v[74:77], v[122:125], v[186:189], v[74:77]
	v_lshl_add_u64 v[216:217], s[30:31], 0, v[194:195]
	v_mfma_f32_16x16x32_bf16 v[162:165], v[110:113], v[166:169], v[162:165]
	v_mfma_f32_16x16x32_bf16 v[158:161], v[126:129], v[166:169], v[158:161]
	v_lshl_add_u64 v[214:215], s[30:31], 0, v[190:191]
	v_mfma_f32_16x16x32_bf16 v[118:121], v[110:113], v[174:177], v[118:121]
	v_mfma_f32_16x16x32_bf16 v[114:117], v[126:129], v[174:177], v[114:117]
	v_mfma_f32_16x16x32_bf16 v[94:97], v[110:113], v[182:185], v[94:97]
	v_mfma_f32_16x16x32_bf16 v[90:93], v[126:129], v[182:185], v[90:93]
	v_mfma_f32_16x16x32_bf16 v[78:81], v[110:113], v[206:209], v[78:81]
	v_mfma_f32_16x16x32_bf16 v[74:77], v[126:129], v[206:209], v[74:77]
	s_setprio 0
	s_setprio 3
	v_mfma_f32_16x16x32_bf16 v[134:137], v[138:141], v[154:157], v[134:137]
	v_mfma_f32_16x16x32_bf16 v[130:133], v[146:149], v[154:157], v[130:133]
	v_mfma_f32_16x16x32_bf16 v[106:109], v[138:141], v[170:173], v[106:109]
	v_mfma_f32_16x16x32_bf16 v[102:105], v[146:149], v[170:173], v[102:105]
	v_mfma_f32_16x16x32_bf16 v[86:89], v[138:141], v[178:181], v[86:89]
	v_mfma_f32_16x16x32_bf16 v[82:85], v[146:149], v[178:181], v[82:85]
	v_mfma_f32_16x16x32_bf16 v[70:73], v[138:141], v[186:189], v[70:73]
	v_mfma_f32_16x16x32_bf16 v[66:69], v[146:149], v[186:189], v[66:69]
	v_mfma_f32_16x16x32_bf16 v[134:137], v[142:145], v[166:169], v[134:137]
	v_mfma_f32_16x16x32_bf16 v[130:133], v[150:153], v[166:169], v[130:133]
	v_mfma_f32_16x16x32_bf16 v[106:109], v[142:145], v[174:177], v[106:109]
	v_mfma_f32_16x16x32_bf16 v[102:105], v[150:153], v[174:177], v[102:105]
	v_mfma_f32_16x16x32_bf16 v[86:89], v[142:145], v[182:185], v[86:89]
	v_mfma_f32_16x16x32_bf16 v[82:85], v[150:153], v[182:185], v[82:85]
	v_mfma_f32_16x16x32_bf16 v[70:73], v[142:145], v[206:209], v[70:73]
	v_mfma_f32_16x16x32_bf16 v[66:69], v[150:153], v[206:209], v[66:69]
	s_setprio 0
	s_barrier
	s_add_i32 s64, s57, s2
	s_mov_b32 m0, s64
	ds_read_b128 v[154:157], v236 offset:16384
	ds_read_b128 v[166:169], v236 offset:17408
	ds_read_b128 v[170:173], v236 offset:18432
	ds_read_b128 v[174:177], v236 offset:19456
	ds_read_b128 v[178:181], v236 offset:20480
	ds_read_b128 v[182:185], v236 offset:21504
	ds_read_b128 v[186:189], v236 offset:22528
	ds_read_b128 v[206:209], v236 offset:23552
	global_load_lds_dwordx4 v[210:211], off
	s_add_i32 m0, s64, 0x2000
	s_add_u32 s64, s28, 0x40000
	s_addc_u32 s65, s29, 0
	s_add_i32 s66, s58, s2
	global_load_lds_dwordx4 v[212:213], off
	s_mov_b32 m0, s66
	s_nop 0
	global_load_lds_dwordx4 v192, s[64:65]
	s_add_i32 m0, s66, 0x2000
	s_nop 0
	global_load_lds_dwordx4 v196, s[64:65]
	s_mov_b32 m0, s3
	s_nop 0
	global_load_lds_dwordx4 v[214:215], off
	s_mov_b32 m0, s34
	s_nop 0
	global_load_lds_dwordx4 v[216:217], off
	s_waitcnt vmcnt(8)
	s_waitcnt lgkmcnt(0)
	s_barrier
	s_setprio 3
	s_waitcnt lgkmcnt(0)
	v_mfma_f32_16x16x32_bf16 v[62:65], v[98:101], v[154:157], v[62:65]
	v_mfma_f32_16x16x32_bf16 v[58:61], v[122:125], v[154:157], v[58:61]
	v_mfma_f32_16x16x32_bf16 v[46:49], v[98:101], v[170:173], v[46:49]
	v_mfma_f32_16x16x32_bf16 v[42:45], v[122:125], v[170:173], v[42:45]
	v_mfma_f32_16x16x32_bf16 v[30:33], v[98:101], v[178:181], v[30:33]
	v_mfma_f32_16x16x32_bf16 v[26:29], v[122:125], v[178:181], v[26:29]
	v_mfma_f32_16x16x32_bf16 v[14:17], v[98:101], v[186:189], v[14:17]
	v_mfma_f32_16x16x32_bf16 v[10:13], v[122:125], v[186:189], v[10:13]
	v_mfma_f32_16x16x32_bf16 v[62:65], v[110:113], v[166:169], v[62:65]
	v_mfma_f32_16x16x32_bf16 v[58:61], v[126:129], v[166:169], v[58:61]
	v_mfma_f32_16x16x32_bf16 v[46:49], v[110:113], v[174:177], v[46:49]
	v_mfma_f32_16x16x32_bf16 v[42:45], v[126:129], v[174:177], v[42:45]
	v_mfma_f32_16x16x32_bf16 v[30:33], v[110:113], v[182:185], v[30:33]
	v_mfma_f32_16x16x32_bf16 v[26:29], v[126:129], v[182:185], v[26:29]
	v_mfma_f32_16x16x32_bf16 v[14:17], v[110:113], v[206:209], v[14:17]
	v_mfma_f32_16x16x32_bf16 v[10:13], v[126:129], v[206:209], v[10:13]
	s_setprio 0
	s_setprio 3
	v_mfma_f32_16x16x32_bf16 v[54:57], v[138:141], v[154:157], v[54:57]
	v_mfma_f32_16x16x32_bf16 v[50:53], v[146:149], v[154:157], v[50:53]
	v_mfma_f32_16x16x32_bf16 v[38:41], v[138:141], v[170:173], v[38:41]
	v_mfma_f32_16x16x32_bf16 v[34:37], v[146:149], v[170:173], v[34:37]
	v_mfma_f32_16x16x32_bf16 v[22:25], v[138:141], v[178:181], v[22:25]
	v_mfma_f32_16x16x32_bf16 v[18:21], v[146:149], v[178:181], v[18:21]
	v_mfma_f32_16x16x32_bf16 v[6:9], v[138:141], v[186:189], v[6:9]
	v_mfma_f32_16x16x32_bf16 v[2:5], v[146:149], v[186:189], v[2:5]
	v_mfma_f32_16x16x32_bf16 v[54:57], v[142:145], v[166:169], v[54:57]
	v_mfma_f32_16x16x32_bf16 v[50:53], v[150:153], v[166:169], v[50:53]
	v_mfma_f32_16x16x32_bf16 v[38:41], v[142:145], v[174:177], v[38:41]
	v_mfma_f32_16x16x32_bf16 v[34:37], v[150:153], v[174:177], v[34:37]
	v_mfma_f32_16x16x32_bf16 v[22:25], v[142:145], v[182:185], v[22:25]
	v_mfma_f32_16x16x32_bf16 v[18:21], v[150:153], v[182:185], v[18:21]
	v_mfma_f32_16x16x32_bf16 v[6:9], v[142:145], v[206:209], v[6:9]
	v_mfma_f32_16x16x32_bf16 v[2:5], v[150:153], v[206:209], v[2:5]
	s_setprio 0
	s_barrier
; #define PG8_STAGE_A(b, h, ptr, NX) do { if constexpr (Sched::GATHER) { unsigned gs_[2]; gs_[0] = ((NX) && last_) ? gN[h][0] : gA[h][0]; gs_[1] = ((NX) && last_) ? gN[h][1] : gA[h][1]; PG8_STAGE(PG8_SA(b, h), ptr, gs_); } \
;         else PG8_STAGE(PG8_SA(b, h), (ptr) + ((h) ? hstep : (size_t)0), voffA); } while (0)
; #define PG8_STAGE(bufoff, gbase, voff) do { _Pragma("unroll") for (int _i = 0; _i < 2; ++_i) \
;         __builtin_amdgcn_global_load_lds((const unsigned*)((const char*)(gbase) + (voff)[_i]), (PG8_LAS unsigned*)(lds + (bufoff) + ldsw + _i * 8192), 16, 0, 0); } while (0)
; #define PG8_LDA(dst, b, h) do { _Pragma("unroll") for (int m = 0; m < 4; ++m) _Pragma("unroll") for (int k = 0; k < 2; ++k) dst[m][k] = *(const PG8_LAS bf16x8*)(lds + PG8_SA(b, h) + aoff + m * 2048 + k * 1024); } while (0)
; #define PG8_LDB(dst, b, h) do { _Pragma("unroll") for (int n = 0; n < 2; ++n) _Pragma("unroll") for (int k = 0; k < 2; ++k) dst[n][k] = *(const PG8_LAS bf16x8*)(lds + PG8_SB(b, h) + boff + n * 2048 + k * 1024); } while (0)
; #define PG8_MMA(ai, bj, At, Bt) do { __builtin_amdgcn_s_setprio(1); _Pragma("unroll") for (int m = 0; m < 4; ++m) _Pragma("unroll") for (int n = 0; n < 2; ++n) _Pragma("unroll") for (int k = 0; k < 2; ++k) \
;         acc[ai][bj][m][n] = __builtin_amdgcn_mfma_f32_16x16x32_bf16(Bt[n][k], At[m][k], acc[ai][bj][m][n], 0, 0, 0); __builtin_amdgcn_s_setprio(0); } while (0)
; #define PG8_WAIT_V(n) asm volatile("s_waitcnt vmcnt(" #n ")" ::: "memory")
; #define PG8_WAIT_L(n) asm volatile("s_waitcnt lgkmcnt(" #n ")" ::: "memory")
; #define PG8_BAR __builtin_amdgcn_s_barrier()
; template <class Epi, class Sched, bool ALIGN_EPI = false, bool SP2 = false>
; __device__ __forceinline__ void gemm_phase(PG8_LAS unsigned char* lds, const Gemm g, const Sched& S, const Epi& E, const bool skip_epi = false) {
;     ...
;             PG8_LDB(B0, 1, 0); PG8_LDB(B1, 1, 1); PG8_SCHED; PG8_LDA(At, 1, 0); PG8_STAGE_A(0, 1, a2, true);
;             PG8_WAIT_V(8); PG8_WAIT_L(0); PG8_BAR; PG8_MMA(0, 0, At, B0); PG8_MMA(0, 1, At, B1); PG8_BAR; PG8_SCHED;
;             PG8_LDA(At, 1, 1); PG8_STAGE(PG8_SB(1, 0), b3, voffB); PG8_STAGE(PG8_SB(1, 1), b3 + hstep, voffB); PG8_STAGE_A(1, 0, a3, true);
;             PG8_WAIT_V(8); PG8_WAIT_L(0); PG8_BAR; PG8_MMA(1, 0, At, B0); PG8_MMA(1, 1, At, B1); PG8_BAR; PG8_SCHED;
;     ...
;         if constexpr (ALIGN_EPI) { if (wr == 0) PG8_BAR; }
	s_add_i32 s64, 0, 0x18000
	s_add_i32 s65, 0, 0x1c000
	v_add_u32_e32 v126, s64, v229
	v_add_u32_e32 v150, s65, v229
	ds_read_b128 v[98:101], v126
	ds_read_b128 v[110:113], v126 offset:1024
	ds_read_b128 v[122:125], v126 offset:2048
	ds_read_b128 v[126:129], v126 offset:3072
	ds_read_b128 v[138:141], v150
	ds_read_b128 v[142:145], v150 offset:1024
	ds_read_b128 v[146:149], v150 offset:2048
	ds_read_b128 v[150:153], v150 offset:3072
	s_add_u32 s30, s30, 0x40000
	s_addc_u32 s31, s31, 0
	s_mov_b32 m0, s35
	ds_read_b128 v[154:157], v236 offset:32768
	ds_read_b128 v[166:169], v236 offset:33792
	ds_read_b128 v[170:173], v236 offset:34816
	ds_read_b128 v[174:177], v236 offset:35840
	ds_read_b128 v[178:181], v236 offset:36864
	ds_read_b128 v[182:185], v236 offset:37888
	ds_read_b128 v[186:189], v236 offset:38912
	ds_read_b128 v[206:209], v236 offset:39936
	global_load_lds_dwordx4 v190, s[30:31]
	s_mov_b32 m0, s36
	s_nop 0
	global_load_lds_dwordx4 v194, s[30:31]
	s_waitcnt vmcnt(8)
	s_waitcnt lgkmcnt(0)
	s_barrier
	s_setprio 3
	s_waitcnt lgkmcnt(0)
	v_mfma_f32_16x16x32_bf16 v[162:165], v[98:101], v[154:157], v[162:165]
	v_mfma_f32_16x16x32_bf16 v[158:161], v[122:125], v[154:157], v[158:161]
	v_mfma_f32_16x16x32_bf16 v[118:121], v[98:101], v[170:173], v[118:121]
	v_mfma_f32_16x16x32_bf16 v[114:117], v[122:125], v[170:173], v[114:117]
	v_mfma_f32_16x16x32_bf16 v[94:97], v[98:101], v[178:181], v[94:97]
	v_mfma_f32_16x16x32_bf16 v[90:93], v[122:125], v[178:181], v[90:93]
	v_mfma_f32_16x16x32_bf16 v[78:81], v[98:101], v[186:189], v[78:81]
	v_mfma_f32_16x16x32_bf16 v[74:77], v[122:125], v[186:189], v[74:77]
	v_mfma_f32_16x16x32_bf16 v[162:165], v[110:113], v[166:169], v[162:165]
	v_mfma_f32_16x16x32_bf16 v[158:161], v[126:129], v[166:169], v[158:161]
	v_mfma_f32_16x16x32_bf16 v[118:121], v[110:113], v[174:177], v[118:121]
	v_mfma_f32_16x16x32_bf16 v[114:117], v[126:129], v[174:177], v[114:117]
	v_mfma_f32_16x16x32_bf16 v[94:97], v[110:113], v[182:185], v[94:97]
	v_mfma_f32_16x16x32_bf16 v[90:93], v[126:129], v[182:185], v[90:93]
	v_mfma_f32_16x16x32_bf16 v[78:81], v[110:113], v[206:209], v[78:81]
	v_mfma_f32_16x16x32_bf16 v[74:77], v[126:129], v[206:209], v[74:77]
	s_setprio 0
	s_setprio 3
	v_mfma_f32_16x16x32_bf16 v[134:137], v[138:141], v[154:157], v[134:137]
	v_mfma_f32_16x16x32_bf16 v[130:133], v[146:149], v[154:157], v[130:133]
	v_mfma_f32_16x16x32_bf16 v[106:109], v[138:141], v[170:173], v[106:109]
	v_mfma_f32_16x16x32_bf16 v[102:105], v[146:149], v[170:173], v[102:105]
	v_mfma_f32_16x16x32_bf16 v[86:89], v[138:141], v[178:181], v[86:89]
	v_mfma_f32_16x16x32_bf16 v[82:85], v[146:149], v[178:181], v[82:85]
	v_mfma_f32_16x16x32_bf16 v[70:73], v[138:141], v[186:189], v[70:73]
	v_mfma_f32_16x16x32_bf16 v[66:69], v[146:149], v[186:189], v[66:69]
	v_mfma_f32_16x16x32_bf16 v[134:137], v[142:145], v[166:169], v[134:137]
	v_mfma_f32_16x16x32_bf16 v[130:133], v[150:153], v[166:169], v[130:133]
	v_mfma_f32_16x16x32_bf16 v[106:109], v[142:145], v[174:177], v[106:109]
	v_mfma_f32_16x16x32_bf16 v[102:105], v[150:153], v[174:177], v[102:105]
	v_mfma_f32_16x16x32_bf16 v[86:89], v[142:145], v[182:185], v[86:89]
	v_mfma_f32_16x16x32_bf16 v[82:85], v[150:153], v[182:185], v[82:85]
	v_mfma_f32_16x16x32_bf16 v[70:73], v[142:145], v[206:209], v[70:73]
	v_mfma_f32_16x16x32_bf16 v[66:69], v[150:153], v[206:209], v[66:69]
	s_setprio 0
	s_barrier
	s_add_i32 s30, s64, s2
	s_add_i32 m0, s30, 0xffffff80
	ds_read_b128 v[154:157], v236 offset:49152
	ds_read_b128 v[166:169], v236 offset:50176
	ds_read_b128 v[170:173], v236 offset:51200
	ds_read_b128 v[174:177], v236 offset:52224
	ds_read_b128 v[178:181], v236 offset:53248
	ds_read_b128 v[182:185], v236 offset:54272
	ds_read_b128 v[186:189], v236 offset:55296
	ds_read_b128 v[206:209], v236 offset:56320
	global_load_lds_dwordx4 v[210:211], off offset:128
	s_add_i32 m0, s30, 0x1f80
	s_add_u32 s28, s28, 0x40080
	s_addc_u32 s29, s29, 0
	s_add_i32 s30, s65, s2
	global_load_lds_dwordx4 v[212:213], off offset:128
	s_mov_b32 m0, s30
	s_nop 0
	global_load_lds_dwordx4 v192, s[28:29]
	s_add_i32 m0, s30, 0x2000
	s_nop 0
	global_load_lds_dwordx4 v196, s[28:29]
	s_add_i32 m0, s39, 0xffffff80
	s_nop 0
	global_load_lds_dwordx4 v[214:215], off offset:128
	s_add_i32 m0, s48, 0xffffff80
	s_nop 0
	global_load_lds_dwordx4 v[216:217], off offset:128
	s_waitcnt vmcnt(8)
	s_waitcnt lgkmcnt(0)
	s_barrier
	s_setprio 3
	s_waitcnt lgkmcnt(0)
	v_mfma_f32_16x16x32_bf16 v[62:65], v[98:101], v[154:157], v[62:65]
	v_mfma_f32_16x16x32_bf16 v[58:61], v[122:125], v[154:157], v[58:61]
	v_mfma_f32_16x16x32_bf16 v[46:49], v[98:101], v[170:173], v[46:49]
	v_mfma_f32_16x16x32_bf16 v[42:45], v[122:125], v[170:173], v[42:45]
	v_mfma_f32_16x16x32_bf16 v[30:33], v[98:101], v[178:181], v[30:33]
	v_mfma_f32_16x16x32_bf16 v[26:29], v[122:125], v[178:181], v[26:29]
	v_mfma_f32_16x16x32_bf16 v[14:17], v[98:101], v[186:189], v[14:17]
	v_mfma_f32_16x16x32_bf16 v[10:13], v[122:125], v[186:189], v[10:13]
	v_mfma_f32_16x16x32_bf16 v[62:65], v[110:113], v[166:169], v[62:65]
	v_mfma_f32_16x16x32_bf16 v[58:61], v[126:129], v[166:169], v[58:61]
	v_mfma_f32_16x16x32_bf16 v[46:49], v[110:113], v[174:177], v[46:49]
	v_mfma_f32_16x16x32_bf16 v[42:45], v[126:129], v[174:177], v[42:45]
	v_mfma_f32_16x16x32_bf16 v[30:33], v[110:113], v[182:185], v[30:33]
	v_mfma_f32_16x16x32_bf16 v[26:29], v[126:129], v[182:185], v[26:29]
	v_mfma_f32_16x16x32_bf16 v[14:17], v[110:113], v[206:209], v[14:17]
	v_mfma_f32_16x16x32_bf16 v[10:13], v[126:129], v[206:209], v[10:13]
	s_setprio 0
	s_setprio 3
	v_mfma_f32_16x16x32_bf16 v[54:57], v[138:141], v[154:157], v[54:57]
	v_mfma_f32_16x16x32_bf16 v[50:53], v[146:149], v[154:157], v[50:53]
	v_mfma_f32_16x16x32_bf16 v[38:41], v[138:141], v[170:173], v[38:41]
	v_mfma_f32_16x16x32_bf16 v[34:37], v[146:149], v[170:173], v[34:37]
	v_mfma_f32_16x16x32_bf16 v[22:25], v[138:141], v[178:181], v[22:25]
	v_mfma_f32_16x16x32_bf16 v[18:21], v[146:149], v[178:181], v[18:21]
	v_mfma_f32_16x16x32_bf16 v[6:9], v[138:141], v[186:189], v[6:9]
	v_mfma_f32_16x16x32_bf16 v[2:5], v[146:149], v[186:189], v[2:5]
	v_mfma_f32_16x16x32_bf16 v[54:57], v[142:145], v[166:169], v[54:57]
	v_mfma_f32_16x16x32_bf16 v[50:53], v[150:153], v[166:169], v[50:53]
	v_mfma_f32_16x16x32_bf16 v[38:41], v[142:145], v[174:177], v[38:41]
	v_mfma_f32_16x16x32_bf16 v[34:37], v[150:153], v[174:177], v[34:37]
	v_mfma_f32_16x16x32_bf16 v[22:25], v[142:145], v[182:185], v[22:25]
	v_mfma_f32_16x16x32_bf16 v[18:21], v[150:153], v[182:185], v[18:21]
	v_mfma_f32_16x16x32_bf16 v[6:9], v[142:145], v[206:209], v[6:9]
	v_mfma_f32_16x16x32_bf16 v[2:5], v[150:153], v[206:209], v[2:5]
	s_setprio 0
	s_barrier
	s_add_i32 s63, s63, 2
	s_add_u32 s26, s26, 0x100
	s_addc_u32 s27, s27, 0
	s_add_u32 s61, s61, 0x100
	s_addc_u32 s62, s62, 0
	s_cmp_gt_u32 s63, 13
	s_cbranch_scc0 .LBB0_634
	s_and_b64 vcc, exec, s[14:15]
	s_cbranch_vccz .LBB0_637
	s_barrier

; #define PG8_STAGE_A(b, h, ptr, NX) do { if constexpr (Sched::GATHER) { unsigned gs_[2]; gs_[0] = ((NX) && last_) ? gN[h][0] : gA[h][0]; gs_[1] = ((NX) && last_) ? gN[h][1] : gA[h][1]; PG8_STAGE(PG8_SA(b, h), ptr, gs_); } \
;         else PG8_STAGE(PG8_SA(b, h), (ptr) + ((h) ? hstep : (size_t)0), voffA); } while (0)
; #define PG8_STAGE(bufoff, gbase, voff) do { _Pragma("unroll") for (int _i = 0; _i < 2; ++_i) \
;         __builtin_amdgcn_global_load_lds((const unsigned*)((const char*)(gbase) + (voff)[_i]), (PG8_LAS unsigned*)(lds + (bufoff) + ldsw + _i * 8192), 16, 0, 0); } while (0)
; #define PG8_LDA(dst, b, h) do { _Pragma("unroll") for (int m = 0; m < 4; ++m) _Pragma("unroll") for (int k = 0; k < 2; ++k) dst[m][k] = *(const PG8_LAS bf16x8*)(lds + PG8_SA(b, h) + aoff + m * 2048 + k * 1024); } while (0)
; #define PG8_WAIT_V(n) asm volatile("s_waitcnt vmcnt(" #n ")" ::: "memory")
; #define PG8_WAIT_L(n) asm volatile("s_waitcnt lgkmcnt(" #n ")" ::: "memory")
; #define PG8_BAR __builtin_amdgcn_s_barrier()
; template <class Epi, class Sched, bool ALIGN_EPI = false, bool SP2 = false>
; __device__ __forceinline__ void gemm_phase(PG8_LAS unsigned char* lds, const Gemm g, const Sched& S, const Epi& E, const bool skip_epi = false) {
;     ...
;         const char* nA = has_next ? (const char*)g.A + (size_t)nxt.pm * pmstepA + nxt.ko : cA; const char* nB = has_next ? (const char*)g.Bt + (size_t)nxt.pn * tstep + nxt.ko : cB;
;         for (int t = 0; t < nt; t += 2) {
;             const bool last = (t == nt - 2); last_ = last && has_next;
;             const char* a1 = cA + (size_t)(t + 1) * kstep;
;             const char* a2 = last ? nA : cA + (size_t)(t + 2) * kstep; const char* b2 = last ? nB : cB + (size_t)(t + 2) * kstep;
;             const char* a3 = a2 + kstep; const char* b3 = b2 + kstep;
;             if (last && has_next) S.a_ready(nxt);
;             if constexpr (SP2) {
;             PG8_LDB(B0, 0, 0); PG8_LDB(B1, 0, 1); PG8_SCHED; PG8_LDA(At, 0, 0); PG8_STAGE_A(1, 1, a1, false);
;             PG8_WAIT_V(8); PG8_WAIT_L(0); PG8_BAR; PG8_MMA(0, 0, At, B0); PG8_MMA(0, 1, At, B1); PG8_BAR; PG8_SCHED;
;             PG8_LDA(At, 0, 1); PG8_STAGE(PG8_SB(0, 0), b2, voffB); PG8_STAGE(PG8_SB(0, 1), b2 + hstep, voffB); PG8_STAGE_A(0, 0, a2, true);
;             PG8_WAIT_V(8); PG8_WAIT_L(0); PG8_BAR; PG8_MMA(1, 0, At, B0); PG8_MMA(1, 1, At, B1); PG8_BAR; PG8_SCHED;
.LBB0_720:
	s_ashr_i32 s15, s14, 31
	s_lshl_b64 s[16:17], s[14:15], 19
	s_add_u32 s16, s86, s16
	s_addc_u32 s17, s87, s17
	s_and_b64 s[18:19], s[4:5], exec
	s_cselect_b32 s15, s17, s23
	s_cselect_b32 s56, s16, s22
	s_ashr_i32 s13, s12, 31
	s_lshl_b64 s[18:19], s[12:13], 19
	v_readlane_b32 s26, v254, 15
	v_readlane_b32 s27, v254, 16
	s_add_u32 s18, s26, s18
	s_addc_u32 s19, s27, s19
	s_and_b64 s[26:27], s[4:5], exec
	s_cselect_b32 s13, s19, s25
	s_cselect_b32 s57, s18, s24
	s_add_u32 s22, s22, 0x40080
	s_addc_u32 s23, s23, 0
	s_add_u32 s58, s24, 0x100
	s_addc_u32 s59, s25, 0
	s_mov_b32 s60, -2
	s_waitcnt vmcnt(0)
	v_lshl_add_u32 v130, s20, 8, v175
	v_ashrrev_i32_e32 v131, 31, v130
	v_lshlrev_b64 v[130:131], 6, v[130:131]
	v_lshl_add_u64 v[130:131], v[150:151], 0, v[130:131]
	global_load_dwordx4 v[238:241], v[130:131], off
	global_load_dwordx4 v[242:245], v[130:131], off offset:1024
	global_load_dwordx4 v[246:249], v[130:131], off offset:2048
	global_load_dwordx4 v[250:253], v[130:131], off offset:3072
	ds_read_b128 v[130:133], v187
	ds_read_b128 v[134:137], v187 offset:1024
	ds_read_b128 v[138:141], v187 offset:2048
	ds_read_b128 v[160:163], v187 offset:3072
	ds_read_b128 v[164:167], v188
	ds_read_b128 v[182:185], v188 offset:1024
	ds_read_b128 v[192:195], v188 offset:2048
	ds_read_b128 v[196:199], v188 offset:3072
	s_add_u32 s24, s22, 0xfffc0080
	s_addc_u32 s25, s23, -1
	s_cmp_eq_u32 s60, 12
	s_cselect_b32 s27, s15, s25
	s_cselect_b32 s26, s56, s24
	s_cselect_b32 s25, s13, s59
	s_cselect_b32 s24, s57, s58
	s_add_i32 m0, s29, 0xc000
	ds_read_b128 v[200:203], v189
	ds_read_b128 v[204:207], v189 offset:1024
	ds_read_b128 v[208:211], v189 offset:2048
	ds_read_b128 v[212:215], v189 offset:3072
	ds_read_b128 v[216:219], v189 offset:4096
	ds_read_b128 v[220:223], v189 offset:5120
	ds_read_b128 v[224:227], v189 offset:6144
	ds_read_b128 v[230:233], v189 offset:7168
	global_load_lds_dwordx4 v152, s[22:23]
	s_add_i32 m0, s29, 0xe000
	s_nop 0
	global_load_lds_dwordx4 v154, s[22:23]
	s_waitcnt vmcnt(8)
	s_waitcnt lgkmcnt(0)
	s_barrier
	s_setprio 3
	s_waitcnt lgkmcnt(0)
	v_mfma_f32_16x16x32_bf16 v[126:129], v[130:133], v[200:203], 0
	v_mfma_f32_16x16x32_bf16 v[122:125], v[138:141], v[200:203], 0
	v_mfma_f32_16x16x32_bf16 v[110:113], v[130:133], v[208:211], 0
	v_mfma_f32_16x16x32_bf16 v[106:109], v[138:141], v[208:211], 0
	v_lshl_add_u64 v[168:169], s[24:25], 0, v[146:147]
	v_mfma_f32_16x16x32_bf16 v[94:97], v[130:133], v[216:219], 0
	v_mfma_f32_16x16x32_bf16 v[90:93], v[138:141], v[216:219], 0
	v_lshl_add_u64 v[172:173], s[24:25], 0, v[142:143]
	v_mfma_f32_16x16x32_bf16 v[78:81], v[130:133], v[224:227], 0
	v_mfma_f32_16x16x32_bf16 v[74:77], v[138:141], v[224:227], 0
	v_lshl_add_u64 v[234:235], s[26:27], 0, v[144:145]
	v_mfma_f32_16x16x32_bf16 v[126:129], v[134:137], v[204:207], v[126:129]
	v_mfma_f32_16x16x32_bf16 v[122:125], v[160:163], v[204:207], v[122:125]
	v_lshl_add_u64 v[176:177], s[26:27], 0, v[148:149]
	v_mfma_f32_16x16x32_bf16 v[110:113], v[134:137], v[212:215], v[110:113]
	v_mfma_f32_16x16x32_bf16 v[106:109], v[160:163], v[212:215], v[106:109]
	v_mfma_f32_16x16x32_bf16 v[94:97], v[134:137], v[220:223], v[94:97]
	v_mfma_f32_16x16x32_bf16 v[90:93], v[160:163], v[220:223], v[90:93]
	v_mfma_f32_16x16x32_bf16 v[78:81], v[134:137], v[230:233], v[78:81]
	v_mfma_f32_16x16x32_bf16 v[74:77], v[160:163], v[230:233], v[74:77]
	s_setprio 0
	s_setprio 3
	v_mfma_f32_16x16x32_bf16 v[118:121], v[164:167], v[200:203], 0
	v_mfma_f32_16x16x32_bf16 v[114:117], v[192:195], v[200:203], 0
	v_mfma_f32_16x16x32_bf16 v[102:105], v[164:167], v[208:211], 0
	v_mfma_f32_16x16x32_bf16 v[98:101], v[192:195], v[208:211], 0
	v_mfma_f32_16x16x32_bf16 v[86:89], v[164:167], v[216:219], 0
	v_mfma_f32_16x16x32_bf16 v[82:85], v[192:195], v[216:219], 0
	v_mfma_f32_16x16x32_bf16 v[70:73], v[164:167], v[224:227], 0
	v_mfma_f32_16x16x32_bf16 v[66:69], v[192:195], v[224:227], 0
	v_mfma_f32_16x16x32_bf16 v[118:121], v[182:185], v[204:207], v[118:121]
	v_mfma_f32_16x16x32_bf16 v[114:117], v[196:199], v[204:207], v[114:117]
	v_mfma_f32_16x16x32_bf16 v[102:105], v[182:185], v[212:215], v[102:105]
	v_mfma_f32_16x16x32_bf16 v[98:101], v[196:199], v[212:215], v[98:101]
	v_mfma_f32_16x16x32_bf16 v[86:89], v[182:185], v[220:223], v[86:89]
	v_mfma_f32_16x16x32_bf16 v[82:85], v[196:199], v[220:223], v[82:85]
	v_mfma_f32_16x16x32_bf16 v[70:73], v[182:185], v[230:233], v[70:73]
	v_mfma_f32_16x16x32_bf16 v[66:69], v[196:199], v[230:233], v[66:69]
	s_setprio 0
	s_barrier
	s_add_i32 s61, s39, s2
	s_mov_b32 m0, s61
	ds_read_b128 v[200:203], v189 offset:16384
	ds_read_b128 v[204:207], v189 offset:17408
	ds_read_b128 v[208:211], v189 offset:18432
	ds_read_b128 v[212:215], v189 offset:19456
	ds_read_b128 v[216:219], v189 offset:20480
	ds_read_b128 v[220:223], v189 offset:21504
	ds_read_b128 v[224:227], v189 offset:22528
	ds_read_b128 v[230:233], v189 offset:23552
	global_load_lds_dwordx4 v[168:169], off
	s_add_i32 m0, s61, 0x2000
	s_add_u32 s62, s24, 0x40000
	s_addc_u32 s63, s25, 0
	s_add_i32 s61, s48, s2
	global_load_lds_dwordx4 v[172:173], off
	s_mov_b32 m0, s61
	s_nop 0
	global_load_lds_dwordx4 v146, s[62:63]
	s_add_i32 m0, s61, 0x2000
	s_nop 0
	global_load_lds_dwordx4 v142, s[62:63]
	s_mov_b32 m0, s29
	s_nop 0
	global_load_lds_dwordx4 v[176:177], off
	s_mov_b32 m0, s30
	s_nop 0
	global_load_lds_dwordx4 v[234:235], off
	s_waitcnt vmcnt(8)
	s_waitcnt lgkmcnt(0)
	s_barrier
; #define PG8_STAGE_A(b, h, ptr, NX) do { if constexpr (Sched::GATHER) { unsigned gs_[2]; gs_[0] = ((NX) && last_) ? gN[h][0] : gA[h][0]; gs_[1] = ((NX) && last_) ? gN[h][1] : gA[h][1]; PG8_STAGE(PG8_SA(b, h), ptr, gs_); } \
;         else PG8_STAGE(PG8_SA(b, h), (ptr) + ((h) ? hstep : (size_t)0), voffA); } while (0)
; #define PG8_LDA(dst, b, h) do { _Pragma("unroll") for (int m = 0; m < 4; ++m) _Pragma("unroll") for (int k = 0; k < 2; ++k) dst[m][k] = *(const PG8_LAS bf16x8*)(lds + PG8_SA(b, h) + aoff + m * 2048 + k * 1024); } while (0)
; #define PG8_LDB(dst, b, h) do { _Pragma("unroll") for (int n = 0; n < 2; ++n) _Pragma("unroll") for (int k = 0; k < 2; ++k) dst[n][k] = *(const PG8_LAS bf16x8*)(lds + PG8_SB(b, h) + boff + n * 2048 + k * 1024); } while (0)
; #define PG8_MMA(ai, bj, At, Bt) do { __builtin_amdgcn_s_setprio(1); _Pragma("unroll") for (int m = 0; m < 4; ++m) _Pragma("unroll") for (int n = 0; n < 2; ++n) _Pragma("unroll") for (int k = 0; k < 2; ++k) \
;         acc[ai][bj][m][n] = __builtin_amdgcn_mfma_f32_16x16x32_bf16(Bt[n][k], At[m][k], acc[ai][bj][m][n], 0, 0, 0); __builtin_amdgcn_s_setprio(0); } while (0)
; #define PG8_WAIT_V(n) asm volatile("s_waitcnt vmcnt(" #n ")" ::: "memory")
; #define PG8_WAIT_L(n) asm volatile("s_waitcnt lgkmcnt(" #n ")" ::: "memory")
; #define PG8_BAR __builtin_amdgcn_s_barrier()
; #define PG8_SCHED __builtin_amdgcn_sched_barrier(0)
; template <class Epi, class Sched, bool ALIGN_EPI = false, bool SP2 = false>
; __device__ __forceinline__ void gemm_phase(PG8_LAS unsigned char* lds, const Gemm g, const Sched& S, const Epi& E, const bool skip_epi = false) {
;     ...
;             PG8_WAIT_V(8); PG8_WAIT_L(0); PG8_BAR; PG8_MMA(1, 0, At, B0); PG8_MMA(1, 1, At, B1); PG8_BAR; PG8_SCHED;
;             PG8_LDB(B0, 1, 0); PG8_LDB(B1, 1, 1); PG8_SCHED; PG8_LDA(At, 1, 0); PG8_STAGE_A(0, 1, a2, true);
;             PG8_WAIT_V(8); PG8_WAIT_L(0); PG8_BAR; PG8_MMA(0, 0, At, B0); PG8_MMA(0, 1, At, B1); PG8_BAR; PG8_SCHED;
	s_setprio 3
	s_waitcnt lgkmcnt(0)
	v_mfma_f32_16x16x32_bf16 v[62:65], v[130:133], v[200:203], 0
	v_mfma_f32_16x16x32_bf16 v[58:61], v[138:141], v[200:203], 0
	v_mfma_f32_16x16x32_bf16 v[46:49], v[130:133], v[208:211], 0
	v_mfma_f32_16x16x32_bf16 v[42:45], v[138:141], v[208:211], 0
	v_mfma_f32_16x16x32_bf16 v[30:33], v[130:133], v[216:219], 0
	v_mfma_f32_16x16x32_bf16 v[26:29], v[138:141], v[216:219], 0
	v_mfma_f32_16x16x32_bf16 v[14:17], v[130:133], v[224:227], 0
	v_mfma_f32_16x16x32_bf16 v[10:13], v[138:141], v[224:227], 0
	v_mfma_f32_16x16x32_bf16 v[62:65], v[134:137], v[204:207], v[62:65]
	v_mfma_f32_16x16x32_bf16 v[58:61], v[160:163], v[204:207], v[58:61]
	v_mfma_f32_16x16x32_bf16 v[46:49], v[134:137], v[212:215], v[46:49]
	v_mfma_f32_16x16x32_bf16 v[42:45], v[160:163], v[212:215], v[42:45]
	v_mfma_f32_16x16x32_bf16 v[30:33], v[134:137], v[220:223], v[30:33]
	v_mfma_f32_16x16x32_bf16 v[26:29], v[160:163], v[220:223], v[26:29]
	v_mfma_f32_16x16x32_bf16 v[14:17], v[134:137], v[230:233], v[14:17]
	v_mfma_f32_16x16x32_bf16 v[10:13], v[160:163], v[230:233], v[10:13]
	s_setprio 0
	s_setprio 3
	v_mfma_f32_16x16x32_bf16 v[54:57], v[164:167], v[200:203], 0
	v_mfma_f32_16x16x32_bf16 v[50:53], v[192:195], v[200:203], 0
	v_mfma_f32_16x16x32_bf16 v[38:41], v[164:167], v[208:211], 0
	v_mfma_f32_16x16x32_bf16 v[34:37], v[192:195], v[208:211], 0
	v_mfma_f32_16x16x32_bf16 v[22:25], v[164:167], v[216:219], 0
	v_mfma_f32_16x16x32_bf16 v[18:21], v[192:195], v[216:219], 0
	v_mfma_f32_16x16x32_bf16 v[6:9], v[164:167], v[224:227], 0
	v_mfma_f32_16x16x32_bf16 v[2:5], v[192:195], v[224:227], 0
	v_mfma_f32_16x16x32_bf16 v[54:57], v[182:185], v[204:207], v[54:57]
	v_mfma_f32_16x16x32_bf16 v[50:53], v[196:199], v[204:207], v[50:53]
	v_mfma_f32_16x16x32_bf16 v[38:41], v[182:185], v[212:215], v[38:41]
	v_mfma_f32_16x16x32_bf16 v[34:37], v[196:199], v[212:215], v[34:37]
	v_mfma_f32_16x16x32_bf16 v[22:25], v[182:185], v[220:223], v[22:25]
	v_mfma_f32_16x16x32_bf16 v[18:21], v[196:199], v[220:223], v[18:21]
	v_mfma_f32_16x16x32_bf16 v[6:9], v[182:185], v[230:233], v[6:9]
	v_mfma_f32_16x16x32_bf16 v[2:5], v[196:199], v[230:233], v[2:5]
	s_setprio 0
	s_barrier
	s_add_i32 s61, 0, 0x18000
	s_add_i32 s62, 0, 0x1c000
	v_add_u32_e32 v160, s61, v1
	v_add_u32_e32 v170, s62, v1
	ds_read_b128 v[130:133], v160
	ds_read_b128 v[134:137], v160 offset:1024
	ds_read_b128 v[138:141], v160 offset:2048
	ds_read_b128 v[160:163], v160 offset:3072
	ds_read_b128 v[164:167], v170
	ds_read_b128 v[182:185], v170 offset:1024
	ds_read_b128 v[192:195], v170 offset:2048
	ds_read_b128 v[196:199], v170 offset:3072
	s_add_u32 s26, s26, 0x40000
	s_addc_u32 s27, s27, 0
	s_mov_b32 m0, s31
	ds_read_b128 v[200:203], v189 offset:32768
	ds_read_b128 v[204:207], v189 offset:33792
	ds_read_b128 v[208:211], v189 offset:34816
	ds_read_b128 v[212:215], v189 offset:35840
	ds_read_b128 v[216:219], v189 offset:36864
	ds_read_b128 v[220:223], v189 offset:37888
	ds_read_b128 v[224:227], v189 offset:38912
	ds_read_b128 v[230:233], v189 offset:39936
	global_load_lds_dwordx4 v148, s[26:27]
	s_mov_b32 m0, s34
	s_nop 0
	global_load_lds_dwordx4 v144, s[26:27]
	s_waitcnt vmcnt(8)
	s_waitcnt lgkmcnt(0)
	s_barrier
	s_setprio 3
	s_waitcnt lgkmcnt(0)
	v_mfma_f32_16x16x32_bf16 v[126:129], v[130:133], v[200:203], v[126:129]
	v_mfma_f32_16x16x32_bf16 v[122:125], v[138:141], v[200:203], v[122:125]
	v_mfma_f32_16x16x32_bf16 v[110:113], v[130:133], v[208:211], v[110:113]
	v_mfma_f32_16x16x32_bf16 v[106:109], v[138:141], v[208:211], v[106:109]
	v_mfma_f32_16x16x32_bf16 v[94:97], v[130:133], v[216:219], v[94:97]
	v_mfma_f32_16x16x32_bf16 v[90:93], v[138:141], v[216:219], v[90:93]
	v_mfma_f32_16x16x32_bf16 v[78:81], v[130:133], v[224:227], v[78:81]
	v_mfma_f32_16x16x32_bf16 v[74:77], v[138:141], v[224:227], v[74:77]
	v_mfma_f32_16x16x32_bf16 v[126:129], v[134:137], v[204:207], v[126:129]
	v_mfma_f32_16x16x32_bf16 v[122:125], v[160:163], v[204:207], v[122:125]
	v_mfma_f32_16x16x32_bf16 v[110:113], v[134:137], v[212:215], v[110:113]
	v_mfma_f32_16x16x32_bf16 v[106:109], v[160:163], v[212:215], v[106:109]
	v_mfma_f32_16x16x32_bf16 v[94:97], v[134:137], v[220:223], v[94:97]
	v_mfma_f32_16x16x32_bf16 v[90:93], v[160:163], v[220:223], v[90:93]
	v_mfma_f32_16x16x32_bf16 v[78:81], v[134:137], v[230:233], v[78:81]
	v_mfma_f32_16x16x32_bf16 v[74:77], v[160:163], v[230:233], v[74:77]
	s_setprio 0
	s_setprio 3
	v_mfma_f32_16x16x32_bf16 v[118:121], v[164:167], v[200:203], v[118:121]
	v_mfma_f32_16x16x32_bf16 v[114:117], v[192:195], v[200:203], v[114:117]
	v_mfma_f32_16x16x32_bf16 v[102:105], v[164:167], v[208:211], v[102:105]
	v_mfma_f32_16x16x32_bf16 v[98:101], v[192:195], v[208:211], v[98:101]
	v_mfma_f32_16x16x32_bf16 v[86:89], v[164:167], v[216:219], v[86:89]
	v_mfma_f32_16x16x32_bf16 v[82:85], v[192:195], v[216:219], v[82:85]
	v_mfma_f32_16x16x32_bf16 v[70:73], v[164:167], v[224:227], v[70:73]
	v_mfma_f32_16x16x32_bf16 v[66:69], v[192:195], v[224:227], v[66:69]
	v_mfma_f32_16x16x32_bf16 v[118:121], v[182:185], v[204:207], v[118:121]
	v_mfma_f32_16x16x32_bf16 v[114:117], v[196:199], v[204:207], v[114:117]
	v_mfma_f32_16x16x32_bf16 v[102:105], v[182:185], v[212:215], v[102:105]
	v_mfma_f32_16x16x32_bf16 v[98:101], v[196:199], v[212:215], v[98:101]
	v_mfma_f32_16x16x32_bf16 v[86:89], v[182:185], v[220:223], v[86:89]
	v_mfma_f32_16x16x32_bf16 v[82:85], v[196:199], v[220:223], v[82:85]
	v_mfma_f32_16x16x32_bf16 v[70:73], v[182:185], v[230:233], v[70:73]
	v_mfma_f32_16x16x32_bf16 v[66:69], v[196:199], v[230:233], v[66:69]
	s_setprio 0
	s_barrier
; #define PG8_STAGE_A(b, h, ptr, NX) do { if constexpr (Sched::GATHER) { unsigned gs_[2]; gs_[0] = ((NX) && last_) ? gN[h][0] : gA[h][0]; gs_[1] = ((NX) && last_) ? gN[h][1] : gA[h][1]; PG8_STAGE(PG8_SA(b, h), ptr, gs_); } \
;         else PG8_STAGE(PG8_SA(b, h), (ptr) + ((h) ? hstep : (size_t)0), voffA); } while (0)
; #define PG8_STAGE(bufoff, gbase, voff) do { _Pragma("unroll") for (int _i = 0; _i < 2; ++_i) \
;         __builtin_amdgcn_global_load_lds((const unsigned*)((const char*)(gbase) + (voff)[_i]), (PG8_LAS unsigned*)(lds + (bufoff) + ldsw + _i * 8192), 16, 0, 0); } while (0)
; #define PG8_LDA(dst, b, h) do { _Pragma("unroll") for (int m = 0; m < 4; ++m) _Pragma("unroll") for (int k = 0; k < 2; ++k) dst[m][k] = *(const PG8_LAS bf16x8*)(lds + PG8_SA(b, h) + aoff + m * 2048 + k * 1024); } while (0)
; #define PG8_LDB(dst, b, h) do { _Pragma("unroll") for (int n = 0; n < 2; ++n) _Pragma("unroll") for (int k = 0; k < 2; ++k) dst[n][k] = *(const PG8_LAS bf16x8*)(lds + PG8_SB(b, h) + boff + n * 2048 + k * 1024); } while (0)
; #define PG8_WAIT_V(n) asm volatile("s_waitcnt vmcnt(" #n ")" ::: "memory")
; #define PG8_BAR __builtin_amdgcn_s_barrier()
; template <class Epi, class Sched, bool ALIGN_EPI = false, bool SP2 = false>
; __device__ __forceinline__ void gemm_phase(PG8_LAS unsigned char* lds, const Gemm g, const Sched& S, const Epi& E, const bool skip_epi = false) {
;     ...
;             PG8_LDB(B0, 0, 0); PG8_LDB(B1, 0, 1); PG8_SCHED; PG8_LDA(At, 0, 0); PG8_STAGE_A(1, 1, a1, false);
;             PG8_WAIT_V(8); PG8_WAIT_L(0); PG8_BAR; PG8_MMA(0, 0, At, B0); PG8_MMA(0, 1, At, B1); PG8_BAR; PG8_SCHED;
;             PG8_LDA(At, 0, 1); PG8_STAGE(PG8_SB(0, 0), b2, voffB); PG8_STAGE(PG8_SB(0, 1), b2 + hstep, voffB); PG8_STAGE_A(0, 0, a2, true);
;             PG8_WAIT_V(8); PG8_WAIT_L(0); PG8_BAR; PG8_MMA(1, 0, At, B0); PG8_MMA(1, 1, At, B1); PG8_BAR; PG8_SCHED;
;             PG8_LDB(B0, 1, 0); PG8_LDB(B1, 1, 1); PG8_SCHED; PG8_LDA(At, 1, 0); PG8_STAGE_A(0, 1, a2, true);
;             PG8_WAIT_V(8); PG8_WAIT_L(0); PG8_BAR; PG8_MMA(0, 0, At, B0); PG8_MMA(0, 1, At, B1); PG8_BAR; PG8_SCHED;
;             PG8_LDA(At, 1, 1); PG8_STAGE(PG8_SB(1, 0), b3, voffB); PG8_STAGE(PG8_SB(1, 1), b3 + hstep, voffB); PG8_STAGE_A(1, 0, a3, true);
;             PG8_WAIT_V(8); PG8_WAIT_L(0); PG8_BAR; PG8_MMA(1, 0, At, B0); PG8_MMA(1, 1, At, B1); PG8_BAR; PG8_SCHED;
	s_add_i32 s26, s61, s2
	s_add_i32 m0, s26, 0xffffff80
	ds_read_b128 v[200:203], v189 offset:49152
	ds_read_b128 v[204:207], v189 offset:50176
	ds_read_b128 v[208:211], v189 offset:51200
	ds_read_b128 v[212:215], v189 offset:52224
	ds_read_b128 v[216:219], v189 offset:53248
	ds_read_b128 v[220:223], v189 offset:54272
	ds_read_b128 v[224:227], v189 offset:55296
	ds_read_b128 v[230:233], v189 offset:56320
	global_load_lds_dwordx4 v[168:169], off offset:128
	s_add_i32 m0, s26, 0x1f80
	s_add_u32 s24, s24, 0x40080
	s_addc_u32 s25, s25, 0
	s_add_i32 s26, s62, s2
	global_load_lds_dwordx4 v[172:173], off offset:128
	s_mov_b32 m0, s26
	s_nop 0
	global_load_lds_dwordx4 v146, s[24:25]
	s_add_i32 m0, s26, 0x2000
	s_nop 0
	global_load_lds_dwordx4 v142, s[24:25]
	s_add_i32 m0, s36, 0xffffff80
	s_nop 0
	global_load_lds_dwordx4 v[176:177], off offset:128
	s_add_i32 m0, s37, 0xffffff80
	s_nop 0
	global_load_lds_dwordx4 v[234:235], off offset:128
	s_waitcnt vmcnt(8)
	s_waitcnt lgkmcnt(0)
	s_barrier
	s_setprio 3
	s_waitcnt lgkmcnt(0)
	v_mfma_f32_16x16x32_bf16 v[62:65], v[130:133], v[200:203], v[62:65]
	v_mfma_f32_16x16x32_bf16 v[58:61], v[138:141], v[200:203], v[58:61]
	v_mfma_f32_16x16x32_bf16 v[46:49], v[130:133], v[208:211], v[46:49]
	v_mfma_f32_16x16x32_bf16 v[42:45], v[138:141], v[208:211], v[42:45]
	v_mfma_f32_16x16x32_bf16 v[30:33], v[130:133], v[216:219], v[30:33]
	v_mfma_f32_16x16x32_bf16 v[26:29], v[138:141], v[216:219], v[26:29]
	v_mfma_f32_16x16x32_bf16 v[14:17], v[130:133], v[224:227], v[14:17]
	v_mfma_f32_16x16x32_bf16 v[10:13], v[138:141], v[224:227], v[10:13]
	v_mfma_f32_16x16x32_bf16 v[62:65], v[134:137], v[204:207], v[62:65]
	v_mfma_f32_16x16x32_bf16 v[58:61], v[160:163], v[204:207], v[58:61]
	v_mfma_f32_16x16x32_bf16 v[46:49], v[134:137], v[212:215], v[46:49]
	v_mfma_f32_16x16x32_bf16 v[42:45], v[160:163], v[212:215], v[42:45]
	v_mfma_f32_16x16x32_bf16 v[30:33], v[134:137], v[220:223], v[30:33]
	v_mfma_f32_16x16x32_bf16 v[26:29], v[160:163], v[220:223], v[26:29]
	v_mfma_f32_16x16x32_bf16 v[14:17], v[134:137], v[230:233], v[14:17]
	v_mfma_f32_16x16x32_bf16 v[10:13], v[160:163], v[230:233], v[10:13]
	s_setprio 0
	s_setprio 3
	v_mfma_f32_16x16x32_bf16 v[54:57], v[164:167], v[200:203], v[54:57]
	v_mfma_f32_16x16x32_bf16 v[50:53], v[192:195], v[200:203], v[50:53]
	v_mfma_f32_16x16x32_bf16 v[38:41], v[164:167], v[208:211], v[38:41]
	v_mfma_f32_16x16x32_bf16 v[34:37], v[192:195], v[208:211], v[34:37]
	v_mfma_f32_16x16x32_bf16 v[22:25], v[164:167], v[216:219], v[22:25]
	v_mfma_f32_16x16x32_bf16 v[18:21], v[192:195], v[216:219], v[18:21]
	v_mfma_f32_16x16x32_bf16 v[6:9], v[164:167], v[224:227], v[6:9]
	v_mfma_f32_16x16x32_bf16 v[2:5], v[192:195], v[224:227], v[2:5]
	v_mfma_f32_16x16x32_bf16 v[54:57], v[182:185], v[204:207], v[54:57]
	v_mfma_f32_16x16x32_bf16 v[50:53], v[196:199], v[204:207], v[50:53]
	v_mfma_f32_16x16x32_bf16 v[38:41], v[182:185], v[212:215], v[38:41]
	v_mfma_f32_16x16x32_bf16 v[34:37], v[196:199], v[212:215], v[34:37]
	v_mfma_f32_16x16x32_bf16 v[22:25], v[182:185], v[220:223], v[22:25]
	v_mfma_f32_16x16x32_bf16 v[18:21], v[196:199], v[220:223], v[18:21]
	v_mfma_f32_16x16x32_bf16 v[6:9], v[182:185], v[230:233], v[6:9]
	v_mfma_f32_16x16x32_bf16 v[2:5], v[196:199], v[230:233], v[2:5]
	s_setprio 0
	s_barrier
	s_add_i32 s60, s60, 2
	s_add_u32 s22, s22, 0x100
	s_addc_u32 s23, s23, 0
	s_add_u32 s58, s58, 0x100
	s_addc_u32 s59, s59, 0
	s_cmp_gt_u32 s60, 13
.LBB0_721:
	ds_read_b128 v[130:133], v187
	ds_read_b128 v[134:137], v187 offset:1024
	ds_read_b128 v[138:141], v187 offset:2048
	ds_read_b128 v[160:163], v187 offset:3072
	ds_read_b128 v[164:167], v188
	ds_read_b128 v[182:185], v188 offset:1024
	ds_read_b128 v[192:195], v188 offset:2048
	ds_read_b128 v[196:199], v188 offset:3072
	s_add_u32 s24, s22, 0xfffc0080
	s_addc_u32 s25, s23, -1
	s_cmp_eq_u32 s60, 12
	s_cselect_b32 s27, s15, s25
	s_cselect_b32 s26, s56, s24
	s_cselect_b32 s25, s13, s59
	s_cselect_b32 s24, s57, s58
	s_add_i32 m0, s29, 0xc000
	ds_read_b128 v[200:203], v189
	ds_read_b128 v[204:207], v189 offset:1024
	ds_read_b128 v[208:211], v189 offset:2048
	ds_read_b128 v[212:215], v189 offset:3072
	ds_read_b128 v[216:219], v189 offset:4096
	ds_read_b128 v[220:223], v189 offset:5120
	ds_read_b128 v[224:227], v189 offset:6144
	ds_read_b128 v[230:233], v189 offset:7168
	global_load_lds_dwordx4 v152, s[22:23]
	s_add_i32 m0, s29, 0xe000
	s_nop 0
	global_load_lds_dwordx4 v154, s[22:23]
	s_waitcnt vmcnt(8)
	s_waitcnt lgkmcnt(0)
	s_barrier
; #define PG8_STAGE_A(b, h, ptr, NX) do { if constexpr (Sched::GATHER) { unsigned gs_[2]; gs_[0] = ((NX) && last_) ? gN[h][0] : gA[h][0]; gs_[1] = ((NX) && last_) ? gN[h][1] : gA[h][1]; PG8_STAGE(PG8_SA(b, h), ptr, gs_); } \
;         else PG8_STAGE(PG8_SA(b, h), (ptr) + ((h) ? hstep : (size_t)0), voffA); } while (0)
; #define PG8_STAGE(bufoff, gbase, voff) do { _Pragma("unroll") for (int _i = 0; _i < 2; ++_i) \
;         __builtin_amdgcn_global_load_lds((const unsigned*)((const char*)(gbase) + (voff)[_i]), (PG8_LAS unsigned*)(lds + (bufoff) + ldsw + _i * 8192), 16, 0, 0); } while (0)
; #define PG8_LDA(dst, b, h) do { _Pragma("unroll") for (int m = 0; m < 4; ++m) _Pragma("unroll") for (int k = 0; k < 2; ++k) dst[m][k] = *(const PG8_LAS bf16x8*)(lds + PG8_SA(b, h) + aoff + m * 2048 + k * 1024); } while (0)
; #define PG8_MMA(ai, bj, At, Bt) do { __builtin_amdgcn_s_setprio(1); _Pragma("unroll") for (int m = 0; m < 4; ++m) _Pragma("unroll") for (int n = 0; n < 2; ++n) _Pragma("unroll") for (int k = 0; k < 2; ++k) \
;         acc[ai][bj][m][n] = __builtin_amdgcn_mfma_f32_16x16x32_bf16(Bt[n][k], At[m][k], acc[ai][bj][m][n], 0, 0, 0); __builtin_amdgcn_s_setprio(0); } while (0)
; #define PG8_WAIT_V(n) asm volatile("s_waitcnt vmcnt(" #n ")" ::: "memory")
; #define PG8_WAIT_L(n) asm volatile("s_waitcnt lgkmcnt(" #n ")" ::: "memory")
; #define PG8_BAR __builtin_amdgcn_s_barrier()
; #define PG8_SCHED __builtin_amdgcn_sched_barrier(0)
; template <class Epi, class Sched, bool ALIGN_EPI = false, bool SP2 = false>
; __device__ __forceinline__ void gemm_phase(PG8_LAS unsigned char* lds, const Gemm g, const Sched& S, const Epi& E, const bool skip_epi = false) {
;     ...
;             PG8_WAIT_V(8); PG8_WAIT_L(0); PG8_BAR; PG8_MMA(0, 0, At, B0); PG8_MMA(0, 1, At, B1); PG8_BAR; PG8_SCHED;
;             PG8_LDA(At, 0, 1); PG8_STAGE(PG8_SB(0, 0), b2, voffB); PG8_STAGE(PG8_SB(0, 1), b2 + hstep, voffB); PG8_STAGE_A(0, 0, a2, true);
;             PG8_WAIT_V(8); PG8_WAIT_L(0); PG8_BAR; PG8_MMA(1, 0, At, B0); PG8_MMA(1, 1, At, B1); PG8_BAR; PG8_SCHED;
	s_setprio 3
	s_waitcnt lgkmcnt(0)
	v_mfma_f32_16x16x32_bf16 v[126:129], v[130:133], v[200:203], v[126:129]
	v_mfma_f32_16x16x32_bf16 v[122:125], v[138:141], v[200:203], v[122:125]
	v_mfma_f32_16x16x32_bf16 v[110:113], v[130:133], v[208:211], v[110:113]
	v_mfma_f32_16x16x32_bf16 v[106:109], v[138:141], v[208:211], v[106:109]
	v_lshl_add_u64 v[168:169], s[24:25], 0, v[146:147]
	v_mfma_f32_16x16x32_bf16 v[94:97], v[130:133], v[216:219], v[94:97]
	v_mfma_f32_16x16x32_bf16 v[90:93], v[138:141], v[216:219], v[90:93]
	v_lshl_add_u64 v[172:173], s[24:25], 0, v[142:143]
	v_mfma_f32_16x16x32_bf16 v[78:81], v[130:133], v[224:227], v[78:81]
	v_mfma_f32_16x16x32_bf16 v[74:77], v[138:141], v[224:227], v[74:77]
	v_lshl_add_u64 v[234:235], s[26:27], 0, v[144:145]
	v_mfma_f32_16x16x32_bf16 v[126:129], v[134:137], v[204:207], v[126:129]
	v_mfma_f32_16x16x32_bf16 v[122:125], v[160:163], v[204:207], v[122:125]
	v_lshl_add_u64 v[176:177], s[26:27], 0, v[148:149]
	v_mfma_f32_16x16x32_bf16 v[110:113], v[134:137], v[212:215], v[110:113]
	v_mfma_f32_16x16x32_bf16 v[106:109], v[160:163], v[212:215], v[106:109]
	v_mfma_f32_16x16x32_bf16 v[94:97], v[134:137], v[220:223], v[94:97]
	v_mfma_f32_16x16x32_bf16 v[90:93], v[160:163], v[220:223], v[90:93]
	v_mfma_f32_16x16x32_bf16 v[78:81], v[134:137], v[230:233], v[78:81]
	v_mfma_f32_16x16x32_bf16 v[74:77], v[160:163], v[230:233], v[74:77]
	s_setprio 0
	s_setprio 3
	v_mfma_f32_16x16x32_bf16 v[118:121], v[164:167], v[200:203], v[118:121]
	v_mfma_f32_16x16x32_bf16 v[114:117], v[192:195], v[200:203], v[114:117]
	v_mfma_f32_16x16x32_bf16 v[102:105], v[164:167], v[208:211], v[102:105]
	v_mfma_f32_16x16x32_bf16 v[98:101], v[192:195], v[208:211], v[98:101]
	v_mfma_f32_16x16x32_bf16 v[86:89], v[164:167], v[216:219], v[86:89]
	v_mfma_f32_16x16x32_bf16 v[82:85], v[192:195], v[216:219], v[82:85]
	v_mfma_f32_16x16x32_bf16 v[70:73], v[164:167], v[224:227], v[70:73]
	v_mfma_f32_16x16x32_bf16 v[66:69], v[192:195], v[224:227], v[66:69]
	v_mfma_f32_16x16x32_bf16 v[118:121], v[182:185], v[204:207], v[118:121]
	v_mfma_f32_16x16x32_bf16 v[114:117], v[196:199], v[204:207], v[114:117]
	v_mfma_f32_16x16x32_bf16 v[102:105], v[182:185], v[212:215], v[102:105]
	v_mfma_f32_16x16x32_bf16 v[98:101], v[196:199], v[212:215], v[98:101]
	v_mfma_f32_16x16x32_bf16 v[86:89], v[182:185], v[220:223], v[86:89]
	v_mfma_f32_16x16x32_bf16 v[82:85], v[196:199], v[220:223], v[82:85]
	v_mfma_f32_16x16x32_bf16 v[70:73], v[182:185], v[230:233], v[70:73]
	v_mfma_f32_16x16x32_bf16 v[66:69], v[196:199], v[230:233], v[66:69]
	s_setprio 0
	s_barrier
	s_add_i32 s61, s39, s2
	s_mov_b32 m0, s61
	ds_read_b128 v[200:203], v189 offset:16384
	ds_read_b128 v[204:207], v189 offset:17408
	ds_read_b128 v[208:211], v189 offset:18432
	ds_read_b128 v[212:215], v189 offset:19456
	ds_read_b128 v[216:219], v189 offset:20480
	ds_read_b128 v[220:223], v189 offset:21504
	ds_read_b128 v[224:227], v189 offset:22528
	ds_read_b128 v[230:233], v189 offset:23552
	global_load_lds_dwordx4 v[168:169], off
	s_add_i32 m0, s61, 0x2000
	s_add_u32 s62, s24, 0x40000
	s_addc_u32 s63, s25, 0
	s_add_i32 s61, s48, s2
	global_load_lds_dwordx4 v[172:173], off
	s_mov_b32 m0, s61
	s_nop 0
	global_load_lds_dwordx4 v146, s[62:63]
	s_add_i32 m0, s61, 0x2000
	s_nop 0
	global_load_lds_dwordx4 v142, s[62:63]
	s_mov_b32 m0, s29
	s_nop 0
	global_load_lds_dwordx4 v[176:177], off
	s_mov_b32 m0, s30
	s_nop 0
	global_load_lds_dwordx4 v[234:235], off
	s_waitcnt vmcnt(8)
	s_waitcnt lgkmcnt(0)
	s_barrier
	s_setprio 3
	s_waitcnt lgkmcnt(0)
	v_mfma_f32_16x16x32_bf16 v[62:65], v[130:133], v[200:203], v[62:65]
	v_mfma_f32_16x16x32_bf16 v[58:61], v[138:141], v[200:203], v[58:61]
	v_mfma_f32_16x16x32_bf16 v[46:49], v[130:133], v[208:211], v[46:49]
	v_mfma_f32_16x16x32_bf16 v[42:45], v[138:141], v[208:211], v[42:45]
	v_mfma_f32_16x16x32_bf16 v[30:33], v[130:133], v[216:219], v[30:33]
	v_mfma_f32_16x16x32_bf16 v[26:29], v[138:141], v[216:219], v[26:29]
	v_mfma_f32_16x16x32_bf16 v[14:17], v[130:133], v[224:227], v[14:17]
	v_mfma_f32_16x16x32_bf16 v[10:13], v[138:141], v[224:227], v[10:13]
	v_mfma_f32_16x16x32_bf16 v[62:65], v[134:137], v[204:207], v[62:65]
	v_mfma_f32_16x16x32_bf16 v[58:61], v[160:163], v[204:207], v[58:61]
	v_mfma_f32_16x16x32_bf16 v[46:49], v[134:137], v[212:215], v[46:49]
	v_mfma_f32_16x16x32_bf16 v[42:45], v[160:163], v[212:215], v[42:45]
	v_mfma_f32_16x16x32_bf16 v[30:33], v[134:137], v[220:223], v[30:33]
	v_mfma_f32_16x16x32_bf16 v[26:29], v[160:163], v[220:223], v[26:29]
	v_mfma_f32_16x16x32_bf16 v[14:17], v[134:137], v[230:233], v[14:17]
	v_mfma_f32_16x16x32_bf16 v[10:13], v[160:163], v[230:233], v[10:13]
	s_setprio 0
	s_setprio 3
	v_mfma_f32_16x16x32_bf16 v[54:57], v[164:167], v[200:203], v[54:57]
	v_mfma_f32_16x16x32_bf16 v[50:53], v[192:195], v[200:203], v[50:53]
	v_mfma_f32_16x16x32_bf16 v[38:41], v[164:167], v[208:211], v[38:41]
	v_mfma_f32_16x16x32_bf16 v[34:37], v[192:195], v[208:211], v[34:37]
	v_mfma_f32_16x16x32_bf16 v[22:25], v[164:167], v[216:219], v[22:25]
	v_mfma_f32_16x16x32_bf16 v[18:21], v[192:195], v[216:219], v[18:21]
	v_mfma_f32_16x16x32_bf16 v[6:9], v[164:167], v[224:227], v[6:9]
	v_mfma_f32_16x16x32_bf16 v[2:5], v[192:195], v[224:227], v[2:5]
	v_mfma_f32_16x16x32_bf16 v[54:57], v[182:185], v[204:207], v[54:57]
	v_mfma_f32_16x16x32_bf16 v[50:53], v[196:199], v[204:207], v[50:53]
	v_mfma_f32_16x16x32_bf16 v[38:41], v[182:185], v[212:215], v[38:41]
	v_mfma_f32_16x16x32_bf16 v[34:37], v[196:199], v[212:215], v[34:37]
	v_mfma_f32_16x16x32_bf16 v[22:25], v[182:185], v[220:223], v[22:25]
	v_mfma_f32_16x16x32_bf16 v[18:21], v[196:199], v[220:223], v[18:21]
	v_mfma_f32_16x16x32_bf16 v[6:9], v[182:185], v[230:233], v[6:9]
	v_mfma_f32_16x16x32_bf16 v[2:5], v[196:199], v[230:233], v[2:5]
	s_setprio 0
	s_barrier
; #define PG8_STAGE_A(b, h, ptr, NX) do { if constexpr (Sched::GATHER) { unsigned gs_[2]; gs_[0] = ((NX) && last_) ? gN[h][0] : gA[h][0]; gs_[1] = ((NX) && last_) ? gN[h][1] : gA[h][1]; PG8_STAGE(PG8_SA(b, h), ptr, gs_); } \
;         else PG8_STAGE(PG8_SA(b, h), (ptr) + ((h) ? hstep : (size_t)0), voffA); } while (0)
; #define PG8_STAGE(bufoff, gbase, voff) do { _Pragma("unroll") for (int _i = 0; _i < 2; ++_i) \
;         __builtin_amdgcn_global_load_lds((const unsigned*)((const char*)(gbase) + (voff)[_i]), (PG8_LAS unsigned*)(lds + (bufoff) + ldsw + _i * 8192), 16, 0, 0); } while (0)
; #define PG8_LDA(dst, b, h) do { _Pragma("unroll") for (int m = 0; m < 4; ++m) _Pragma("unroll") for (int k = 0; k < 2; ++k) dst[m][k] = *(const PG8_LAS bf16x8*)(lds + PG8_SA(b, h) + aoff + m * 2048 + k * 1024); } while (0)
; #define PG8_LDB(dst, b, h) do { _Pragma("unroll") for (int n = 0; n < 2; ++n) _Pragma("unroll") for (int k = 0; k < 2; ++k) dst[n][k] = *(const PG8_LAS bf16x8*)(lds + PG8_SB(b, h) + boff + n * 2048 + k * 1024); } while (0)
; #define PG8_MMA(ai, bj, At, Bt) do { __builtin_amdgcn_s_setprio(1); _Pragma("unroll") for (int m = 0; m < 4; ++m) _Pragma("unroll") for (int n = 0; n < 2; ++n) _Pragma("unroll") for (int k = 0; k < 2; ++k) \
;         acc[ai][bj][m][n] = __builtin_amdgcn_mfma_f32_16x16x32_bf16(Bt[n][k], At[m][k], acc[ai][bj][m][n], 0, 0, 0); __builtin_amdgcn_s_setprio(0); } while (0)
; #define PG8_WAIT_V(n) asm volatile("s_waitcnt vmcnt(" #n ")" ::: "memory")
; #define PG8_WAIT_L(n) asm volatile("s_waitcnt lgkmcnt(" #n ")" ::: "memory")
; #define PG8_BAR __builtin_amdgcn_s_barrier()
; #define PG8_SCHED __builtin_amdgcn_sched_barrier(0)
; template <class Epi, class Sched, bool ALIGN_EPI = false, bool SP2 = false>
; __device__ __forceinline__ void gemm_phase(PG8_LAS unsigned char* lds, const Gemm g, const Sched& S, const Epi& E, const bool skip_epi = false) {
;     ...
;             PG8_LDB(B0, 1, 0); PG8_LDB(B1, 1, 1); PG8_SCHED; PG8_LDA(At, 1, 0); PG8_STAGE_A(0, 1, a2, true);
;             PG8_WAIT_V(8); PG8_WAIT_L(0); PG8_BAR; PG8_MMA(0, 0, At, B0); PG8_MMA(0, 1, At, B1); PG8_BAR; PG8_SCHED;
;             PG8_LDA(At, 1, 1); PG8_STAGE(PG8_SB(1, 0), b3, voffB); PG8_STAGE(PG8_SB(1, 1), b3 + hstep, voffB); PG8_STAGE_A(1, 0, a3, true);
;             PG8_WAIT_V(8); PG8_WAIT_L(0); PG8_BAR; PG8_MMA(1, 0, At, B0); PG8_MMA(1, 1, At, B1); PG8_BAR; PG8_SCHED;
	s_add_i32 s61, 0, 0x18000
	s_add_i32 s62, 0, 0x1c000
	v_add_u32_e32 v160, s61, v1
	v_add_u32_e32 v170, s62, v1
	ds_read_b128 v[130:133], v160
	ds_read_b128 v[134:137], v160 offset:1024
	ds_read_b128 v[138:141], v160 offset:2048
	ds_read_b128 v[160:163], v160 offset:3072
	ds_read_b128 v[164:167], v170
	ds_read_b128 v[182:185], v170 offset:1024
	ds_read_b128 v[192:195], v170 offset:2048
	ds_read_b128 v[196:199], v170 offset:3072
	s_add_u32 s26, s26, 0x40000
	s_addc_u32 s27, s27, 0
	s_mov_b32 m0, s31
	ds_read_b128 v[200:203], v189 offset:32768
	ds_read_b128 v[204:207], v189 offset:33792
	ds_read_b128 v[208:211], v189 offset:34816
	ds_read_b128 v[212:215], v189 offset:35840
	ds_read_b128 v[216:219], v189 offset:36864
	ds_read_b128 v[220:223], v189 offset:37888
	ds_read_b128 v[224:227], v189 offset:38912
	ds_read_b128 v[230:233], v189 offset:39936
	global_load_lds_dwordx4 v148, s[26:27]
	s_mov_b32 m0, s34
	s_nop 0
	global_load_lds_dwordx4 v144, s[26:27]
	s_waitcnt vmcnt(8)
	s_waitcnt lgkmcnt(0)
	s_barrier
	s_setprio 3
	s_waitcnt lgkmcnt(0)
	v_mfma_f32_16x16x32_bf16 v[126:129], v[130:133], v[200:203], v[126:129]
	v_mfma_f32_16x16x32_bf16 v[122:125], v[138:141], v[200:203], v[122:125]
	v_mfma_f32_16x16x32_bf16 v[110:113], v[130:133], v[208:211], v[110:113]
	v_mfma_f32_16x16x32_bf16 v[106:109], v[138:141], v[208:211], v[106:109]
	v_mfma_f32_16x16x32_bf16 v[94:97], v[130:133], v[216:219], v[94:97]
	v_mfma_f32_16x16x32_bf16 v[90:93], v[138:141], v[216:219], v[90:93]
	v_mfma_f32_16x16x32_bf16 v[78:81], v[130:133], v[224:227], v[78:81]
	v_mfma_f32_16x16x32_bf16 v[74:77], v[138:141], v[224:227], v[74:77]
	v_mfma_f32_16x16x32_bf16 v[126:129], v[134:137], v[204:207], v[126:129]
	v_mfma_f32_16x16x32_bf16 v[122:125], v[160:163], v[204:207], v[122:125]
	v_mfma_f32_16x16x32_bf16 v[110:113], v[134:137], v[212:215], v[110:113]
	v_mfma_f32_16x16x32_bf16 v[106:109], v[160:163], v[212:215], v[106:109]
	v_mfma_f32_16x16x32_bf16 v[94:97], v[134:137], v[220:223], v[94:97]
	v_mfma_f32_16x16x32_bf16 v[90:93], v[160:163], v[220:223], v[90:93]
	v_mfma_f32_16x16x32_bf16 v[78:81], v[134:137], v[230:233], v[78:81]
	v_mfma_f32_16x16x32_bf16 v[74:77], v[160:163], v[230:233], v[74:77]
	s_setprio 0
	s_setprio 3
	v_mfma_f32_16x16x32_bf16 v[118:121], v[164:167], v[200:203], v[118:121]
	v_mfma_f32_16x16x32_bf16 v[114:117], v[192:195], v[200:203], v[114:117]
	v_mfma_f32_16x16x32_bf16 v[102:105], v[164:167], v[208:211], v[102:105]
	v_mfma_f32_16x16x32_bf16 v[98:101], v[192:195], v[208:211], v[98:101]
	v_mfma_f32_16x16x32_bf16 v[86:89], v[164:167], v[216:219], v[86:89]
	v_mfma_f32_16x16x32_bf16 v[82:85], v[192:195], v[216:219], v[82:85]
	v_mfma_f32_16x16x32_bf16 v[70:73], v[164:167], v[224:227], v[70:73]
	v_mfma_f32_16x16x32_bf16 v[66:69], v[192:195], v[224:227], v[66:69]
	v_mfma_f32_16x16x32_bf16 v[118:121], v[182:185], v[204:207], v[118:121]
	v_mfma_f32_16x16x32_bf16 v[114:117], v[196:199], v[204:207], v[114:117]
	v_mfma_f32_16x16x32_bf16 v[102:105], v[182:185], v[212:215], v[102:105]
	v_mfma_f32_16x16x32_bf16 v[98:101], v[196:199], v[212:215], v[98:101]
	v_mfma_f32_16x16x32_bf16 v[86:89], v[182:185], v[220:223], v[86:89]
	v_mfma_f32_16x16x32_bf16 v[82:85], v[196:199], v[220:223], v[82:85]
	v_mfma_f32_16x16x32_bf16 v[70:73], v[182:185], v[230:233], v[70:73]
	v_mfma_f32_16x16x32_bf16 v[66:69], v[196:199], v[230:233], v[66:69]
	s_setprio 0
	s_barrier
	s_add_i32 s26, s61, s2
	s_add_i32 m0, s26, 0xffffff80
	ds_read_b128 v[200:203], v189 offset:49152
	ds_read_b128 v[204:207], v189 offset:50176
	ds_read_b128 v[208:211], v189 offset:51200
	ds_read_b128 v[212:215], v189 offset:52224
	ds_read_b128 v[216:219], v189 offset:53248
	ds_read_b128 v[220:223], v189 offset:54272
	ds_read_b128 v[224:227], v189 offset:55296
	ds_read_b128 v[230:233], v189 offset:56320
	global_load_lds_dwordx4 v[168:169], off offset:128
	s_add_i32 m0, s26, 0x1f80
	s_add_u32 s24, s24, 0x40080
	s_addc_u32 s25, s25, 0
	s_add_i32 s26, s62, s2
	global_load_lds_dwordx4 v[172:173], off offset:128
	s_mov_b32 m0, s26
	s_nop 0
	global_load_lds_dwordx4 v146, s[24:25]
	s_add_i32 m0, s26, 0x2000
	s_nop 0
	global_load_lds_dwordx4 v142, s[24:25]
	s_add_i32 m0, s36, 0xffffff80
	s_nop 0
	global_load_lds_dwordx4 v[176:177], off offset:128
	s_add_i32 m0, s37, 0xffffff80
	s_nop 0
	global_load_lds_dwordx4 v[234:235], off offset:128
	s_waitcnt vmcnt(8)
	s_waitcnt lgkmcnt(0)
	s_barrier
	s_setprio 3
	s_waitcnt lgkmcnt(0)
	v_mfma_f32_16x16x32_bf16 v[62:65], v[130:133], v[200:203], v[62:65]
	v_mfma_f32_16x16x32_bf16 v[58:61], v[138:141], v[200:203], v[58:61]
	v_mfma_f32_16x16x32_bf16 v[46:49], v[130:133], v[208:211], v[46:49]
	v_mfma_f32_16x16x32_bf16 v[42:45], v[138:141], v[208:211], v[42:45]
	v_mfma_f32_16x16x32_bf16 v[30:33], v[130:133], v[216:219], v[30:33]
	v_mfma_f32_16x16x32_bf16 v[26:29], v[138:141], v[216:219], v[26:29]
	v_mfma_f32_16x16x32_bf16 v[14:17], v[130:133], v[224:227], v[14:17]
	v_mfma_f32_16x16x32_bf16 v[10:13], v[138:141], v[224:227], v[10:13]
	v_mfma_f32_16x16x32_bf16 v[62:65], v[134:137], v[204:207], v[62:65]
	v_mfma_f32_16x16x32_bf16 v[58:61], v[160:163], v[204:207], v[58:61]
	v_mfma_f32_16x16x32_bf16 v[46:49], v[134:137], v[212:215], v[46:49]
	v_mfma_f32_16x16x32_bf16 v[42:45], v[160:163], v[212:215], v[42:45]
	v_mfma_f32_16x16x32_bf16 v[30:33], v[134:137], v[220:223], v[30:33]
	v_mfma_f32_16x16x32_bf16 v[26:29], v[160:163], v[220:223], v[26:29]
	v_mfma_f32_16x16x32_bf16 v[14:17], v[134:137], v[230:233], v[14:17]
	v_mfma_f32_16x16x32_bf16 v[10:13], v[160:163], v[230:233], v[10:13]
	s_setprio 0
	s_setprio 3
	v_mfma_f32_16x16x32_bf16 v[54:57], v[164:167], v[200:203], v[54:57]
	v_mfma_f32_16x16x32_bf16 v[50:53], v[192:195], v[200:203], v[50:53]
	v_mfma_f32_16x16x32_bf16 v[38:41], v[164:167], v[208:211], v[38:41]
	v_mfma_f32_16x16x32_bf16 v[34:37], v[192:195], v[208:211], v[34:37]
	v_mfma_f32_16x16x32_bf16 v[22:25], v[164:167], v[216:219], v[22:25]
	v_mfma_f32_16x16x32_bf16 v[18:21], v[192:195], v[216:219], v[18:21]
	v_mfma_f32_16x16x32_bf16 v[6:9], v[164:167], v[224:227], v[6:9]
	v_mfma_f32_16x16x32_bf16 v[2:5], v[192:195], v[224:227], v[2:5]
	v_mfma_f32_16x16x32_bf16 v[54:57], v[182:185], v[204:207], v[54:57]
	v_mfma_f32_16x16x32_bf16 v[50:53], v[196:199], v[204:207], v[50:53]
	v_mfma_f32_16x16x32_bf16 v[38:41], v[182:185], v[212:215], v[38:41]
	v_mfma_f32_16x16x32_bf16 v[34:37], v[196:199], v[212:215], v[34:37]
	v_mfma_f32_16x16x32_bf16 v[22:25], v[182:185], v[220:223], v[22:25]
	v_mfma_f32_16x16x32_bf16 v[18:21], v[196:199], v[220:223], v[18:21]
	v_mfma_f32_16x16x32_bf16 v[6:9], v[182:185], v[230:233], v[6:9]
	v_mfma_f32_16x16x32_bf16 v[2:5], v[196:199], v[230:233], v[2:5]
	s_setprio 0
	s_barrier
	s_add_i32 s60, s60, 2
	s_add_u32 s22, s22, 0x100
	s_addc_u32 s23, s23, 0
	s_add_u32 s58, s58, 0x100
	s_addc_u32 s59, s59, 0
	s_cmp_gt_u32 s60, 13
	s_cbranch_scc0 .LBB0_721
	s_and_b64 vcc, exec, s[10:11]
	s_cbranch_vccz .LBB0_724
	s_barrier

; #define PG8_STAGE_A(b, h, ptr, NX) do { if constexpr (Sched::GATHER) { unsigned gs_[2]; gs_[0] = ((NX) && last_) ? gN[h][0] : gA[h][0]; gs_[1] = ((NX) && last_) ? gN[h][1] : gA[h][1]; PG8_STAGE(PG8_SA(b, h), ptr, gs_); } \
;         else PG8_STAGE(PG8_SA(b, h), (ptr) + ((h) ? hstep : (size_t)0), voffA); } while (0)
; #define PG8_STAGE(bufoff, gbase, voff) do { _Pragma("unroll") for (int _i = 0; _i < 2; ++_i) \
;         __builtin_amdgcn_global_load_lds((const unsigned*)((const char*)(gbase) + (voff)[_i]), (PG8_LAS unsigned*)(lds + (bufoff) + ldsw + _i * 8192), 16, 0, 0); } while (0)
; #define PG8_LDA(dst, b, h) do { _Pragma("unroll") for (int m = 0; m < 4; ++m) _Pragma("unroll") for (int k = 0; k < 2; ++k) dst[m][k] = *(const PG8_LAS bf16x8*)(lds + PG8_SA(b, h) + aoff + m * 2048 + k * 1024); } while (0)
; #define PG8_WAIT_V(n) asm volatile("s_waitcnt vmcnt(" #n ")" ::: "memory")
; #define PG8_WAIT_L(n) asm volatile("s_waitcnt lgkmcnt(" #n ")" ::: "memory")
; #define PG8_BAR __builtin_amdgcn_s_barrier()
; template <class Epi, class Sched, bool ALIGN_EPI = false, bool SP2 = false>
; __device__ __forceinline__ void gemm_phase(PG8_LAS unsigned char* lds, const Gemm g, const Sched& S, const Epi& E, const bool skip_epi = false) {
;     ...
;         const char* nA = has_next ? (const char*)g.A + (size_t)nxt.pm * pmstepA + nxt.ko : cA; const char* nB = has_next ? (const char*)g.Bt + (size_t)nxt.pn * tstep + nxt.ko : cB;
;         for (int t = 0; t < nt; t += 2) {
;             const bool last = (t == nt - 2); last_ = last && has_next;
;             const char* a1 = cA + (size_t)(t + 1) * kstep;
;             const char* a2 = last ? nA : cA + (size_t)(t + 2) * kstep; const char* b2 = last ? nB : cB + (size_t)(t + 2) * kstep;
;             const char* a3 = a2 + kstep; const char* b3 = b2 + kstep;
;             if (last && has_next) S.a_ready(nxt);
;             if constexpr (SP2) {
;             PG8_LDB(B0, 0, 0); PG8_LDB(B1, 0, 1); PG8_SCHED; PG8_LDA(At, 0, 0); PG8_STAGE_A(1, 1, a1, false);
;             PG8_WAIT_V(8); PG8_WAIT_L(0); PG8_BAR; PG8_MMA(0, 0, At, B0); PG8_MMA(0, 1, At, B1); PG8_BAR; PG8_SCHED;
;             PG8_LDA(At, 0, 1); PG8_STAGE(PG8_SB(0, 0), b2, voffB); PG8_STAGE(PG8_SB(0, 1), b2 + hstep, voffB); PG8_STAGE_A(0, 0, a2, true);
;             PG8_WAIT_V(8); PG8_WAIT_L(0); PG8_BAR; PG8_MMA(1, 0, At, B0); PG8_MMA(1, 1, At, B1); PG8_BAR; PG8_SCHED;
.LBB0_856:
	s_add_u32 s55, s22, 0x100
	s_addc_u32 s56, s23, 0
	s_mov_b32 s57, -2
	s_waitcnt vmcnt(0)
	s_waitcnt lgkmcnt(0)
	ds_read_b128 v[98:101], v234
	ds_read_b128 v[110:113], v234 offset:1024
	ds_read_b128 v[122:125], v234 offset:2048
	ds_read_b128 v[126:129], v234 offset:3072
	ds_read_b128 v[138:141], v235
	ds_read_b128 v[142:145], v235 offset:1024
	ds_read_b128 v[146:149], v235 offset:2048
	ds_read_b128 v[150:153], v235 offset:3072
	s_add_u32 s22, s20, 0x100
	s_addc_u32 s23, s21, 0
	s_cmp_eq_u32 s57, 40
	s_cselect_b32 s27, s9, s23
	s_cselect_b32 s26, s8, s22
	s_cselect_b32 s25, s19, s56
	s_cselect_b32 s24, s18, s55
	v_lshl_add_u64 v[210:211], s[20:21], 0, v[198:199]
	s_add_i32 m0, s3, 0xc000
	ds_read_b128 v[154:157], v236
	ds_read_b128 v[166:169], v236 offset:1024
	ds_read_b128 v[170:173], v236 offset:2048
	ds_read_b128 v[174:177], v236 offset:3072
	ds_read_b128 v[178:181], v236 offset:4096
	ds_read_b128 v[182:185], v236 offset:5120
	ds_read_b128 v[186:189], v236 offset:6144
	ds_read_b128 v[206:209], v236 offset:7168
	global_load_lds_dwordx4 v[210:211], off
	v_lshl_add_u64 v[210:211], s[20:21], 0, v[200:201]
	s_add_i32 m0, s3, 0xe000
	s_nop 0
	global_load_lds_dwordx4 v[210:211], off
	s_waitcnt vmcnt(8)
	s_waitcnt lgkmcnt(0)
	s_barrier
	s_setprio 3
	s_waitcnt lgkmcnt(0)
	v_mfma_f32_16x16x32_bf16 v[162:165], v[98:101], v[154:157], 0
	v_mfma_f32_16x16x32_bf16 v[158:161], v[122:125], v[154:157], 0
	v_mfma_f32_16x16x32_bf16 v[118:121], v[98:101], v[170:173], 0
	v_mfma_f32_16x16x32_bf16 v[114:117], v[122:125], v[170:173], 0
	v_lshl_add_u64 v[210:211], s[24:25], 0, v[192:193]
	v_mfma_f32_16x16x32_bf16 v[94:97], v[98:101], v[178:181], 0
	v_mfma_f32_16x16x32_bf16 v[90:93], v[122:125], v[178:181], 0
	v_lshl_add_u64 v[212:213], s[24:25], 0, v[196:197]
	v_mfma_f32_16x16x32_bf16 v[78:81], v[98:101], v[186:189], 0
	v_mfma_f32_16x16x32_bf16 v[74:77], v[122:125], v[186:189], 0
	v_lshl_add_u64 v[216:217], s[26:27], 0, v[194:195]
	v_mfma_f32_16x16x32_bf16 v[162:165], v[110:113], v[166:169], v[162:165]
	v_mfma_f32_16x16x32_bf16 v[158:161], v[126:129], v[166:169], v[158:161]
	v_lshl_add_u64 v[214:215], s[26:27], 0, v[190:191]
	v_mfma_f32_16x16x32_bf16 v[118:121], v[110:113], v[174:177], v[118:121]
	v_mfma_f32_16x16x32_bf16 v[114:117], v[126:129], v[174:177], v[114:117]
	v_mfma_f32_16x16x32_bf16 v[94:97], v[110:113], v[182:185], v[94:97]
	v_mfma_f32_16x16x32_bf16 v[90:93], v[126:129], v[182:185], v[90:93]
	v_mfma_f32_16x16x32_bf16 v[78:81], v[110:113], v[206:209], v[78:81]
	v_mfma_f32_16x16x32_bf16 v[74:77], v[126:129], v[206:209], v[74:77]
	s_setprio 0
	s_setprio 3
	v_mfma_f32_16x16x32_bf16 v[134:137], v[138:141], v[154:157], 0
	v_mfma_f32_16x16x32_bf16 v[130:133], v[146:149], v[154:157], 0
	v_mfma_f32_16x16x32_bf16 v[106:109], v[138:141], v[170:173], 0
	v_mfma_f32_16x16x32_bf16 v[102:105], v[146:149], v[170:173], 0
	v_mfma_f32_16x16x32_bf16 v[86:89], v[138:141], v[178:181], 0
	v_mfma_f32_16x16x32_bf16 v[82:85], v[146:149], v[178:181], 0
	v_mfma_f32_16x16x32_bf16 v[70:73], v[138:141], v[186:189], 0
	v_mfma_f32_16x16x32_bf16 v[66:69], v[146:149], v[186:189], 0
	v_mfma_f32_16x16x32_bf16 v[134:137], v[142:145], v[166:169], v[134:137]
	v_mfma_f32_16x16x32_bf16 v[130:133], v[150:153], v[166:169], v[130:133]
	v_mfma_f32_16x16x32_bf16 v[106:109], v[142:145], v[174:177], v[106:109]
	v_mfma_f32_16x16x32_bf16 v[102:105], v[150:153], v[174:177], v[102:105]
	v_mfma_f32_16x16x32_bf16 v[86:89], v[142:145], v[182:185], v[86:89]
	v_mfma_f32_16x16x32_bf16 v[82:85], v[150:153], v[182:185], v[82:85]
	v_mfma_f32_16x16x32_bf16 v[70:73], v[142:145], v[206:209], v[70:73]
	v_mfma_f32_16x16x32_bf16 v[66:69], v[150:153], v[206:209], v[66:69]
	s_setprio 0
	s_barrier
	s_add_i32 s20, s39, s2
	s_mov_b32 m0, s20
	ds_read_b128 v[154:157], v236 offset:16384
	ds_read_b128 v[166:169], v236 offset:17408
	ds_read_b128 v[170:173], v236 offset:18432
	ds_read_b128 v[174:177], v236 offset:19456
	ds_read_b128 v[178:181], v236 offset:20480
	ds_read_b128 v[182:185], v236 offset:21504
	ds_read_b128 v[186:189], v236 offset:22528
	ds_read_b128 v[206:209], v236 offset:23552
	global_load_lds_dwordx4 v[210:211], off
	s_add_i32 m0, s20, 0x2000
	s_add_u32 s20, s24, 0xb0000
	s_addc_u32 s21, s25, 0
	s_add_i32 s58, s48, s2
	global_load_lds_dwordx4 v[212:213], off
	s_mov_b32 m0, s58
	s_nop 0
	global_load_lds_dwordx4 v192, s[20:21]
	s_add_i32 m0, s58, 0x2000
	s_nop 0
	global_load_lds_dwordx4 v196, s[20:21]
	s_mov_b32 m0, s3
	s_nop 0
	global_load_lds_dwordx4 v[214:215], off
	s_mov_b32 m0, s28
	s_nop 0
	global_load_lds_dwordx4 v[216:217], off
	s_waitcnt vmcnt(8)
	s_waitcnt lgkmcnt(0)
	s_barrier
; #define PG8_STAGE_A(b, h, ptr, NX) do { if constexpr (Sched::GATHER) { unsigned gs_[2]; gs_[0] = ((NX) && last_) ? gN[h][0] : gA[h][0]; gs_[1] = ((NX) && last_) ? gN[h][1] : gA[h][1]; PG8_STAGE(PG8_SA(b, h), ptr, gs_); } \
;         else PG8_STAGE(PG8_SA(b, h), (ptr) + ((h) ? hstep : (size_t)0), voffA); } while (0)
; #define PG8_LDA(dst, b, h) do { _Pragma("unroll") for (int m = 0; m < 4; ++m) _Pragma("unroll") for (int k = 0; k < 2; ++k) dst[m][k] = *(const PG8_LAS bf16x8*)(lds + PG8_SA(b, h) + aoff + m * 2048 + k * 1024); } while (0)
; #define PG8_LDB(dst, b, h) do { _Pragma("unroll") for (int n = 0; n < 2; ++n) _Pragma("unroll") for (int k = 0; k < 2; ++k) dst[n][k] = *(const PG8_LAS bf16x8*)(lds + PG8_SB(b, h) + boff + n * 2048 + k * 1024); } while (0)
; #define PG8_MMA(ai, bj, At, Bt) do { __builtin_amdgcn_s_setprio(1); _Pragma("unroll") for (int m = 0; m < 4; ++m) _Pragma("unroll") for (int n = 0; n < 2; ++n) _Pragma("unroll") for (int k = 0; k < 2; ++k) \
;         acc[ai][bj][m][n] = __builtin_amdgcn_mfma_f32_16x16x32_bf16(Bt[n][k], At[m][k], acc[ai][bj][m][n], 0, 0, 0); __builtin_amdgcn_s_setprio(0); } while (0)
; #define PG8_WAIT_V(n) asm volatile("s_waitcnt vmcnt(" #n ")" ::: "memory")
; #define PG8_WAIT_L(n) asm volatile("s_waitcnt lgkmcnt(" #n ")" ::: "memory")
; #define PG8_BAR __builtin_amdgcn_s_barrier()
; #define PG8_SCHED __builtin_amdgcn_sched_barrier(0)
; template <class Epi, class Sched, bool ALIGN_EPI = false, bool SP2 = false>
; __device__ __forceinline__ void gemm_phase(PG8_LAS unsigned char* lds, const Gemm g, const Sched& S, const Epi& E, const bool skip_epi = false) {
;     ...
;             PG8_WAIT_V(8); PG8_WAIT_L(0); PG8_BAR; PG8_MMA(1, 0, At, B0); PG8_MMA(1, 1, At, B1); PG8_BAR; PG8_SCHED;
;             PG8_LDB(B0, 1, 0); PG8_LDB(B1, 1, 1); PG8_SCHED; PG8_LDA(At, 1, 0); PG8_STAGE_A(0, 1, a2, true);
;             PG8_WAIT_V(8); PG8_WAIT_L(0); PG8_BAR; PG8_MMA(0, 0, At, B0); PG8_MMA(0, 1, At, B1); PG8_BAR; PG8_SCHED;
	s_setprio 3
	s_waitcnt lgkmcnt(0)
	v_mfma_f32_16x16x32_bf16 v[62:65], v[98:101], v[154:157], 0
	v_mfma_f32_16x16x32_bf16 v[58:61], v[122:125], v[154:157], 0
	v_mfma_f32_16x16x32_bf16 v[46:49], v[98:101], v[170:173], 0
	v_mfma_f32_16x16x32_bf16 v[42:45], v[122:125], v[170:173], 0
	v_mfma_f32_16x16x32_bf16 v[30:33], v[98:101], v[178:181], 0
	v_mfma_f32_16x16x32_bf16 v[26:29], v[122:125], v[178:181], 0
	v_mfma_f32_16x16x32_bf16 v[14:17], v[98:101], v[186:189], 0
	v_mfma_f32_16x16x32_bf16 v[10:13], v[122:125], v[186:189], 0
	v_mfma_f32_16x16x32_bf16 v[62:65], v[110:113], v[166:169], v[62:65]
	v_mfma_f32_16x16x32_bf16 v[58:61], v[126:129], v[166:169], v[58:61]
	v_mfma_f32_16x16x32_bf16 v[46:49], v[110:113], v[174:177], v[46:49]
	v_mfma_f32_16x16x32_bf16 v[42:45], v[126:129], v[174:177], v[42:45]
	v_mfma_f32_16x16x32_bf16 v[30:33], v[110:113], v[182:185], v[30:33]
	v_mfma_f32_16x16x32_bf16 v[26:29], v[126:129], v[182:185], v[26:29]
	v_mfma_f32_16x16x32_bf16 v[14:17], v[110:113], v[206:209], v[14:17]
	v_mfma_f32_16x16x32_bf16 v[10:13], v[126:129], v[206:209], v[10:13]
	s_setprio 0
	s_setprio 3
	v_mfma_f32_16x16x32_bf16 v[54:57], v[138:141], v[154:157], 0
	v_mfma_f32_16x16x32_bf16 v[50:53], v[146:149], v[154:157], 0
	v_mfma_f32_16x16x32_bf16 v[38:41], v[138:141], v[170:173], 0
	v_mfma_f32_16x16x32_bf16 v[34:37], v[146:149], v[170:173], 0
	v_mfma_f32_16x16x32_bf16 v[22:25], v[138:141], v[178:181], 0
	v_mfma_f32_16x16x32_bf16 v[18:21], v[146:149], v[178:181], 0
	v_mfma_f32_16x16x32_bf16 v[6:9], v[138:141], v[186:189], 0
	v_mfma_f32_16x16x32_bf16 v[2:5], v[146:149], v[186:189], 0
	v_mfma_f32_16x16x32_bf16 v[54:57], v[142:145], v[166:169], v[54:57]
	v_mfma_f32_16x16x32_bf16 v[50:53], v[150:153], v[166:169], v[50:53]
	v_mfma_f32_16x16x32_bf16 v[38:41], v[142:145], v[174:177], v[38:41]
	v_mfma_f32_16x16x32_bf16 v[34:37], v[150:153], v[174:177], v[34:37]
	v_mfma_f32_16x16x32_bf16 v[22:25], v[142:145], v[182:185], v[22:25]
	v_mfma_f32_16x16x32_bf16 v[18:21], v[150:153], v[182:185], v[18:21]
	v_mfma_f32_16x16x32_bf16 v[6:9], v[142:145], v[206:209], v[6:9]
	v_mfma_f32_16x16x32_bf16 v[2:5], v[150:153], v[206:209], v[2:5]
	s_setprio 0
	s_barrier
	s_add_i32 s58, 0, 0x18000
	s_add_i32 s59, 0, 0x1c000
	v_add_u32_e32 v126, s58, v229
	v_add_u32_e32 v150, s59, v229
	ds_read_b128 v[98:101], v126
	ds_read_b128 v[110:113], v126 offset:1024
	ds_read_b128 v[122:125], v126 offset:2048
	ds_read_b128 v[126:129], v126 offset:3072
	ds_read_b128 v[138:141], v150
	ds_read_b128 v[142:145], v150 offset:1024
	ds_read_b128 v[146:149], v150 offset:2048
	ds_read_b128 v[150:153], v150 offset:3072
	s_add_u32 s20, s26, 0xb0000
	s_addc_u32 s21, s27, 0
	s_mov_b32 m0, s29
	ds_read_b128 v[154:157], v236 offset:32768
	ds_read_b128 v[166:169], v236 offset:33792
	ds_read_b128 v[170:173], v236 offset:34816
	ds_read_b128 v[174:177], v236 offset:35840
	ds_read_b128 v[178:181], v236 offset:36864
	ds_read_b128 v[182:185], v236 offset:37888
	ds_read_b128 v[186:189], v236 offset:38912
	ds_read_b128 v[206:209], v236 offset:39936
	global_load_lds_dwordx4 v190, s[20:21]
	s_mov_b32 m0, s30
	s_nop 0
	global_load_lds_dwordx4 v194, s[20:21]
	s_waitcnt vmcnt(8)
	s_waitcnt lgkmcnt(0)
	s_barrier
	s_setprio 3
	s_waitcnt lgkmcnt(0)
	v_mfma_f32_16x16x32_bf16 v[162:165], v[98:101], v[154:157], v[162:165]
	v_mfma_f32_16x16x32_bf16 v[158:161], v[122:125], v[154:157], v[158:161]
	v_mfma_f32_16x16x32_bf16 v[118:121], v[98:101], v[170:173], v[118:121]
	v_mfma_f32_16x16x32_bf16 v[114:117], v[122:125], v[170:173], v[114:117]
	v_mfma_f32_16x16x32_bf16 v[94:97], v[98:101], v[178:181], v[94:97]
	v_mfma_f32_16x16x32_bf16 v[90:93], v[122:125], v[178:181], v[90:93]
	v_mfma_f32_16x16x32_bf16 v[78:81], v[98:101], v[186:189], v[78:81]
	v_mfma_f32_16x16x32_bf16 v[74:77], v[122:125], v[186:189], v[74:77]
	v_mfma_f32_16x16x32_bf16 v[162:165], v[110:113], v[166:169], v[162:165]
	v_mfma_f32_16x16x32_bf16 v[158:161], v[126:129], v[166:169], v[158:161]
	v_mfma_f32_16x16x32_bf16 v[118:121], v[110:113], v[174:177], v[118:121]
	v_mfma_f32_16x16x32_bf16 v[114:117], v[126:129], v[174:177], v[114:117]
	v_mfma_f32_16x16x32_bf16 v[94:97], v[110:113], v[182:185], v[94:97]
	v_mfma_f32_16x16x32_bf16 v[90:93], v[126:129], v[182:185], v[90:93]
	v_mfma_f32_16x16x32_bf16 v[78:81], v[110:113], v[206:209], v[78:81]
	v_mfma_f32_16x16x32_bf16 v[74:77], v[126:129], v[206:209], v[74:77]
	s_setprio 0
	s_setprio 3
	v_mfma_f32_16x16x32_bf16 v[134:137], v[138:141], v[154:157], v[134:137]
	v_mfma_f32_16x16x32_bf16 v[130:133], v[146:149], v[154:157], v[130:133]
	v_mfma_f32_16x16x32_bf16 v[106:109], v[138:141], v[170:173], v[106:109]
	v_mfma_f32_16x16x32_bf16 v[102:105], v[146:149], v[170:173], v[102:105]
	v_mfma_f32_16x16x32_bf16 v[86:89], v[138:141], v[178:181], v[86:89]
	v_mfma_f32_16x16x32_bf16 v[82:85], v[146:149], v[178:181], v[82:85]
	v_mfma_f32_16x16x32_bf16 v[70:73], v[138:141], v[186:189], v[70:73]
	v_mfma_f32_16x16x32_bf16 v[66:69], v[146:149], v[186:189], v[66:69]
	v_mfma_f32_16x16x32_bf16 v[134:137], v[142:145], v[166:169], v[134:137]
	v_mfma_f32_16x16x32_bf16 v[130:133], v[150:153], v[166:169], v[130:133]
	v_mfma_f32_16x16x32_bf16 v[106:109], v[142:145], v[174:177], v[106:109]
	v_mfma_f32_16x16x32_bf16 v[102:105], v[150:153], v[174:177], v[102:105]
	v_mfma_f32_16x16x32_bf16 v[86:89], v[142:145], v[182:185], v[86:89]
	v_mfma_f32_16x16x32_bf16 v[82:85], v[150:153], v[182:185], v[82:85]
	v_mfma_f32_16x16x32_bf16 v[70:73], v[142:145], v[206:209], v[70:73]
	v_mfma_f32_16x16x32_bf16 v[66:69], v[150:153], v[206:209], v[66:69]
	s_setprio 0
	s_barrier
; #define PG8_STAGE_A(b, h, ptr, NX) do { if constexpr (Sched::GATHER) { unsigned gs_[2]; gs_[0] = ((NX) && last_) ? gN[h][0] : gA[h][0]; gs_[1] = ((NX) && last_) ? gN[h][1] : gA[h][1]; PG8_STAGE(PG8_SA(b, h), ptr, gs_); } \
;         else PG8_STAGE(PG8_SA(b, h), (ptr) + ((h) ? hstep : (size_t)0), voffA); } while (0)
; #define PG8_STAGE(bufoff, gbase, voff) do { _Pragma("unroll") for (int _i = 0; _i < 2; ++_i) \
;         __builtin_amdgcn_global_load_lds((const unsigned*)((const char*)(gbase) + (voff)[_i]), (PG8_LAS unsigned*)(lds + (bufoff) + ldsw + _i * 8192), 16, 0, 0); } while (0)
; #define PG8_LDA(dst, b, h) do { _Pragma("unroll") for (int m = 0; m < 4; ++m) _Pragma("unroll") for (int k = 0; k < 2; ++k) dst[m][k] = *(const PG8_LAS bf16x8*)(lds + PG8_SA(b, h) + aoff + m * 2048 + k * 1024); } while (0)
; #define PG8_LDB(dst, b, h) do { _Pragma("unroll") for (int n = 0; n < 2; ++n) _Pragma("unroll") for (int k = 0; k < 2; ++k) dst[n][k] = *(const PG8_LAS bf16x8*)(lds + PG8_SB(b, h) + boff + n * 2048 + k * 1024); } while (0)
; #define PG8_WAIT_V(n) asm volatile("s_waitcnt vmcnt(" #n ")" ::: "memory")
; #define PG8_BAR __builtin_amdgcn_s_barrier()
; template <class Epi, class Sched, bool ALIGN_EPI = false, bool SP2 = false>
; __device__ __forceinline__ void gemm_phase(PG8_LAS unsigned char* lds, const Gemm g, const Sched& S, const Epi& E, const bool skip_epi = false) {
;     ...
;             PG8_LDB(B0, 0, 0); PG8_LDB(B1, 0, 1); PG8_SCHED; PG8_LDA(At, 0, 0); PG8_STAGE_A(1, 1, a1, false);
;             PG8_WAIT_V(8); PG8_WAIT_L(0); PG8_BAR; PG8_MMA(0, 0, At, B0); PG8_MMA(0, 1, At, B1); PG8_BAR; PG8_SCHED;
;             PG8_LDA(At, 0, 1); PG8_STAGE(PG8_SB(0, 0), b2, voffB); PG8_STAGE(PG8_SB(0, 1), b2 + hstep, voffB); PG8_STAGE_A(0, 0, a2, true);
;             PG8_WAIT_V(8); PG8_WAIT_L(0); PG8_BAR; PG8_MMA(1, 0, At, B0); PG8_MMA(1, 1, At, B1); PG8_BAR; PG8_SCHED;
;             PG8_LDB(B0, 1, 0); PG8_LDB(B1, 1, 1); PG8_SCHED; PG8_LDA(At, 1, 0); PG8_STAGE_A(0, 1, a2, true);
;             PG8_WAIT_V(8); PG8_WAIT_L(0); PG8_BAR; PG8_MMA(0, 0, At, B0); PG8_MMA(0, 1, At, B1); PG8_BAR; PG8_SCHED;
;             PG8_LDA(At, 1, 1); PG8_STAGE(PG8_SB(1, 0), b3, voffB); PG8_STAGE(PG8_SB(1, 1), b3 + hstep, voffB); PG8_STAGE_A(1, 0, a3, true);
;             PG8_WAIT_V(8); PG8_WAIT_L(0); PG8_BAR; PG8_MMA(1, 0, At, B0); PG8_MMA(1, 1, At, B1); PG8_BAR; PG8_SCHED;
	s_add_i32 s20, s58, s2
	s_add_i32 m0, s20, 0xffffff80
	ds_read_b128 v[154:157], v236 offset:49152
	ds_read_b128 v[166:169], v236 offset:50176
	ds_read_b128 v[170:173], v236 offset:51200
	ds_read_b128 v[174:177], v236 offset:52224
	ds_read_b128 v[178:181], v236 offset:53248
	ds_read_b128 v[182:185], v236 offset:54272
	ds_read_b128 v[186:189], v236 offset:55296
	ds_read_b128 v[206:209], v236 offset:56320
	global_load_lds_dwordx4 v[210:211], off offset:128
	s_add_i32 m0, s20, 0x1f80
	s_add_u32 s20, s24, 0xb0080
	s_addc_u32 s21, s25, 0
	s_add_i32 s24, s59, s2
	global_load_lds_dwordx4 v[212:213], off offset:128
	s_mov_b32 m0, s24
	s_nop 0
	global_load_lds_dwordx4 v192, s[20:21]
	s_add_i32 m0, s24, 0x2000
	s_nop 0
	global_load_lds_dwordx4 v196, s[20:21]
	s_add_i32 m0, s35, 0xffffff80
	s_nop 0
	global_load_lds_dwordx4 v[214:215], off offset:128
	s_add_i32 m0, s36, 0xffffff80
	s_nop 0
	global_load_lds_dwordx4 v[216:217], off offset:128
	s_waitcnt vmcnt(8)
	s_waitcnt lgkmcnt(0)
	s_barrier
	s_setprio 3
	s_waitcnt lgkmcnt(0)
	v_mfma_f32_16x16x32_bf16 v[62:65], v[98:101], v[154:157], v[62:65]
	v_mfma_f32_16x16x32_bf16 v[58:61], v[122:125], v[154:157], v[58:61]
	v_mfma_f32_16x16x32_bf16 v[46:49], v[98:101], v[170:173], v[46:49]
	v_mfma_f32_16x16x32_bf16 v[42:45], v[122:125], v[170:173], v[42:45]
	v_mfma_f32_16x16x32_bf16 v[30:33], v[98:101], v[178:181], v[30:33]
	v_mfma_f32_16x16x32_bf16 v[26:29], v[122:125], v[178:181], v[26:29]
	v_mfma_f32_16x16x32_bf16 v[14:17], v[98:101], v[186:189], v[14:17]
	v_mfma_f32_16x16x32_bf16 v[10:13], v[122:125], v[186:189], v[10:13]
	v_mfma_f32_16x16x32_bf16 v[62:65], v[110:113], v[166:169], v[62:65]
	v_mfma_f32_16x16x32_bf16 v[58:61], v[126:129], v[166:169], v[58:61]
	v_mfma_f32_16x16x32_bf16 v[46:49], v[110:113], v[174:177], v[46:49]
	v_mfma_f32_16x16x32_bf16 v[42:45], v[126:129], v[174:177], v[42:45]
	v_mfma_f32_16x16x32_bf16 v[30:33], v[110:113], v[182:185], v[30:33]
	v_mfma_f32_16x16x32_bf16 v[26:29], v[126:129], v[182:185], v[26:29]
	v_mfma_f32_16x16x32_bf16 v[14:17], v[110:113], v[206:209], v[14:17]
	v_mfma_f32_16x16x32_bf16 v[10:13], v[126:129], v[206:209], v[10:13]
	s_setprio 0
	s_setprio 3
	v_mfma_f32_16x16x32_bf16 v[54:57], v[138:141], v[154:157], v[54:57]
	v_mfma_f32_16x16x32_bf16 v[50:53], v[146:149], v[154:157], v[50:53]
	v_mfma_f32_16x16x32_bf16 v[38:41], v[138:141], v[170:173], v[38:41]
	v_mfma_f32_16x16x32_bf16 v[34:37], v[146:149], v[170:173], v[34:37]
	v_mfma_f32_16x16x32_bf16 v[22:25], v[138:141], v[178:181], v[22:25]
	v_mfma_f32_16x16x32_bf16 v[18:21], v[146:149], v[178:181], v[18:21]
	v_mfma_f32_16x16x32_bf16 v[6:9], v[138:141], v[186:189], v[6:9]
	v_mfma_f32_16x16x32_bf16 v[2:5], v[146:149], v[186:189], v[2:5]
	v_mfma_f32_16x16x32_bf16 v[54:57], v[142:145], v[166:169], v[54:57]
	v_mfma_f32_16x16x32_bf16 v[50:53], v[150:153], v[166:169], v[50:53]
	v_mfma_f32_16x16x32_bf16 v[38:41], v[142:145], v[174:177], v[38:41]
	v_mfma_f32_16x16x32_bf16 v[34:37], v[150:153], v[174:177], v[34:37]
	v_mfma_f32_16x16x32_bf16 v[22:25], v[142:145], v[182:185], v[22:25]
	v_mfma_f32_16x16x32_bf16 v[18:21], v[150:153], v[182:185], v[18:21]
	v_mfma_f32_16x16x32_bf16 v[6:9], v[142:145], v[206:209], v[6:9]
	v_mfma_f32_16x16x32_bf16 v[2:5], v[150:153], v[206:209], v[2:5]
	s_setprio 0
	s_barrier
	s_add_i32 s57, s57, 2
	s_add_u32 s55, s55, 0x100
	s_addc_u32 s56, s56, 0
	s_cmp_gt_u32 s57, 41
	s_mov_b64 s[20:21], s[22:23]
.LBB0_857:
	ds_read_b128 v[98:101], v234
	ds_read_b128 v[110:113], v234 offset:1024
	ds_read_b128 v[122:125], v234 offset:2048
	ds_read_b128 v[126:129], v234 offset:3072
	ds_read_b128 v[138:141], v235
	ds_read_b128 v[142:145], v235 offset:1024
	ds_read_b128 v[146:149], v235 offset:2048
	ds_read_b128 v[150:153], v235 offset:3072
	s_add_u32 s22, s20, 0x100
	s_addc_u32 s23, s21, 0
	s_cmp_eq_u32 s57, 40
	s_cselect_b32 s27, s9, s23
	s_cselect_b32 s26, s8, s22
	s_cselect_b32 s25, s19, s56
	s_cselect_b32 s24, s18, s55
	v_lshl_add_u64 v[210:211], s[20:21], 0, v[198:199]
	s_add_i32 m0, s3, 0xc000
	ds_read_b128 v[154:157], v236
	ds_read_b128 v[166:169], v236 offset:1024
	ds_read_b128 v[170:173], v236 offset:2048
	ds_read_b128 v[174:177], v236 offset:3072
	ds_read_b128 v[178:181], v236 offset:4096
	ds_read_b128 v[182:185], v236 offset:5120
	ds_read_b128 v[186:189], v236 offset:6144
	ds_read_b128 v[206:209], v236 offset:7168
	global_load_lds_dwordx4 v[210:211], off
	v_lshl_add_u64 v[210:211], s[20:21], 0, v[200:201]
	s_add_i32 m0, s3, 0xe000
	s_nop 0
	global_load_lds_dwordx4 v[210:211], off
	s_waitcnt vmcnt(8)
	s_waitcnt lgkmcnt(0)
	s_barrier
; #define PG8_STAGE_A(b, h, ptr, NX) do { if constexpr (Sched::GATHER) { unsigned gs_[2]; gs_[0] = ((NX) && last_) ? gN[h][0] : gA[h][0]; gs_[1] = ((NX) && last_) ? gN[h][1] : gA[h][1]; PG8_STAGE(PG8_SA(b, h), ptr, gs_); } \
;         else PG8_STAGE(PG8_SA(b, h), (ptr) + ((h) ? hstep : (size_t)0), voffA); } while (0)
; #define PG8_STAGE(bufoff, gbase, voff) do { _Pragma("unroll") for (int _i = 0; _i < 2; ++_i) \
;         __builtin_amdgcn_global_load_lds((const unsigned*)((const char*)(gbase) + (voff)[_i]), (PG8_LAS unsigned*)(lds + (bufoff) + ldsw + _i * 8192), 16, 0, 0); } while (0)
; #define PG8_LDA(dst, b, h) do { _Pragma("unroll") for (int m = 0; m < 4; ++m) _Pragma("unroll") for (int k = 0; k < 2; ++k) dst[m][k] = *(const PG8_LAS bf16x8*)(lds + PG8_SA(b, h) + aoff + m * 2048 + k * 1024); } while (0)
; #define PG8_MMA(ai, bj, At, Bt) do { __builtin_amdgcn_s_setprio(1); _Pragma("unroll") for (int m = 0; m < 4; ++m) _Pragma("unroll") for (int n = 0; n < 2; ++n) _Pragma("unroll") for (int k = 0; k < 2; ++k) \
;         acc[ai][bj][m][n] = __builtin_amdgcn_mfma_f32_16x16x32_bf16(Bt[n][k], At[m][k], acc[ai][bj][m][n], 0, 0, 0); __builtin_amdgcn_s_setprio(0); } while (0)
; #define PG8_WAIT_V(n) asm volatile("s_waitcnt vmcnt(" #n ")" ::: "memory")
; #define PG8_WAIT_L(n) asm volatile("s_waitcnt lgkmcnt(" #n ")" ::: "memory")
; #define PG8_BAR __builtin_amdgcn_s_barrier()
; #define PG8_SCHED __builtin_amdgcn_sched_barrier(0)
; template <class Epi, class Sched, bool ALIGN_EPI = false, bool SP2 = false>
; __device__ __forceinline__ void gemm_phase(PG8_LAS unsigned char* lds, const Gemm g, const Sched& S, const Epi& E, const bool skip_epi = false) {
;     ...
;             PG8_WAIT_V(8); PG8_WAIT_L(0); PG8_BAR; PG8_MMA(0, 0, At, B0); PG8_MMA(0, 1, At, B1); PG8_BAR; PG8_SCHED;
;             PG8_LDA(At, 0, 1); PG8_STAGE(PG8_SB(0, 0), b2, voffB); PG8_STAGE(PG8_SB(0, 1), b2 + hstep, voffB); PG8_STAGE_A(0, 0, a2, true);
;             PG8_WAIT_V(8); PG8_WAIT_L(0); PG8_BAR; PG8_MMA(1, 0, At, B0); PG8_MMA(1, 1, At, B1); PG8_BAR; PG8_SCHED;
	s_setprio 3
	s_waitcnt lgkmcnt(0)
	v_mfma_f32_16x16x32_bf16 v[162:165], v[98:101], v[154:157], v[162:165]
	v_mfma_f32_16x16x32_bf16 v[158:161], v[122:125], v[154:157], v[158:161]
	v_mfma_f32_16x16x32_bf16 v[118:121], v[98:101], v[170:173], v[118:121]
	v_mfma_f32_16x16x32_bf16 v[114:117], v[122:125], v[170:173], v[114:117]
	v_lshl_add_u64 v[210:211], s[24:25], 0, v[192:193]
	v_mfma_f32_16x16x32_bf16 v[94:97], v[98:101], v[178:181], v[94:97]
	v_mfma_f32_16x16x32_bf16 v[90:93], v[122:125], v[178:181], v[90:93]
	v_lshl_add_u64 v[212:213], s[24:25], 0, v[196:197]
	v_mfma_f32_16x16x32_bf16 v[78:81], v[98:101], v[186:189], v[78:81]
	v_mfma_f32_16x16x32_bf16 v[74:77], v[122:125], v[186:189], v[74:77]
	v_lshl_add_u64 v[216:217], s[26:27], 0, v[194:195]
	v_mfma_f32_16x16x32_bf16 v[162:165], v[110:113], v[166:169], v[162:165]
	v_mfma_f32_16x16x32_bf16 v[158:161], v[126:129], v[166:169], v[158:161]
	v_lshl_add_u64 v[214:215], s[26:27], 0, v[190:191]
	v_mfma_f32_16x16x32_bf16 v[118:121], v[110:113], v[174:177], v[118:121]
	v_mfma_f32_16x16x32_bf16 v[114:117], v[126:129], v[174:177], v[114:117]
	v_mfma_f32_16x16x32_bf16 v[94:97], v[110:113], v[182:185], v[94:97]
	v_mfma_f32_16x16x32_bf16 v[90:93], v[126:129], v[182:185], v[90:93]
	v_mfma_f32_16x16x32_bf16 v[78:81], v[110:113], v[206:209], v[78:81]
	v_mfma_f32_16x16x32_bf16 v[74:77], v[126:129], v[206:209], v[74:77]
	s_setprio 0
	s_setprio 3
	v_mfma_f32_16x16x32_bf16 v[134:137], v[138:141], v[154:157], v[134:137]
	v_mfma_f32_16x16x32_bf16 v[130:133], v[146:149], v[154:157], v[130:133]
	v_mfma_f32_16x16x32_bf16 v[106:109], v[138:141], v[170:173], v[106:109]
	v_mfma_f32_16x16x32_bf16 v[102:105], v[146:149], v[170:173], v[102:105]
	v_mfma_f32_16x16x32_bf16 v[86:89], v[138:141], v[178:181], v[86:89]
	v_mfma_f32_16x16x32_bf16 v[82:85], v[146:149], v[178:181], v[82:85]
	v_mfma_f32_16x16x32_bf16 v[70:73], v[138:141], v[186:189], v[70:73]
	v_mfma_f32_16x16x32_bf16 v[66:69], v[146:149], v[186:189], v[66:69]
	v_mfma_f32_16x16x32_bf16 v[134:137], v[142:145], v[166:169], v[134:137]
	v_mfma_f32_16x16x32_bf16 v[130:133], v[150:153], v[166:169], v[130:133]
	v_mfma_f32_16x16x32_bf16 v[106:109], v[142:145], v[174:177], v[106:109]
	v_mfma_f32_16x16x32_bf16 v[102:105], v[150:153], v[174:177], v[102:105]
	v_mfma_f32_16x16x32_bf16 v[86:89], v[142:145], v[182:185], v[86:89]
	v_mfma_f32_16x16x32_bf16 v[82:85], v[150:153], v[182:185], v[82:85]
	v_mfma_f32_16x16x32_bf16 v[70:73], v[142:145], v[206:209], v[70:73]
	v_mfma_f32_16x16x32_bf16 v[66:69], v[150:153], v[206:209], v[66:69]
	s_setprio 0
	s_barrier
	s_add_i32 s20, s39, s2
	s_mov_b32 m0, s20
	ds_read_b128 v[154:157], v236 offset:16384
	ds_read_b128 v[166:169], v236 offset:17408
	ds_read_b128 v[170:173], v236 offset:18432
	ds_read_b128 v[174:177], v236 offset:19456
	ds_read_b128 v[178:181], v236 offset:20480
	ds_read_b128 v[182:185], v236 offset:21504
	ds_read_b128 v[186:189], v236 offset:22528
	ds_read_b128 v[206:209], v236 offset:23552
	global_load_lds_dwordx4 v[210:211], off
	s_add_i32 m0, s20, 0x2000
	s_add_u32 s20, s24, 0xb0000
	s_addc_u32 s21, s25, 0
	s_add_i32 s58, s48, s2
	global_load_lds_dwordx4 v[212:213], off
	s_mov_b32 m0, s58
	s_nop 0
	global_load_lds_dwordx4 v192, s[20:21]
	s_add_i32 m0, s58, 0x2000
	s_nop 0
	global_load_lds_dwordx4 v196, s[20:21]
	s_mov_b32 m0, s3
	s_nop 0
	global_load_lds_dwordx4 v[214:215], off
	s_mov_b32 m0, s28
	s_nop 0
	global_load_lds_dwordx4 v[216:217], off
	s_waitcnt vmcnt(8)
	s_waitcnt lgkmcnt(0)
	s_barrier
	s_setprio 3
	s_waitcnt lgkmcnt(0)
	v_mfma_f32_16x16x32_bf16 v[62:65], v[98:101], v[154:157], v[62:65]
	v_mfma_f32_16x16x32_bf16 v[58:61], v[122:125], v[154:157], v[58:61]
	v_mfma_f32_16x16x32_bf16 v[46:49], v[98:101], v[170:173], v[46:49]
	v_mfma_f32_16x16x32_bf16 v[42:45], v[122:125], v[170:173], v[42:45]
	v_mfma_f32_16x16x32_bf16 v[30:33], v[98:101], v[178:181], v[30:33]
	v_mfma_f32_16x16x32_bf16 v[26:29], v[122:125], v[178:181], v[26:29]
	v_mfma_f32_16x16x32_bf16 v[14:17], v[98:101], v[186:189], v[14:17]
	v_mfma_f32_16x16x32_bf16 v[10:13], v[122:125], v[186:189], v[10:13]
	v_mfma_f32_16x16x32_bf16 v[62:65], v[110:113], v[166:169], v[62:65]
	v_mfma_f32_16x16x32_bf16 v[58:61], v[126:129], v[166:169], v[58:61]
	v_mfma_f32_16x16x32_bf16 v[46:49], v[110:113], v[174:177], v[46:49]
	v_mfma_f32_16x16x32_bf16 v[42:45], v[126:129], v[174:177], v[42:45]
	v_mfma_f32_16x16x32_bf16 v[30:33], v[110:113], v[182:185], v[30:33]
	v_mfma_f32_16x16x32_bf16 v[26:29], v[126:129], v[182:185], v[26:29]
	v_mfma_f32_16x16x32_bf16 v[14:17], v[110:113], v[206:209], v[14:17]
	v_mfma_f32_16x16x32_bf16 v[10:13], v[126:129], v[206:209], v[10:13]
	s_setprio 0
	s_setprio 3
	v_mfma_f32_16x16x32_bf16 v[54:57], v[138:141], v[154:157], v[54:57]
	v_mfma_f32_16x16x32_bf16 v[50:53], v[146:149], v[154:157], v[50:53]
	v_mfma_f32_16x16x32_bf16 v[38:41], v[138:141], v[170:173], v[38:41]
	v_mfma_f32_16x16x32_bf16 v[34:37], v[146:149], v[170:173], v[34:37]
	v_mfma_f32_16x16x32_bf16 v[22:25], v[138:141], v[178:181], v[22:25]
	v_mfma_f32_16x16x32_bf16 v[18:21], v[146:149], v[178:181], v[18:21]
	v_mfma_f32_16x16x32_bf16 v[6:9], v[138:141], v[186:189], v[6:9]
	v_mfma_f32_16x16x32_bf16 v[2:5], v[146:149], v[186:189], v[2:5]
	v_mfma_f32_16x16x32_bf16 v[54:57], v[142:145], v[166:169], v[54:57]
	v_mfma_f32_16x16x32_bf16 v[50:53], v[150:153], v[166:169], v[50:53]
	v_mfma_f32_16x16x32_bf16 v[38:41], v[142:145], v[174:177], v[38:41]
	v_mfma_f32_16x16x32_bf16 v[34:37], v[150:153], v[174:177], v[34:37]
	v_mfma_f32_16x16x32_bf16 v[22:25], v[142:145], v[182:185], v[22:25]
	v_mfma_f32_16x16x32_bf16 v[18:21], v[150:153], v[182:185], v[18:21]
	v_mfma_f32_16x16x32_bf16 v[6:9], v[142:145], v[206:209], v[6:9]
	v_mfma_f32_16x16x32_bf16 v[2:5], v[150:153], v[206:209], v[2:5]
	s_setprio 0
	s_barrier
; #define PG8_STAGE_A(b, h, ptr, NX) do { if constexpr (Sched::GATHER) { unsigned gs_[2]; gs_[0] = ((NX) && last_) ? gN[h][0] : gA[h][0]; gs_[1] = ((NX) && last_) ? gN[h][1] : gA[h][1]; PG8_STAGE(PG8_SA(b, h), ptr, gs_); } \
;         else PG8_STAGE(PG8_SA(b, h), (ptr) + ((h) ? hstep : (size_t)0), voffA); } while (0)
; #define PG8_STAGE(bufoff, gbase, voff) do { _Pragma("unroll") for (int _i = 0; _i < 2; ++_i) \
;         __builtin_amdgcn_global_load_lds((const unsigned*)((const char*)(gbase) + (voff)[_i]), (PG8_LAS unsigned*)(lds + (bufoff) + ldsw + _i * 8192), 16, 0, 0); } while (0)
; #define PG8_LDA(dst, b, h) do { _Pragma("unroll") for (int m = 0; m < 4; ++m) _Pragma("unroll") for (int k = 0; k < 2; ++k) dst[m][k] = *(const PG8_LAS bf16x8*)(lds + PG8_SA(b, h) + aoff + m * 2048 + k * 1024); } while (0)
; #define PG8_LDB(dst, b, h) do { _Pragma("unroll") for (int n = 0; n < 2; ++n) _Pragma("unroll") for (int k = 0; k < 2; ++k) dst[n][k] = *(const PG8_LAS bf16x8*)(lds + PG8_SB(b, h) + boff + n * 2048 + k * 1024); } while (0)
; #define PG8_MMA(ai, bj, At, Bt) do { __builtin_amdgcn_s_setprio(1); _Pragma("unroll") for (int m = 0; m < 4; ++m) _Pragma("unroll") for (int n = 0; n < 2; ++n) _Pragma("unroll") for (int k = 0; k < 2; ++k) \
;         acc[ai][bj][m][n] = __builtin_amdgcn_mfma_f32_16x16x32_bf16(Bt[n][k], At[m][k], acc[ai][bj][m][n], 0, 0, 0); __builtin_amdgcn_s_setprio(0); } while (0)
; #define PG8_WAIT_V(n) asm volatile("s_waitcnt vmcnt(" #n ")" ::: "memory")
; #define PG8_WAIT_L(n) asm volatile("s_waitcnt lgkmcnt(" #n ")" ::: "memory")
; #define PG8_BAR __builtin_amdgcn_s_barrier()
; #define PG8_SCHED __builtin_amdgcn_sched_barrier(0)
; template <class Epi, class Sched, bool ALIGN_EPI = false, bool SP2 = false>
; __device__ __forceinline__ void gemm_phase(PG8_LAS unsigned char* lds, const Gemm g, const Sched& S, const Epi& E, const bool skip_epi = false) {
;     ...
;             PG8_LDB(B0, 1, 0); PG8_LDB(B1, 1, 1); PG8_SCHED; PG8_LDA(At, 1, 0); PG8_STAGE_A(0, 1, a2, true);
;             PG8_WAIT_V(8); PG8_WAIT_L(0); PG8_BAR; PG8_MMA(0, 0, At, B0); PG8_MMA(0, 1, At, B1); PG8_BAR; PG8_SCHED;
;             PG8_LDA(At, 1, 1); PG8_STAGE(PG8_SB(1, 0), b3, voffB); PG8_STAGE(PG8_SB(1, 1), b3 + hstep, voffB); PG8_STAGE_A(1, 0, a3, true);
;             PG8_WAIT_V(8); PG8_WAIT_L(0); PG8_BAR; PG8_MMA(1, 0, At, B0); PG8_MMA(1, 1, At, B1); PG8_BAR; PG8_SCHED;
	s_add_i32 s58, 0, 0x18000
	s_add_i32 s59, 0, 0x1c000
	v_add_u32_e32 v126, s58, v229
	v_add_u32_e32 v150, s59, v229
	ds_read_b128 v[98:101], v126
	ds_read_b128 v[110:113], v126 offset:1024
	ds_read_b128 v[122:125], v126 offset:2048
	ds_read_b128 v[126:129], v126 offset:3072
	ds_read_b128 v[138:141], v150
	ds_read_b128 v[142:145], v150 offset:1024
	ds_read_b128 v[146:149], v150 offset:2048
	ds_read_b128 v[150:153], v150 offset:3072
	s_add_u32 s20, s26, 0xb0000
	s_addc_u32 s21, s27, 0
	s_mov_b32 m0, s29
	ds_read_b128 v[154:157], v236 offset:32768
	ds_read_b128 v[166:169], v236 offset:33792
	ds_read_b128 v[170:173], v236 offset:34816
	ds_read_b128 v[174:177], v236 offset:35840
	ds_read_b128 v[178:181], v236 offset:36864
	ds_read_b128 v[182:185], v236 offset:37888
	ds_read_b128 v[186:189], v236 offset:38912
	ds_read_b128 v[206:209], v236 offset:39936
	global_load_lds_dwordx4 v190, s[20:21]
	s_mov_b32 m0, s30
	s_nop 0
	global_load_lds_dwordx4 v194, s[20:21]
	s_waitcnt vmcnt(8)
	s_waitcnt lgkmcnt(0)
	s_barrier
	s_setprio 3
	s_waitcnt lgkmcnt(0)
	v_mfma_f32_16x16x32_bf16 v[162:165], v[98:101], v[154:157], v[162:165]
	v_mfma_f32_16x16x32_bf16 v[158:161], v[122:125], v[154:157], v[158:161]
	v_mfma_f32_16x16x32_bf16 v[118:121], v[98:101], v[170:173], v[118:121]
	v_mfma_f32_16x16x32_bf16 v[114:117], v[122:125], v[170:173], v[114:117]
	v_mfma_f32_16x16x32_bf16 v[94:97], v[98:101], v[178:181], v[94:97]
	v_mfma_f32_16x16x32_bf16 v[90:93], v[122:125], v[178:181], v[90:93]
	v_mfma_f32_16x16x32_bf16 v[78:81], v[98:101], v[186:189], v[78:81]
	v_mfma_f32_16x16x32_bf16 v[74:77], v[122:125], v[186:189], v[74:77]
	v_mfma_f32_16x16x32_bf16 v[162:165], v[110:113], v[166:169], v[162:165]
	v_mfma_f32_16x16x32_bf16 v[158:161], v[126:129], v[166:169], v[158:161]
	v_mfma_f32_16x16x32_bf16 v[118:121], v[110:113], v[174:177], v[118:121]
	v_mfma_f32_16x16x32_bf16 v[114:117], v[126:129], v[174:177], v[114:117]
	v_mfma_f32_16x16x32_bf16 v[94:97], v[110:113], v[182:185], v[94:97]
	v_mfma_f32_16x16x32_bf16 v[90:93], v[126:129], v[182:185], v[90:93]
	v_mfma_f32_16x16x32_bf16 v[78:81], v[110:113], v[206:209], v[78:81]
	v_mfma_f32_16x16x32_bf16 v[74:77], v[126:129], v[206:209], v[74:77]
	s_setprio 0
	s_setprio 3
	v_mfma_f32_16x16x32_bf16 v[134:137], v[138:141], v[154:157], v[134:137]
	v_mfma_f32_16x16x32_bf16 v[130:133], v[146:149], v[154:157], v[130:133]
	v_mfma_f32_16x16x32_bf16 v[106:109], v[138:141], v[170:173], v[106:109]
	v_mfma_f32_16x16x32_bf16 v[102:105], v[146:149], v[170:173], v[102:105]
	v_mfma_f32_16x16x32_bf16 v[86:89], v[138:141], v[178:181], v[86:89]
	v_mfma_f32_16x16x32_bf16 v[82:85], v[146:149], v[178:181], v[82:85]
	v_mfma_f32_16x16x32_bf16 v[70:73], v[138:141], v[186:189], v[70:73]
	v_mfma_f32_16x16x32_bf16 v[66:69], v[146:149], v[186:189], v[66:69]
	v_mfma_f32_16x16x32_bf16 v[134:137], v[142:145], v[166:169], v[134:137]
	v_mfma_f32_16x16x32_bf16 v[130:133], v[150:153], v[166:169], v[130:133]
	v_mfma_f32_16x16x32_bf16 v[106:109], v[142:145], v[174:177], v[106:109]
	v_mfma_f32_16x16x32_bf16 v[102:105], v[150:153], v[174:177], v[102:105]
	v_mfma_f32_16x16x32_bf16 v[86:89], v[142:145], v[182:185], v[86:89]
	v_mfma_f32_16x16x32_bf16 v[82:85], v[150:153], v[182:185], v[82:85]
	v_mfma_f32_16x16x32_bf16 v[70:73], v[142:145], v[206:209], v[70:73]
	v_mfma_f32_16x16x32_bf16 v[66:69], v[150:153], v[206:209], v[66:69]
	s_setprio 0
	s_barrier
	s_add_i32 s20, s58, s2
	s_add_i32 m0, s20, 0xffffff80
	ds_read_b128 v[154:157], v236 offset:49152
	ds_read_b128 v[166:169], v236 offset:50176
	ds_read_b128 v[170:173], v236 offset:51200
	ds_read_b128 v[174:177], v236 offset:52224
	ds_read_b128 v[178:181], v236 offset:53248
	ds_read_b128 v[182:185], v236 offset:54272
	ds_read_b128 v[186:189], v236 offset:55296
	ds_read_b128 v[206:209], v236 offset:56320
	global_load_lds_dwordx4 v[210:211], off offset:128
	s_add_i32 m0, s20, 0x1f80
	s_add_u32 s20, s24, 0xb0080
	s_addc_u32 s21, s25, 0
	s_add_i32 s24, s59, s2
	global_load_lds_dwordx4 v[212:213], off offset:128
	s_mov_b32 m0, s24
	s_nop 0
	global_load_lds_dwordx4 v192, s[20:21]
	s_add_i32 m0, s24, 0x2000
	s_nop 0
	global_load_lds_dwordx4 v196, s[20:21]
	s_add_i32 m0, s35, 0xffffff80
	s_nop 0
	global_load_lds_dwordx4 v[214:215], off offset:128
	s_add_i32 m0, s36, 0xffffff80
	s_nop 0
	global_load_lds_dwordx4 v[216:217], off offset:128
	s_waitcnt vmcnt(8)
	s_waitcnt lgkmcnt(0)
	s_barrier
	s_setprio 3
	s_waitcnt lgkmcnt(0)
	v_mfma_f32_16x16x32_bf16 v[62:65], v[98:101], v[154:157], v[62:65]
	v_mfma_f32_16x16x32_bf16 v[58:61], v[122:125], v[154:157], v[58:61]
	v_mfma_f32_16x16x32_bf16 v[46:49], v[98:101], v[170:173], v[46:49]
	v_mfma_f32_16x16x32_bf16 v[42:45], v[122:125], v[170:173], v[42:45]
	v_mfma_f32_16x16x32_bf16 v[30:33], v[98:101], v[178:181], v[30:33]
	v_mfma_f32_16x16x32_bf16 v[26:29], v[122:125], v[178:181], v[26:29]
	v_mfma_f32_16x16x32_bf16 v[14:17], v[98:101], v[186:189], v[14:17]
	v_mfma_f32_16x16x32_bf16 v[10:13], v[122:125], v[186:189], v[10:13]
	v_mfma_f32_16x16x32_bf16 v[62:65], v[110:113], v[166:169], v[62:65]
	v_mfma_f32_16x16x32_bf16 v[58:61], v[126:129], v[166:169], v[58:61]
	v_mfma_f32_16x16x32_bf16 v[46:49], v[110:113], v[174:177], v[46:49]
	v_mfma_f32_16x16x32_bf16 v[42:45], v[126:129], v[174:177], v[42:45]
	v_mfma_f32_16x16x32_bf16 v[30:33], v[110:113], v[182:185], v[30:33]
	v_mfma_f32_16x16x32_bf16 v[26:29], v[126:129], v[182:185], v[26:29]
	v_mfma_f32_16x16x32_bf16 v[14:17], v[110:113], v[206:209], v[14:17]
	v_mfma_f32_16x16x32_bf16 v[10:13], v[126:129], v[206:209], v[10:13]
	s_setprio 0
	s_setprio 3
	v_mfma_f32_16x16x32_bf16 v[54:57], v[138:141], v[154:157], v[54:57]
	v_mfma_f32_16x16x32_bf16 v[50:53], v[146:149], v[154:157], v[50:53]
	v_mfma_f32_16x16x32_bf16 v[38:41], v[138:141], v[170:173], v[38:41]
	v_mfma_f32_16x16x32_bf16 v[34:37], v[146:149], v[170:173], v[34:37]
	v_mfma_f32_16x16x32_bf16 v[22:25], v[138:141], v[178:181], v[22:25]
	v_mfma_f32_16x16x32_bf16 v[18:21], v[146:149], v[178:181], v[18:21]
	v_mfma_f32_16x16x32_bf16 v[6:9], v[138:141], v[186:189], v[6:9]
	v_mfma_f32_16x16x32_bf16 v[2:5], v[146:149], v[186:189], v[2:5]
	v_mfma_f32_16x16x32_bf16 v[54:57], v[142:145], v[166:169], v[54:57]
	v_mfma_f32_16x16x32_bf16 v[50:53], v[150:153], v[166:169], v[50:53]
	v_mfma_f32_16x16x32_bf16 v[38:41], v[142:145], v[174:177], v[38:41]
	v_mfma_f32_16x16x32_bf16 v[34:37], v[150:153], v[174:177], v[34:37]
	v_mfma_f32_16x16x32_bf16 v[22:25], v[142:145], v[182:185], v[22:25]
	v_mfma_f32_16x16x32_bf16 v[18:21], v[150:153], v[182:185], v[18:21]
	v_mfma_f32_16x16x32_bf16 v[6:9], v[142:145], v[206:209], v[6:9]
	v_mfma_f32_16x16x32_bf16 v[2:5], v[150:153], v[206:209], v[2:5]
	s_setprio 0
	s_barrier
	s_add_i32 s57, s57, 2
	s_add_u32 s55, s55, 0x100
	s_addc_u32 s56, s56, 0
	s_cmp_gt_u32 s57, 41
	s_mov_b64 s[20:21], s[22:23]
	s_cbranch_scc0 .LBB0_857
	s_and_b64 vcc, exec, s[16:17]
	s_cbranch_vccz .LBB0_860
	s_barrier

; #define PG8_STAGE_A(b, h, ptr, NX) do { if constexpr (Sched::GATHER) { unsigned gs_[2]; gs_[0] = ((NX) && last_) ? gN[h][0] : gA[h][0]; gs_[1] = ((NX) && last_) ? gN[h][1] : gA[h][1]; PG8_STAGE(PG8_SA(b, h), ptr, gs_); } \
;         else PG8_STAGE(PG8_SA(b, h), (ptr) + ((h) ? hstep : (size_t)0), voffA); } while (0)
; #define PG8_STAGE(bufoff, gbase, voff) do { _Pragma("unroll") for (int _i = 0; _i < 2; ++_i) \
;         __builtin_amdgcn_global_load_lds((const unsigned*)((const char*)(gbase) + (voff)[_i]), (PG8_LAS unsigned*)(lds + (bufoff) + ldsw + _i * 8192), 16, 0, 0); } while (0)
; #define PG8_LDA(dst, b, h) do { _Pragma("unroll") for (int m = 0; m < 4; ++m) _Pragma("unroll") for (int k = 0; k < 2; ++k) dst[m][k] = *(const PG8_LAS bf16x8*)(lds + PG8_SA(b, h) + aoff + m * 2048 + k * 1024); } while (0)
; #define PG8_WAIT_V(n) asm volatile("s_waitcnt vmcnt(" #n ")" ::: "memory")
; #define PG8_WAIT_L(n) asm volatile("s_waitcnt lgkmcnt(" #n ")" ::: "memory")
; #define PG8_BAR __builtin_amdgcn_s_barrier()
; template <class Epi, class Sched, bool ALIGN_EPI = false, bool SP2 = false>
; __device__ __forceinline__ void gemm_phase(PG8_LAS unsigned char* lds, const Gemm g, const Sched& S, const Epi& E, const bool skip_epi = false) {
;     ...
;         const char* nA = has_next ? (const char*)g.A + (size_t)nxt.pm * pmstepA + nxt.ko : cA; const char* nB = has_next ? (const char*)g.Bt + (size_t)nxt.pn * tstep + nxt.ko : cB;
;         for (int t = 0; t < nt; t += 2) {
;             const bool last = (t == nt - 2); last_ = last && has_next;
;             const char* a1 = cA + (size_t)(t + 1) * kstep;
;             const char* a2 = last ? nA : cA + (size_t)(t + 2) * kstep; const char* b2 = last ? nB : cB + (size_t)(t + 2) * kstep;
;             const char* a3 = a2 + kstep; const char* b3 = b2 + kstep;
;             if (last && has_next) S.a_ready(nxt);
;             if constexpr (SP2) {
;             PG8_LDB(B0, 0, 0); PG8_LDB(B1, 0, 1); PG8_SCHED; PG8_LDA(At, 0, 0); PG8_STAGE_A(1, 1, a1, false);
;             PG8_WAIT_V(8); PG8_WAIT_L(0); PG8_BAR; PG8_MMA(0, 0, At, B0); PG8_MMA(0, 1, At, B1); PG8_BAR; PG8_SCHED;
;             PG8_LDA(At, 0, 1); PG8_STAGE(PG8_SB(0, 0), b2, voffB); PG8_STAGE(PG8_SB(0, 1), b2 + hstep, voffB); PG8_STAGE_A(0, 0, a2, true);
;             PG8_WAIT_V(8); PG8_WAIT_L(0); PG8_BAR; PG8_MMA(1, 0, At, B0); PG8_MMA(1, 1, At, B1); PG8_BAR; PG8_SCHED;
.LBB0_943:
	s_ashr_i32 s15, s14, 31
	s_lshl_b64 s[16:17], s[14:15], 19
	s_add_u32 s16, s86, s16
	s_addc_u32 s17, s87, s17
	s_and_b64 s[18:19], s[4:5], exec
	s_cselect_b32 s15, s17, s23
	s_cselect_b32 s54, s16, s22
	s_ashr_i32 s13, s12, 31
	s_lshl_b64 s[18:19], s[12:13], 19
	s_add_u32 s18, s2, s18
	s_addc_u32 s19, s3, s19
	s_and_b64 s[26:27], s[4:5], exec
	s_cselect_b32 s13, s19, s25
	s_cselect_b32 s55, s18, s24
	s_add_u32 s22, s22, 0x40080
	s_addc_u32 s23, s23, 0
	s_add_u32 s56, s24, 0x100
	s_addc_u32 s57, s25, 0
	s_mov_b32 s58, -2
	s_waitcnt vmcnt(0)
	ds_read_b128 v[148:151], v170
	ds_read_b128 v[152:155], v170 offset:1024
	ds_read_b128 v[156:159], v170 offset:2048
	ds_read_b128 v[160:163], v170 offset:3072
	ds_read_b128 v[176:179], v171
	ds_read_b128 v[180:183], v171 offset:1024
	ds_read_b128 v[184:187], v171 offset:2048
	ds_read_b128 v[188:191], v171 offset:3072
	s_add_u32 s24, s22, 0xfffc0080
	s_addc_u32 s25, s23, -1
	s_cmp_eq_u32 s58, 12
	s_cselect_b32 s27, s15, s25
	s_cselect_b32 s26, s54, s24
	s_cselect_b32 s25, s13, s57
	s_cselect_b32 s24, s55, s56
	s_add_i32 m0, s21, 0xc000
	ds_read_b128 v[192:195], v172
	ds_read_b128 v[196:199], v172 offset:1024
	ds_read_b128 v[200:203], v172 offset:2048
	ds_read_b128 v[204:207], v172 offset:3072
	ds_read_b128 v[208:211], v172 offset:4096
	ds_read_b128 v[212:215], v172 offset:5120
	ds_read_b128 v[216:219], v172 offset:6144
	ds_read_b128 v[220:223], v172 offset:7168
	global_load_lds_dwordx4 v140, s[22:23]
	s_add_i32 m0, s21, 0xe000
	s_nop 0
	global_load_lds_dwordx4 v142, s[22:23]
	s_waitcnt vmcnt(8)
	s_waitcnt lgkmcnt(0)
	s_barrier
	s_setprio 3
	s_waitcnt lgkmcnt(0)
	v_mfma_f32_16x16x32_bf16 v[126:129], v[148:151], v[192:195], 0
	v_mfma_f32_16x16x32_bf16 v[122:125], v[156:159], v[192:195], 0
	v_mfma_f32_16x16x32_bf16 v[114:117], v[148:151], v[200:203], 0
	v_mfma_f32_16x16x32_bf16 v[106:109], v[156:159], v[200:203], 0
	v_lshl_add_u64 v[164:165], s[24:25], 0, v[134:135]
	v_mfma_f32_16x16x32_bf16 v[98:101], v[148:151], v[208:211], 0
	v_mfma_f32_16x16x32_bf16 v[90:93], v[156:159], v[208:211], 0
	v_lshl_add_u64 v[224:225], s[24:25], 0, v[130:131]
	v_mfma_f32_16x16x32_bf16 v[82:85], v[148:151], v[216:219], 0
	v_mfma_f32_16x16x32_bf16 v[74:77], v[156:159], v[216:219], 0
	v_lshl_add_u64 v[230:231], s[26:27], 0, v[132:133]
	v_mfma_f32_16x16x32_bf16 v[126:129], v[152:155], v[196:199], v[126:129]
	v_mfma_f32_16x16x32_bf16 v[122:125], v[160:163], v[196:199], v[122:125]
	v_lshl_add_u64 v[226:227], s[26:27], 0, v[136:137]
	v_mfma_f32_16x16x32_bf16 v[114:117], v[152:155], v[204:207], v[114:117]
	v_mfma_f32_16x16x32_bf16 v[106:109], v[160:163], v[204:207], v[106:109]
	v_mfma_f32_16x16x32_bf16 v[98:101], v[152:155], v[212:215], v[98:101]
	v_mfma_f32_16x16x32_bf16 v[90:93], v[160:163], v[212:215], v[90:93]
	v_mfma_f32_16x16x32_bf16 v[82:85], v[152:155], v[220:223], v[82:85]
	v_mfma_f32_16x16x32_bf16 v[74:77], v[160:163], v[220:223], v[74:77]
	s_setprio 0
	s_setprio 3
	v_mfma_f32_16x16x32_bf16 v[118:121], v[176:179], v[192:195], 0
	v_mfma_f32_16x16x32_bf16 v[110:113], v[184:187], v[192:195], 0
	v_mfma_f32_16x16x32_bf16 v[102:105], v[176:179], v[200:203], 0
	v_mfma_f32_16x16x32_bf16 v[94:97], v[184:187], v[200:203], 0
	v_mfma_f32_16x16x32_bf16 v[86:89], v[176:179], v[208:211], 0
	v_mfma_f32_16x16x32_bf16 v[78:81], v[184:187], v[208:211], 0
	v_mfma_f32_16x16x32_bf16 v[70:73], v[176:179], v[216:219], 0
	v_mfma_f32_16x16x32_bf16 v[66:69], v[184:187], v[216:219], 0
	v_mfma_f32_16x16x32_bf16 v[118:121], v[180:183], v[196:199], v[118:121]
	v_mfma_f32_16x16x32_bf16 v[110:113], v[188:191], v[196:199], v[110:113]
	v_mfma_f32_16x16x32_bf16 v[102:105], v[180:183], v[204:207], v[102:105]
	v_mfma_f32_16x16x32_bf16 v[94:97], v[188:191], v[204:207], v[94:97]
	v_mfma_f32_16x16x32_bf16 v[86:89], v[180:183], v[212:215], v[86:89]
	v_mfma_f32_16x16x32_bf16 v[78:81], v[188:191], v[212:215], v[78:81]
	v_mfma_f32_16x16x32_bf16 v[70:73], v[180:183], v[220:223], v[70:73]
	v_mfma_f32_16x16x32_bf16 v[66:69], v[188:191], v[220:223], v[66:69]
	s_setprio 0
	s_barrier
	s_add_i32 s59, s48, s28
	s_mov_b32 m0, s59
	ds_read_b128 v[192:195], v172 offset:16384
	ds_read_b128 v[196:199], v172 offset:17408
	ds_read_b128 v[200:203], v172 offset:18432
	ds_read_b128 v[204:207], v172 offset:19456
	ds_read_b128 v[208:211], v172 offset:20480
	ds_read_b128 v[212:215], v172 offset:21504
	ds_read_b128 v[216:219], v172 offset:22528
	ds_read_b128 v[220:223], v172 offset:23552
	global_load_lds_dwordx4 v[164:165], off
	s_add_i32 m0, s59, 0x2000
	s_add_u32 s60, s24, 0x40000
	s_addc_u32 s61, s25, 0
	s_add_i32 s59, s49, s28
	global_load_lds_dwordx4 v[224:225], off
	s_mov_b32 m0, s59
	s_nop 0
	global_load_lds_dwordx4 v134, s[60:61]
	s_add_i32 m0, s59, 0x2000
	s_nop 0
	global_load_lds_dwordx4 v130, s[60:61]
	s_mov_b32 m0, s21
	s_nop 0
	global_load_lds_dwordx4 v[226:227], off
	s_mov_b32 m0, s31
	s_nop 0
	global_load_lds_dwordx4 v[230:231], off
	s_waitcnt vmcnt(8)
	s_waitcnt lgkmcnt(0)
	s_barrier
; #define PG8_STAGE_A(b, h, ptr, NX) do { if constexpr (Sched::GATHER) { unsigned gs_[2]; gs_[0] = ((NX) && last_) ? gN[h][0] : gA[h][0]; gs_[1] = ((NX) && last_) ? gN[h][1] : gA[h][1]; PG8_STAGE(PG8_SA(b, h), ptr, gs_); } \
;         else PG8_STAGE(PG8_SA(b, h), (ptr) + ((h) ? hstep : (size_t)0), voffA); } while (0)
; #define PG8_LDA(dst, b, h) do { _Pragma("unroll") for (int m = 0; m < 4; ++m) _Pragma("unroll") for (int k = 0; k < 2; ++k) dst[m][k] = *(const PG8_LAS bf16x8*)(lds + PG8_SA(b, h) + aoff + m * 2048 + k * 1024); } while (0)
; #define PG8_LDB(dst, b, h) do { _Pragma("unroll") for (int n = 0; n < 2; ++n) _Pragma("unroll") for (int k = 0; k < 2; ++k) dst[n][k] = *(const PG8_LAS bf16x8*)(lds + PG8_SB(b, h) + boff + n * 2048 + k * 1024); } while (0)
; #define PG8_MMA(ai, bj, At, Bt) do { __builtin_amdgcn_s_setprio(1); _Pragma("unroll") for (int m = 0; m < 4; ++m) _Pragma("unroll") for (int n = 0; n < 2; ++n) _Pragma("unroll") for (int k = 0; k < 2; ++k) \
;         acc[ai][bj][m][n] = __builtin_amdgcn_mfma_f32_16x16x32_bf16(Bt[n][k], At[m][k], acc[ai][bj][m][n], 0, 0, 0); __builtin_amdgcn_s_setprio(0); } while (0)
; #define PG8_WAIT_V(n) asm volatile("s_waitcnt vmcnt(" #n ")" ::: "memory")
; #define PG8_WAIT_L(n) asm volatile("s_waitcnt lgkmcnt(" #n ")" ::: "memory")
; #define PG8_BAR __builtin_amdgcn_s_barrier()
; #define PG8_SCHED __builtin_amdgcn_sched_barrier(0)
; template <class Epi, class Sched, bool ALIGN_EPI = false, bool SP2 = false>
; __device__ __forceinline__ void gemm_phase(PG8_LAS unsigned char* lds, const Gemm g, const Sched& S, const Epi& E, const bool skip_epi = false) {
;     ...
;             PG8_WAIT_V(8); PG8_WAIT_L(0); PG8_BAR; PG8_MMA(1, 0, At, B0); PG8_MMA(1, 1, At, B1); PG8_BAR; PG8_SCHED;
;             PG8_LDB(B0, 1, 0); PG8_LDB(B1, 1, 1); PG8_SCHED; PG8_LDA(At, 1, 0); PG8_STAGE_A(0, 1, a2, true);
;             PG8_WAIT_V(8); PG8_WAIT_L(0); PG8_BAR; PG8_MMA(0, 0, At, B0); PG8_MMA(0, 1, At, B1); PG8_BAR; PG8_SCHED;
	s_setprio 3
	s_waitcnt lgkmcnt(0)
	v_mfma_f32_16x16x32_bf16 v[62:65], v[148:151], v[192:195], 0
	v_mfma_f32_16x16x32_bf16 v[58:61], v[156:159], v[192:195], 0
	v_mfma_f32_16x16x32_bf16 v[50:53], v[148:151], v[200:203], 0
	v_mfma_f32_16x16x32_bf16 v[42:45], v[156:159], v[200:203], 0
	v_mfma_f32_16x16x32_bf16 v[34:37], v[148:151], v[208:211], 0
	v_mfma_f32_16x16x32_bf16 v[26:29], v[156:159], v[208:211], 0
	v_mfma_f32_16x16x32_bf16 v[18:21], v[148:151], v[216:219], 0
	v_mfma_f32_16x16x32_bf16 v[10:13], v[156:159], v[216:219], 0
	v_mfma_f32_16x16x32_bf16 v[62:65], v[152:155], v[196:199], v[62:65]
	v_mfma_f32_16x16x32_bf16 v[58:61], v[160:163], v[196:199], v[58:61]
	v_mfma_f32_16x16x32_bf16 v[50:53], v[152:155], v[204:207], v[50:53]
	v_mfma_f32_16x16x32_bf16 v[42:45], v[160:163], v[204:207], v[42:45]
	v_mfma_f32_16x16x32_bf16 v[34:37], v[152:155], v[212:215], v[34:37]
	v_mfma_f32_16x16x32_bf16 v[26:29], v[160:163], v[212:215], v[26:29]
	v_mfma_f32_16x16x32_bf16 v[18:21], v[152:155], v[220:223], v[18:21]
	v_mfma_f32_16x16x32_bf16 v[10:13], v[160:163], v[220:223], v[10:13]
	s_setprio 0
	s_setprio 3
	v_mfma_f32_16x16x32_bf16 v[54:57], v[176:179], v[192:195], 0
	v_mfma_f32_16x16x32_bf16 v[46:49], v[184:187], v[192:195], 0
	v_mfma_f32_16x16x32_bf16 v[38:41], v[176:179], v[200:203], 0
	v_mfma_f32_16x16x32_bf16 v[30:33], v[184:187], v[200:203], 0
	v_mfma_f32_16x16x32_bf16 v[22:25], v[176:179], v[208:211], 0
	v_mfma_f32_16x16x32_bf16 v[14:17], v[184:187], v[208:211], 0
	v_mfma_f32_16x16x32_bf16 v[6:9], v[176:179], v[216:219], 0
	v_mfma_f32_16x16x32_bf16 v[2:5], v[184:187], v[216:219], 0
	v_mfma_f32_16x16x32_bf16 v[54:57], v[180:183], v[196:199], v[54:57]
	v_mfma_f32_16x16x32_bf16 v[46:49], v[188:191], v[196:199], v[46:49]
	v_mfma_f32_16x16x32_bf16 v[38:41], v[180:183], v[204:207], v[38:41]
	v_mfma_f32_16x16x32_bf16 v[30:33], v[188:191], v[204:207], v[30:33]
	v_mfma_f32_16x16x32_bf16 v[22:25], v[180:183], v[212:215], v[22:25]
	v_mfma_f32_16x16x32_bf16 v[14:17], v[188:191], v[212:215], v[14:17]
	v_mfma_f32_16x16x32_bf16 v[6:9], v[180:183], v[220:223], v[6:9]
	v_mfma_f32_16x16x32_bf16 v[2:5], v[188:191], v[220:223], v[2:5]
	s_setprio 0
	s_barrier
	s_add_i32 s59, 0, 0x18000
	s_add_i32 s60, 0, 0x1c000
	v_add_u32_e32 v160, s59, v1
	v_add_u32_e32 v188, s60, v1
	ds_read_b128 v[148:151], v160
	ds_read_b128 v[152:155], v160 offset:1024
	ds_read_b128 v[156:159], v160 offset:2048
	ds_read_b128 v[160:163], v160 offset:3072
	ds_read_b128 v[176:179], v188
	ds_read_b128 v[180:183], v188 offset:1024
	ds_read_b128 v[184:187], v188 offset:2048
	ds_read_b128 v[188:191], v188 offset:3072
	s_add_u32 s26, s26, 0x40000
	s_addc_u32 s27, s27, 0
	s_mov_b32 m0, s34
	ds_read_b128 v[192:195], v172 offset:32768
	ds_read_b128 v[196:199], v172 offset:33792
	ds_read_b128 v[200:203], v172 offset:34816
	ds_read_b128 v[204:207], v172 offset:35840
	ds_read_b128 v[208:211], v172 offset:36864
	ds_read_b128 v[212:215], v172 offset:37888
	ds_read_b128 v[216:219], v172 offset:38912
	ds_read_b128 v[220:223], v172 offset:39936
	global_load_lds_dwordx4 v136, s[26:27]
	s_mov_b32 m0, s35
	s_nop 0
	global_load_lds_dwordx4 v132, s[26:27]
	s_waitcnt vmcnt(8)
	s_waitcnt lgkmcnt(0)
	s_barrier
	s_setprio 3
	s_waitcnt lgkmcnt(0)
	v_mfma_f32_16x16x32_bf16 v[126:129], v[148:151], v[192:195], v[126:129]
	v_mfma_f32_16x16x32_bf16 v[122:125], v[156:159], v[192:195], v[122:125]
	v_mfma_f32_16x16x32_bf16 v[114:117], v[148:151], v[200:203], v[114:117]
	v_mfma_f32_16x16x32_bf16 v[106:109], v[156:159], v[200:203], v[106:109]
	v_mfma_f32_16x16x32_bf16 v[98:101], v[148:151], v[208:211], v[98:101]
	v_mfma_f32_16x16x32_bf16 v[90:93], v[156:159], v[208:211], v[90:93]
	v_mfma_f32_16x16x32_bf16 v[82:85], v[148:151], v[216:219], v[82:85]
	v_mfma_f32_16x16x32_bf16 v[74:77], v[156:159], v[216:219], v[74:77]
	v_mfma_f32_16x16x32_bf16 v[126:129], v[152:155], v[196:199], v[126:129]
	v_mfma_f32_16x16x32_bf16 v[122:125], v[160:163], v[196:199], v[122:125]
	v_mfma_f32_16x16x32_bf16 v[114:117], v[152:155], v[204:207], v[114:117]
	v_mfma_f32_16x16x32_bf16 v[106:109], v[160:163], v[204:207], v[106:109]
	v_mfma_f32_16x16x32_bf16 v[98:101], v[152:155], v[212:215], v[98:101]
	v_mfma_f32_16x16x32_bf16 v[90:93], v[160:163], v[212:215], v[90:93]
	v_mfma_f32_16x16x32_bf16 v[82:85], v[152:155], v[220:223], v[82:85]
	v_mfma_f32_16x16x32_bf16 v[74:77], v[160:163], v[220:223], v[74:77]
	s_setprio 0
	s_setprio 3
	v_mfma_f32_16x16x32_bf16 v[118:121], v[176:179], v[192:195], v[118:121]
	v_mfma_f32_16x16x32_bf16 v[110:113], v[184:187], v[192:195], v[110:113]
	v_mfma_f32_16x16x32_bf16 v[102:105], v[176:179], v[200:203], v[102:105]
	v_mfma_f32_16x16x32_bf16 v[94:97], v[184:187], v[200:203], v[94:97]
	v_mfma_f32_16x16x32_bf16 v[86:89], v[176:179], v[208:211], v[86:89]
	v_mfma_f32_16x16x32_bf16 v[78:81], v[184:187], v[208:211], v[78:81]
	v_mfma_f32_16x16x32_bf16 v[70:73], v[176:179], v[216:219], v[70:73]
	v_mfma_f32_16x16x32_bf16 v[66:69], v[184:187], v[216:219], v[66:69]
	v_mfma_f32_16x16x32_bf16 v[118:121], v[180:183], v[196:199], v[118:121]
	v_mfma_f32_16x16x32_bf16 v[110:113], v[188:191], v[196:199], v[110:113]
	v_mfma_f32_16x16x32_bf16 v[102:105], v[180:183], v[204:207], v[102:105]
	v_mfma_f32_16x16x32_bf16 v[94:97], v[188:191], v[204:207], v[94:97]
	v_mfma_f32_16x16x32_bf16 v[86:89], v[180:183], v[212:215], v[86:89]
	v_mfma_f32_16x16x32_bf16 v[78:81], v[188:191], v[212:215], v[78:81]
	v_mfma_f32_16x16x32_bf16 v[70:73], v[180:183], v[220:223], v[70:73]
	v_mfma_f32_16x16x32_bf16 v[66:69], v[188:191], v[220:223], v[66:69]
	s_setprio 0
	s_barrier
; #define PG8_STAGE_A(b, h, ptr, NX) do { if constexpr (Sched::GATHER) { unsigned gs_[2]; gs_[0] = ((NX) && last_) ? gN[h][0] : gA[h][0]; gs_[1] = ((NX) && last_) ? gN[h][1] : gA[h][1]; PG8_STAGE(PG8_SA(b, h), ptr, gs_); } \
;         else PG8_STAGE(PG8_SA(b, h), (ptr) + ((h) ? hstep : (size_t)0), voffA); } while (0)
; #define PG8_STAGE(bufoff, gbase, voff) do { _Pragma("unroll") for (int _i = 0; _i < 2; ++_i) \
;         __builtin_amdgcn_global_load_lds((const unsigned*)((const char*)(gbase) + (voff)[_i]), (PG8_LAS unsigned*)(lds + (bufoff) + ldsw + _i * 8192), 16, 0, 0); } while (0)
; #define PG8_LDA(dst, b, h) do { _Pragma("unroll") for (int m = 0; m < 4; ++m) _Pragma("unroll") for (int k = 0; k < 2; ++k) dst[m][k] = *(const PG8_LAS bf16x8*)(lds + PG8_SA(b, h) + aoff + m * 2048 + k * 1024); } while (0)
; #define PG8_LDB(dst, b, h) do { _Pragma("unroll") for (int n = 0; n < 2; ++n) _Pragma("unroll") for (int k = 0; k < 2; ++k) dst[n][k] = *(const PG8_LAS bf16x8*)(lds + PG8_SB(b, h) + boff + n * 2048 + k * 1024); } while (0)
; #define PG8_WAIT_V(n) asm volatile("s_waitcnt vmcnt(" #n ")" ::: "memory")
; #define PG8_BAR __builtin_amdgcn_s_barrier()
; template <class Epi, class Sched, bool ALIGN_EPI = false, bool SP2 = false>
; __device__ __forceinline__ void gemm_phase(PG8_LAS unsigned char* lds, const Gemm g, const Sched& S, const Epi& E, const bool skip_epi = false) {
;     ...
;             PG8_LDB(B0, 0, 0); PG8_LDB(B1, 0, 1); PG8_SCHED; PG8_LDA(At, 0, 0); PG8_STAGE_A(1, 1, a1, false);
;             PG8_WAIT_V(8); PG8_WAIT_L(0); PG8_BAR; PG8_MMA(0, 0, At, B0); PG8_MMA(0, 1, At, B1); PG8_BAR; PG8_SCHED;
;             PG8_LDA(At, 0, 1); PG8_STAGE(PG8_SB(0, 0), b2, voffB); PG8_STAGE(PG8_SB(0, 1), b2 + hstep, voffB); PG8_STAGE_A(0, 0, a2, true);
;             PG8_WAIT_V(8); PG8_WAIT_L(0); PG8_BAR; PG8_MMA(1, 0, At, B0); PG8_MMA(1, 1, At, B1); PG8_BAR; PG8_SCHED;
;             PG8_LDB(B0, 1, 0); PG8_LDB(B1, 1, 1); PG8_SCHED; PG8_LDA(At, 1, 0); PG8_STAGE_A(0, 1, a2, true);
;             PG8_WAIT_V(8); PG8_WAIT_L(0); PG8_BAR; PG8_MMA(0, 0, At, B0); PG8_MMA(0, 1, At, B1); PG8_BAR; PG8_SCHED;
;             PG8_LDA(At, 1, 1); PG8_STAGE(PG8_SB(1, 0), b3, voffB); PG8_STAGE(PG8_SB(1, 1), b3 + hstep, voffB); PG8_STAGE_A(1, 0, a3, true);
;             PG8_WAIT_V(8); PG8_WAIT_L(0); PG8_BAR; PG8_MMA(1, 0, At, B0); PG8_MMA(1, 1, At, B1); PG8_BAR; PG8_SCHED;
	s_add_i32 s26, s59, s28
	s_add_i32 m0, s26, 0xffffff80
	ds_read_b128 v[192:195], v172 offset:49152
	ds_read_b128 v[196:199], v172 offset:50176
	ds_read_b128 v[200:203], v172 offset:51200
	ds_read_b128 v[204:207], v172 offset:52224
	ds_read_b128 v[208:211], v172 offset:53248
	ds_read_b128 v[212:215], v172 offset:54272
	ds_read_b128 v[216:219], v172 offset:55296
	ds_read_b128 v[220:223], v172 offset:56320
	global_load_lds_dwordx4 v[164:165], off offset:128
	s_add_i32 m0, s26, 0x1f80
	s_add_u32 s24, s24, 0x40080
	s_addc_u32 s25, s25, 0
	s_add_i32 s26, s60, s28
	global_load_lds_dwordx4 v[224:225], off offset:128
	s_mov_b32 m0, s26
	s_nop 0
	global_load_lds_dwordx4 v134, s[24:25]
	s_add_i32 m0, s26, 0x2000
	s_nop 0
	global_load_lds_dwordx4 v130, s[24:25]
	s_add_i32 m0, s37, 0xffffff80
	s_nop 0
	global_load_lds_dwordx4 v[226:227], off offset:128
	s_add_i32 m0, s38, 0xffffff80
	s_nop 0
	global_load_lds_dwordx4 v[230:231], off offset:128
	s_waitcnt vmcnt(8)
	s_waitcnt lgkmcnt(0)
	s_barrier
	s_setprio 3
	s_waitcnt lgkmcnt(0)
	v_mfma_f32_16x16x32_bf16 v[62:65], v[148:151], v[192:195], v[62:65]
	v_mfma_f32_16x16x32_bf16 v[58:61], v[156:159], v[192:195], v[58:61]
	v_mfma_f32_16x16x32_bf16 v[50:53], v[148:151], v[200:203], v[50:53]
	v_mfma_f32_16x16x32_bf16 v[42:45], v[156:159], v[200:203], v[42:45]
	v_mfma_f32_16x16x32_bf16 v[34:37], v[148:151], v[208:211], v[34:37]
	v_mfma_f32_16x16x32_bf16 v[26:29], v[156:159], v[208:211], v[26:29]
	v_mfma_f32_16x16x32_bf16 v[18:21], v[148:151], v[216:219], v[18:21]
	v_mfma_f32_16x16x32_bf16 v[10:13], v[156:159], v[216:219], v[10:13]
	v_mfma_f32_16x16x32_bf16 v[62:65], v[152:155], v[196:199], v[62:65]
	v_mfma_f32_16x16x32_bf16 v[58:61], v[160:163], v[196:199], v[58:61]
	v_mfma_f32_16x16x32_bf16 v[50:53], v[152:155], v[204:207], v[50:53]
	v_mfma_f32_16x16x32_bf16 v[42:45], v[160:163], v[204:207], v[42:45]
	v_mfma_f32_16x16x32_bf16 v[34:37], v[152:155], v[212:215], v[34:37]
	v_mfma_f32_16x16x32_bf16 v[26:29], v[160:163], v[212:215], v[26:29]
	v_mfma_f32_16x16x32_bf16 v[18:21], v[152:155], v[220:223], v[18:21]
	v_mfma_f32_16x16x32_bf16 v[10:13], v[160:163], v[220:223], v[10:13]
	s_setprio 0
	s_setprio 3
	v_mfma_f32_16x16x32_bf16 v[54:57], v[176:179], v[192:195], v[54:57]
	v_mfma_f32_16x16x32_bf16 v[46:49], v[184:187], v[192:195], v[46:49]
	v_mfma_f32_16x16x32_bf16 v[38:41], v[176:179], v[200:203], v[38:41]
	v_mfma_f32_16x16x32_bf16 v[30:33], v[184:187], v[200:203], v[30:33]
	v_mfma_f32_16x16x32_bf16 v[22:25], v[176:179], v[208:211], v[22:25]
	v_mfma_f32_16x16x32_bf16 v[14:17], v[184:187], v[208:211], v[14:17]
	v_mfma_f32_16x16x32_bf16 v[6:9], v[176:179], v[216:219], v[6:9]
	v_mfma_f32_16x16x32_bf16 v[2:5], v[184:187], v[216:219], v[2:5]
	v_mfma_f32_16x16x32_bf16 v[54:57], v[180:183], v[196:199], v[54:57]
	v_mfma_f32_16x16x32_bf16 v[46:49], v[188:191], v[196:199], v[46:49]
	v_mfma_f32_16x16x32_bf16 v[38:41], v[180:183], v[204:207], v[38:41]
	v_mfma_f32_16x16x32_bf16 v[30:33], v[188:191], v[204:207], v[30:33]
	v_mfma_f32_16x16x32_bf16 v[22:25], v[180:183], v[212:215], v[22:25]
	v_mfma_f32_16x16x32_bf16 v[14:17], v[188:191], v[212:215], v[14:17]
	v_mfma_f32_16x16x32_bf16 v[6:9], v[180:183], v[220:223], v[6:9]
	v_mfma_f32_16x16x32_bf16 v[2:5], v[188:191], v[220:223], v[2:5]
	s_setprio 0
	s_barrier
	s_add_i32 s58, s58, 2
	s_add_u32 s22, s22, 0x100
	s_addc_u32 s23, s23, 0
	s_add_u32 s56, s56, 0x100
	s_addc_u32 s57, s57, 0
	s_cmp_gt_u32 s58, 13
.LBB0_944:
	ds_read_b128 v[148:151], v170
	ds_read_b128 v[152:155], v170 offset:1024
	ds_read_b128 v[156:159], v170 offset:2048
	ds_read_b128 v[160:163], v170 offset:3072
	ds_read_b128 v[176:179], v171
	ds_read_b128 v[180:183], v171 offset:1024
	ds_read_b128 v[184:187], v171 offset:2048
	ds_read_b128 v[188:191], v171 offset:3072
	s_add_u32 s24, s22, 0xfffc0080
	s_addc_u32 s25, s23, -1
	s_cmp_eq_u32 s58, 12
	s_cselect_b32 s27, s15, s25
	s_cselect_b32 s26, s54, s24
	s_cselect_b32 s25, s13, s57
	s_cselect_b32 s24, s55, s56
	s_add_i32 m0, s21, 0xc000
	ds_read_b128 v[192:195], v172
	ds_read_b128 v[196:199], v172 offset:1024
	ds_read_b128 v[200:203], v172 offset:2048
	ds_read_b128 v[204:207], v172 offset:3072
	ds_read_b128 v[208:211], v172 offset:4096
	ds_read_b128 v[212:215], v172 offset:5120
	ds_read_b128 v[216:219], v172 offset:6144
	ds_read_b128 v[220:223], v172 offset:7168
	global_load_lds_dwordx4 v140, s[22:23]
	s_add_i32 m0, s21, 0xe000
	s_nop 0
	global_load_lds_dwordx4 v142, s[22:23]
	s_waitcnt vmcnt(8)
	s_waitcnt lgkmcnt(0)
	s_barrier
; #define PG8_STAGE_A(b, h, ptr, NX) do { if constexpr (Sched::GATHER) { unsigned gs_[2]; gs_[0] = ((NX) && last_) ? gN[h][0] : gA[h][0]; gs_[1] = ((NX) && last_) ? gN[h][1] : gA[h][1]; PG8_STAGE(PG8_SA(b, h), ptr, gs_); } \
;         else PG8_STAGE(PG8_SA(b, h), (ptr) + ((h) ? hstep : (size_t)0), voffA); } while (0)
; #define PG8_STAGE(bufoff, gbase, voff) do { _Pragma("unroll") for (int _i = 0; _i < 2; ++_i) \
;         __builtin_amdgcn_global_load_lds((const unsigned*)((const char*)(gbase) + (voff)[_i]), (PG8_LAS unsigned*)(lds + (bufoff) + ldsw + _i * 8192), 16, 0, 0); } while (0)
; #define PG8_LDA(dst, b, h) do { _Pragma("unroll") for (int m = 0; m < 4; ++m) _Pragma("unroll") for (int k = 0; k < 2; ++k) dst[m][k] = *(const PG8_LAS bf16x8*)(lds + PG8_SA(b, h) + aoff + m * 2048 + k * 1024); } while (0)
; #define PG8_MMA(ai, bj, At, Bt) do { __builtin_amdgcn_s_setprio(1); _Pragma("unroll") for (int m = 0; m < 4; ++m) _Pragma("unroll") for (int n = 0; n < 2; ++n) _Pragma("unroll") for (int k = 0; k < 2; ++k) \
;         acc[ai][bj][m][n] = __builtin_amdgcn_mfma_f32_16x16x32_bf16(Bt[n][k], At[m][k], acc[ai][bj][m][n], 0, 0, 0); __builtin_amdgcn_s_setprio(0); } while (0)
; #define PG8_WAIT_V(n) asm volatile("s_waitcnt vmcnt(" #n ")" ::: "memory")
; #define PG8_WAIT_L(n) asm volatile("s_waitcnt lgkmcnt(" #n ")" ::: "memory")
; #define PG8_BAR __builtin_amdgcn_s_barrier()
; #define PG8_SCHED __builtin_amdgcn_sched_barrier(0)
; template <class Epi, class Sched, bool ALIGN_EPI = false, bool SP2 = false>
; __device__ __forceinline__ void gemm_phase(PG8_LAS unsigned char* lds, const Gemm g, const Sched& S, const Epi& E, const bool skip_epi = false) {
;     ...
;             PG8_WAIT_V(8); PG8_WAIT_L(0); PG8_BAR; PG8_MMA(0, 0, At, B0); PG8_MMA(0, 1, At, B1); PG8_BAR; PG8_SCHED;
;             PG8_LDA(At, 0, 1); PG8_STAGE(PG8_SB(0, 0), b2, voffB); PG8_STAGE(PG8_SB(0, 1), b2 + hstep, voffB); PG8_STAGE_A(0, 0, a2, true);
;             PG8_WAIT_V(8); PG8_WAIT_L(0); PG8_BAR; PG8_MMA(1, 0, At, B0); PG8_MMA(1, 1, At, B1); PG8_BAR; PG8_SCHED;
	s_setprio 3
	s_waitcnt lgkmcnt(0)
	v_mfma_f32_16x16x32_bf16 v[126:129], v[148:151], v[192:195], v[126:129]
	v_mfma_f32_16x16x32_bf16 v[122:125], v[156:159], v[192:195], v[122:125]
	v_mfma_f32_16x16x32_bf16 v[114:117], v[148:151], v[200:203], v[114:117]
	v_mfma_f32_16x16x32_bf16 v[106:109], v[156:159], v[200:203], v[106:109]
	v_lshl_add_u64 v[164:165], s[24:25], 0, v[134:135]
	v_mfma_f32_16x16x32_bf16 v[98:101], v[148:151], v[208:211], v[98:101]
	v_mfma_f32_16x16x32_bf16 v[90:93], v[156:159], v[208:211], v[90:93]
	v_lshl_add_u64 v[224:225], s[24:25], 0, v[130:131]
	v_mfma_f32_16x16x32_bf16 v[82:85], v[148:151], v[216:219], v[82:85]
	v_mfma_f32_16x16x32_bf16 v[74:77], v[156:159], v[216:219], v[74:77]
	v_lshl_add_u64 v[230:231], s[26:27], 0, v[132:133]
	v_mfma_f32_16x16x32_bf16 v[126:129], v[152:155], v[196:199], v[126:129]
	v_mfma_f32_16x16x32_bf16 v[122:125], v[160:163], v[196:199], v[122:125]
	v_lshl_add_u64 v[226:227], s[26:27], 0, v[136:137]
	v_mfma_f32_16x16x32_bf16 v[114:117], v[152:155], v[204:207], v[114:117]
	v_mfma_f32_16x16x32_bf16 v[106:109], v[160:163], v[204:207], v[106:109]
	v_mfma_f32_16x16x32_bf16 v[98:101], v[152:155], v[212:215], v[98:101]
	v_mfma_f32_16x16x32_bf16 v[90:93], v[160:163], v[212:215], v[90:93]
	v_mfma_f32_16x16x32_bf16 v[82:85], v[152:155], v[220:223], v[82:85]
	v_mfma_f32_16x16x32_bf16 v[74:77], v[160:163], v[220:223], v[74:77]
	s_setprio 0
	s_setprio 3
	v_mfma_f32_16x16x32_bf16 v[118:121], v[176:179], v[192:195], v[118:121]
	v_mfma_f32_16x16x32_bf16 v[110:113], v[184:187], v[192:195], v[110:113]
	v_mfma_f32_16x16x32_bf16 v[102:105], v[176:179], v[200:203], v[102:105]
	v_mfma_f32_16x16x32_bf16 v[94:97], v[184:187], v[200:203], v[94:97]
	v_mfma_f32_16x16x32_bf16 v[86:89], v[176:179], v[208:211], v[86:89]
	v_mfma_f32_16x16x32_bf16 v[78:81], v[184:187], v[208:211], v[78:81]
	v_mfma_f32_16x16x32_bf16 v[70:73], v[176:179], v[216:219], v[70:73]
	v_mfma_f32_16x16x32_bf16 v[66:69], v[184:187], v[216:219], v[66:69]
	v_mfma_f32_16x16x32_bf16 v[118:121], v[180:183], v[196:199], v[118:121]
	v_mfma_f32_16x16x32_bf16 v[110:113], v[188:191], v[196:199], v[110:113]
	v_mfma_f32_16x16x32_bf16 v[102:105], v[180:183], v[204:207], v[102:105]
	v_mfma_f32_16x16x32_bf16 v[94:97], v[188:191], v[204:207], v[94:97]
	v_mfma_f32_16x16x32_bf16 v[86:89], v[180:183], v[212:215], v[86:89]
	v_mfma_f32_16x16x32_bf16 v[78:81], v[188:191], v[212:215], v[78:81]
	v_mfma_f32_16x16x32_bf16 v[70:73], v[180:183], v[220:223], v[70:73]
	v_mfma_f32_16x16x32_bf16 v[66:69], v[188:191], v[220:223], v[66:69]
	s_setprio 0
	s_barrier
	s_add_i32 s59, s48, s28
	s_mov_b32 m0, s59
	ds_read_b128 v[192:195], v172 offset:16384
	ds_read_b128 v[196:199], v172 offset:17408
	ds_read_b128 v[200:203], v172 offset:18432
	ds_read_b128 v[204:207], v172 offset:19456
	ds_read_b128 v[208:211], v172 offset:20480
	ds_read_b128 v[212:215], v172 offset:21504
	ds_read_b128 v[216:219], v172 offset:22528
	ds_read_b128 v[220:223], v172 offset:23552
	global_load_lds_dwordx4 v[164:165], off
	s_add_i32 m0, s59, 0x2000
	s_add_u32 s60, s24, 0x40000
	s_addc_u32 s61, s25, 0
	s_add_i32 s59, s49, s28
	global_load_lds_dwordx4 v[224:225], off
	s_mov_b32 m0, s59
	s_nop 0
	global_load_lds_dwordx4 v134, s[60:61]
	s_add_i32 m0, s59, 0x2000
	s_nop 0
	global_load_lds_dwordx4 v130, s[60:61]
	s_mov_b32 m0, s21
	s_nop 0
	global_load_lds_dwordx4 v[226:227], off
	s_mov_b32 m0, s31
	s_nop 0
	global_load_lds_dwordx4 v[230:231], off
	s_waitcnt vmcnt(8)
	s_waitcnt lgkmcnt(0)
	s_barrier
	s_setprio 3
	s_waitcnt lgkmcnt(0)
	v_mfma_f32_16x16x32_bf16 v[62:65], v[148:151], v[192:195], v[62:65]
	v_mfma_f32_16x16x32_bf16 v[58:61], v[156:159], v[192:195], v[58:61]
	v_mfma_f32_16x16x32_bf16 v[50:53], v[148:151], v[200:203], v[50:53]
	v_mfma_f32_16x16x32_bf16 v[42:45], v[156:159], v[200:203], v[42:45]
	v_mfma_f32_16x16x32_bf16 v[34:37], v[148:151], v[208:211], v[34:37]
	v_mfma_f32_16x16x32_bf16 v[26:29], v[156:159], v[208:211], v[26:29]
	v_mfma_f32_16x16x32_bf16 v[18:21], v[148:151], v[216:219], v[18:21]
	v_mfma_f32_16x16x32_bf16 v[10:13], v[156:159], v[216:219], v[10:13]
	v_mfma_f32_16x16x32_bf16 v[62:65], v[152:155], v[196:199], v[62:65]
	v_mfma_f32_16x16x32_bf16 v[58:61], v[160:163], v[196:199], v[58:61]
	v_mfma_f32_16x16x32_bf16 v[50:53], v[152:155], v[204:207], v[50:53]
	v_mfma_f32_16x16x32_bf16 v[42:45], v[160:163], v[204:207], v[42:45]
	v_mfma_f32_16x16x32_bf16 v[34:37], v[152:155], v[212:215], v[34:37]
	v_mfma_f32_16x16x32_bf16 v[26:29], v[160:163], v[212:215], v[26:29]
	v_mfma_f32_16x16x32_bf16 v[18:21], v[152:155], v[220:223], v[18:21]
	v_mfma_f32_16x16x32_bf16 v[10:13], v[160:163], v[220:223], v[10:13]
	s_setprio 0
	s_setprio 3
	v_mfma_f32_16x16x32_bf16 v[54:57], v[176:179], v[192:195], v[54:57]
	v_mfma_f32_16x16x32_bf16 v[46:49], v[184:187], v[192:195], v[46:49]
	v_mfma_f32_16x16x32_bf16 v[38:41], v[176:179], v[200:203], v[38:41]
	v_mfma_f32_16x16x32_bf16 v[30:33], v[184:187], v[200:203], v[30:33]
	v_mfma_f32_16x16x32_bf16 v[22:25], v[176:179], v[208:211], v[22:25]
	v_mfma_f32_16x16x32_bf16 v[14:17], v[184:187], v[208:211], v[14:17]
	v_mfma_f32_16x16x32_bf16 v[6:9], v[176:179], v[216:219], v[6:9]
	v_mfma_f32_16x16x32_bf16 v[2:5], v[184:187], v[216:219], v[2:5]
	v_mfma_f32_16x16x32_bf16 v[54:57], v[180:183], v[196:199], v[54:57]
	v_mfma_f32_16x16x32_bf16 v[46:49], v[188:191], v[196:199], v[46:49]
	v_mfma_f32_16x16x32_bf16 v[38:41], v[180:183], v[204:207], v[38:41]
	v_mfma_f32_16x16x32_bf16 v[30:33], v[188:191], v[204:207], v[30:33]
	v_mfma_f32_16x16x32_bf16 v[22:25], v[180:183], v[212:215], v[22:25]
	v_mfma_f32_16x16x32_bf16 v[14:17], v[188:191], v[212:215], v[14:17]
	v_mfma_f32_16x16x32_bf16 v[6:9], v[180:183], v[220:223], v[6:9]
	v_mfma_f32_16x16x32_bf16 v[2:5], v[188:191], v[220:223], v[2:5]
	s_setprio 0
	s_barrier
; #define PG8_STAGE_A(b, h, ptr, NX) do { if constexpr (Sched::GATHER) { unsigned gs_[2]; gs_[0] = ((NX) && last_) ? gN[h][0] : gA[h][0]; gs_[1] = ((NX) && last_) ? gN[h][1] : gA[h][1]; PG8_STAGE(PG8_SA(b, h), ptr, gs_); } \
;         else PG8_STAGE(PG8_SA(b, h), (ptr) + ((h) ? hstep : (size_t)0), voffA); } while (0)
; #define PG8_LDA(dst, b, h) do { _Pragma("unroll") for (int m = 0; m < 4; ++m) _Pragma("unroll") for (int k = 0; k < 2; ++k) dst[m][k] = *(const PG8_LAS bf16x8*)(lds + PG8_SA(b, h) + aoff + m * 2048 + k * 1024); } while (0)
; #define PG8_LDB(dst, b, h) do { _Pragma("unroll") for (int n = 0; n < 2; ++n) _Pragma("unroll") for (int k = 0; k < 2; ++k) dst[n][k] = *(const PG8_LAS bf16x8*)(lds + PG8_SB(b, h) + boff + n * 2048 + k * 1024); } while (0)
; #define PG8_MMA(ai, bj, At, Bt) do { __builtin_amdgcn_s_setprio(1); _Pragma("unroll") for (int m = 0; m < 4; ++m) _Pragma("unroll") for (int n = 0; n < 2; ++n) _Pragma("unroll") for (int k = 0; k < 2; ++k) \
;         acc[ai][bj][m][n] = __builtin_amdgcn_mfma_f32_16x16x32_bf16(Bt[n][k], At[m][k], acc[ai][bj][m][n], 0, 0, 0); __builtin_amdgcn_s_setprio(0); } while (0)
; #define PG8_WAIT_V(n) asm volatile("s_waitcnt vmcnt(" #n ")" ::: "memory")
; #define PG8_WAIT_L(n) asm volatile("s_waitcnt lgkmcnt(" #n ")" ::: "memory")
; #define PG8_BAR __builtin_amdgcn_s_barrier()
; #define PG8_SCHED __builtin_amdgcn_sched_barrier(0)
; template <class Epi, class Sched, bool ALIGN_EPI = false, bool SP2 = false>
; __device__ __forceinline__ void gemm_phase(PG8_LAS unsigned char* lds, const Gemm g, const Sched& S, const Epi& E, const bool skip_epi = false) {
;     ...
;             PG8_LDB(B0, 1, 0); PG8_LDB(B1, 1, 1); PG8_SCHED; PG8_LDA(At, 1, 0); PG8_STAGE_A(0, 1, a2, true);
;             PG8_WAIT_V(8); PG8_WAIT_L(0); PG8_BAR; PG8_MMA(0, 0, At, B0); PG8_MMA(0, 1, At, B1); PG8_BAR; PG8_SCHED;
	s_add_i32 s59, 0, 0x18000
	s_add_i32 s60, 0, 0x1c000
	v_add_u32_e32 v160, s59, v1
	v_add_u32_e32 v188, s60, v1
	ds_read_b128 v[148:151], v160
	ds_read_b128 v[152:155], v160 offset:1024
	ds_read_b128 v[156:159], v160 offset:2048
	ds_read_b128 v[160:163], v160 offset:3072
	ds_read_b128 v[176:179], v188
	ds_read_b128 v[180:183], v188 offset:1024
	ds_read_b128 v[184:187], v188 offset:2048
	ds_read_b128 v[188:191], v188 offset:3072
	s_add_u32 s26, s26, 0x40000
	s_addc_u32 s27, s27, 0
	s_mov_b32 m0, s34
	ds_read_b128 v[192:195], v172 offset:32768
	ds_read_b128 v[196:199], v172 offset:33792
	ds_read_b128 v[200:203], v172 offset:34816
	ds_read_b128 v[204:207], v172 offset:35840
	ds_read_b128 v[208:211], v172 offset:36864
	ds_read_b128 v[212:215], v172 offset:37888
	ds_read_b128 v[216:219], v172 offset:38912
	ds_read_b128 v[220:223], v172 offset:39936
	global_load_lds_dwordx4 v136, s[26:27]
	s_mov_b32 m0, s35
	s_nop 0
	global_load_lds_dwordx4 v132, s[26:27]
	s_waitcnt vmcnt(8)
	s_waitcnt lgkmcnt(0)
	s_barrier
	s_setprio 3
	s_waitcnt lgkmcnt(0)
	v_mfma_f32_16x16x32_bf16 v[126:129], v[148:151], v[192:195], v[126:129]
	v_mfma_f32_16x16x32_bf16 v[122:125], v[156:159], v[192:195], v[122:125]
	v_mfma_f32_16x16x32_bf16 v[114:117], v[148:151], v[200:203], v[114:117]
	v_mfma_f32_16x16x32_bf16 v[106:109], v[156:159], v[200:203], v[106:109]
	v_mfma_f32_16x16x32_bf16 v[98:101], v[148:151], v[208:211], v[98:101]
	v_mfma_f32_16x16x32_bf16 v[90:93], v[156:159], v[208:211], v[90:93]
	v_mfma_f32_16x16x32_bf16 v[82:85], v[148:151], v[216:219], v[82:85]
	v_mfma_f32_16x16x32_bf16 v[74:77], v[156:159], v[216:219], v[74:77]
	v_mfma_f32_16x16x32_bf16 v[126:129], v[152:155], v[196:199], v[126:129]
	v_mfma_f32_16x16x32_bf16 v[122:125], v[160:163], v[196:199], v[122:125]
	v_mfma_f32_16x16x32_bf16 v[114:117], v[152:155], v[204:207], v[114:117]
	v_mfma_f32_16x16x32_bf16 v[106:109], v[160:163], v[204:207], v[106:109]
	v_mfma_f32_16x16x32_bf16 v[98:101], v[152:155], v[212:215], v[98:101]
	v_mfma_f32_16x16x32_bf16 v[90:93], v[160:163], v[212:215], v[90:93]
	v_mfma_f32_16x16x32_bf16 v[82:85], v[152:155], v[220:223], v[82:85]
	v_mfma_f32_16x16x32_bf16 v[74:77], v[160:163], v[220:223], v[74:77]
	s_setprio 0
	s_setprio 3
	v_mfma_f32_16x16x32_bf16 v[118:121], v[176:179], v[192:195], v[118:121]
	v_mfma_f32_16x16x32_bf16 v[110:113], v[184:187], v[192:195], v[110:113]
	v_mfma_f32_16x16x32_bf16 v[102:105], v[176:179], v[200:203], v[102:105]
	v_mfma_f32_16x16x32_bf16 v[94:97], v[184:187], v[200:203], v[94:97]
	v_mfma_f32_16x16x32_bf16 v[86:89], v[176:179], v[208:211], v[86:89]
	v_mfma_f32_16x16x32_bf16 v[78:81], v[184:187], v[208:211], v[78:81]
	v_mfma_f32_16x16x32_bf16 v[70:73], v[176:179], v[216:219], v[70:73]
	v_mfma_f32_16x16x32_bf16 v[66:69], v[184:187], v[216:219], v[66:69]
	v_mfma_f32_16x16x32_bf16 v[118:121], v[180:183], v[196:199], v[118:121]
	v_mfma_f32_16x16x32_bf16 v[110:113], v[188:191], v[196:199], v[110:113]
	v_mfma_f32_16x16x32_bf16 v[102:105], v[180:183], v[204:207], v[102:105]
	v_mfma_f32_16x16x32_bf16 v[94:97], v[188:191], v[204:207], v[94:97]
	v_mfma_f32_16x16x32_bf16 v[86:89], v[180:183], v[212:215], v[86:89]
	v_mfma_f32_16x16x32_bf16 v[78:81], v[188:191], v[212:215], v[78:81]
	v_mfma_f32_16x16x32_bf16 v[70:73], v[180:183], v[220:223], v[70:73]
	v_mfma_f32_16x16x32_bf16 v[66:69], v[188:191], v[220:223], v[66:69]
	s_setprio 0
	s_barrier
; #define PG8_STAGE_A(b, h, ptr, NX) do { if constexpr (Sched::GATHER) { unsigned gs_[2]; gs_[0] = ((NX) && last_) ? gN[h][0] : gA[h][0]; gs_[1] = ((NX) && last_) ? gN[h][1] : gA[h][1]; PG8_STAGE(PG8_SA(b, h), ptr, gs_); } \
;         else PG8_STAGE(PG8_SA(b, h), (ptr) + ((h) ? hstep : (size_t)0), voffA); } while (0)
; #define PG8_STAGE(bufoff, gbase, voff) do { _Pragma("unroll") for (int _i = 0; _i < 2; ++_i) \
;         __builtin_amdgcn_global_load_lds((const unsigned*)((const char*)(gbase) + (voff)[_i]), (PG8_LAS unsigned*)(lds + (bufoff) + ldsw + _i * 8192), 16, 0, 0); } while (0)
; #define PG8_LDA(dst, b, h) do { _Pragma("unroll") for (int m = 0; m < 4; ++m) _Pragma("unroll") for (int k = 0; k < 2; ++k) dst[m][k] = *(const PG8_LAS bf16x8*)(lds + PG8_SA(b, h) + aoff + m * 2048 + k * 1024); } while (0)
; #define PG8_MMA(ai, bj, At, Bt) do { __builtin_amdgcn_s_setprio(1); _Pragma("unroll") for (int m = 0; m < 4; ++m) _Pragma("unroll") for (int n = 0; n < 2; ++n) _Pragma("unroll") for (int k = 0; k < 2; ++k) \
;         acc[ai][bj][m][n] = __builtin_amdgcn_mfma_f32_16x16x32_bf16(Bt[n][k], At[m][k], acc[ai][bj][m][n], 0, 0, 0); __builtin_amdgcn_s_setprio(0); } while (0)
; #define PG8_WAIT_V(n) asm volatile("s_waitcnt vmcnt(" #n ")" ::: "memory")
; #define PG8_WAIT_L(n) asm volatile("s_waitcnt lgkmcnt(" #n ")" ::: "memory")
; #define PG8_BAR __builtin_amdgcn_s_barrier()
; #define PG8_SCHED __builtin_amdgcn_sched_barrier(0)
; __device__ __forceinline__ void rstd8(const float* SS, int rowb, int lane, float (&rs)[2][4]) {
;     ...
;         for (int m = 0; m < 4; ++m) p[ai][m] = *(const f32x4*)(SS + (size_t)(rowb + HALF * ai + 16 * m + (lane >> 2)) * 16 + 4 * (lane & 3));
;     asm volatile("" : "+v"(p[0][0]), "+v"(p[0][1]), "+v"(p[0][2]), "+v"(p[0][3]), "+v"(p[1][0]), "+v"(p[1][1]), "+v"(p[1][2]), "+v"(p[1][3]));
; template <class Epi, class Sched, bool ALIGN_EPI = false, bool SP2 = false>
; __device__ __forceinline__ void gemm_phase(PG8_LAS unsigned char* lds, const Gemm g, const Sched& S, const Epi& E, const bool skip_epi = false) {
;     ...
;             PG8_LDA(At, 1, 1); PG8_STAGE(PG8_SB(1, 0), b3, voffB); PG8_STAGE(PG8_SB(1, 1), b3 + hstep, voffB); PG8_STAGE_A(1, 0, a3, true);
;             PG8_WAIT_V(8); PG8_WAIT_L(0); PG8_BAR; PG8_MMA(1, 0, At, B0); PG8_MMA(1, 1, At, B1); PG8_BAR; PG8_SCHED;
	s_add_i32 s26, s59, s28
	s_add_i32 m0, s26, 0xffffff80
	ds_read_b128 v[192:195], v172 offset:49152
	ds_read_b128 v[196:199], v172 offset:50176
	ds_read_b128 v[200:203], v172 offset:51200
	ds_read_b128 v[204:207], v172 offset:52224
	ds_read_b128 v[208:211], v172 offset:53248
	ds_read_b128 v[212:215], v172 offset:54272
	ds_read_b128 v[216:219], v172 offset:55296
	ds_read_b128 v[220:223], v172 offset:56320
	global_load_lds_dwordx4 v[164:165], off offset:128
	s_add_i32 m0, s26, 0x1f80
	s_add_u32 s24, s24, 0x40080
	s_addc_u32 s25, s25, 0
	s_add_i32 s26, s60, s28
	global_load_lds_dwordx4 v[224:225], off offset:128
	s_mov_b32 m0, s26
	s_nop 0
	global_load_lds_dwordx4 v134, s[24:25]
	s_add_i32 m0, s26, 0x2000
	s_nop 0
	global_load_lds_dwordx4 v130, s[24:25]
	s_add_i32 m0, s37, 0xffffff80
	s_nop 0
	global_load_lds_dwordx4 v[226:227], off offset:128
	s_add_i32 m0, s38, 0xffffff80
	s_nop 0
	global_load_lds_dwordx4 v[230:231], off offset:128
	s_waitcnt vmcnt(8)
	s_waitcnt lgkmcnt(0)
	s_barrier
	s_setprio 3
	s_waitcnt lgkmcnt(0)
	v_mfma_f32_16x16x32_bf16 v[62:65], v[148:151], v[192:195], v[62:65]
	v_mfma_f32_16x16x32_bf16 v[58:61], v[156:159], v[192:195], v[58:61]
	v_mfma_f32_16x16x32_bf16 v[50:53], v[148:151], v[200:203], v[50:53]
	v_mfma_f32_16x16x32_bf16 v[42:45], v[156:159], v[200:203], v[42:45]
	v_mfma_f32_16x16x32_bf16 v[34:37], v[148:151], v[208:211], v[34:37]
	v_mfma_f32_16x16x32_bf16 v[26:29], v[156:159], v[208:211], v[26:29]
	v_mfma_f32_16x16x32_bf16 v[18:21], v[148:151], v[216:219], v[18:21]
	v_mfma_f32_16x16x32_bf16 v[10:13], v[156:159], v[216:219], v[10:13]
	v_mfma_f32_16x16x32_bf16 v[62:65], v[152:155], v[196:199], v[62:65]
	v_mfma_f32_16x16x32_bf16 v[58:61], v[160:163], v[196:199], v[58:61]
	v_mfma_f32_16x16x32_bf16 v[50:53], v[152:155], v[204:207], v[50:53]
	v_mfma_f32_16x16x32_bf16 v[42:45], v[160:163], v[204:207], v[42:45]
	v_mfma_f32_16x16x32_bf16 v[34:37], v[152:155], v[212:215], v[34:37]
	v_mfma_f32_16x16x32_bf16 v[26:29], v[160:163], v[212:215], v[26:29]
	v_mfma_f32_16x16x32_bf16 v[18:21], v[152:155], v[220:223], v[18:21]
	v_mfma_f32_16x16x32_bf16 v[10:13], v[160:163], v[220:223], v[10:13]
	s_setprio 0
	s_setprio 3
	v_mfma_f32_16x16x32_bf16 v[54:57], v[176:179], v[192:195], v[54:57]
	v_mfma_f32_16x16x32_bf16 v[46:49], v[184:187], v[192:195], v[46:49]
	v_mfma_f32_16x16x32_bf16 v[38:41], v[176:179], v[200:203], v[38:41]
	v_mfma_f32_16x16x32_bf16 v[30:33], v[184:187], v[200:203], v[30:33]
	v_mfma_f32_16x16x32_bf16 v[22:25], v[176:179], v[208:211], v[22:25]
	v_mfma_f32_16x16x32_bf16 v[14:17], v[184:187], v[208:211], v[14:17]
	v_mfma_f32_16x16x32_bf16 v[6:9], v[176:179], v[216:219], v[6:9]
	v_mfma_f32_16x16x32_bf16 v[2:5], v[184:187], v[216:219], v[2:5]
	v_mfma_f32_16x16x32_bf16 v[54:57], v[180:183], v[196:199], v[54:57]
	v_mfma_f32_16x16x32_bf16 v[46:49], v[188:191], v[196:199], v[46:49]
	v_mfma_f32_16x16x32_bf16 v[38:41], v[180:183], v[204:207], v[38:41]
	v_mfma_f32_16x16x32_bf16 v[30:33], v[188:191], v[204:207], v[30:33]
	v_mfma_f32_16x16x32_bf16 v[22:25], v[180:183], v[212:215], v[22:25]
	v_mfma_f32_16x16x32_bf16 v[14:17], v[188:191], v[212:215], v[14:17]
	v_mfma_f32_16x16x32_bf16 v[6:9], v[180:183], v[220:223], v[6:9]
	v_mfma_f32_16x16x32_bf16 v[2:5], v[188:191], v[220:223], v[2:5]
	s_setprio 0
	s_barrier
	s_add_i32 s58, s58, 2
	s_add_u32 s22, s22, 0x100
	s_addc_u32 s23, s23, 0
	s_add_u32 s56, s56, 0x100
	s_addc_u32 s57, s57, 0
	s_cmp_gt_u32 s58, 13
	s_cbranch_scc0 .LBB0_944
	v_lshl_add_u32 v164, s20, 8, v167
	v_ashrrev_i32_e32 v165, 31, v164
	v_lshlrev_b64 v[148:149], 6, v[164:165]
	v_lshl_add_u64 v[148:149], v[138:139], 0, v[148:149]
	v_add_co_u32_e32 v150, vcc, 0x2000, v148
	v_addc_co_u32_e32 v151, vcc, 0, v149, vcc
	global_load_dwordx4 v[176:179], v[148:149], off
	global_load_dwordx4 v[180:183], v[148:149], off offset:1024
	global_load_dwordx4 v[184:187], v[148:149], off offset:2048
	global_load_dwordx4 v[188:191], v[148:149], off offset:3072
	global_load_dwordx4 v[192:195], v[150:151], off
	global_load_dwordx4 v[196:199], v[150:151], off offset:1024
	global_load_dwordx4 v[200:203], v[150:151], off offset:2048
	global_load_dwordx4 v[204:207], v[150:151], off offset:3072
	s_and_b64 vcc, exec, s[10:11]
	s_cbranch_vccz .LBB0_947
	s_barrier

; #define PG8_STAGE_A(b, h, ptr, NX) do { if constexpr (Sched::GATHER) { unsigned gs_[2]; gs_[0] = ((NX) && last_) ? gN[h][0] : gA[h][0]; gs_[1] = ((NX) && last_) ? gN[h][1] : gA[h][1]; PG8_STAGE(PG8_SA(b, h), ptr, gs_); } \
;         else PG8_STAGE(PG8_SA(b, h), (ptr) + ((h) ? hstep : (size_t)0), voffA); } while (0)
; #define PG8_STAGE(bufoff, gbase, voff) do { _Pragma("unroll") for (int _i = 0; _i < 2; ++_i) \
;         __builtin_amdgcn_global_load_lds((const unsigned*)((const char*)(gbase) + (voff)[_i]), (PG8_LAS unsigned*)(lds + (bufoff) + ldsw + _i * 8192), 16, 0, 0); } while (0)
; #define PG8_LDA(dst, b, h) do { _Pragma("unroll") for (int m = 0; m < 4; ++m) _Pragma("unroll") for (int k = 0; k < 2; ++k) dst[m][k] = *(const PG8_LAS bf16x8*)(lds + PG8_SA(b, h) + aoff + m * 2048 + k * 1024); } while (0)
; #define PG8_WAIT_V(n) asm volatile("s_waitcnt vmcnt(" #n ")" ::: "memory")
; #define PG8_WAIT_L(n) asm volatile("s_waitcnt lgkmcnt(" #n ")" ::: "memory")
; #define PG8_BAR __builtin_amdgcn_s_barrier()
; template <class Epi, class Sched, bool ALIGN_EPI = false, bool SP2 = false>
; __device__ __forceinline__ void gemm_phase(PG8_LAS unsigned char* lds, const Gemm g, const Sched& S, const Epi& E, const bool skip_epi = false) {
;     ...
;         const char* nA = has_next ? (const char*)g.A + (size_t)nxt.pm * pmstepA + nxt.ko : cA; const char* nB = has_next ? (const char*)g.Bt + (size_t)nxt.pn * tstep + nxt.ko : cB;
;         for (int t = 0; t < nt; t += 2) {
;             const bool last = (t == nt - 2); last_ = last && has_next;
;             const char* a1 = cA + (size_t)(t + 1) * kstep;
;             const char* a2 = last ? nA : cA + (size_t)(t + 2) * kstep; const char* b2 = last ? nB : cB + (size_t)(t + 2) * kstep;
;             const char* a3 = a2 + kstep; const char* b3 = b2 + kstep;
;             if (last && has_next) S.a_ready(nxt);
;             if constexpr (SP2) {
;             PG8_LDB(B0, 0, 0); PG8_LDB(B1, 0, 1); PG8_SCHED; PG8_LDA(At, 0, 0); PG8_STAGE_A(1, 1, a1, false);
;             PG8_WAIT_V(8); PG8_WAIT_L(0); PG8_BAR; PG8_MMA(0, 0, At, B0); PG8_MMA(0, 1, At, B1); PG8_BAR; PG8_SCHED;
;             PG8_LDA(At, 0, 1); PG8_STAGE(PG8_SB(0, 0), b2, voffB); PG8_STAGE(PG8_SB(0, 1), b2 + hstep, voffB); PG8_STAGE_A(0, 0, a2, true);
;             PG8_WAIT_V(8); PG8_WAIT_L(0); PG8_BAR; PG8_MMA(1, 0, At, B0); PG8_MMA(1, 1, At, B1); PG8_BAR; PG8_SCHED;
.LBB0_1323:
	s_ashr_i32 s25, s24, 31
	s_lshl_b64 s[26:27], s[24:25], 19
	s_add_u32 s26, s46, s26
	s_addc_u32 s27, s47, s27
	s_and_b64 s[28:29], s[6:7], exec
	s_cselect_b32 s25, s27, s35
	s_cselect_b32 s31, s26, s34
	s_ashr_i32 s23, s22, 31
	s_lshl_b64 s[28:29], s[22:23], 19
	s_add_u32 s28, s2, s28
	s_addc_u32 s29, s3, s29
	s_and_b64 s[38:39], s[6:7], exec
	s_cselect_b32 s23, s29, s37
	s_cselect_b32 s60, s28, s36
	s_add_u32 s34, s34, 0x40080
	s_addc_u32 s35, s35, 0
	s_add_u32 s61, s36, 0x100
	s_addc_u32 s62, s37, 0
	s_mov_b32 s63, -2
	s_waitcnt vmcnt(0)
	s_waitcnt lgkmcnt(0)
	ds_read_b128 v[98:101], v225
	ds_read_b128 v[110:113], v225 offset:1024
	ds_read_b128 v[122:125], v225 offset:2048
	ds_read_b128 v[130:133], v225 offset:3072
	ds_read_b128 v[146:149], v226
	ds_read_b128 v[150:153], v226 offset:1024
	ds_read_b128 v[154:157], v226 offset:2048
	ds_read_b128 v[158:161], v226 offset:3072
	s_add_u32 s36, s34, 0xfffc0080
	s_addc_u32 s37, s35, -1
	s_cmp_eq_u32 s63, 12
	s_cselect_b32 s39, s25, s37
	s_cselect_b32 s38, s31, s36
	s_cselect_b32 s37, s23, s62
	s_cselect_b32 s36, s60, s61
	s_add_i32 m0, s41, 0xc000
	ds_read_b128 v[162:165], v227
	ds_read_b128 v[166:169], v227 offset:1024
	ds_read_b128 v[170:173], v227 offset:2048
	ds_read_b128 v[174:177], v227 offset:3072
	ds_read_b128 v[178:181], v227 offset:4096
	ds_read_b128 v[182:185], v227 offset:5120
	ds_read_b128 v[202:205], v227 offset:6144
	ds_read_b128 v[206:209], v227 offset:7168
	global_load_lds_dwordx4 v194, s[34:35]
	s_add_i32 m0, s41, 0xe000
	s_nop 0
	global_load_lds_dwordx4 v196, s[34:35]
	s_waitcnt vmcnt(8)
	s_waitcnt lgkmcnt(0)
	s_barrier
	s_setprio 3
	s_waitcnt lgkmcnt(0)
	v_mfma_f32_16x16x32_bf16 v[142:145], v[98:101], v[162:165], 0
	v_mfma_f32_16x16x32_bf16 v[138:141], v[122:125], v[162:165], 0
	v_mfma_f32_16x16x32_bf16 v[118:121], v[98:101], v[170:173], 0
	v_mfma_f32_16x16x32_bf16 v[114:117], v[122:125], v[170:173], 0
	v_lshl_add_u64 v[210:211], s[36:37], 0, v[188:189]
	v_mfma_f32_16x16x32_bf16 v[94:97], v[98:101], v[178:181], 0
	v_mfma_f32_16x16x32_bf16 v[90:93], v[122:125], v[178:181], 0
	v_lshl_add_u64 v[212:213], s[36:37], 0, v[192:193]
	v_mfma_f32_16x16x32_bf16 v[78:81], v[98:101], v[202:205], 0
	v_mfma_f32_16x16x32_bf16 v[74:77], v[122:125], v[202:205], 0
	v_lshl_add_u64 v[216:217], s[38:39], 0, v[190:191]
	v_mfma_f32_16x16x32_bf16 v[142:145], v[110:113], v[166:169], v[142:145]
	v_mfma_f32_16x16x32_bf16 v[138:141], v[130:133], v[166:169], v[138:141]
	v_lshl_add_u64 v[214:215], s[38:39], 0, v[186:187]
	v_mfma_f32_16x16x32_bf16 v[118:121], v[110:113], v[174:177], v[118:121]
	v_mfma_f32_16x16x32_bf16 v[114:117], v[130:133], v[174:177], v[114:117]
	v_mfma_f32_16x16x32_bf16 v[94:97], v[110:113], v[182:185], v[94:97]
	v_mfma_f32_16x16x32_bf16 v[90:93], v[130:133], v[182:185], v[90:93]
	v_mfma_f32_16x16x32_bf16 v[78:81], v[110:113], v[206:209], v[78:81]
	v_mfma_f32_16x16x32_bf16 v[74:77], v[130:133], v[206:209], v[74:77]
	s_setprio 0
	s_setprio 3
	v_mfma_f32_16x16x32_bf16 v[134:137], v[146:149], v[162:165], 0
	v_mfma_f32_16x16x32_bf16 v[126:129], v[154:157], v[162:165], 0
	v_mfma_f32_16x16x32_bf16 v[106:109], v[146:149], v[170:173], 0
	v_mfma_f32_16x16x32_bf16 v[102:105], v[154:157], v[170:173], 0
	v_mfma_f32_16x16x32_bf16 v[86:89], v[146:149], v[178:181], 0
	v_mfma_f32_16x16x32_bf16 v[82:85], v[154:157], v[178:181], 0
	v_mfma_f32_16x16x32_bf16 v[70:73], v[146:149], v[202:205], 0
	v_mfma_f32_16x16x32_bf16 v[66:69], v[154:157], v[202:205], 0
	v_mfma_f32_16x16x32_bf16 v[134:137], v[150:153], v[166:169], v[134:137]
	v_mfma_f32_16x16x32_bf16 v[126:129], v[158:161], v[166:169], v[126:129]
	v_mfma_f32_16x16x32_bf16 v[106:109], v[150:153], v[174:177], v[106:109]
	v_mfma_f32_16x16x32_bf16 v[102:105], v[158:161], v[174:177], v[102:105]
	v_mfma_f32_16x16x32_bf16 v[86:89], v[150:153], v[182:185], v[86:89]
	v_mfma_f32_16x16x32_bf16 v[82:85], v[158:161], v[182:185], v[82:85]
	v_mfma_f32_16x16x32_bf16 v[70:73], v[150:153], v[206:209], v[70:73]
	v_mfma_f32_16x16x32_bf16 v[66:69], v[158:161], v[206:209], v[66:69]
	s_setprio 0
	s_barrier
	s_add_i32 s64, s57, s40
	s_mov_b32 m0, s64
	ds_read_b128 v[162:165], v227 offset:16384
	ds_read_b128 v[166:169], v227 offset:17408
	ds_read_b128 v[170:173], v227 offset:18432
	ds_read_b128 v[174:177], v227 offset:19456
	ds_read_b128 v[178:181], v227 offset:20480
	ds_read_b128 v[182:185], v227 offset:21504
	ds_read_b128 v[202:205], v227 offset:22528
	ds_read_b128 v[206:209], v227 offset:23552
	global_load_lds_dwordx4 v[210:211], off
	s_add_i32 m0, s64, 0x2000
	s_add_u32 s64, s36, 0x40000
	s_addc_u32 s65, s37, 0
	s_add_i32 s66, s58, s40
	global_load_lds_dwordx4 v[212:213], off
	s_mov_b32 m0, s66
	s_nop 0
	global_load_lds_dwordx4 v188, s[64:65]
	s_add_i32 m0, s66, 0x2000
	s_nop 0
	global_load_lds_dwordx4 v192, s[64:65]
	s_mov_b32 m0, s41
	s_nop 0
	global_load_lds_dwordx4 v[214:215], off
	s_mov_b32 m0, s44
	s_nop 0
	global_load_lds_dwordx4 v[216:217], off
	s_waitcnt vmcnt(8)
	s_waitcnt lgkmcnt(0)
	s_barrier
; #define PG8_STAGE_A(b, h, ptr, NX) do { if constexpr (Sched::GATHER) { unsigned gs_[2]; gs_[0] = ((NX) && last_) ? gN[h][0] : gA[h][0]; gs_[1] = ((NX) && last_) ? gN[h][1] : gA[h][1]; PG8_STAGE(PG8_SA(b, h), ptr, gs_); } \
;         else PG8_STAGE(PG8_SA(b, h), (ptr) + ((h) ? hstep : (size_t)0), voffA); } while (0)
; #define PG8_LDA(dst, b, h) do { _Pragma("unroll") for (int m = 0; m < 4; ++m) _Pragma("unroll") for (int k = 0; k < 2; ++k) dst[m][k] = *(const PG8_LAS bf16x8*)(lds + PG8_SA(b, h) + aoff + m * 2048 + k * 1024); } while (0)
; #define PG8_LDB(dst, b, h) do { _Pragma("unroll") for (int n = 0; n < 2; ++n) _Pragma("unroll") for (int k = 0; k < 2; ++k) dst[n][k] = *(const PG8_LAS bf16x8*)(lds + PG8_SB(b, h) + boff + n * 2048 + k * 1024); } while (0)
; #define PG8_MMA(ai, bj, At, Bt) do { __builtin_amdgcn_s_setprio(1); _Pragma("unroll") for (int m = 0; m < 4; ++m) _Pragma("unroll") for (int n = 0; n < 2; ++n) _Pragma("unroll") for (int k = 0; k < 2; ++k) \
;         acc[ai][bj][m][n] = __builtin_amdgcn_mfma_f32_16x16x32_bf16(Bt[n][k], At[m][k], acc[ai][bj][m][n], 0, 0, 0); __builtin_amdgcn_s_setprio(0); } while (0)
; #define PG8_WAIT_V(n) asm volatile("s_waitcnt vmcnt(" #n ")" ::: "memory")
; #define PG8_WAIT_L(n) asm volatile("s_waitcnt lgkmcnt(" #n ")" ::: "memory")
; #define PG8_BAR __builtin_amdgcn_s_barrier()
; #define PG8_SCHED __builtin_amdgcn_sched_barrier(0)
; template <class Epi, class Sched, bool ALIGN_EPI = false, bool SP2 = false>
; __device__ __forceinline__ void gemm_phase(PG8_LAS unsigned char* lds, const Gemm g, const Sched& S, const Epi& E, const bool skip_epi = false) {
;     ...
;             PG8_WAIT_V(8); PG8_WAIT_L(0); PG8_BAR; PG8_MMA(1, 0, At, B0); PG8_MMA(1, 1, At, B1); PG8_BAR; PG8_SCHED;
;             PG8_LDB(B0, 1, 0); PG8_LDB(B1, 1, 1); PG8_SCHED; PG8_LDA(At, 1, 0); PG8_STAGE_A(0, 1, a2, true);
;             PG8_WAIT_V(8); PG8_WAIT_L(0); PG8_BAR; PG8_MMA(0, 0, At, B0); PG8_MMA(0, 1, At, B1); PG8_BAR; PG8_SCHED;
	s_setprio 3
	s_waitcnt lgkmcnt(0)
	v_mfma_f32_16x16x32_bf16 v[62:65], v[98:101], v[162:165], 0
	v_mfma_f32_16x16x32_bf16 v[58:61], v[122:125], v[162:165], 0
	v_mfma_f32_16x16x32_bf16 v[46:49], v[98:101], v[170:173], 0
	v_mfma_f32_16x16x32_bf16 v[42:45], v[122:125], v[170:173], 0
	v_mfma_f32_16x16x32_bf16 v[30:33], v[98:101], v[178:181], 0
	v_mfma_f32_16x16x32_bf16 v[26:29], v[122:125], v[178:181], 0
	v_mfma_f32_16x16x32_bf16 v[14:17], v[98:101], v[202:205], 0
	v_mfma_f32_16x16x32_bf16 v[10:13], v[122:125], v[202:205], 0
	v_mfma_f32_16x16x32_bf16 v[62:65], v[110:113], v[166:169], v[62:65]
	v_mfma_f32_16x16x32_bf16 v[58:61], v[130:133], v[166:169], v[58:61]
	v_mfma_f32_16x16x32_bf16 v[46:49], v[110:113], v[174:177], v[46:49]
	v_mfma_f32_16x16x32_bf16 v[42:45], v[130:133], v[174:177], v[42:45]
	v_mfma_f32_16x16x32_bf16 v[30:33], v[110:113], v[182:185], v[30:33]
	v_mfma_f32_16x16x32_bf16 v[26:29], v[130:133], v[182:185], v[26:29]
	v_mfma_f32_16x16x32_bf16 v[14:17], v[110:113], v[206:209], v[14:17]
	v_mfma_f32_16x16x32_bf16 v[10:13], v[130:133], v[206:209], v[10:13]
	s_setprio 0
	s_setprio 3
	v_mfma_f32_16x16x32_bf16 v[54:57], v[146:149], v[162:165], 0
	v_mfma_f32_16x16x32_bf16 v[50:53], v[154:157], v[162:165], 0
	v_mfma_f32_16x16x32_bf16 v[38:41], v[146:149], v[170:173], 0
	v_mfma_f32_16x16x32_bf16 v[34:37], v[154:157], v[170:173], 0
	v_mfma_f32_16x16x32_bf16 v[22:25], v[146:149], v[178:181], 0
	v_mfma_f32_16x16x32_bf16 v[18:21], v[154:157], v[178:181], 0
	v_mfma_f32_16x16x32_bf16 v[6:9], v[146:149], v[202:205], 0
	v_mfma_f32_16x16x32_bf16 v[2:5], v[154:157], v[202:205], 0
	v_mfma_f32_16x16x32_bf16 v[54:57], v[150:153], v[166:169], v[54:57]
	v_mfma_f32_16x16x32_bf16 v[50:53], v[158:161], v[166:169], v[50:53]
	v_mfma_f32_16x16x32_bf16 v[38:41], v[150:153], v[174:177], v[38:41]
	v_mfma_f32_16x16x32_bf16 v[34:37], v[158:161], v[174:177], v[34:37]
	v_mfma_f32_16x16x32_bf16 v[22:25], v[150:153], v[182:185], v[22:25]
	v_mfma_f32_16x16x32_bf16 v[18:21], v[158:161], v[182:185], v[18:21]
	v_mfma_f32_16x16x32_bf16 v[6:9], v[150:153], v[206:209], v[6:9]
	v_mfma_f32_16x16x32_bf16 v[2:5], v[158:161], v[206:209], v[2:5]
	s_setprio 0
	s_barrier
	s_add_i32 s64, 0, 0x18000
	s_add_i32 s65, 0, 0x1c000
	v_add_u32_e32 v130, s64, v220
	v_add_u32_e32 v158, s65, v220
	ds_read_b128 v[98:101], v130
	ds_read_b128 v[110:113], v130 offset:1024
	ds_read_b128 v[122:125], v130 offset:2048
	ds_read_b128 v[130:133], v130 offset:3072
	ds_read_b128 v[146:149], v158
	ds_read_b128 v[150:153], v158 offset:1024
	ds_read_b128 v[154:157], v158 offset:2048
	ds_read_b128 v[158:161], v158 offset:3072
	s_add_u32 s38, s38, 0x40000
	s_addc_u32 s39, s39, 0
	s_mov_b32 m0, s45
	ds_read_b128 v[162:165], v227 offset:32768
	ds_read_b128 v[166:169], v227 offset:33792
	ds_read_b128 v[170:173], v227 offset:34816
	ds_read_b128 v[174:177], v227 offset:35840
	ds_read_b128 v[178:181], v227 offset:36864
	ds_read_b128 v[182:185], v227 offset:37888
	ds_read_b128 v[202:205], v227 offset:38912
	ds_read_b128 v[206:209], v227 offset:39936
	global_load_lds_dwordx4 v186, s[38:39]
	s_mov_b32 m0, s48
	s_nop 0
	global_load_lds_dwordx4 v190, s[38:39]
	s_waitcnt vmcnt(8)
	s_waitcnt lgkmcnt(0)
	s_barrier
	s_setprio 3
	s_waitcnt lgkmcnt(0)
	v_mfma_f32_16x16x32_bf16 v[142:145], v[98:101], v[162:165], v[142:145]
	v_mfma_f32_16x16x32_bf16 v[138:141], v[122:125], v[162:165], v[138:141]
	v_mfma_f32_16x16x32_bf16 v[118:121], v[98:101], v[170:173], v[118:121]
	v_mfma_f32_16x16x32_bf16 v[114:117], v[122:125], v[170:173], v[114:117]
	v_mfma_f32_16x16x32_bf16 v[94:97], v[98:101], v[178:181], v[94:97]
	v_mfma_f32_16x16x32_bf16 v[90:93], v[122:125], v[178:181], v[90:93]
	v_mfma_f32_16x16x32_bf16 v[78:81], v[98:101], v[202:205], v[78:81]
	v_mfma_f32_16x16x32_bf16 v[74:77], v[122:125], v[202:205], v[74:77]
	v_mfma_f32_16x16x32_bf16 v[142:145], v[110:113], v[166:169], v[142:145]
	v_mfma_f32_16x16x32_bf16 v[138:141], v[130:133], v[166:169], v[138:141]
	v_mfma_f32_16x16x32_bf16 v[118:121], v[110:113], v[174:177], v[118:121]
	v_mfma_f32_16x16x32_bf16 v[114:117], v[130:133], v[174:177], v[114:117]
	v_mfma_f32_16x16x32_bf16 v[94:97], v[110:113], v[182:185], v[94:97]
	v_mfma_f32_16x16x32_bf16 v[90:93], v[130:133], v[182:185], v[90:93]
	v_mfma_f32_16x16x32_bf16 v[78:81], v[110:113], v[206:209], v[78:81]
	v_mfma_f32_16x16x32_bf16 v[74:77], v[130:133], v[206:209], v[74:77]
	s_setprio 0
	s_setprio 3
	v_mfma_f32_16x16x32_bf16 v[134:137], v[146:149], v[162:165], v[134:137]
	v_mfma_f32_16x16x32_bf16 v[126:129], v[154:157], v[162:165], v[126:129]
	v_mfma_f32_16x16x32_bf16 v[106:109], v[146:149], v[170:173], v[106:109]
	v_mfma_f32_16x16x32_bf16 v[102:105], v[154:157], v[170:173], v[102:105]
	v_mfma_f32_16x16x32_bf16 v[86:89], v[146:149], v[178:181], v[86:89]
	v_mfma_f32_16x16x32_bf16 v[82:85], v[154:157], v[178:181], v[82:85]
	v_mfma_f32_16x16x32_bf16 v[70:73], v[146:149], v[202:205], v[70:73]
	v_mfma_f32_16x16x32_bf16 v[66:69], v[154:157], v[202:205], v[66:69]
	v_mfma_f32_16x16x32_bf16 v[134:137], v[150:153], v[166:169], v[134:137]
	v_mfma_f32_16x16x32_bf16 v[126:129], v[158:161], v[166:169], v[126:129]
	v_mfma_f32_16x16x32_bf16 v[106:109], v[150:153], v[174:177], v[106:109]
	v_mfma_f32_16x16x32_bf16 v[102:105], v[158:161], v[174:177], v[102:105]
	v_mfma_f32_16x16x32_bf16 v[86:89], v[150:153], v[182:185], v[86:89]
	v_mfma_f32_16x16x32_bf16 v[82:85], v[158:161], v[182:185], v[82:85]
	v_mfma_f32_16x16x32_bf16 v[70:73], v[150:153], v[206:209], v[70:73]
	v_mfma_f32_16x16x32_bf16 v[66:69], v[158:161], v[206:209], v[66:69]
	s_setprio 0
	s_barrier
; #define PG8_STAGE_A(b, h, ptr, NX) do { if constexpr (Sched::GATHER) { unsigned gs_[2]; gs_[0] = ((NX) && last_) ? gN[h][0] : gA[h][0]; gs_[1] = ((NX) && last_) ? gN[h][1] : gA[h][1]; PG8_STAGE(PG8_SA(b, h), ptr, gs_); } \
;         else PG8_STAGE(PG8_SA(b, h), (ptr) + ((h) ? hstep : (size_t)0), voffA); } while (0)
; #define PG8_STAGE(bufoff, gbase, voff) do { _Pragma("unroll") for (int _i = 0; _i < 2; ++_i) \
;         __builtin_amdgcn_global_load_lds((const unsigned*)((const char*)(gbase) + (voff)[_i]), (PG8_LAS unsigned*)(lds + (bufoff) + ldsw + _i * 8192), 16, 0, 0); } while (0)
; #define PG8_LDA(dst, b, h) do { _Pragma("unroll") for (int m = 0; m < 4; ++m) _Pragma("unroll") for (int k = 0; k < 2; ++k) dst[m][k] = *(const PG8_LAS bf16x8*)(lds + PG8_SA(b, h) + aoff + m * 2048 + k * 1024); } while (0)
; #define PG8_LDB(dst, b, h) do { _Pragma("unroll") for (int n = 0; n < 2; ++n) _Pragma("unroll") for (int k = 0; k < 2; ++k) dst[n][k] = *(const PG8_LAS bf16x8*)(lds + PG8_SB(b, h) + boff + n * 2048 + k * 1024); } while (0)
; #define PG8_WAIT_V(n) asm volatile("s_waitcnt vmcnt(" #n ")" ::: "memory")
; #define PG8_BAR __builtin_amdgcn_s_barrier()
; template <class Epi, class Sched, bool ALIGN_EPI = false, bool SP2 = false>
; __device__ __forceinline__ void gemm_phase(PG8_LAS unsigned char* lds, const Gemm g, const Sched& S, const Epi& E, const bool skip_epi = false) {
;     ...
;             PG8_LDB(B0, 0, 0); PG8_LDB(B1, 0, 1); PG8_SCHED; PG8_LDA(At, 0, 0); PG8_STAGE_A(1, 1, a1, false);
;             PG8_WAIT_V(8); PG8_WAIT_L(0); PG8_BAR; PG8_MMA(0, 0, At, B0); PG8_MMA(0, 1, At, B1); PG8_BAR; PG8_SCHED;
;             PG8_LDA(At, 0, 1); PG8_STAGE(PG8_SB(0, 0), b2, voffB); PG8_STAGE(PG8_SB(0, 1), b2 + hstep, voffB); PG8_STAGE_A(0, 0, a2, true);
;             PG8_WAIT_V(8); PG8_WAIT_L(0); PG8_BAR; PG8_MMA(1, 0, At, B0); PG8_MMA(1, 1, At, B1); PG8_BAR; PG8_SCHED;
;             PG8_LDB(B0, 1, 0); PG8_LDB(B1, 1, 1); PG8_SCHED; PG8_LDA(At, 1, 0); PG8_STAGE_A(0, 1, a2, true);
;             PG8_WAIT_V(8); PG8_WAIT_L(0); PG8_BAR; PG8_MMA(0, 0, At, B0); PG8_MMA(0, 1, At, B1); PG8_BAR; PG8_SCHED;
;             PG8_LDA(At, 1, 1); PG8_STAGE(PG8_SB(1, 0), b3, voffB); PG8_STAGE(PG8_SB(1, 1), b3 + hstep, voffB); PG8_STAGE_A(1, 0, a3, true);
;             PG8_WAIT_V(8); PG8_WAIT_L(0); PG8_BAR; PG8_MMA(1, 0, At, B0); PG8_MMA(1, 1, At, B1); PG8_BAR; PG8_SCHED;
	s_add_i32 s38, s64, s40
	s_add_i32 m0, s38, 0xffffff80
	ds_read_b128 v[162:165], v227 offset:49152
	ds_read_b128 v[166:169], v227 offset:50176
	ds_read_b128 v[170:173], v227 offset:51200
	ds_read_b128 v[174:177], v227 offset:52224
	ds_read_b128 v[178:181], v227 offset:53248
	ds_read_b128 v[182:185], v227 offset:54272
	ds_read_b128 v[202:205], v227 offset:55296
	ds_read_b128 v[206:209], v227 offset:56320
	global_load_lds_dwordx4 v[210:211], off offset:128
	s_add_i32 m0, s38, 0x1f80
	s_add_u32 s36, s36, 0x40080
	s_addc_u32 s37, s37, 0
	s_add_i32 s38, s65, s40
	global_load_lds_dwordx4 v[212:213], off offset:128
	s_mov_b32 m0, s38
	s_nop 0
	global_load_lds_dwordx4 v188, s[36:37]
	s_add_i32 m0, s38, 0x2000
	s_nop 0
	global_load_lds_dwordx4 v192, s[36:37]
	s_add_i32 m0, s53, 0xffffff80
	s_nop 0
	global_load_lds_dwordx4 v[214:215], off offset:128
	s_add_i32 m0, s54, 0xffffff80
	s_nop 0
	global_load_lds_dwordx4 v[216:217], off offset:128
	s_waitcnt vmcnt(8)
	s_waitcnt lgkmcnt(0)
	s_barrier
	s_setprio 3
	s_waitcnt lgkmcnt(0)
	v_mfma_f32_16x16x32_bf16 v[62:65], v[98:101], v[162:165], v[62:65]
	v_mfma_f32_16x16x32_bf16 v[58:61], v[122:125], v[162:165], v[58:61]
	v_mfma_f32_16x16x32_bf16 v[46:49], v[98:101], v[170:173], v[46:49]
	v_mfma_f32_16x16x32_bf16 v[42:45], v[122:125], v[170:173], v[42:45]
	v_mfma_f32_16x16x32_bf16 v[30:33], v[98:101], v[178:181], v[30:33]
	v_mfma_f32_16x16x32_bf16 v[26:29], v[122:125], v[178:181], v[26:29]
	v_mfma_f32_16x16x32_bf16 v[14:17], v[98:101], v[202:205], v[14:17]
	v_mfma_f32_16x16x32_bf16 v[10:13], v[122:125], v[202:205], v[10:13]
	v_mfma_f32_16x16x32_bf16 v[62:65], v[110:113], v[166:169], v[62:65]
	v_mfma_f32_16x16x32_bf16 v[58:61], v[130:133], v[166:169], v[58:61]
	v_mfma_f32_16x16x32_bf16 v[46:49], v[110:113], v[174:177], v[46:49]
	v_mfma_f32_16x16x32_bf16 v[42:45], v[130:133], v[174:177], v[42:45]
	v_mfma_f32_16x16x32_bf16 v[30:33], v[110:113], v[182:185], v[30:33]
	v_mfma_f32_16x16x32_bf16 v[26:29], v[130:133], v[182:185], v[26:29]
	v_mfma_f32_16x16x32_bf16 v[14:17], v[110:113], v[206:209], v[14:17]
	v_mfma_f32_16x16x32_bf16 v[10:13], v[130:133], v[206:209], v[10:13]
	s_setprio 0
	s_setprio 3
	v_mfma_f32_16x16x32_bf16 v[54:57], v[146:149], v[162:165], v[54:57]
	v_mfma_f32_16x16x32_bf16 v[50:53], v[154:157], v[162:165], v[50:53]
	v_mfma_f32_16x16x32_bf16 v[38:41], v[146:149], v[170:173], v[38:41]
	v_mfma_f32_16x16x32_bf16 v[34:37], v[154:157], v[170:173], v[34:37]
	v_mfma_f32_16x16x32_bf16 v[22:25], v[146:149], v[178:181], v[22:25]
	v_mfma_f32_16x16x32_bf16 v[18:21], v[154:157], v[178:181], v[18:21]
	v_mfma_f32_16x16x32_bf16 v[6:9], v[146:149], v[202:205], v[6:9]
	v_mfma_f32_16x16x32_bf16 v[2:5], v[154:157], v[202:205], v[2:5]
	v_mfma_f32_16x16x32_bf16 v[54:57], v[150:153], v[166:169], v[54:57]
	v_mfma_f32_16x16x32_bf16 v[50:53], v[158:161], v[166:169], v[50:53]
	v_mfma_f32_16x16x32_bf16 v[38:41], v[150:153], v[174:177], v[38:41]
	v_mfma_f32_16x16x32_bf16 v[34:37], v[158:161], v[174:177], v[34:37]
	v_mfma_f32_16x16x32_bf16 v[22:25], v[150:153], v[182:185], v[22:25]
	v_mfma_f32_16x16x32_bf16 v[18:21], v[158:161], v[182:185], v[18:21]
	v_mfma_f32_16x16x32_bf16 v[6:9], v[150:153], v[206:209], v[6:9]
	v_mfma_f32_16x16x32_bf16 v[2:5], v[158:161], v[206:209], v[2:5]
	s_setprio 0
	s_barrier
	s_add_i32 s63, s63, 2
	s_add_u32 s34, s34, 0x100
	s_addc_u32 s35, s35, 0
	s_add_u32 s61, s61, 0x100
	s_addc_u32 s62, s62, 0
	s_cmp_gt_u32 s63, 13
.LBB0_1324:
	ds_read_b128 v[98:101], v225
	ds_read_b128 v[110:113], v225 offset:1024
	ds_read_b128 v[122:125], v225 offset:2048
	ds_read_b128 v[130:133], v225 offset:3072
	ds_read_b128 v[146:149], v226
	ds_read_b128 v[150:153], v226 offset:1024
	ds_read_b128 v[154:157], v226 offset:2048
	ds_read_b128 v[158:161], v226 offset:3072
	s_add_u32 s36, s34, 0xfffc0080
	s_addc_u32 s37, s35, -1
	s_cmp_eq_u32 s63, 12
	s_cselect_b32 s39, s25, s37
	s_cselect_b32 s38, s31, s36
	s_cselect_b32 s37, s23, s62
	s_cselect_b32 s36, s60, s61
	s_add_i32 m0, s41, 0xc000
	ds_read_b128 v[162:165], v227
	ds_read_b128 v[166:169], v227 offset:1024
	ds_read_b128 v[170:173], v227 offset:2048
	ds_read_b128 v[174:177], v227 offset:3072
	ds_read_b128 v[178:181], v227 offset:4096
	ds_read_b128 v[182:185], v227 offset:5120
	ds_read_b128 v[202:205], v227 offset:6144
	ds_read_b128 v[206:209], v227 offset:7168
	global_load_lds_dwordx4 v194, s[34:35]
	s_add_i32 m0, s41, 0xe000
	s_nop 0
	global_load_lds_dwordx4 v196, s[34:35]
	s_waitcnt vmcnt(8)
	s_waitcnt lgkmcnt(0)
	s_barrier
; #define PG8_STAGE_A(b, h, ptr, NX) do { if constexpr (Sched::GATHER) { unsigned gs_[2]; gs_[0] = ((NX) && last_) ? gN[h][0] : gA[h][0]; gs_[1] = ((NX) && last_) ? gN[h][1] : gA[h][1]; PG8_STAGE(PG8_SA(b, h), ptr, gs_); } \
;         else PG8_STAGE(PG8_SA(b, h), (ptr) + ((h) ? hstep : (size_t)0), voffA); } while (0)
; #define PG8_STAGE(bufoff, gbase, voff) do { _Pragma("unroll") for (int _i = 0; _i < 2; ++_i) \
;         __builtin_amdgcn_global_load_lds((const unsigned*)((const char*)(gbase) + (voff)[_i]), (PG8_LAS unsigned*)(lds + (bufoff) + ldsw + _i * 8192), 16, 0, 0); } while (0)
; #define PG8_LDA(dst, b, h) do { _Pragma("unroll") for (int m = 0; m < 4; ++m) _Pragma("unroll") for (int k = 0; k < 2; ++k) dst[m][k] = *(const PG8_LAS bf16x8*)(lds + PG8_SA(b, h) + aoff + m * 2048 + k * 1024); } while (0)
; #define PG8_MMA(ai, bj, At, Bt) do { __builtin_amdgcn_s_setprio(1); _Pragma("unroll") for (int m = 0; m < 4; ++m) _Pragma("unroll") for (int n = 0; n < 2; ++n) _Pragma("unroll") for (int k = 0; k < 2; ++k) \
;         acc[ai][bj][m][n] = __builtin_amdgcn_mfma_f32_16x16x32_bf16(Bt[n][k], At[m][k], acc[ai][bj][m][n], 0, 0, 0); __builtin_amdgcn_s_setprio(0); } while (0)
; #define PG8_WAIT_V(n) asm volatile("s_waitcnt vmcnt(" #n ")" ::: "memory")
; #define PG8_WAIT_L(n) asm volatile("s_waitcnt lgkmcnt(" #n ")" ::: "memory")
; #define PG8_BAR __builtin_amdgcn_s_barrier()
; #define PG8_SCHED __builtin_amdgcn_sched_barrier(0)
; template <class Epi, class Sched, bool ALIGN_EPI = false, bool SP2 = false>
; __device__ __forceinline__ void gemm_phase(PG8_LAS unsigned char* lds, const Gemm g, const Sched& S, const Epi& E, const bool skip_epi = false) {
;     ...
;             PG8_WAIT_V(8); PG8_WAIT_L(0); PG8_BAR; PG8_MMA(0, 0, At, B0); PG8_MMA(0, 1, At, B1); PG8_BAR; PG8_SCHED;
;             PG8_LDA(At, 0, 1); PG8_STAGE(PG8_SB(0, 0), b2, voffB); PG8_STAGE(PG8_SB(0, 1), b2 + hstep, voffB); PG8_STAGE_A(0, 0, a2, true);
;             PG8_WAIT_V(8); PG8_WAIT_L(0); PG8_BAR; PG8_MMA(1, 0, At, B0); PG8_MMA(1, 1, At, B1); PG8_BAR; PG8_SCHED;
	s_setprio 3
	s_waitcnt lgkmcnt(0)
	v_mfma_f32_16x16x32_bf16 v[142:145], v[98:101], v[162:165], v[142:145]
	v_mfma_f32_16x16x32_bf16 v[138:141], v[122:125], v[162:165], v[138:141]
	v_mfma_f32_16x16x32_bf16 v[118:121], v[98:101], v[170:173], v[118:121]
	v_mfma_f32_16x16x32_bf16 v[114:117], v[122:125], v[170:173], v[114:117]
	v_lshl_add_u64 v[210:211], s[36:37], 0, v[188:189]
	v_mfma_f32_16x16x32_bf16 v[94:97], v[98:101], v[178:181], v[94:97]
	v_mfma_f32_16x16x32_bf16 v[90:93], v[122:125], v[178:181], v[90:93]
	v_lshl_add_u64 v[212:213], s[36:37], 0, v[192:193]
	v_mfma_f32_16x16x32_bf16 v[78:81], v[98:101], v[202:205], v[78:81]
	v_mfma_f32_16x16x32_bf16 v[74:77], v[122:125], v[202:205], v[74:77]
	v_lshl_add_u64 v[216:217], s[38:39], 0, v[190:191]
	v_mfma_f32_16x16x32_bf16 v[142:145], v[110:113], v[166:169], v[142:145]
	v_mfma_f32_16x16x32_bf16 v[138:141], v[130:133], v[166:169], v[138:141]
	v_lshl_add_u64 v[214:215], s[38:39], 0, v[186:187]
	v_mfma_f32_16x16x32_bf16 v[118:121], v[110:113], v[174:177], v[118:121]
	v_mfma_f32_16x16x32_bf16 v[114:117], v[130:133], v[174:177], v[114:117]
	v_mfma_f32_16x16x32_bf16 v[94:97], v[110:113], v[182:185], v[94:97]
	v_mfma_f32_16x16x32_bf16 v[90:93], v[130:133], v[182:185], v[90:93]
	v_mfma_f32_16x16x32_bf16 v[78:81], v[110:113], v[206:209], v[78:81]
	v_mfma_f32_16x16x32_bf16 v[74:77], v[130:133], v[206:209], v[74:77]
	s_setprio 0
	s_setprio 3
	v_mfma_f32_16x16x32_bf16 v[134:137], v[146:149], v[162:165], v[134:137]
	v_mfma_f32_16x16x32_bf16 v[126:129], v[154:157], v[162:165], v[126:129]
	v_mfma_f32_16x16x32_bf16 v[106:109], v[146:149], v[170:173], v[106:109]
	v_mfma_f32_16x16x32_bf16 v[102:105], v[154:157], v[170:173], v[102:105]
	v_mfma_f32_16x16x32_bf16 v[86:89], v[146:149], v[178:181], v[86:89]
	v_mfma_f32_16x16x32_bf16 v[82:85], v[154:157], v[178:181], v[82:85]
	v_mfma_f32_16x16x32_bf16 v[70:73], v[146:149], v[202:205], v[70:73]
	v_mfma_f32_16x16x32_bf16 v[66:69], v[154:157], v[202:205], v[66:69]
	v_mfma_f32_16x16x32_bf16 v[134:137], v[150:153], v[166:169], v[134:137]
	v_mfma_f32_16x16x32_bf16 v[126:129], v[158:161], v[166:169], v[126:129]
	v_mfma_f32_16x16x32_bf16 v[106:109], v[150:153], v[174:177], v[106:109]
	v_mfma_f32_16x16x32_bf16 v[102:105], v[158:161], v[174:177], v[102:105]
	v_mfma_f32_16x16x32_bf16 v[86:89], v[150:153], v[182:185], v[86:89]
	v_mfma_f32_16x16x32_bf16 v[82:85], v[158:161], v[182:185], v[82:85]
	v_mfma_f32_16x16x32_bf16 v[70:73], v[150:153], v[206:209], v[70:73]
	v_mfma_f32_16x16x32_bf16 v[66:69], v[158:161], v[206:209], v[66:69]
	s_setprio 0
	s_barrier
	s_add_i32 s64, s57, s40
	s_mov_b32 m0, s64
	ds_read_b128 v[162:165], v227 offset:16384
	ds_read_b128 v[166:169], v227 offset:17408
	ds_read_b128 v[170:173], v227 offset:18432
	ds_read_b128 v[174:177], v227 offset:19456
	ds_read_b128 v[178:181], v227 offset:20480
	ds_read_b128 v[182:185], v227 offset:21504
	ds_read_b128 v[202:205], v227 offset:22528
	ds_read_b128 v[206:209], v227 offset:23552
	global_load_lds_dwordx4 v[210:211], off
	s_add_i32 m0, s64, 0x2000
	s_add_u32 s64, s36, 0x40000
	s_addc_u32 s65, s37, 0
	s_add_i32 s66, s58, s40
	global_load_lds_dwordx4 v[212:213], off
	s_mov_b32 m0, s66
	s_nop 0
	global_load_lds_dwordx4 v188, s[64:65]
	s_add_i32 m0, s66, 0x2000
	s_nop 0
	global_load_lds_dwordx4 v192, s[64:65]
	s_mov_b32 m0, s41
	s_nop 0
	global_load_lds_dwordx4 v[214:215], off
	s_mov_b32 m0, s44
	s_nop 0
	global_load_lds_dwordx4 v[216:217], off
	s_waitcnt vmcnt(8)
	s_waitcnt lgkmcnt(0)
	s_barrier
	s_setprio 3
	s_waitcnt lgkmcnt(0)
	v_mfma_f32_16x16x32_bf16 v[62:65], v[98:101], v[162:165], v[62:65]
	v_mfma_f32_16x16x32_bf16 v[58:61], v[122:125], v[162:165], v[58:61]
	v_mfma_f32_16x16x32_bf16 v[46:49], v[98:101], v[170:173], v[46:49]
	v_mfma_f32_16x16x32_bf16 v[42:45], v[122:125], v[170:173], v[42:45]
	v_mfma_f32_16x16x32_bf16 v[30:33], v[98:101], v[178:181], v[30:33]
	v_mfma_f32_16x16x32_bf16 v[26:29], v[122:125], v[178:181], v[26:29]
	v_mfma_f32_16x16x32_bf16 v[14:17], v[98:101], v[202:205], v[14:17]
	v_mfma_f32_16x16x32_bf16 v[10:13], v[122:125], v[202:205], v[10:13]
	v_mfma_f32_16x16x32_bf16 v[62:65], v[110:113], v[166:169], v[62:65]
	v_mfma_f32_16x16x32_bf16 v[58:61], v[130:133], v[166:169], v[58:61]
	v_mfma_f32_16x16x32_bf16 v[46:49], v[110:113], v[174:177], v[46:49]
	v_mfma_f32_16x16x32_bf16 v[42:45], v[130:133], v[174:177], v[42:45]
	v_mfma_f32_16x16x32_bf16 v[30:33], v[110:113], v[182:185], v[30:33]
	v_mfma_f32_16x16x32_bf16 v[26:29], v[130:133], v[182:185], v[26:29]
	v_mfma_f32_16x16x32_bf16 v[14:17], v[110:113], v[206:209], v[14:17]
	v_mfma_f32_16x16x32_bf16 v[10:13], v[130:133], v[206:209], v[10:13]
	s_setprio 0
	s_setprio 3
	v_mfma_f32_16x16x32_bf16 v[54:57], v[146:149], v[162:165], v[54:57]
	v_mfma_f32_16x16x32_bf16 v[50:53], v[154:157], v[162:165], v[50:53]
	v_mfma_f32_16x16x32_bf16 v[38:41], v[146:149], v[170:173], v[38:41]
	v_mfma_f32_16x16x32_bf16 v[34:37], v[154:157], v[170:173], v[34:37]
	v_mfma_f32_16x16x32_bf16 v[22:25], v[146:149], v[178:181], v[22:25]
	v_mfma_f32_16x16x32_bf16 v[18:21], v[154:157], v[178:181], v[18:21]
	v_mfma_f32_16x16x32_bf16 v[6:9], v[146:149], v[202:205], v[6:9]
	v_mfma_f32_16x16x32_bf16 v[2:5], v[154:157], v[202:205], v[2:5]
	v_mfma_f32_16x16x32_bf16 v[54:57], v[150:153], v[166:169], v[54:57]
	v_mfma_f32_16x16x32_bf16 v[50:53], v[158:161], v[166:169], v[50:53]
	v_mfma_f32_16x16x32_bf16 v[38:41], v[150:153], v[174:177], v[38:41]
	v_mfma_f32_16x16x32_bf16 v[34:37], v[158:161], v[174:177], v[34:37]
	v_mfma_f32_16x16x32_bf16 v[22:25], v[150:153], v[182:185], v[22:25]
	v_mfma_f32_16x16x32_bf16 v[18:21], v[158:161], v[182:185], v[18:21]
	v_mfma_f32_16x16x32_bf16 v[6:9], v[150:153], v[206:209], v[6:9]
	v_mfma_f32_16x16x32_bf16 v[2:5], v[158:161], v[206:209], v[2:5]
	s_setprio 0
	s_barrier
; #define PG8_STAGE_A(b, h, ptr, NX) do { if constexpr (Sched::GATHER) { unsigned gs_[2]; gs_[0] = ((NX) && last_) ? gN[h][0] : gA[h][0]; gs_[1] = ((NX) && last_) ? gN[h][1] : gA[h][1]; PG8_STAGE(PG8_SA(b, h), ptr, gs_); } \
;         else PG8_STAGE(PG8_SA(b, h), (ptr) + ((h) ? hstep : (size_t)0), voffA); } while (0)
; #define PG8_STAGE(bufoff, gbase, voff) do { _Pragma("unroll") for (int _i = 0; _i < 2; ++_i) \
;         __builtin_amdgcn_global_load_lds((const unsigned*)((const char*)(gbase) + (voff)[_i]), (PG8_LAS unsigned*)(lds + (bufoff) + ldsw + _i * 8192), 16, 0, 0); } while (0)
; #define PG8_LDA(dst, b, h) do { _Pragma("unroll") for (int m = 0; m < 4; ++m) _Pragma("unroll") for (int k = 0; k < 2; ++k) dst[m][k] = *(const PG8_LAS bf16x8*)(lds + PG8_SA(b, h) + aoff + m * 2048 + k * 1024); } while (0)
; #define PG8_LDB(dst, b, h) do { _Pragma("unroll") for (int n = 0; n < 2; ++n) _Pragma("unroll") for (int k = 0; k < 2; ++k) dst[n][k] = *(const PG8_LAS bf16x8*)(lds + PG8_SB(b, h) + boff + n * 2048 + k * 1024); } while (0)
; #define PG8_MMA(ai, bj, At, Bt) do { __builtin_amdgcn_s_setprio(1); _Pragma("unroll") for (int m = 0; m < 4; ++m) _Pragma("unroll") for (int n = 0; n < 2; ++n) _Pragma("unroll") for (int k = 0; k < 2; ++k) \
;         acc[ai][bj][m][n] = __builtin_amdgcn_mfma_f32_16x16x32_bf16(Bt[n][k], At[m][k], acc[ai][bj][m][n], 0, 0, 0); __builtin_amdgcn_s_setprio(0); } while (0)
; #define PG8_WAIT_V(n) asm volatile("s_waitcnt vmcnt(" #n ")" ::: "memory")
; #define PG8_WAIT_L(n) asm volatile("s_waitcnt lgkmcnt(" #n ")" ::: "memory")
; #define PG8_BAR __builtin_amdgcn_s_barrier()
; #define PG8_SCHED __builtin_amdgcn_sched_barrier(0)
; template <class Epi, class Sched, bool ALIGN_EPI = false, bool SP2 = false>
; __device__ __forceinline__ void gemm_phase(PG8_LAS unsigned char* lds, const Gemm g, const Sched& S, const Epi& E, const bool skip_epi = false) {
;     ...
;             PG8_LDB(B0, 1, 0); PG8_LDB(B1, 1, 1); PG8_SCHED; PG8_LDA(At, 1, 0); PG8_STAGE_A(0, 1, a2, true);
;             PG8_WAIT_V(8); PG8_WAIT_L(0); PG8_BAR; PG8_MMA(0, 0, At, B0); PG8_MMA(0, 1, At, B1); PG8_BAR; PG8_SCHED;
;             PG8_LDA(At, 1, 1); PG8_STAGE(PG8_SB(1, 0), b3, voffB); PG8_STAGE(PG8_SB(1, 1), b3 + hstep, voffB); PG8_STAGE_A(1, 0, a3, true);
;             PG8_WAIT_V(8); PG8_WAIT_L(0); PG8_BAR; PG8_MMA(1, 0, At, B0); PG8_MMA(1, 1, At, B1); PG8_BAR; PG8_SCHED;
	s_add_i32 s64, 0, 0x18000
	s_add_i32 s65, 0, 0x1c000
	v_add_u32_e32 v130, s64, v220
	v_add_u32_e32 v158, s65, v220
	ds_read_b128 v[98:101], v130
	ds_read_b128 v[110:113], v130 offset:1024
	ds_read_b128 v[122:125], v130 offset:2048
	ds_read_b128 v[130:133], v130 offset:3072
	ds_read_b128 v[146:149], v158
	ds_read_b128 v[150:153], v158 offset:1024
	ds_read_b128 v[154:157], v158 offset:2048
	ds_read_b128 v[158:161], v158 offset:3072
	s_add_u32 s38, s38, 0x40000
	s_addc_u32 s39, s39, 0
	s_mov_b32 m0, s45
	ds_read_b128 v[162:165], v227 offset:32768
	ds_read_b128 v[166:169], v227 offset:33792
	ds_read_b128 v[170:173], v227 offset:34816
	ds_read_b128 v[174:177], v227 offset:35840
	ds_read_b128 v[178:181], v227 offset:36864
	ds_read_b128 v[182:185], v227 offset:37888
	ds_read_b128 v[202:205], v227 offset:38912
	ds_read_b128 v[206:209], v227 offset:39936
	global_load_lds_dwordx4 v186, s[38:39]
	s_mov_b32 m0, s48
	s_nop 0
	global_load_lds_dwordx4 v190, s[38:39]
	s_waitcnt vmcnt(8)
	s_waitcnt lgkmcnt(0)
	s_barrier
	s_setprio 3
	s_waitcnt lgkmcnt(0)
	v_mfma_f32_16x16x32_bf16 v[142:145], v[98:101], v[162:165], v[142:145]
	v_mfma_f32_16x16x32_bf16 v[138:141], v[122:125], v[162:165], v[138:141]
	v_mfma_f32_16x16x32_bf16 v[118:121], v[98:101], v[170:173], v[118:121]
	v_mfma_f32_16x16x32_bf16 v[114:117], v[122:125], v[170:173], v[114:117]
	v_mfma_f32_16x16x32_bf16 v[94:97], v[98:101], v[178:181], v[94:97]
	v_mfma_f32_16x16x32_bf16 v[90:93], v[122:125], v[178:181], v[90:93]
	v_mfma_f32_16x16x32_bf16 v[78:81], v[98:101], v[202:205], v[78:81]
	v_mfma_f32_16x16x32_bf16 v[74:77], v[122:125], v[202:205], v[74:77]
	v_mfma_f32_16x16x32_bf16 v[142:145], v[110:113], v[166:169], v[142:145]
	v_mfma_f32_16x16x32_bf16 v[138:141], v[130:133], v[166:169], v[138:141]
	v_mfma_f32_16x16x32_bf16 v[118:121], v[110:113], v[174:177], v[118:121]
	v_mfma_f32_16x16x32_bf16 v[114:117], v[130:133], v[174:177], v[114:117]
	v_mfma_f32_16x16x32_bf16 v[94:97], v[110:113], v[182:185], v[94:97]
	v_mfma_f32_16x16x32_bf16 v[90:93], v[130:133], v[182:185], v[90:93]
	v_mfma_f32_16x16x32_bf16 v[78:81], v[110:113], v[206:209], v[78:81]
	v_mfma_f32_16x16x32_bf16 v[74:77], v[130:133], v[206:209], v[74:77]
	s_setprio 0
	s_setprio 3
	v_mfma_f32_16x16x32_bf16 v[134:137], v[146:149], v[162:165], v[134:137]
	v_mfma_f32_16x16x32_bf16 v[126:129], v[154:157], v[162:165], v[126:129]
	v_mfma_f32_16x16x32_bf16 v[106:109], v[146:149], v[170:173], v[106:109]
	v_mfma_f32_16x16x32_bf16 v[102:105], v[154:157], v[170:173], v[102:105]
	v_mfma_f32_16x16x32_bf16 v[86:89], v[146:149], v[178:181], v[86:89]
	v_mfma_f32_16x16x32_bf16 v[82:85], v[154:157], v[178:181], v[82:85]
	v_mfma_f32_16x16x32_bf16 v[70:73], v[146:149], v[202:205], v[70:73]
	v_mfma_f32_16x16x32_bf16 v[66:69], v[154:157], v[202:205], v[66:69]
	v_mfma_f32_16x16x32_bf16 v[134:137], v[150:153], v[166:169], v[134:137]
	v_mfma_f32_16x16x32_bf16 v[126:129], v[158:161], v[166:169], v[126:129]
	v_mfma_f32_16x16x32_bf16 v[106:109], v[150:153], v[174:177], v[106:109]
	v_mfma_f32_16x16x32_bf16 v[102:105], v[158:161], v[174:177], v[102:105]
	v_mfma_f32_16x16x32_bf16 v[86:89], v[150:153], v[182:185], v[86:89]
	v_mfma_f32_16x16x32_bf16 v[82:85], v[158:161], v[182:185], v[82:85]
	v_mfma_f32_16x16x32_bf16 v[70:73], v[150:153], v[206:209], v[70:73]
	v_mfma_f32_16x16x32_bf16 v[66:69], v[158:161], v[206:209], v[66:69]
	s_setprio 0
	s_barrier
	s_add_i32 s38, s64, s40
	s_add_i32 m0, s38, 0xffffff80
	ds_read_b128 v[162:165], v227 offset:49152
	ds_read_b128 v[166:169], v227 offset:50176
	ds_read_b128 v[170:173], v227 offset:51200
	ds_read_b128 v[174:177], v227 offset:52224
	ds_read_b128 v[178:181], v227 offset:53248
	ds_read_b128 v[182:185], v227 offset:54272
	ds_read_b128 v[202:205], v227 offset:55296
	ds_read_b128 v[206:209], v227 offset:56320
	global_load_lds_dwordx4 v[210:211], off offset:128
	s_add_i32 m0, s38, 0x1f80
	s_add_u32 s36, s36, 0x40080
	s_addc_u32 s37, s37, 0
	s_add_i32 s38, s65, s40
	global_load_lds_dwordx4 v[212:213], off offset:128
	s_mov_b32 m0, s38
	s_nop 0
	global_load_lds_dwordx4 v188, s[36:37]
	s_add_i32 m0, s38, 0x2000
	s_nop 0
	global_load_lds_dwordx4 v192, s[36:37]
	s_add_i32 m0, s53, 0xffffff80
	s_nop 0
	global_load_lds_dwordx4 v[214:215], off offset:128
	s_add_i32 m0, s54, 0xffffff80
	s_nop 0
	global_load_lds_dwordx4 v[216:217], off offset:128
	s_waitcnt vmcnt(8)
	s_waitcnt lgkmcnt(0)
	s_barrier
	s_setprio 3
	s_waitcnt lgkmcnt(0)
	v_mfma_f32_16x16x32_bf16 v[62:65], v[98:101], v[162:165], v[62:65]
	v_mfma_f32_16x16x32_bf16 v[58:61], v[122:125], v[162:165], v[58:61]
	v_mfma_f32_16x16x32_bf16 v[46:49], v[98:101], v[170:173], v[46:49]
	v_mfma_f32_16x16x32_bf16 v[42:45], v[122:125], v[170:173], v[42:45]
	v_mfma_f32_16x16x32_bf16 v[30:33], v[98:101], v[178:181], v[30:33]
	v_mfma_f32_16x16x32_bf16 v[26:29], v[122:125], v[178:181], v[26:29]
	v_mfma_f32_16x16x32_bf16 v[14:17], v[98:101], v[202:205], v[14:17]
	v_mfma_f32_16x16x32_bf16 v[10:13], v[122:125], v[202:205], v[10:13]
	v_mfma_f32_16x16x32_bf16 v[62:65], v[110:113], v[166:169], v[62:65]
	v_mfma_f32_16x16x32_bf16 v[58:61], v[130:133], v[166:169], v[58:61]
	v_mfma_f32_16x16x32_bf16 v[46:49], v[110:113], v[174:177], v[46:49]
	v_mfma_f32_16x16x32_bf16 v[42:45], v[130:133], v[174:177], v[42:45]
	v_mfma_f32_16x16x32_bf16 v[30:33], v[110:113], v[182:185], v[30:33]
	v_mfma_f32_16x16x32_bf16 v[26:29], v[130:133], v[182:185], v[26:29]
	v_mfma_f32_16x16x32_bf16 v[14:17], v[110:113], v[206:209], v[14:17]
	v_mfma_f32_16x16x32_bf16 v[10:13], v[130:133], v[206:209], v[10:13]
	s_setprio 0
	s_setprio 3
	v_mfma_f32_16x16x32_bf16 v[54:57], v[146:149], v[162:165], v[54:57]
	v_mfma_f32_16x16x32_bf16 v[50:53], v[154:157], v[162:165], v[50:53]
	v_mfma_f32_16x16x32_bf16 v[38:41], v[146:149], v[170:173], v[38:41]
	v_mfma_f32_16x16x32_bf16 v[34:37], v[154:157], v[170:173], v[34:37]
	v_mfma_f32_16x16x32_bf16 v[22:25], v[146:149], v[178:181], v[22:25]
	v_mfma_f32_16x16x32_bf16 v[18:21], v[154:157], v[178:181], v[18:21]
	v_mfma_f32_16x16x32_bf16 v[6:9], v[146:149], v[202:205], v[6:9]
	v_mfma_f32_16x16x32_bf16 v[2:5], v[154:157], v[202:205], v[2:5]
	v_mfma_f32_16x16x32_bf16 v[54:57], v[150:153], v[166:169], v[54:57]
	v_mfma_f32_16x16x32_bf16 v[50:53], v[158:161], v[166:169], v[50:53]
	v_mfma_f32_16x16x32_bf16 v[38:41], v[150:153], v[174:177], v[38:41]
	v_mfma_f32_16x16x32_bf16 v[34:37], v[158:161], v[174:177], v[34:37]
	v_mfma_f32_16x16x32_bf16 v[22:25], v[150:153], v[182:185], v[22:25]
	v_mfma_f32_16x16x32_bf16 v[18:21], v[158:161], v[182:185], v[18:21]
	v_mfma_f32_16x16x32_bf16 v[6:9], v[150:153], v[206:209], v[6:9]
	v_mfma_f32_16x16x32_bf16 v[2:5], v[158:161], v[206:209], v[2:5]
	s_setprio 0
	s_barrier
	s_add_i32 s63, s63, 2
	s_add_u32 s34, s34, 0x100
	s_addc_u32 s35, s35, 0
	s_add_u32 s61, s61, 0x100
	s_addc_u32 s62, s62, 0
	s_cmp_gt_u32 s63, 13
	s_cbranch_scc0 .LBB0_1324
	s_and_b64 vcc, exec, s[14:15]
	s_cbranch_vccz .LBB0_1327
	s_barrier

; #define PG8_STAGE_A(b, h, ptr, NX) do { if constexpr (Sched::GATHER) { unsigned gs_[2]; gs_[0] = ((NX) && last_) ? gN[h][0] : gA[h][0]; gs_[1] = ((NX) && last_) ? gN[h][1] : gA[h][1]; PG8_STAGE(PG8_SA(b, h), ptr, gs_); } \
;         else PG8_STAGE(PG8_SA(b, h), (ptr) + ((h) ? hstep : (size_t)0), voffA); } while (0)
; #define PG8_STAGE(bufoff, gbase, voff) do { _Pragma("unroll") for (int _i = 0; _i < 2; ++_i) \
;         __builtin_amdgcn_global_load_lds((const unsigned*)((const char*)(gbase) + (voff)[_i]), (PG8_LAS unsigned*)(lds + (bufoff) + ldsw + _i * 8192), 16, 0, 0); } while (0)
; #define PG8_LDA(dst, b, h) do { _Pragma("unroll") for (int m = 0; m < 4; ++m) _Pragma("unroll") for (int k = 0; k < 2; ++k) dst[m][k] = *(const PG8_LAS bf16x8*)(lds + PG8_SA(b, h) + aoff + m * 2048 + k * 1024); } while (0)
; #define PG8_LDB(dst, b, h) do { _Pragma("unroll") for (int n = 0; n < 2; ++n) _Pragma("unroll") for (int k = 0; k < 2; ++k) dst[n][k] = *(const PG8_LAS bf16x8*)(lds + PG8_SB(b, h) + boff + n * 2048 + k * 1024); } while (0)
; #define PG8_WAIT_V(n) asm volatile("s_waitcnt vmcnt(" #n ")" ::: "memory")
; #define PG8_WAIT_L(n) asm volatile("s_waitcnt lgkmcnt(" #n ")" ::: "memory")
; #define PG8_BAR __builtin_amdgcn_s_barrier()
; template <class Epi, class Sched, bool ALIGN_EPI = false, bool SP2 = false>
; __device__ __forceinline__ void gemm_phase(PG8_LAS unsigned char* lds, const Gemm g, const Sched& S, const Epi& E, const bool skip_epi = false) {
;     ...
;             const bool last = (t == nt - 2); last_ = last && has_next;
;             const char* a1 = cA + (size_t)(t + 1) * kstep;
;             const char* a2 = last ? nA : cA + (size_t)(t + 2) * kstep; const char* b2 = last ? nB : cB + (size_t)(t + 2) * kstep;
;             const char* a3 = a2 + kstep; const char* b3 = b2 + kstep;
;             if (last && has_next) S.a_ready(nxt);
;             if constexpr (SP2) {
;             PG8_LDB(B0, 0, 0); PG8_LDB(B1, 0, 1); PG8_SCHED; PG8_LDA(At, 0, 0); PG8_STAGE_A(1, 1, a1, false);
;             PG8_WAIT_V(8); PG8_WAIT_L(0); PG8_BAR; PG8_MMA(0, 0, At, B0); PG8_MMA(0, 1, At, B1); PG8_BAR; PG8_SCHED;
;             PG8_LDA(At, 0, 1); PG8_STAGE(PG8_SB(0, 0), b2, voffB); PG8_STAGE(PG8_SB(0, 1), b2 + hstep, voffB); PG8_STAGE_A(0, 0, a2, true);
;             PG8_WAIT_V(8); PG8_WAIT_L(0); PG8_BAR; PG8_MMA(1, 0, At, B0); PG8_MMA(1, 1, At, B1); PG8_BAR; PG8_SCHED;
.Lg5_zero:
.LBB0_1727:
	s_mov_b32 s29, s41
	s_mov_b32 s31, s40
	v_mov_b32_e32 v143, v133
	v_mov_b32_e32 v141, v133
	s_add_u32 s61, s40, 0x100
	v_lshl_add_u64 v[146:147], s[24:25], 0, v[140:141]
	v_lshl_add_u64 v[148:149], s[24:25], 0, v[142:143]
	s_addc_u32 s62, s41, 0
	s_mov_b32 s63, -2
	s_mov_b64 s[40:41], 0
	ds_read_b128 v[166:169], v158
	ds_read_b128 v[170:173], v158 offset:1024
	ds_read_b128 v[174:177], v158 offset:2048
	ds_read_b128 v[178:181], v158 offset:3072
	ds_read_b128 v[182:185], v159
	ds_read_b128 v[186:189], v159 offset:1024
	ds_read_b128 v[190:193], v159 offset:2048
	ds_read_b128 v[194:197], v159 offset:3072
	s_add_u32 s42, s78, s40
	s_addc_u32 s43, s79, s41
	s_add_u32 s44, s42, 0x1aa00100
	s_addc_u32 s45, s43, 0
	s_add_u32 s66, s61, s40
	s_addc_u32 s67, s62, s41
	s_cmpk_eq_i32 s40, 0x700
	s_cselect_b64 s[64:65], -1, 0
	s_and_b64 s[42:43], s[64:65], exec
	s_cselect_b32 s45, s87, s45
	s_cselect_b32 s44, s86, s44
	s_cselect_b32 s42, s31, s66
	s_cselect_b32 s43, s29, s67
	s_and_b64 vcc, s[6:7], s[64:65]
	v_lshl_add_u64 v[226:227], v[148:149], 0, s[40:41]
	s_add_i32 m0, s37, 0xc000
	ds_read_b128 v[198:201], v160
	ds_read_b128 v[202:205], v160 offset:1024
	ds_read_b128 v[206:209], v160 offset:2048
	ds_read_b128 v[210:213], v160 offset:3072
	ds_read_b128 v[214:217], v160 offset:4096
	ds_read_b128 v[218:221], v160 offset:5120
	ds_read_b128 v[222:225], v160 offset:6144
	ds_read_b128 v[230:233], v160 offset:7168
	global_load_lds_dwordx4 v[226:227], off
	v_lshl_add_u64 v[226:227], v[146:147], 0, s[40:41]
	s_add_i32 m0, s37, 0xe000
	s_nop 0
	global_load_lds_dwordx4 v[226:227], off
	s_waitcnt vmcnt(8)
	s_waitcnt lgkmcnt(0)
	s_barrier
	s_setprio 3
	s_waitcnt lgkmcnt(0)
	v_mfma_f32_16x16x32_bf16 v[126:129], v[166:169], v[198:201], 0
	v_mfma_f32_16x16x32_bf16 v[122:125], v[174:177], v[198:201], 0
	v_mfma_f32_16x16x32_bf16 v[110:113], v[166:169], v[206:209], 0
	v_mfma_f32_16x16x32_bf16 v[106:109], v[174:177], v[206:209], 0
	v_lshl_add_u64 v[226:227], s[42:43], 0, v[134:135]
	v_mfma_f32_16x16x32_bf16 v[94:97], v[166:169], v[214:217], 0
	v_mfma_f32_16x16x32_bf16 v[90:93], v[174:177], v[214:217], 0
	v_lshl_add_u64 v[234:235], s[42:43], 0, v[136:137]
	v_mfma_f32_16x16x32_bf16 v[78:81], v[166:169], v[222:225], 0
	v_mfma_f32_16x16x32_bf16 v[74:77], v[174:177], v[222:225], 0
	v_cndmask_b32_e32 v132, v130, v164, vcc
	v_mfma_f32_16x16x32_bf16 v[126:129], v[170:173], v[202:205], v[126:129]
	v_mfma_f32_16x16x32_bf16 v[122:125], v[178:181], v[202:205], v[122:125]
	v_lshl_add_u64 v[238:239], s[44:45], 0, v[132:133]
	v_mfma_f32_16x16x32_bf16 v[110:113], v[170:173], v[210:213], v[110:113]
	v_mfma_f32_16x16x32_bf16 v[106:109], v[178:181], v[210:213], v[106:109]
	v_cndmask_b32_e32 v236, v144, v163, vcc
	v_mfma_f32_16x16x32_bf16 v[94:97], v[170:173], v[218:221], v[94:97]
	v_mfma_f32_16x16x32_bf16 v[90:93], v[178:181], v[218:221], v[90:93]
	v_mov_b32_e32 v237, v133
	v_mfma_f32_16x16x32_bf16 v[78:81], v[170:173], v[230:233], v[78:81]
	v_mfma_f32_16x16x32_bf16 v[74:77], v[178:181], v[230:233], v[74:77]
	s_setprio 0
	s_setprio 3
	v_mfma_f32_16x16x32_bf16 v[118:121], v[182:185], v[198:201], 0
	v_mfma_f32_16x16x32_bf16 v[114:117], v[190:193], v[198:201], 0
	v_mfma_f32_16x16x32_bf16 v[102:105], v[182:185], v[206:209], 0
	v_mfma_f32_16x16x32_bf16 v[98:101], v[190:193], v[206:209], 0
	v_mfma_f32_16x16x32_bf16 v[86:89], v[182:185], v[214:217], 0
	v_mfma_f32_16x16x32_bf16 v[82:85], v[190:193], v[214:217], 0
	v_mfma_f32_16x16x32_bf16 v[70:73], v[182:185], v[222:225], 0
	v_mfma_f32_16x16x32_bf16 v[66:69], v[190:193], v[222:225], 0
	v_mfma_f32_16x16x32_bf16 v[118:121], v[186:189], v[202:205], v[118:121]
	v_mfma_f32_16x16x32_bf16 v[114:117], v[194:197], v[202:205], v[114:117]
	v_mfma_f32_16x16x32_bf16 v[102:105], v[186:189], v[210:213], v[102:105]
	v_mfma_f32_16x16x32_bf16 v[98:101], v[194:197], v[210:213], v[98:101]
	v_mfma_f32_16x16x32_bf16 v[86:89], v[186:189], v[218:221], v[86:89]
	v_mfma_f32_16x16x32_bf16 v[82:85], v[194:197], v[218:221], v[82:85]
	v_mfma_f32_16x16x32_bf16 v[70:73], v[186:189], v[230:233], v[70:73]
	v_mfma_f32_16x16x32_bf16 v[66:69], v[194:197], v[230:233], v[66:69]
	s_setprio 0
	s_barrier
	s_add_i32 s64, s58, s50
	s_mov_b32 m0, s64
	ds_read_b128 v[198:201], v160 offset:16384
	ds_read_b128 v[202:205], v160 offset:17408
	ds_read_b128 v[206:209], v160 offset:18432
	ds_read_b128 v[210:213], v160 offset:19456
	ds_read_b128 v[214:217], v160 offset:20480
	ds_read_b128 v[218:221], v160 offset:21504
	ds_read_b128 v[222:225], v160 offset:22528
	ds_read_b128 v[230:233], v160 offset:23552
	global_load_lds_dwordx4 v[226:227], off
	s_add_i32 m0, s64, 0x2000
	s_add_u32 s64, s42, 0x40000
	s_addc_u32 s65, s43, 0
	s_add_i32 s66, s59, s50
	global_load_lds_dwordx4 v[234:235], off
	s_mov_b32 m0, s66
	s_nop 0
	global_load_lds_dwordx4 v134, s[64:65]
	s_add_i32 m0, s66, 0x2000
	s_nop 0
	global_load_lds_dwordx4 v136, s[64:65]
	s_mov_b32 m0, s37
	s_nop 0
	global_load_lds_dwordx4 v132, s[44:45]
	s_mov_b32 m0, s39
	s_nop 0
	global_load_lds_dwordx4 v236, s[44:45]
	s_waitcnt vmcnt(8)
	s_waitcnt lgkmcnt(0)
	v_lshl_add_u64 v[236:237], s[44:45], 0, v[236:237]
	s_barrier
; #define PG8_STAGE_A(b, h, ptr, NX) do { if constexpr (Sched::GATHER) { unsigned gs_[2]; gs_[0] = ((NX) && last_) ? gN[h][0] : gA[h][0]; gs_[1] = ((NX) && last_) ? gN[h][1] : gA[h][1]; PG8_STAGE(PG8_SA(b, h), ptr, gs_); } \
;         else PG8_STAGE(PG8_SA(b, h), (ptr) + ((h) ? hstep : (size_t)0), voffA); } while (0)
; #define PG8_LDA(dst, b, h) do { _Pragma("unroll") for (int m = 0; m < 4; ++m) _Pragma("unroll") for (int k = 0; k < 2; ++k) dst[m][k] = *(const PG8_LAS bf16x8*)(lds + PG8_SA(b, h) + aoff + m * 2048 + k * 1024); } while (0)
; #define PG8_LDB(dst, b, h) do { _Pragma("unroll") for (int n = 0; n < 2; ++n) _Pragma("unroll") for (int k = 0; k < 2; ++k) dst[n][k] = *(const PG8_LAS bf16x8*)(lds + PG8_SB(b, h) + boff + n * 2048 + k * 1024); } while (0)
; #define PG8_MMA(ai, bj, At, Bt) do { __builtin_amdgcn_s_setprio(1); _Pragma("unroll") for (int m = 0; m < 4; ++m) _Pragma("unroll") for (int n = 0; n < 2; ++n) _Pragma("unroll") for (int k = 0; k < 2; ++k) \
;         acc[ai][bj][m][n] = __builtin_amdgcn_mfma_f32_16x16x32_bf16(Bt[n][k], At[m][k], acc[ai][bj][m][n], 0, 0, 0); __builtin_amdgcn_s_setprio(0); } while (0)
; #define PG8_WAIT_V(n) asm volatile("s_waitcnt vmcnt(" #n ")" ::: "memory")
; #define PG8_WAIT_L(n) asm volatile("s_waitcnt lgkmcnt(" #n ")" ::: "memory")
; #define PG8_BAR __builtin_amdgcn_s_barrier()
; #define PG8_SCHED __builtin_amdgcn_sched_barrier(0)
; template <class Epi, class Sched, bool ALIGN_EPI = false, bool SP2 = false>
; __device__ __forceinline__ void gemm_phase(PG8_LAS unsigned char* lds, const Gemm g, const Sched& S, const Epi& E, const bool skip_epi = false) {
;     ...
;             PG8_WAIT_V(8); PG8_WAIT_L(0); PG8_BAR; PG8_MMA(1, 0, At, B0); PG8_MMA(1, 1, At, B1); PG8_BAR; PG8_SCHED;
;             PG8_LDB(B0, 1, 0); PG8_LDB(B1, 1, 1); PG8_SCHED; PG8_LDA(At, 1, 0); PG8_STAGE_A(0, 1, a2, true);
;             PG8_WAIT_V(8); PG8_WAIT_L(0); PG8_BAR; PG8_MMA(0, 0, At, B0); PG8_MMA(0, 1, At, B1); PG8_BAR; PG8_SCHED;
	s_setprio 3
	s_waitcnt lgkmcnt(0)
	v_mfma_f32_16x16x32_bf16 v[62:65], v[166:169], v[198:201], 0
	v_mfma_f32_16x16x32_bf16 v[58:61], v[174:177], v[198:201], 0
	v_mfma_f32_16x16x32_bf16 v[38:41], v[166:169], v[206:209], 0
	v_mfma_f32_16x16x32_bf16 v[34:37], v[174:177], v[206:209], 0
	v_cndmask_b32_e32 v141, v140, v161, vcc
	v_mfma_f32_16x16x32_bf16 v[22:25], v[166:169], v[214:217], 0
	v_mfma_f32_16x16x32_bf16 v[18:21], v[174:177], v[214:217], 0
	v_mfma_f32_16x16x32_bf16 v[6:9], v[166:169], v[222:225], 0
	v_mfma_f32_16x16x32_bf16 v[2:5], v[174:177], v[222:225], 0
	v_mfma_f32_16x16x32_bf16 v[62:65], v[170:173], v[202:205], v[62:65]
	v_mfma_f32_16x16x32_bf16 v[58:61], v[178:181], v[202:205], v[58:61]
	v_mfma_f32_16x16x32_bf16 v[38:41], v[170:173], v[210:213], v[38:41]
	v_mfma_f32_16x16x32_bf16 v[34:37], v[178:181], v[210:213], v[34:37]
	v_mfma_f32_16x16x32_bf16 v[22:25], v[170:173], v[218:221], v[22:25]
	v_mfma_f32_16x16x32_bf16 v[18:21], v[178:181], v[218:221], v[18:21]
	v_mfma_f32_16x16x32_bf16 v[6:9], v[170:173], v[230:233], v[6:9]
	v_mfma_f32_16x16x32_bf16 v[2:5], v[178:181], v[230:233], v[2:5]
	s_setprio 0
	s_setprio 3
	v_mfma_f32_16x16x32_bf16 v[50:53], v[182:185], v[198:201], 0
	v_mfma_f32_16x16x32_bf16 v[42:45], v[190:193], v[198:201], 0
	v_mfma_f32_16x16x32_bf16 v[54:57], v[182:185], v[206:209], 0
	v_mfma_f32_16x16x32_bf16 v[46:49], v[190:193], v[206:209], 0
	v_mfma_f32_16x16x32_bf16 v[30:33], v[182:185], v[214:217], 0
	v_mfma_f32_16x16x32_bf16 v[26:29], v[190:193], v[214:217], 0
	v_mfma_f32_16x16x32_bf16 v[14:17], v[182:185], v[222:225], 0
	v_mfma_f32_16x16x32_bf16 v[10:13], v[190:193], v[222:225], 0
	v_mfma_f32_16x16x32_bf16 v[50:53], v[186:189], v[202:205], v[50:53]
	v_mfma_f32_16x16x32_bf16 v[42:45], v[194:197], v[202:205], v[42:45]
	v_mfma_f32_16x16x32_bf16 v[54:57], v[186:189], v[210:213], v[54:57]
	v_mfma_f32_16x16x32_bf16 v[46:49], v[194:197], v[210:213], v[46:49]
	v_mfma_f32_16x16x32_bf16 v[30:33], v[186:189], v[218:221], v[30:33]
	v_mfma_f32_16x16x32_bf16 v[26:29], v[194:197], v[218:221], v[26:29]
	v_mfma_f32_16x16x32_bf16 v[14:17], v[186:189], v[230:233], v[14:17]
	v_mfma_f32_16x16x32_bf16 v[10:13], v[194:197], v[230:233], v[10:13]
	s_setprio 0
	s_barrier
	s_add_i32 s64, 0, 0x18000
	v_add_u32_e32 v132, s64, v154
	s_add_i32 s65, 0, 0x1c000
	ds_read_b128 v[166:169], v132
	ds_read_b128 v[170:173], v132 offset:1024
	ds_read_b128 v[174:177], v132 offset:2048
	ds_read_b128 v[178:181], v132 offset:3072
	v_add_u32_e32 v132, s65, v154
	ds_read_b128 v[182:185], v132
	ds_read_b128 v[186:189], v132 offset:1024
	ds_read_b128 v[190:193], v132 offset:2048
	ds_read_b128 v[194:197], v132 offset:3072
	s_mov_b32 m0, s51
	v_cndmask_b32_e32 v132, v142, v162, vcc
	ds_read_b128 v[198:201], v160 offset:32768
	ds_read_b128 v[202:205], v160 offset:33792
	ds_read_b128 v[206:209], v160 offset:34816
	ds_read_b128 v[210:213], v160 offset:35840
	ds_read_b128 v[214:217], v160 offset:36864
	ds_read_b128 v[218:221], v160 offset:37888
	ds_read_b128 v[222:225], v160 offset:38912
	ds_read_b128 v[230:233], v160 offset:39936
	global_load_lds_dwordx4 v132, s[44:45]
	s_mov_b32 m0, s52
	s_nop 0
	global_load_lds_dwordx4 v141, s[44:45]
	s_waitcnt vmcnt(8)
	s_waitcnt lgkmcnt(0)
	s_barrier
	s_setprio 3
	s_waitcnt lgkmcnt(0)
	v_mfma_f32_16x16x32_bf16 v[126:129], v[166:169], v[198:201], v[126:129]
	v_mfma_f32_16x16x32_bf16 v[122:125], v[174:177], v[198:201], v[122:125]
	v_mfma_f32_16x16x32_bf16 v[110:113], v[166:169], v[206:209], v[110:113]
	v_mfma_f32_16x16x32_bf16 v[106:109], v[174:177], v[206:209], v[106:109]
	v_mfma_f32_16x16x32_bf16 v[94:97], v[166:169], v[214:217], v[94:97]
	v_mfma_f32_16x16x32_bf16 v[90:93], v[174:177], v[214:217], v[90:93]
	v_mfma_f32_16x16x32_bf16 v[78:81], v[166:169], v[222:225], v[78:81]
	v_mfma_f32_16x16x32_bf16 v[74:77], v[174:177], v[222:225], v[74:77]
	v_mfma_f32_16x16x32_bf16 v[126:129], v[170:173], v[202:205], v[126:129]
	v_mfma_f32_16x16x32_bf16 v[122:125], v[178:181], v[202:205], v[122:125]
	v_mfma_f32_16x16x32_bf16 v[110:113], v[170:173], v[210:213], v[110:113]
	v_mfma_f32_16x16x32_bf16 v[106:109], v[178:181], v[210:213], v[106:109]
	v_mfma_f32_16x16x32_bf16 v[94:97], v[170:173], v[218:221], v[94:97]
	v_mfma_f32_16x16x32_bf16 v[90:93], v[178:181], v[218:221], v[90:93]
	v_mfma_f32_16x16x32_bf16 v[78:81], v[170:173], v[230:233], v[78:81]
	v_mfma_f32_16x16x32_bf16 v[74:77], v[178:181], v[230:233], v[74:77]
	s_setprio 0
	s_setprio 3
	v_mfma_f32_16x16x32_bf16 v[118:121], v[182:185], v[198:201], v[118:121]
	v_mfma_f32_16x16x32_bf16 v[114:117], v[190:193], v[198:201], v[114:117]
	v_mfma_f32_16x16x32_bf16 v[102:105], v[182:185], v[206:209], v[102:105]
	v_mfma_f32_16x16x32_bf16 v[98:101], v[190:193], v[206:209], v[98:101]
	v_mfma_f32_16x16x32_bf16 v[86:89], v[182:185], v[214:217], v[86:89]
	v_mfma_f32_16x16x32_bf16 v[82:85], v[190:193], v[214:217], v[82:85]
	v_mfma_f32_16x16x32_bf16 v[70:73], v[182:185], v[222:225], v[70:73]
	v_mfma_f32_16x16x32_bf16 v[66:69], v[190:193], v[222:225], v[66:69]
	v_mfma_f32_16x16x32_bf16 v[118:121], v[186:189], v[202:205], v[118:121]
	v_mfma_f32_16x16x32_bf16 v[114:117], v[194:197], v[202:205], v[114:117]
	v_mfma_f32_16x16x32_bf16 v[102:105], v[186:189], v[210:213], v[102:105]
	v_mfma_f32_16x16x32_bf16 v[98:101], v[194:197], v[210:213], v[98:101]
	v_mfma_f32_16x16x32_bf16 v[86:89], v[186:189], v[218:221], v[86:89]
	v_mfma_f32_16x16x32_bf16 v[82:85], v[194:197], v[218:221], v[82:85]
	v_mfma_f32_16x16x32_bf16 v[70:73], v[186:189], v[230:233], v[70:73]
	v_mfma_f32_16x16x32_bf16 v[66:69], v[194:197], v[230:233], v[66:69]
	s_setprio 0
	s_barrier
; #define PG8_GIDX(G_, PM_) do { if constexpr (Sched::GATHER) { _Pragma("unroll") for (int h_ = 0; h_ < 2; ++h_) _Pragma("unroll") for (int i_ = 0; i_ < 2; ++i_) { int R_, C_; stage_rc(tid * 16 + i_ * 8192, R_, C_); \
;         const int src_ = S.rowsrc[(PM_) * BM + h_ * HALF + R_]; G_[h_][i_] = (unsigned)(src_ * K + C_) * 2u; } } } while (0)
; #define PG8_STAGE_A(b, h, ptr, NX) do { if constexpr (Sched::GATHER) { unsigned gs_[2]; gs_[0] = ((NX) && last_) ? gN[h][0] : gA[h][0]; gs_[1] = ((NX) && last_) ? gN[h][1] : gA[h][1]; PG8_STAGE(PG8_SA(b, h), ptr, gs_); } \
;         else PG8_STAGE(PG8_SA(b, h), (ptr) + ((h) ? hstep : (size_t)0), voffA); } while (0)
; #define PG8_STAGE(bufoff, gbase, voff) do { _Pragma("unroll") for (int _i = 0; _i < 2; ++_i) \
;         __builtin_amdgcn_global_load_lds((const unsigned*)((const char*)(gbase) + (voff)[_i]), (PG8_LAS unsigned*)(lds + (bufoff) + ldsw + _i * 8192), 16, 0, 0); } while (0)
; #define PG8_LDA(dst, b, h) do { _Pragma("unroll") for (int m = 0; m < 4; ++m) _Pragma("unroll") for (int k = 0; k < 2; ++k) dst[m][k] = *(const PG8_LAS bf16x8*)(lds + PG8_SA(b, h) + aoff + m * 2048 + k * 1024); } while (0)
; #define PG8_MMA(ai, bj, At, Bt) do { __builtin_amdgcn_s_setprio(1); _Pragma("unroll") for (int m = 0; m < 4; ++m) _Pragma("unroll") for (int n = 0; n < 2; ++n) _Pragma("unroll") for (int k = 0; k < 2; ++k) \
;         acc[ai][bj][m][n] = __builtin_amdgcn_mfma_f32_16x16x32_bf16(Bt[n][k], At[m][k], acc[ai][bj][m][n], 0, 0, 0); __builtin_amdgcn_s_setprio(0); } while (0)
; #define PG8_WAIT_V(n) asm volatile("s_waitcnt vmcnt(" #n ")" ::: "memory")
; template <class Epi, class Sched, bool ALIGN_EPI = false, bool SP2 = false>
; __device__ __forceinline__ void gemm_phase(PG8_LAS unsigned char* lds, const Gemm g, const Sched& S, const Epi& E, const bool skip_epi = false) {
;     ...
;         const bool has_next = S.next(ui + 1, nxt);
;         if (has_next) PG8_GIDX(gN, nxt.pm);
;         const char* nA = has_next ? (const char*)g.A + (size_t)nxt.pm * pmstepA + nxt.ko : cA; const char* nB = has_next ? (const char*)g.Bt + (size_t)nxt.pn * tstep + nxt.ko : cB;
;     ...
;             PG8_LDA(At, 1, 1); PG8_STAGE(PG8_SB(1, 0), b3, voffB); PG8_STAGE(PG8_SB(1, 1), b3 + hstep, voffB); PG8_STAGE_A(1, 0, a3, true);
;             PG8_WAIT_V(8); PG8_WAIT_L(0); PG8_BAR; PG8_MMA(1, 0, At, B0); PG8_MMA(1, 1, At, B1); PG8_BAR; PG8_SCHED;
	s_add_i32 s44, s64, s50
	s_add_i32 m0, s44, 0xffffff80
	ds_read_b128 v[198:201], v160 offset:49152
	ds_read_b128 v[202:205], v160 offset:50176
	ds_read_b128 v[206:209], v160 offset:51200
	ds_read_b128 v[210:213], v160 offset:52224
	ds_read_b128 v[214:217], v160 offset:53248
	ds_read_b128 v[218:221], v160 offset:54272
	ds_read_b128 v[222:225], v160 offset:55296
	ds_read_b128 v[230:233], v160 offset:56320
	global_load_lds_dwordx4 v[226:227], off offset:128
	s_add_i32 m0, s44, 0x1f80
	s_add_u32 s42, s42, 0x40080
	s_addc_u32 s43, s43, 0
	s_add_i32 s44, s65, s50
	global_load_lds_dwordx4 v[234:235], off offset:128
	s_mov_b32 m0, s44
	s_nop 0
	global_load_lds_dwordx4 v134, s[42:43]
	s_add_i32 m0, s44, 0x2000
	s_nop 0
	global_load_lds_dwordx4 v136, s[42:43]
	s_add_i32 m0, s55, 0xffffff80
	s_nop 0
	global_load_lds_dwordx4 v[238:239], off offset:128
	s_add_i32 m0, s56, 0xffffff80
	s_nop 0
	global_load_lds_dwordx4 v[236:237], off offset:128
	s_waitcnt vmcnt(8)
	s_waitcnt lgkmcnt(0)
	s_barrier
	s_setprio 3
	s_waitcnt lgkmcnt(0)
	v_mfma_f32_16x16x32_bf16 v[62:65], v[166:169], v[198:201], v[62:65]
	v_mfma_f32_16x16x32_bf16 v[58:61], v[174:177], v[198:201], v[58:61]
	v_mfma_f32_16x16x32_bf16 v[38:41], v[166:169], v[206:209], v[38:41]
	v_mfma_f32_16x16x32_bf16 v[34:37], v[174:177], v[206:209], v[34:37]
	v_mfma_f32_16x16x32_bf16 v[22:25], v[166:169], v[214:217], v[22:25]
	v_mfma_f32_16x16x32_bf16 v[18:21], v[174:177], v[214:217], v[18:21]
	v_mfma_f32_16x16x32_bf16 v[6:9], v[166:169], v[222:225], v[6:9]
	v_mfma_f32_16x16x32_bf16 v[2:5], v[174:177], v[222:225], v[2:5]
	v_mfma_f32_16x16x32_bf16 v[62:65], v[170:173], v[202:205], v[62:65]
	v_mfma_f32_16x16x32_bf16 v[58:61], v[178:181], v[202:205], v[58:61]
	v_mfma_f32_16x16x32_bf16 v[38:41], v[170:173], v[210:213], v[38:41]
	v_mfma_f32_16x16x32_bf16 v[34:37], v[178:181], v[210:213], v[34:37]
	v_mfma_f32_16x16x32_bf16 v[22:25], v[170:173], v[218:221], v[22:25]
	v_mfma_f32_16x16x32_bf16 v[18:21], v[178:181], v[218:221], v[18:21]
	v_mfma_f32_16x16x32_bf16 v[6:9], v[170:173], v[230:233], v[6:9]
	v_mfma_f32_16x16x32_bf16 v[2:5], v[178:181], v[230:233], v[2:5]
	s_setprio 0
	s_setprio 3
	v_mfma_f32_16x16x32_bf16 v[50:53], v[182:185], v[198:201], v[50:53]
	v_mfma_f32_16x16x32_bf16 v[42:45], v[190:193], v[198:201], v[42:45]
	v_mfma_f32_16x16x32_bf16 v[54:57], v[182:185], v[206:209], v[54:57]
	v_mfma_f32_16x16x32_bf16 v[46:49], v[190:193], v[206:209], v[46:49]
	v_mfma_f32_16x16x32_bf16 v[30:33], v[182:185], v[214:217], v[30:33]
	v_mfma_f32_16x16x32_bf16 v[26:29], v[190:193], v[214:217], v[26:29]
	v_mfma_f32_16x16x32_bf16 v[14:17], v[182:185], v[222:225], v[14:17]
	v_mfma_f32_16x16x32_bf16 v[10:13], v[190:193], v[222:225], v[10:13]
	v_mfma_f32_16x16x32_bf16 v[50:53], v[186:189], v[202:205], v[50:53]
	v_mfma_f32_16x16x32_bf16 v[42:45], v[194:197], v[202:205], v[42:45]
	v_mfma_f32_16x16x32_bf16 v[54:57], v[186:189], v[210:213], v[54:57]
	v_mfma_f32_16x16x32_bf16 v[46:49], v[194:197], v[210:213], v[46:49]
	v_mfma_f32_16x16x32_bf16 v[30:33], v[186:189], v[218:221], v[30:33]
	v_mfma_f32_16x16x32_bf16 v[26:29], v[194:197], v[218:221], v[26:29]
	v_mfma_f32_16x16x32_bf16 v[14:17], v[186:189], v[230:233], v[14:17]
	v_mfma_f32_16x16x32_bf16 v[10:13], v[194:197], v[230:233], v[10:13]
	s_setprio 0
	s_barrier
	s_add_i32 s63, s63, 2
	s_add_u32 s40, s40, 0x100
	s_addc_u32 s41, s41, 0
	s_cmp_gt_u32 s63, 13
	s_andn2_b64 vcc, exec, s[6:7]
	s_cbranch_vccnz .Lg5_nonext
	s_waitcnt vmcnt(8)
	v_readfirstlane_b32 s34, v250
	v_lshl_add_u32 v164, v229, 11, v152
	v_lshl_add_u32 v163, v251, 11, v153
	v_lshl_add_u32 v162, v252, 11, v152
	v_lshl_add_u32 v161, v253, 11, v153
	s_mul_i32 s34, s34, 28
	s_add_i32 s30, s34, s30
	s_ashr_i32 s31, s30, 31
	s_lshl_b64 s[34:35], s[30:31], 19
	v_readlane_b32 s42, v254, 29
	v_readlane_b32 s43, v254, 30
	s_add_u32 s34, s42, s34
	s_addc_u32 s35, s43, s35
	s_mov_b32 s29, s35
	s_mov_b32 s31, s34
.Lg5_nonext:
.LBB0_1728:
	ds_read_b128 v[166:169], v158
	ds_read_b128 v[170:173], v158 offset:1024
	ds_read_b128 v[174:177], v158 offset:2048
	ds_read_b128 v[178:181], v158 offset:3072
	ds_read_b128 v[182:185], v159
	ds_read_b128 v[186:189], v159 offset:1024
	ds_read_b128 v[190:193], v159 offset:2048
	ds_read_b128 v[194:197], v159 offset:3072
	s_add_u32 s42, s78, s40
	s_addc_u32 s43, s79, s41
	s_add_u32 s44, s42, 0x1aa00100
	s_addc_u32 s45, s43, 0
	s_add_u32 s66, s61, s40
	s_addc_u32 s67, s62, s41
	s_cmpk_eq_i32 s40, 0x700
	s_cselect_b64 s[64:65], -1, 0
	s_and_b64 s[42:43], s[64:65], exec
	s_cselect_b32 s45, s87, s45
	s_cselect_b32 s44, s86, s44
	s_cselect_b32 s42, s31, s66
	s_cselect_b32 s43, s29, s67
	s_and_b64 vcc, s[6:7], s[64:65]
	v_lshl_add_u64 v[226:227], v[148:149], 0, s[40:41]
	s_add_i32 m0, s37, 0xc000
	ds_read_b128 v[198:201], v160
	ds_read_b128 v[202:205], v160 offset:1024
	ds_read_b128 v[206:209], v160 offset:2048
	ds_read_b128 v[210:213], v160 offset:3072
	ds_read_b128 v[214:217], v160 offset:4096
	ds_read_b128 v[218:221], v160 offset:5120
	ds_read_b128 v[222:225], v160 offset:6144
	ds_read_b128 v[230:233], v160 offset:7168
	global_load_lds_dwordx4 v[226:227], off
	v_lshl_add_u64 v[226:227], v[146:147], 0, s[40:41]
	s_add_i32 m0, s37, 0xe000
	s_nop 0
	global_load_lds_dwordx4 v[226:227], off
	s_waitcnt vmcnt(8)
	s_waitcnt lgkmcnt(0)
	s_barrier
; #define PG8_STAGE_A(b, h, ptr, NX) do { if constexpr (Sched::GATHER) { unsigned gs_[2]; gs_[0] = ((NX) && last_) ? gN[h][0] : gA[h][0]; gs_[1] = ((NX) && last_) ? gN[h][1] : gA[h][1]; PG8_STAGE(PG8_SA(b, h), ptr, gs_); } \
;         else PG8_STAGE(PG8_SA(b, h), (ptr) + ((h) ? hstep : (size_t)0), voffA); } while (0)
; #define PG8_STAGE(bufoff, gbase, voff) do { _Pragma("unroll") for (int _i = 0; _i < 2; ++_i) \
;         __builtin_amdgcn_global_load_lds((const unsigned*)((const char*)(gbase) + (voff)[_i]), (PG8_LAS unsigned*)(lds + (bufoff) + ldsw + _i * 8192), 16, 0, 0); } while (0)
; #define PG8_LDA(dst, b, h) do { _Pragma("unroll") for (int m = 0; m < 4; ++m) _Pragma("unroll") for (int k = 0; k < 2; ++k) dst[m][k] = *(const PG8_LAS bf16x8*)(lds + PG8_SA(b, h) + aoff + m * 2048 + k * 1024); } while (0)
; #define PG8_LDB(dst, b, h) do { _Pragma("unroll") for (int n = 0; n < 2; ++n) _Pragma("unroll") for (int k = 0; k < 2; ++k) dst[n][k] = *(const PG8_LAS bf16x8*)(lds + PG8_SB(b, h) + boff + n * 2048 + k * 1024); } while (0)
; #define PG8_MMA(ai, bj, At, Bt) do { __builtin_amdgcn_s_setprio(1); _Pragma("unroll") for (int m = 0; m < 4; ++m) _Pragma("unroll") for (int n = 0; n < 2; ++n) _Pragma("unroll") for (int k = 0; k < 2; ++k) \
;         acc[ai][bj][m][n] = __builtin_amdgcn_mfma_f32_16x16x32_bf16(Bt[n][k], At[m][k], acc[ai][bj][m][n], 0, 0, 0); __builtin_amdgcn_s_setprio(0); } while (0)
; #define PG8_WAIT_V(n) asm volatile("s_waitcnt vmcnt(" #n ")" ::: "memory")
; #define PG8_WAIT_L(n) asm volatile("s_waitcnt lgkmcnt(" #n ")" ::: "memory")
; #define PG8_BAR __builtin_amdgcn_s_barrier()
; #define PG8_SCHED __builtin_amdgcn_sched_barrier(0)
; template <class Epi, class Sched, bool ALIGN_EPI = false, bool SP2 = false>
; __device__ __forceinline__ void gemm_phase(PG8_LAS unsigned char* lds, const Gemm g, const Sched& S, const Epi& E, const bool skip_epi = false) {
;     ...
;             PG8_LDB(B0, 0, 0); PG8_LDB(B1, 0, 1); PG8_SCHED; PG8_LDA(At, 0, 0); PG8_STAGE_A(1, 1, a1, false);
;             PG8_WAIT_V(8); PG8_WAIT_L(0); PG8_BAR; PG8_MMA(0, 0, At, B0); PG8_MMA(0, 1, At, B1); PG8_BAR; PG8_SCHED;
;             PG8_LDA(At, 0, 1); PG8_STAGE(PG8_SB(0, 0), b2, voffB); PG8_STAGE(PG8_SB(0, 1), b2 + hstep, voffB); PG8_STAGE_A(0, 0, a2, true);
;             PG8_WAIT_V(8); PG8_WAIT_L(0); PG8_BAR; PG8_MMA(1, 0, At, B0); PG8_MMA(1, 1, At, B1); PG8_BAR; PG8_SCHED;
	s_setprio 3
	s_waitcnt lgkmcnt(0)
	v_mfma_f32_16x16x32_bf16 v[126:129], v[166:169], v[198:201], v[126:129]
	v_mfma_f32_16x16x32_bf16 v[122:125], v[174:177], v[198:201], v[122:125]
	v_mfma_f32_16x16x32_bf16 v[110:113], v[166:169], v[206:209], v[110:113]
	v_mfma_f32_16x16x32_bf16 v[106:109], v[174:177], v[206:209], v[106:109]
	v_lshl_add_u64 v[226:227], s[42:43], 0, v[134:135]
	v_mfma_f32_16x16x32_bf16 v[94:97], v[166:169], v[214:217], v[94:97]
	v_mfma_f32_16x16x32_bf16 v[90:93], v[174:177], v[214:217], v[90:93]
	v_lshl_add_u64 v[234:235], s[42:43], 0, v[136:137]
	v_mfma_f32_16x16x32_bf16 v[78:81], v[166:169], v[222:225], v[78:81]
	v_mfma_f32_16x16x32_bf16 v[74:77], v[174:177], v[222:225], v[74:77]
	v_cndmask_b32_e32 v132, v130, v164, vcc
	v_mfma_f32_16x16x32_bf16 v[126:129], v[170:173], v[202:205], v[126:129]
	v_mfma_f32_16x16x32_bf16 v[122:125], v[178:181], v[202:205], v[122:125]
	v_lshl_add_u64 v[238:239], s[44:45], 0, v[132:133]
	v_mfma_f32_16x16x32_bf16 v[110:113], v[170:173], v[210:213], v[110:113]
	v_mfma_f32_16x16x32_bf16 v[106:109], v[178:181], v[210:213], v[106:109]
	v_cndmask_b32_e32 v236, v144, v163, vcc
	v_mfma_f32_16x16x32_bf16 v[94:97], v[170:173], v[218:221], v[94:97]
	v_mfma_f32_16x16x32_bf16 v[90:93], v[178:181], v[218:221], v[90:93]
	v_mov_b32_e32 v237, v133
	v_mfma_f32_16x16x32_bf16 v[78:81], v[170:173], v[230:233], v[78:81]
	v_mfma_f32_16x16x32_bf16 v[74:77], v[178:181], v[230:233], v[74:77]
	s_setprio 0
	s_setprio 3
	v_mfma_f32_16x16x32_bf16 v[118:121], v[182:185], v[198:201], v[118:121]
	v_mfma_f32_16x16x32_bf16 v[114:117], v[190:193], v[198:201], v[114:117]
	v_mfma_f32_16x16x32_bf16 v[102:105], v[182:185], v[206:209], v[102:105]
	v_mfma_f32_16x16x32_bf16 v[98:101], v[190:193], v[206:209], v[98:101]
	v_mfma_f32_16x16x32_bf16 v[86:89], v[182:185], v[214:217], v[86:89]
	v_mfma_f32_16x16x32_bf16 v[82:85], v[190:193], v[214:217], v[82:85]
	v_mfma_f32_16x16x32_bf16 v[70:73], v[182:185], v[222:225], v[70:73]
	v_mfma_f32_16x16x32_bf16 v[66:69], v[190:193], v[222:225], v[66:69]
	v_mfma_f32_16x16x32_bf16 v[118:121], v[186:189], v[202:205], v[118:121]
	v_mfma_f32_16x16x32_bf16 v[114:117], v[194:197], v[202:205], v[114:117]
	v_mfma_f32_16x16x32_bf16 v[102:105], v[186:189], v[210:213], v[102:105]
	v_mfma_f32_16x16x32_bf16 v[98:101], v[194:197], v[210:213], v[98:101]
	v_mfma_f32_16x16x32_bf16 v[86:89], v[186:189], v[218:221], v[86:89]
	v_mfma_f32_16x16x32_bf16 v[82:85], v[194:197], v[218:221], v[82:85]
	v_mfma_f32_16x16x32_bf16 v[70:73], v[186:189], v[230:233], v[70:73]
	v_mfma_f32_16x16x32_bf16 v[66:69], v[194:197], v[230:233], v[66:69]
	s_setprio 0
	s_barrier
	s_add_i32 s64, s58, s50
	s_mov_b32 m0, s64
	ds_read_b128 v[198:201], v160 offset:16384
	ds_read_b128 v[202:205], v160 offset:17408
	ds_read_b128 v[206:209], v160 offset:18432
	ds_read_b128 v[210:213], v160 offset:19456
	ds_read_b128 v[214:217], v160 offset:20480
	ds_read_b128 v[218:221], v160 offset:21504
	ds_read_b128 v[222:225], v160 offset:22528
	ds_read_b128 v[230:233], v160 offset:23552
	global_load_lds_dwordx4 v[226:227], off
	s_add_i32 m0, s64, 0x2000
	s_add_u32 s64, s42, 0x40000
	s_addc_u32 s65, s43, 0
	s_add_i32 s66, s59, s50
	global_load_lds_dwordx4 v[234:235], off
	s_mov_b32 m0, s66
	s_nop 0
	global_load_lds_dwordx4 v134, s[64:65]
	s_add_i32 m0, s66, 0x2000
	s_nop 0
	global_load_lds_dwordx4 v136, s[64:65]
	s_mov_b32 m0, s37
	s_nop 0
	global_load_lds_dwordx4 v132, s[44:45]
	s_mov_b32 m0, s39
	s_nop 0
	global_load_lds_dwordx4 v236, s[44:45]
	s_waitcnt vmcnt(8)
	s_waitcnt lgkmcnt(0)
	v_lshl_add_u64 v[236:237], s[44:45], 0, v[236:237]
	s_barrier
	s_setprio 3
	s_waitcnt lgkmcnt(0)
	v_mfma_f32_16x16x32_bf16 v[62:65], v[166:169], v[198:201], v[62:65]
	v_mfma_f32_16x16x32_bf16 v[58:61], v[174:177], v[198:201], v[58:61]
	v_mfma_f32_16x16x32_bf16 v[38:41], v[166:169], v[206:209], v[38:41]
	v_mfma_f32_16x16x32_bf16 v[34:37], v[174:177], v[206:209], v[34:37]
	v_cndmask_b32_e32 v141, v140, v161, vcc
	v_mfma_f32_16x16x32_bf16 v[22:25], v[166:169], v[214:217], v[22:25]
	v_mfma_f32_16x16x32_bf16 v[18:21], v[174:177], v[214:217], v[18:21]
	v_mfma_f32_16x16x32_bf16 v[6:9], v[166:169], v[222:225], v[6:9]
	v_mfma_f32_16x16x32_bf16 v[2:5], v[174:177], v[222:225], v[2:5]
	v_mfma_f32_16x16x32_bf16 v[62:65], v[170:173], v[202:205], v[62:65]
	v_mfma_f32_16x16x32_bf16 v[58:61], v[178:181], v[202:205], v[58:61]
	v_mfma_f32_16x16x32_bf16 v[38:41], v[170:173], v[210:213], v[38:41]
	v_mfma_f32_16x16x32_bf16 v[34:37], v[178:181], v[210:213], v[34:37]
	v_mfma_f32_16x16x32_bf16 v[22:25], v[170:173], v[218:221], v[22:25]
	v_mfma_f32_16x16x32_bf16 v[18:21], v[178:181], v[218:221], v[18:21]
	v_mfma_f32_16x16x32_bf16 v[6:9], v[170:173], v[230:233], v[6:9]
	v_mfma_f32_16x16x32_bf16 v[2:5], v[178:181], v[230:233], v[2:5]
	s_setprio 0
	s_setprio 3
	v_mfma_f32_16x16x32_bf16 v[50:53], v[182:185], v[198:201], v[50:53]
	v_mfma_f32_16x16x32_bf16 v[42:45], v[190:193], v[198:201], v[42:45]
	v_mfma_f32_16x16x32_bf16 v[54:57], v[182:185], v[206:209], v[54:57]
	v_mfma_f32_16x16x32_bf16 v[46:49], v[190:193], v[206:209], v[46:49]
	v_mfma_f32_16x16x32_bf16 v[30:33], v[182:185], v[214:217], v[30:33]
	v_mfma_f32_16x16x32_bf16 v[26:29], v[190:193], v[214:217], v[26:29]
	v_mfma_f32_16x16x32_bf16 v[14:17], v[182:185], v[222:225], v[14:17]
	v_mfma_f32_16x16x32_bf16 v[10:13], v[190:193], v[222:225], v[10:13]
	v_mfma_f32_16x16x32_bf16 v[50:53], v[186:189], v[202:205], v[50:53]
	v_mfma_f32_16x16x32_bf16 v[42:45], v[194:197], v[202:205], v[42:45]
	v_mfma_f32_16x16x32_bf16 v[54:57], v[186:189], v[210:213], v[54:57]
	v_mfma_f32_16x16x32_bf16 v[46:49], v[194:197], v[210:213], v[46:49]
	v_mfma_f32_16x16x32_bf16 v[30:33], v[186:189], v[218:221], v[30:33]
	v_mfma_f32_16x16x32_bf16 v[26:29], v[194:197], v[218:221], v[26:29]
	v_mfma_f32_16x16x32_bf16 v[14:17], v[186:189], v[230:233], v[14:17]
	v_mfma_f32_16x16x32_bf16 v[10:13], v[194:197], v[230:233], v[10:13]
	s_setprio 0
	s_barrier
; #define PG8_STAGE_A(b, h, ptr, NX) do { if constexpr (Sched::GATHER) { unsigned gs_[2]; gs_[0] = ((NX) && last_) ? gN[h][0] : gA[h][0]; gs_[1] = ((NX) && last_) ? gN[h][1] : gA[h][1]; PG8_STAGE(PG8_SA(b, h), ptr, gs_); } \
;         else PG8_STAGE(PG8_SA(b, h), (ptr) + ((h) ? hstep : (size_t)0), voffA); } while (0)
; #define PG8_STAGE(bufoff, gbase, voff) do { _Pragma("unroll") for (int _i = 0; _i < 2; ++_i) \
;         __builtin_amdgcn_global_load_lds((const unsigned*)((const char*)(gbase) + (voff)[_i]), (PG8_LAS unsigned*)(lds + (bufoff) + ldsw + _i * 8192), 16, 0, 0); } while (0)
; #define PG8_LDA(dst, b, h) do { _Pragma("unroll") for (int m = 0; m < 4; ++m) _Pragma("unroll") for (int k = 0; k < 2; ++k) dst[m][k] = *(const PG8_LAS bf16x8*)(lds + PG8_SA(b, h) + aoff + m * 2048 + k * 1024); } while (0)
; #define PG8_LDB(dst, b, h) do { _Pragma("unroll") for (int n = 0; n < 2; ++n) _Pragma("unroll") for (int k = 0; k < 2; ++k) dst[n][k] = *(const PG8_LAS bf16x8*)(lds + PG8_SB(b, h) + boff + n * 2048 + k * 1024); } while (0)
; #define PG8_MMA(ai, bj, At, Bt) do { __builtin_amdgcn_s_setprio(1); _Pragma("unroll") for (int m = 0; m < 4; ++m) _Pragma("unroll") for (int n = 0; n < 2; ++n) _Pragma("unroll") for (int k = 0; k < 2; ++k) \
;         acc[ai][bj][m][n] = __builtin_amdgcn_mfma_f32_16x16x32_bf16(Bt[n][k], At[m][k], acc[ai][bj][m][n], 0, 0, 0); __builtin_amdgcn_s_setprio(0); } while (0)
; #define PG8_WAIT_V(n) asm volatile("s_waitcnt vmcnt(" #n ")" ::: "memory")
; #define PG8_WAIT_L(n) asm volatile("s_waitcnt lgkmcnt(" #n ")" ::: "memory")
; #define PG8_BAR __builtin_amdgcn_s_barrier()
; #define PG8_SCHED __builtin_amdgcn_sched_barrier(0)
; template <class Epi, class Sched, bool ALIGN_EPI = false, bool SP2 = false>
; __device__ __forceinline__ void gemm_phase(PG8_LAS unsigned char* lds, const Gemm g, const Sched& S, const Epi& E, const bool skip_epi = false) {
;     ...
;             PG8_LDB(B0, 1, 0); PG8_LDB(B1, 1, 1); PG8_SCHED; PG8_LDA(At, 1, 0); PG8_STAGE_A(0, 1, a2, true);
;             PG8_WAIT_V(8); PG8_WAIT_L(0); PG8_BAR; PG8_MMA(0, 0, At, B0); PG8_MMA(0, 1, At, B1); PG8_BAR; PG8_SCHED;
;             PG8_LDA(At, 1, 1); PG8_STAGE(PG8_SB(1, 0), b3, voffB); PG8_STAGE(PG8_SB(1, 1), b3 + hstep, voffB); PG8_STAGE_A(1, 0, a3, true);
;             PG8_WAIT_V(8); PG8_WAIT_L(0); PG8_BAR; PG8_MMA(1, 0, At, B0); PG8_MMA(1, 1, At, B1); PG8_BAR; PG8_SCHED;
	s_add_i32 s64, 0, 0x18000
	v_add_u32_e32 v132, s64, v154
	s_add_i32 s65, 0, 0x1c000
	ds_read_b128 v[166:169], v132
	ds_read_b128 v[170:173], v132 offset:1024
	ds_read_b128 v[174:177], v132 offset:2048
	ds_read_b128 v[178:181], v132 offset:3072
	v_add_u32_e32 v132, s65, v154
	ds_read_b128 v[182:185], v132
	ds_read_b128 v[186:189], v132 offset:1024
	ds_read_b128 v[190:193], v132 offset:2048
	ds_read_b128 v[194:197], v132 offset:3072
	s_mov_b32 m0, s51
	v_cndmask_b32_e32 v132, v142, v162, vcc
	ds_read_b128 v[198:201], v160 offset:32768
	ds_read_b128 v[202:205], v160 offset:33792
	ds_read_b128 v[206:209], v160 offset:34816
	ds_read_b128 v[210:213], v160 offset:35840
	ds_read_b128 v[214:217], v160 offset:36864
	ds_read_b128 v[218:221], v160 offset:37888
	ds_read_b128 v[222:225], v160 offset:38912
	ds_read_b128 v[230:233], v160 offset:39936
	global_load_lds_dwordx4 v132, s[44:45]
	s_mov_b32 m0, s52
	s_nop 0
	global_load_lds_dwordx4 v141, s[44:45]
	s_waitcnt vmcnt(8)
	s_waitcnt lgkmcnt(0)
	s_barrier
	s_setprio 3
	s_waitcnt lgkmcnt(0)
	v_mfma_f32_16x16x32_bf16 v[126:129], v[166:169], v[198:201], v[126:129]
	v_mfma_f32_16x16x32_bf16 v[122:125], v[174:177], v[198:201], v[122:125]
	v_mfma_f32_16x16x32_bf16 v[110:113], v[166:169], v[206:209], v[110:113]
	v_mfma_f32_16x16x32_bf16 v[106:109], v[174:177], v[206:209], v[106:109]
	v_mfma_f32_16x16x32_bf16 v[94:97], v[166:169], v[214:217], v[94:97]
	v_mfma_f32_16x16x32_bf16 v[90:93], v[174:177], v[214:217], v[90:93]
	v_mfma_f32_16x16x32_bf16 v[78:81], v[166:169], v[222:225], v[78:81]
	v_mfma_f32_16x16x32_bf16 v[74:77], v[174:177], v[222:225], v[74:77]
	v_mfma_f32_16x16x32_bf16 v[126:129], v[170:173], v[202:205], v[126:129]
	v_mfma_f32_16x16x32_bf16 v[122:125], v[178:181], v[202:205], v[122:125]
	v_mfma_f32_16x16x32_bf16 v[110:113], v[170:173], v[210:213], v[110:113]
	v_mfma_f32_16x16x32_bf16 v[106:109], v[178:181], v[210:213], v[106:109]
	v_mfma_f32_16x16x32_bf16 v[94:97], v[170:173], v[218:221], v[94:97]
	v_mfma_f32_16x16x32_bf16 v[90:93], v[178:181], v[218:221], v[90:93]
	v_mfma_f32_16x16x32_bf16 v[78:81], v[170:173], v[230:233], v[78:81]
	v_mfma_f32_16x16x32_bf16 v[74:77], v[178:181], v[230:233], v[74:77]
	s_setprio 0
	s_setprio 3
	v_mfma_f32_16x16x32_bf16 v[118:121], v[182:185], v[198:201], v[118:121]
	v_mfma_f32_16x16x32_bf16 v[114:117], v[190:193], v[198:201], v[114:117]
	v_mfma_f32_16x16x32_bf16 v[102:105], v[182:185], v[206:209], v[102:105]
	v_mfma_f32_16x16x32_bf16 v[98:101], v[190:193], v[206:209], v[98:101]
	v_mfma_f32_16x16x32_bf16 v[86:89], v[182:185], v[214:217], v[86:89]
	v_mfma_f32_16x16x32_bf16 v[82:85], v[190:193], v[214:217], v[82:85]
	v_mfma_f32_16x16x32_bf16 v[70:73], v[182:185], v[222:225], v[70:73]
	v_mfma_f32_16x16x32_bf16 v[66:69], v[190:193], v[222:225], v[66:69]
	v_mfma_f32_16x16x32_bf16 v[118:121], v[186:189], v[202:205], v[118:121]
	v_mfma_f32_16x16x32_bf16 v[114:117], v[194:197], v[202:205], v[114:117]
	v_mfma_f32_16x16x32_bf16 v[102:105], v[186:189], v[210:213], v[102:105]
	v_mfma_f32_16x16x32_bf16 v[98:101], v[194:197], v[210:213], v[98:101]
	v_mfma_f32_16x16x32_bf16 v[86:89], v[186:189], v[218:221], v[86:89]
	v_mfma_f32_16x16x32_bf16 v[82:85], v[194:197], v[218:221], v[82:85]
	v_mfma_f32_16x16x32_bf16 v[70:73], v[186:189], v[230:233], v[70:73]
	v_mfma_f32_16x16x32_bf16 v[66:69], v[194:197], v[230:233], v[66:69]
	s_setprio 0
	s_barrier
	s_add_i32 s44, s64, s50
	s_add_i32 m0, s44, 0xffffff80
	ds_read_b128 v[198:201], v160 offset:49152
	ds_read_b128 v[202:205], v160 offset:50176
	ds_read_b128 v[206:209], v160 offset:51200
	ds_read_b128 v[210:213], v160 offset:52224
	ds_read_b128 v[214:217], v160 offset:53248
	ds_read_b128 v[218:221], v160 offset:54272
	ds_read_b128 v[222:225], v160 offset:55296
	ds_read_b128 v[230:233], v160 offset:56320
	global_load_lds_dwordx4 v[226:227], off offset:128
	s_add_i32 m0, s44, 0x1f80
	s_add_u32 s42, s42, 0x40080
	s_addc_u32 s43, s43, 0
	s_add_i32 s44, s65, s50
	global_load_lds_dwordx4 v[234:235], off offset:128
	s_mov_b32 m0, s44
	s_nop 0
	global_load_lds_dwordx4 v134, s[42:43]
	s_add_i32 m0, s44, 0x2000
	s_nop 0
	global_load_lds_dwordx4 v136, s[42:43]
	s_add_i32 m0, s55, 0xffffff80
	s_nop 0
	global_load_lds_dwordx4 v[238:239], off offset:128
	s_add_i32 m0, s56, 0xffffff80
	s_nop 0
	global_load_lds_dwordx4 v[236:237], off offset:128
	s_waitcnt vmcnt(8)
	s_waitcnt lgkmcnt(0)
	s_barrier
	s_setprio 3
	s_waitcnt lgkmcnt(0)
	v_mfma_f32_16x16x32_bf16 v[62:65], v[166:169], v[198:201], v[62:65]
	v_mfma_f32_16x16x32_bf16 v[58:61], v[174:177], v[198:201], v[58:61]
	v_mfma_f32_16x16x32_bf16 v[38:41], v[166:169], v[206:209], v[38:41]
	v_mfma_f32_16x16x32_bf16 v[34:37], v[174:177], v[206:209], v[34:37]
	v_mfma_f32_16x16x32_bf16 v[22:25], v[166:169], v[214:217], v[22:25]
	v_mfma_f32_16x16x32_bf16 v[18:21], v[174:177], v[214:217], v[18:21]
	v_mfma_f32_16x16x32_bf16 v[6:9], v[166:169], v[222:225], v[6:9]
	v_mfma_f32_16x16x32_bf16 v[2:5], v[174:177], v[222:225], v[2:5]
	v_mfma_f32_16x16x32_bf16 v[62:65], v[170:173], v[202:205], v[62:65]
	v_mfma_f32_16x16x32_bf16 v[58:61], v[178:181], v[202:205], v[58:61]
	v_mfma_f32_16x16x32_bf16 v[38:41], v[170:173], v[210:213], v[38:41]
	v_mfma_f32_16x16x32_bf16 v[34:37], v[178:181], v[210:213], v[34:37]
	v_mfma_f32_16x16x32_bf16 v[22:25], v[170:173], v[218:221], v[22:25]
	v_mfma_f32_16x16x32_bf16 v[18:21], v[178:181], v[218:221], v[18:21]
	v_mfma_f32_16x16x32_bf16 v[6:9], v[170:173], v[230:233], v[6:9]
	v_mfma_f32_16x16x32_bf16 v[2:5], v[178:181], v[230:233], v[2:5]
	s_setprio 0
	s_setprio 3
	v_mfma_f32_16x16x32_bf16 v[50:53], v[182:185], v[198:201], v[50:53]
	v_mfma_f32_16x16x32_bf16 v[42:45], v[190:193], v[198:201], v[42:45]
	v_mfma_f32_16x16x32_bf16 v[54:57], v[182:185], v[206:209], v[54:57]
	v_mfma_f32_16x16x32_bf16 v[46:49], v[190:193], v[206:209], v[46:49]
	v_mfma_f32_16x16x32_bf16 v[30:33], v[182:185], v[214:217], v[30:33]
	v_mfma_f32_16x16x32_bf16 v[26:29], v[190:193], v[214:217], v[26:29]
	v_mfma_f32_16x16x32_bf16 v[14:17], v[182:185], v[222:225], v[14:17]
	v_mfma_f32_16x16x32_bf16 v[10:13], v[190:193], v[222:225], v[10:13]
	v_mfma_f32_16x16x32_bf16 v[50:53], v[186:189], v[202:205], v[50:53]
	v_mfma_f32_16x16x32_bf16 v[42:45], v[194:197], v[202:205], v[42:45]
	v_mfma_f32_16x16x32_bf16 v[54:57], v[186:189], v[210:213], v[54:57]
	v_mfma_f32_16x16x32_bf16 v[46:49], v[194:197], v[210:213], v[46:49]
	v_mfma_f32_16x16x32_bf16 v[30:33], v[186:189], v[218:221], v[30:33]
	v_mfma_f32_16x16x32_bf16 v[26:29], v[194:197], v[218:221], v[26:29]
	v_mfma_f32_16x16x32_bf16 v[14:17], v[186:189], v[230:233], v[14:17]
	v_mfma_f32_16x16x32_bf16 v[10:13], v[194:197], v[230:233], v[10:13]
	s_setprio 0
	s_barrier
	s_add_i32 s63, s63, 2
	s_add_u32 s40, s40, 0x100
	s_addc_u32 s41, s41, 0
	s_cmp_gt_u32 s63, 13
	s_cbranch_scc0 .LBB0_1728
	s_and_b64 vcc, exec, s[26:27]
	s_cbranch_vccz .LBB0_1731
	s_barrier

; #define PG8_STAGE_A(b, h, ptr, NX) do { if constexpr (Sched::GATHER) { unsigned gs_[2]; gs_[0] = ((NX) && last_) ? gN[h][0] : gA[h][0]; gs_[1] = ((NX) && last_) ? gN[h][1] : gA[h][1]; PG8_STAGE(PG8_SA(b, h), ptr, gs_); } \
;         else PG8_STAGE(PG8_SA(b, h), (ptr) + ((h) ? hstep : (size_t)0), voffA); } while (0)
; #define PG8_STAGE(bufoff, gbase, voff) do { _Pragma("unroll") for (int _i = 0; _i < 2; ++_i) \
;         __builtin_amdgcn_global_load_lds((const unsigned*)((const char*)(gbase) + (voff)[_i]), (PG8_LAS unsigned*)(lds + (bufoff) + ldsw + _i * 8192), 16, 0, 0); } while (0)
; #define PG8_LDA(dst, b, h) do { _Pragma("unroll") for (int m = 0; m < 4; ++m) _Pragma("unroll") for (int k = 0; k < 2; ++k) dst[m][k] = *(const PG8_LAS bf16x8*)(lds + PG8_SA(b, h) + aoff + m * 2048 + k * 1024); } while (0)
; #define PG8_LDB(dst, b, h) do { _Pragma("unroll") for (int n = 0; n < 2; ++n) _Pragma("unroll") for (int k = 0; k < 2; ++k) dst[n][k] = *(const PG8_LAS bf16x8*)(lds + PG8_SB(b, h) + boff + n * 2048 + k * 1024); } while (0)
; #define PG8_WAIT_V(n) asm volatile("s_waitcnt vmcnt(" #n ")" ::: "memory")
; #define PG8_WAIT_L(n) asm volatile("s_waitcnt lgkmcnt(" #n ")" ::: "memory")
; #define PG8_BAR __builtin_amdgcn_s_barrier()
; #define PG8_SCHED __builtin_amdgcn_sched_barrier(0)
; template <class Epi, class Sched, bool ALIGN_EPI = false, bool SP2 = false>
; __device__ __forceinline__ void gemm_phase(PG8_LAS unsigned char* lds, const Gemm g, const Sched& S, const Epi& E, const bool skip_epi = false) {
;     ...
;             const bool last = (t == nt - 2); last_ = last && has_next;
;             const char* a1 = cA + (size_t)(t + 1) * kstep;
;             const char* a2 = last ? nA : cA + (size_t)(t + 2) * kstep; const char* b2 = last ? nB : cB + (size_t)(t + 2) * kstep;
;             const char* a3 = a2 + kstep; const char* b3 = b2 + kstep;
;             if (last && has_next) S.a_ready(nxt);
;             if constexpr (SP2) {
;             PG8_LDB(B0, 0, 0); PG8_LDB(B1, 0, 1); PG8_SCHED; PG8_LDA(At, 0, 0); PG8_STAGE_A(1, 1, a1, false);
;             PG8_WAIT_V(8); PG8_WAIT_L(0); PG8_BAR; PG8_MMA(0, 0, At, B0); PG8_MMA(0, 1, At, B1); PG8_BAR; PG8_SCHED;
;             PG8_LDA(At, 0, 1); PG8_STAGE(PG8_SB(0, 0), b2, voffB); PG8_STAGE(PG8_SB(0, 1), b2 + hstep, voffB); PG8_STAGE_A(0, 0, a2, true);
.LBB0_1822:
	s_add_u32 s67, s40, 0x100
	s_addc_u32 s68, s41, 0
	s_mov_b32 s69, -2
	ds_read_b128 v[160:163], v157
	ds_read_b128 v[164:167], v157 offset:1024
	ds_read_b128 v[168:171], v157 offset:2048
	ds_read_b128 v[172:175], v157 offset:3072
	ds_read_b128 v[176:179], v158
	ds_read_b128 v[180:183], v158 offset:1024
	ds_read_b128 v[184:187], v158 offset:2048
	ds_read_b128 v[188:191], v158 offset:3072
	s_add_u32 s40, s38, 0x100
	s_addc_u32 s41, s39, 0
	s_cmp_eq_u32 s69, 52
	s_cselect_b32 s45, s7, s41
	s_cselect_b32 s44, s6, s40
	s_cselect_b32 s43, s35, s68
	s_cselect_b32 s42, s34, s67
	v_lshl_add_u64 v[152:153], s[38:39], 0, v[140:141]
	s_add_i32 m0, s37, 0xc000
	ds_read_b128 v[192:195], v159
	ds_read_b128 v[196:199], v159 offset:1024
	ds_read_b128 v[200:203], v159 offset:2048
	ds_read_b128 v[204:207], v159 offset:3072
	ds_read_b128 v[208:211], v159 offset:4096
	ds_read_b128 v[212:215], v159 offset:5120
	ds_read_b128 v[216:219], v159 offset:6144
	ds_read_b128 v[220:223], v159 offset:7168
	global_load_lds_dwordx4 v[152:153], off
	v_lshl_add_u64 v[152:153], s[38:39], 0, v[142:143]
	s_add_i32 m0, s37, 0xe000
	s_nop 0
	global_load_lds_dwordx4 v[152:153], off
	s_waitcnt vmcnt(8)
	s_waitcnt lgkmcnt(0)
	s_barrier
	s_setprio 3
	s_waitcnt lgkmcnt(0)
	v_mfma_f32_16x16x32_bf16 v[126:129], v[160:163], v[192:195], 0
	v_mfma_f32_16x16x32_bf16 v[122:125], v[168:171], v[192:195], 0
	v_mfma_f32_16x16x32_bf16 v[118:121], v[160:163], v[200:203], 0
	v_mfma_f32_16x16x32_bf16 v[114:117], v[168:171], v[200:203], 0
	v_lshl_add_u64 v[152:153], s[42:43], 0, v[134:135]
	v_mfma_f32_16x16x32_bf16 v[106:109], v[160:163], v[208:211], 0
	v_mfma_f32_16x16x32_bf16 v[98:101], v[168:171], v[208:211], 0
	v_lshl_add_u64 v[224:225], s[42:43], 0, v[138:139]
	v_mfma_f32_16x16x32_bf16 v[78:81], v[160:163], v[216:219], 0
	v_mfma_f32_16x16x32_bf16 v[74:77], v[168:171], v[216:219], 0
	v_lshl_add_u64 v[230:231], s[44:45], 0, v[136:137]
	v_mfma_f32_16x16x32_bf16 v[126:129], v[164:167], v[196:199], v[126:129]
	v_mfma_f32_16x16x32_bf16 v[122:125], v[172:175], v[196:199], v[122:125]
	v_lshl_add_u64 v[226:227], s[44:45], 0, v[132:133]
	v_mfma_f32_16x16x32_bf16 v[118:121], v[164:167], v[204:207], v[118:121]
	v_mfma_f32_16x16x32_bf16 v[114:117], v[172:175], v[204:207], v[114:117]
	v_mfma_f32_16x16x32_bf16 v[106:109], v[164:167], v[212:215], v[106:109]
	v_mfma_f32_16x16x32_bf16 v[98:101], v[172:175], v[212:215], v[98:101]
	v_mfma_f32_16x16x32_bf16 v[78:81], v[164:167], v[220:223], v[78:81]
	v_mfma_f32_16x16x32_bf16 v[74:77], v[172:175], v[220:223], v[74:77]
	s_setprio 0
	s_setprio 3
	v_mfma_f32_16x16x32_bf16 v[110:113], v[176:179], v[192:195], 0
	v_mfma_f32_16x16x32_bf16 v[102:105], v[184:187], v[192:195], 0
	v_mfma_f32_16x16x32_bf16 v[94:97], v[176:179], v[200:203], 0
	v_mfma_f32_16x16x32_bf16 v[90:93], v[184:187], v[200:203], 0
	v_mfma_f32_16x16x32_bf16 v[86:89], v[176:179], v[208:211], 0
	v_mfma_f32_16x16x32_bf16 v[82:85], v[184:187], v[208:211], 0
	v_mfma_f32_16x16x32_bf16 v[70:73], v[176:179], v[216:219], 0
	v_mfma_f32_16x16x32_bf16 v[66:69], v[184:187], v[216:219], 0
	v_mfma_f32_16x16x32_bf16 v[110:113], v[180:183], v[196:199], v[110:113]
	v_mfma_f32_16x16x32_bf16 v[102:105], v[188:191], v[196:199], v[102:105]
	v_mfma_f32_16x16x32_bf16 v[94:97], v[180:183], v[204:207], v[94:97]
	v_mfma_f32_16x16x32_bf16 v[90:93], v[188:191], v[204:207], v[90:93]
	v_mfma_f32_16x16x32_bf16 v[86:89], v[180:183], v[212:215], v[86:89]
	v_mfma_f32_16x16x32_bf16 v[82:85], v[188:191], v[212:215], v[82:85]
	v_mfma_f32_16x16x32_bf16 v[70:73], v[180:183], v[220:223], v[70:73]
	v_mfma_f32_16x16x32_bf16 v[66:69], v[188:191], v[220:223], v[66:69]
	s_setprio 0
	s_barrier
	s_add_i32 s38, s60, s51
	s_mov_b32 m0, s38
	ds_read_b128 v[192:195], v159 offset:16384
	ds_read_b128 v[196:199], v159 offset:17408
	ds_read_b128 v[200:203], v159 offset:18432
	ds_read_b128 v[204:207], v159 offset:19456
	ds_read_b128 v[208:211], v159 offset:20480
	ds_read_b128 v[212:215], v159 offset:21504
	ds_read_b128 v[216:219], v159 offset:22528
	ds_read_b128 v[220:223], v159 offset:23552
	global_load_lds_dwordx4 v[152:153], off
	s_add_i32 m0, s38, 0x2000
	s_add_u32 s38, s42, 0xe0000
	s_addc_u32 s39, s43, 0
	s_add_i32 s70, s61, s51
	global_load_lds_dwordx4 v[224:225], off
	s_mov_b32 m0, s70
	s_nop 0
	global_load_lds_dwordx4 v134, s[38:39]
	s_add_i32 m0, s70, 0x2000
	s_nop 0
	global_load_lds_dwordx4 v138, s[38:39]
	s_mov_b32 m0, s37
	s_nop 0
	global_load_lds_dwordx4 v[226:227], off
	s_mov_b32 m0, s52
	s_nop 0
	global_load_lds_dwordx4 v[230:231], off
	s_waitcnt vmcnt(8)
	s_waitcnt lgkmcnt(0)
	s_barrier
; #define PG8_STAGE_A(b, h, ptr, NX) do { if constexpr (Sched::GATHER) { unsigned gs_[2]; gs_[0] = ((NX) && last_) ? gN[h][0] : gA[h][0]; gs_[1] = ((NX) && last_) ? gN[h][1] : gA[h][1]; PG8_STAGE(PG8_SA(b, h), ptr, gs_); } \
;         else PG8_STAGE(PG8_SA(b, h), (ptr) + ((h) ? hstep : (size_t)0), voffA); } while (0)
; #define PG8_LDA(dst, b, h) do { _Pragma("unroll") for (int m = 0; m < 4; ++m) _Pragma("unroll") for (int k = 0; k < 2; ++k) dst[m][k] = *(const PG8_LAS bf16x8*)(lds + PG8_SA(b, h) + aoff + m * 2048 + k * 1024); } while (0)
; #define PG8_LDB(dst, b, h) do { _Pragma("unroll") for (int n = 0; n < 2; ++n) _Pragma("unroll") for (int k = 0; k < 2; ++k) dst[n][k] = *(const PG8_LAS bf16x8*)(lds + PG8_SB(b, h) + boff + n * 2048 + k * 1024); } while (0)
; #define PG8_MMA(ai, bj, At, Bt) do { __builtin_amdgcn_s_setprio(1); _Pragma("unroll") for (int m = 0; m < 4; ++m) _Pragma("unroll") for (int n = 0; n < 2; ++n) _Pragma("unroll") for (int k = 0; k < 2; ++k) \
;         acc[ai][bj][m][n] = __builtin_amdgcn_mfma_f32_16x16x32_bf16(Bt[n][k], At[m][k], acc[ai][bj][m][n], 0, 0, 0); __builtin_amdgcn_s_setprio(0); } while (0)
; #define PG8_WAIT_V(n) asm volatile("s_waitcnt vmcnt(" #n ")" ::: "memory")
; #define PG8_WAIT_L(n) asm volatile("s_waitcnt lgkmcnt(" #n ")" ::: "memory")
; #define PG8_BAR __builtin_amdgcn_s_barrier()
; #define PG8_SCHED __builtin_amdgcn_sched_barrier(0)
; template <class Epi, class Sched, bool ALIGN_EPI = false, bool SP2 = false>
; __device__ __forceinline__ void gemm_phase(PG8_LAS unsigned char* lds, const Gemm g, const Sched& S, const Epi& E, const bool skip_epi = false) {
;     ...
;             PG8_WAIT_V(8); PG8_WAIT_L(0); PG8_BAR; PG8_MMA(1, 0, At, B0); PG8_MMA(1, 1, At, B1); PG8_BAR; PG8_SCHED;
;             PG8_LDB(B0, 1, 0); PG8_LDB(B1, 1, 1); PG8_SCHED; PG8_LDA(At, 1, 0); PG8_STAGE_A(0, 1, a2, true);
;             PG8_WAIT_V(8); PG8_WAIT_L(0); PG8_BAR; PG8_MMA(0, 0, At, B0); PG8_MMA(0, 1, At, B1); PG8_BAR; PG8_SCHED;
	s_setprio 3
	s_waitcnt lgkmcnt(0)
	v_mfma_f32_16x16x32_bf16 v[62:65], v[160:163], v[192:195], 0
	v_mfma_f32_16x16x32_bf16 v[58:61], v[168:171], v[192:195], 0
	v_mfma_f32_16x16x32_bf16 v[50:53], v[160:163], v[200:203], 0
	v_mfma_f32_16x16x32_bf16 v[42:45], v[168:171], v[200:203], 0
	v_mfma_f32_16x16x32_bf16 v[34:37], v[160:163], v[208:211], 0
	v_mfma_f32_16x16x32_bf16 v[26:29], v[168:171], v[208:211], 0
	v_mfma_f32_16x16x32_bf16 v[18:21], v[160:163], v[216:219], 0
	v_mfma_f32_16x16x32_bf16 v[10:13], v[168:171], v[216:219], 0
	v_mfma_f32_16x16x32_bf16 v[62:65], v[164:167], v[196:199], v[62:65]
	v_mfma_f32_16x16x32_bf16 v[58:61], v[172:175], v[196:199], v[58:61]
	v_mfma_f32_16x16x32_bf16 v[50:53], v[164:167], v[204:207], v[50:53]
	v_mfma_f32_16x16x32_bf16 v[42:45], v[172:175], v[204:207], v[42:45]
	v_mfma_f32_16x16x32_bf16 v[34:37], v[164:167], v[212:215], v[34:37]
	v_mfma_f32_16x16x32_bf16 v[26:29], v[172:175], v[212:215], v[26:29]
	v_mfma_f32_16x16x32_bf16 v[18:21], v[164:167], v[220:223], v[18:21]
	v_mfma_f32_16x16x32_bf16 v[10:13], v[172:175], v[220:223], v[10:13]
	s_setprio 0
	s_setprio 3
	v_mfma_f32_16x16x32_bf16 v[54:57], v[176:179], v[192:195], 0
	v_mfma_f32_16x16x32_bf16 v[46:49], v[184:187], v[192:195], 0
	v_mfma_f32_16x16x32_bf16 v[38:41], v[176:179], v[200:203], 0
	v_mfma_f32_16x16x32_bf16 v[30:33], v[184:187], v[200:203], 0
	v_mfma_f32_16x16x32_bf16 v[22:25], v[176:179], v[208:211], 0
	v_mfma_f32_16x16x32_bf16 v[14:17], v[184:187], v[208:211], 0
	v_mfma_f32_16x16x32_bf16 v[6:9], v[176:179], v[216:219], 0
	v_mfma_f32_16x16x32_bf16 v[2:5], v[184:187], v[216:219], 0
	v_mfma_f32_16x16x32_bf16 v[54:57], v[180:183], v[196:199], v[54:57]
	v_mfma_f32_16x16x32_bf16 v[46:49], v[188:191], v[196:199], v[46:49]
	v_mfma_f32_16x16x32_bf16 v[38:41], v[180:183], v[204:207], v[38:41]
	v_mfma_f32_16x16x32_bf16 v[30:33], v[188:191], v[204:207], v[30:33]
	v_mfma_f32_16x16x32_bf16 v[22:25], v[180:183], v[212:215], v[22:25]
	v_mfma_f32_16x16x32_bf16 v[14:17], v[188:191], v[212:215], v[14:17]
	v_mfma_f32_16x16x32_bf16 v[6:9], v[180:183], v[220:223], v[6:9]
	v_mfma_f32_16x16x32_bf16 v[2:5], v[188:191], v[220:223], v[2:5]
	s_setprio 0
	s_barrier
	s_add_i32 s70, 0, 0x18000
	v_add_u32_e32 v130, s70, v147
	s_add_i32 s71, 0, 0x1c000
	ds_read_b128 v[160:163], v130
	ds_read_b128 v[164:167], v130 offset:1024
	ds_read_b128 v[168:171], v130 offset:2048
	ds_read_b128 v[172:175], v130 offset:3072
	v_add_u32_e32 v130, s71, v147
	ds_read_b128 v[176:179], v130
	ds_read_b128 v[180:183], v130 offset:1024
	ds_read_b128 v[184:187], v130 offset:2048
	ds_read_b128 v[188:191], v130 offset:3072
	s_add_u32 s38, s44, 0xe0000
	s_addc_u32 s39, s45, 0
	s_mov_b32 m0, s53
	ds_read_b128 v[192:195], v159 offset:32768
	ds_read_b128 v[196:199], v159 offset:33792
	ds_read_b128 v[200:203], v159 offset:34816
	ds_read_b128 v[204:207], v159 offset:35840
	ds_read_b128 v[208:211], v159 offset:36864
	ds_read_b128 v[212:215], v159 offset:37888
	ds_read_b128 v[216:219], v159 offset:38912
	ds_read_b128 v[220:223], v159 offset:39936
	global_load_lds_dwordx4 v132, s[38:39]
	s_mov_b32 m0, s54
	s_nop 0
	global_load_lds_dwordx4 v136, s[38:39]
	s_waitcnt vmcnt(8)
	s_waitcnt lgkmcnt(0)
	s_barrier
	s_setprio 3
	s_waitcnt lgkmcnt(0)
	v_mfma_f32_16x16x32_bf16 v[126:129], v[160:163], v[192:195], v[126:129]
	v_mfma_f32_16x16x32_bf16 v[122:125], v[168:171], v[192:195], v[122:125]
	v_mfma_f32_16x16x32_bf16 v[118:121], v[160:163], v[200:203], v[118:121]
	v_mfma_f32_16x16x32_bf16 v[114:117], v[168:171], v[200:203], v[114:117]
	v_mfma_f32_16x16x32_bf16 v[106:109], v[160:163], v[208:211], v[106:109]
	v_mfma_f32_16x16x32_bf16 v[98:101], v[168:171], v[208:211], v[98:101]
	v_mfma_f32_16x16x32_bf16 v[78:81], v[160:163], v[216:219], v[78:81]
	v_mfma_f32_16x16x32_bf16 v[74:77], v[168:171], v[216:219], v[74:77]
	v_mfma_f32_16x16x32_bf16 v[126:129], v[164:167], v[196:199], v[126:129]
	v_mfma_f32_16x16x32_bf16 v[122:125], v[172:175], v[196:199], v[122:125]
	v_mfma_f32_16x16x32_bf16 v[118:121], v[164:167], v[204:207], v[118:121]
	v_mfma_f32_16x16x32_bf16 v[114:117], v[172:175], v[204:207], v[114:117]
	v_mfma_f32_16x16x32_bf16 v[106:109], v[164:167], v[212:215], v[106:109]
	v_mfma_f32_16x16x32_bf16 v[98:101], v[172:175], v[212:215], v[98:101]
	v_mfma_f32_16x16x32_bf16 v[78:81], v[164:167], v[220:223], v[78:81]
	v_mfma_f32_16x16x32_bf16 v[74:77], v[172:175], v[220:223], v[74:77]
	s_setprio 0
	s_setprio 3
	v_mfma_f32_16x16x32_bf16 v[110:113], v[176:179], v[192:195], v[110:113]
	v_mfma_f32_16x16x32_bf16 v[102:105], v[184:187], v[192:195], v[102:105]
	v_mfma_f32_16x16x32_bf16 v[94:97], v[176:179], v[200:203], v[94:97]
	v_mfma_f32_16x16x32_bf16 v[90:93], v[184:187], v[200:203], v[90:93]
	v_mfma_f32_16x16x32_bf16 v[86:89], v[176:179], v[208:211], v[86:89]
	v_mfma_f32_16x16x32_bf16 v[82:85], v[184:187], v[208:211], v[82:85]
	v_mfma_f32_16x16x32_bf16 v[70:73], v[176:179], v[216:219], v[70:73]
	v_mfma_f32_16x16x32_bf16 v[66:69], v[184:187], v[216:219], v[66:69]
	v_mfma_f32_16x16x32_bf16 v[110:113], v[180:183], v[196:199], v[110:113]
	v_mfma_f32_16x16x32_bf16 v[102:105], v[188:191], v[196:199], v[102:105]
	v_mfma_f32_16x16x32_bf16 v[94:97], v[180:183], v[204:207], v[94:97]
	v_mfma_f32_16x16x32_bf16 v[90:93], v[188:191], v[204:207], v[90:93]
	v_mfma_f32_16x16x32_bf16 v[86:89], v[180:183], v[212:215], v[86:89]
	v_mfma_f32_16x16x32_bf16 v[82:85], v[188:191], v[212:215], v[82:85]
	v_mfma_f32_16x16x32_bf16 v[70:73], v[180:183], v[220:223], v[70:73]
	v_mfma_f32_16x16x32_bf16 v[66:69], v[188:191], v[220:223], v[66:69]
	s_setprio 0
	s_barrier
; #define PG8_STAGE_A(b, h, ptr, NX) do { if constexpr (Sched::GATHER) { unsigned gs_[2]; gs_[0] = ((NX) && last_) ? gN[h][0] : gA[h][0]; gs_[1] = ((NX) && last_) ? gN[h][1] : gA[h][1]; PG8_STAGE(PG8_SA(b, h), ptr, gs_); } \
;         else PG8_STAGE(PG8_SA(b, h), (ptr) + ((h) ? hstep : (size_t)0), voffA); } while (0)
; #define PG8_STAGE(bufoff, gbase, voff) do { _Pragma("unroll") for (int _i = 0; _i < 2; ++_i) \
;         __builtin_amdgcn_global_load_lds((const unsigned*)((const char*)(gbase) + (voff)[_i]), (PG8_LAS unsigned*)(lds + (bufoff) + ldsw + _i * 8192), 16, 0, 0); } while (0)
; #define PG8_LDA(dst, b, h) do { _Pragma("unroll") for (int m = 0; m < 4; ++m) _Pragma("unroll") for (int k = 0; k < 2; ++k) dst[m][k] = *(const PG8_LAS bf16x8*)(lds + PG8_SA(b, h) + aoff + m * 2048 + k * 1024); } while (0)
; #define PG8_MMA(ai, bj, At, Bt) do { __builtin_amdgcn_s_setprio(1); _Pragma("unroll") for (int m = 0; m < 4; ++m) _Pragma("unroll") for (int n = 0; n < 2; ++n) _Pragma("unroll") for (int k = 0; k < 2; ++k) \
;         acc[ai][bj][m][n] = __builtin_amdgcn_mfma_f32_16x16x32_bf16(Bt[n][k], At[m][k], acc[ai][bj][m][n], 0, 0, 0); __builtin_amdgcn_s_setprio(0); } while (0)
; #define PG8_WAIT_V(n) asm volatile("s_waitcnt vmcnt(" #n ")" ::: "memory")
; #define PG8_WAIT_L(n) asm volatile("s_waitcnt lgkmcnt(" #n ")" ::: "memory")
; #define PG8_BAR __builtin_amdgcn_s_barrier()
; #define PG8_SCHED __builtin_amdgcn_sched_barrier(0)
; template <class Epi, class Sched, bool ALIGN_EPI = false, bool SP2 = false>
; __device__ __forceinline__ void gemm_phase(PG8_LAS unsigned char* lds, const Gemm g, const Sched& S, const Epi& E, const bool skip_epi = false) {
;     ...
;             PG8_LDA(At, 1, 1); PG8_STAGE(PG8_SB(1, 0), b3, voffB); PG8_STAGE(PG8_SB(1, 1), b3 + hstep, voffB); PG8_STAGE_A(1, 0, a3, true);
;             PG8_WAIT_V(8); PG8_WAIT_L(0); PG8_BAR; PG8_MMA(1, 0, At, B0); PG8_MMA(1, 1, At, B1); PG8_BAR; PG8_SCHED;
	s_add_i32 s38, s70, s51
	s_add_i32 m0, s38, 0xffffff80
	ds_read_b128 v[192:195], v159 offset:49152
	ds_read_b128 v[196:199], v159 offset:50176
	ds_read_b128 v[200:203], v159 offset:51200
	ds_read_b128 v[204:207], v159 offset:52224
	ds_read_b128 v[208:211], v159 offset:53248
	ds_read_b128 v[212:215], v159 offset:54272
	ds_read_b128 v[216:219], v159 offset:55296
	ds_read_b128 v[220:223], v159 offset:56320
	global_load_lds_dwordx4 v[152:153], off offset:128
	s_add_i32 m0, s38, 0x1f80
	s_add_u32 s38, s42, 0xe0080
	s_addc_u32 s39, s43, 0
	s_add_i32 s42, s71, s51
	global_load_lds_dwordx4 v[224:225], off offset:128
	s_mov_b32 m0, s42
	s_nop 0
	global_load_lds_dwordx4 v134, s[38:39]
	s_add_i32 m0, s42, 0x2000
	s_nop 0
	global_load_lds_dwordx4 v138, s[38:39]
	s_add_i32 m0, s57, 0xffffff80
	s_nop 0
	global_load_lds_dwordx4 v[226:227], off offset:128
	s_add_i32 m0, s58, 0xffffff80
	s_nop 0
	global_load_lds_dwordx4 v[230:231], off offset:128
	s_waitcnt vmcnt(8)
	s_waitcnt lgkmcnt(0)
	s_barrier
	s_setprio 3
	s_waitcnt lgkmcnt(0)
	v_mfma_f32_16x16x32_bf16 v[62:65], v[160:163], v[192:195], v[62:65]
	v_mfma_f32_16x16x32_bf16 v[58:61], v[168:171], v[192:195], v[58:61]
	v_mfma_f32_16x16x32_bf16 v[50:53], v[160:163], v[200:203], v[50:53]
	v_mfma_f32_16x16x32_bf16 v[42:45], v[168:171], v[200:203], v[42:45]
	v_mfma_f32_16x16x32_bf16 v[34:37], v[160:163], v[208:211], v[34:37]
	v_mfma_f32_16x16x32_bf16 v[26:29], v[168:171], v[208:211], v[26:29]
	v_mfma_f32_16x16x32_bf16 v[18:21], v[160:163], v[216:219], v[18:21]
	v_mfma_f32_16x16x32_bf16 v[10:13], v[168:171], v[216:219], v[10:13]
	v_mfma_f32_16x16x32_bf16 v[62:65], v[164:167], v[196:199], v[62:65]
	v_mfma_f32_16x16x32_bf16 v[58:61], v[172:175], v[196:199], v[58:61]
	v_mfma_f32_16x16x32_bf16 v[50:53], v[164:167], v[204:207], v[50:53]
	v_mfma_f32_16x16x32_bf16 v[42:45], v[172:175], v[204:207], v[42:45]
	v_mfma_f32_16x16x32_bf16 v[34:37], v[164:167], v[212:215], v[34:37]
	v_mfma_f32_16x16x32_bf16 v[26:29], v[172:175], v[212:215], v[26:29]
	v_mfma_f32_16x16x32_bf16 v[18:21], v[164:167], v[220:223], v[18:21]
	v_mfma_f32_16x16x32_bf16 v[10:13], v[172:175], v[220:223], v[10:13]
	s_setprio 0
	s_setprio 3
	v_mfma_f32_16x16x32_bf16 v[54:57], v[176:179], v[192:195], v[54:57]
	v_mfma_f32_16x16x32_bf16 v[46:49], v[184:187], v[192:195], v[46:49]
	v_mfma_f32_16x16x32_bf16 v[38:41], v[176:179], v[200:203], v[38:41]
	v_mfma_f32_16x16x32_bf16 v[30:33], v[184:187], v[200:203], v[30:33]
	v_mfma_f32_16x16x32_bf16 v[22:25], v[176:179], v[208:211], v[22:25]
	v_mfma_f32_16x16x32_bf16 v[14:17], v[184:187], v[208:211], v[14:17]
	v_mfma_f32_16x16x32_bf16 v[6:9], v[176:179], v[216:219], v[6:9]
	v_mfma_f32_16x16x32_bf16 v[2:5], v[184:187], v[216:219], v[2:5]
	v_mfma_f32_16x16x32_bf16 v[54:57], v[180:183], v[196:199], v[54:57]
	v_mfma_f32_16x16x32_bf16 v[46:49], v[188:191], v[196:199], v[46:49]
	v_mfma_f32_16x16x32_bf16 v[38:41], v[180:183], v[204:207], v[38:41]
	v_mfma_f32_16x16x32_bf16 v[30:33], v[188:191], v[204:207], v[30:33]
	v_mfma_f32_16x16x32_bf16 v[22:25], v[180:183], v[212:215], v[22:25]
	v_mfma_f32_16x16x32_bf16 v[14:17], v[188:191], v[212:215], v[14:17]
	v_mfma_f32_16x16x32_bf16 v[6:9], v[180:183], v[220:223], v[6:9]
	v_mfma_f32_16x16x32_bf16 v[2:5], v[188:191], v[220:223], v[2:5]
	s_setprio 0
	s_barrier
	s_add_i32 s69, s69, 2
	s_add_u32 s67, s67, 0x100
	s_addc_u32 s68, s68, 0
	s_cmp_gt_u32 s69, 53
	s_mov_b64 s[38:39], s[40:41]
.LBB0_1823:
	ds_read_b128 v[160:163], v157
	ds_read_b128 v[164:167], v157 offset:1024
	ds_read_b128 v[168:171], v157 offset:2048
	ds_read_b128 v[172:175], v157 offset:3072
	ds_read_b128 v[176:179], v158
	ds_read_b128 v[180:183], v158 offset:1024
	ds_read_b128 v[184:187], v158 offset:2048
	ds_read_b128 v[188:191], v158 offset:3072
	s_add_u32 s40, s38, 0x100
	s_addc_u32 s41, s39, 0
	s_cmp_eq_u32 s69, 52
	s_cselect_b32 s45, s7, s41
	s_cselect_b32 s44, s6, s40
	s_cselect_b32 s43, s35, s68
	s_cselect_b32 s42, s34, s67
	v_lshl_add_u64 v[152:153], s[38:39], 0, v[140:141]
	s_add_i32 m0, s37, 0xc000
	ds_read_b128 v[192:195], v159
	ds_read_b128 v[196:199], v159 offset:1024
	ds_read_b128 v[200:203], v159 offset:2048
	ds_read_b128 v[204:207], v159 offset:3072
	ds_read_b128 v[208:211], v159 offset:4096
	ds_read_b128 v[212:215], v159 offset:5120
	ds_read_b128 v[216:219], v159 offset:6144
	ds_read_b128 v[220:223], v159 offset:7168
	global_load_lds_dwordx4 v[152:153], off
	v_lshl_add_u64 v[152:153], s[38:39], 0, v[142:143]
	s_add_i32 m0, s37, 0xe000
	s_nop 0
	global_load_lds_dwordx4 v[152:153], off
	s_waitcnt vmcnt(8)
	s_waitcnt lgkmcnt(0)
	s_barrier
; #define PG8_STAGE_A(b, h, ptr, NX) do { if constexpr (Sched::GATHER) { unsigned gs_[2]; gs_[0] = ((NX) && last_) ? gN[h][0] : gA[h][0]; gs_[1] = ((NX) && last_) ? gN[h][1] : gA[h][1]; PG8_STAGE(PG8_SA(b, h), ptr, gs_); } \
;         else PG8_STAGE(PG8_SA(b, h), (ptr) + ((h) ? hstep : (size_t)0), voffA); } while (0)
; #define PG8_STAGE(bufoff, gbase, voff) do { _Pragma("unroll") for (int _i = 0; _i < 2; ++_i) \
;         __builtin_amdgcn_global_load_lds((const unsigned*)((const char*)(gbase) + (voff)[_i]), (PG8_LAS unsigned*)(lds + (bufoff) + ldsw + _i * 8192), 16, 0, 0); } while (0)
; #define PG8_LDA(dst, b, h) do { _Pragma("unroll") for (int m = 0; m < 4; ++m) _Pragma("unroll") for (int k = 0; k < 2; ++k) dst[m][k] = *(const PG8_LAS bf16x8*)(lds + PG8_SA(b, h) + aoff + m * 2048 + k * 1024); } while (0)
; #define PG8_LDB(dst, b, h) do { _Pragma("unroll") for (int n = 0; n < 2; ++n) _Pragma("unroll") for (int k = 0; k < 2; ++k) dst[n][k] = *(const PG8_LAS bf16x8*)(lds + PG8_SB(b, h) + boff + n * 2048 + k * 1024); } while (0)
; #define PG8_MMA(ai, bj, At, Bt) do { __builtin_amdgcn_s_setprio(1); _Pragma("unroll") for (int m = 0; m < 4; ++m) _Pragma("unroll") for (int n = 0; n < 2; ++n) _Pragma("unroll") for (int k = 0; k < 2; ++k) \
;         acc[ai][bj][m][n] = __builtin_amdgcn_mfma_f32_16x16x32_bf16(Bt[n][k], At[m][k], acc[ai][bj][m][n], 0, 0, 0); __builtin_amdgcn_s_setprio(0); } while (0)
; #define PG8_WAIT_V(n) asm volatile("s_waitcnt vmcnt(" #n ")" ::: "memory")
; #define PG8_WAIT_L(n) asm volatile("s_waitcnt lgkmcnt(" #n ")" ::: "memory")
; #define PG8_BAR __builtin_amdgcn_s_barrier()
; #define PG8_SCHED __builtin_amdgcn_sched_barrier(0)
; template <class Epi, class Sched, bool ALIGN_EPI = false, bool SP2 = false>
; __device__ __forceinline__ void gemm_phase(PG8_LAS unsigned char* lds, const Gemm g, const Sched& S, const Epi& E, const bool skip_epi = false) {
;     ...
;             PG8_LDB(B0, 0, 0); PG8_LDB(B1, 0, 1); PG8_SCHED; PG8_LDA(At, 0, 0); PG8_STAGE_A(1, 1, a1, false);
;             PG8_WAIT_V(8); PG8_WAIT_L(0); PG8_BAR; PG8_MMA(0, 0, At, B0); PG8_MMA(0, 1, At, B1); PG8_BAR; PG8_SCHED;
;             PG8_LDA(At, 0, 1); PG8_STAGE(PG8_SB(0, 0), b2, voffB); PG8_STAGE(PG8_SB(0, 1), b2 + hstep, voffB); PG8_STAGE_A(0, 0, a2, true);
;             PG8_WAIT_V(8); PG8_WAIT_L(0); PG8_BAR; PG8_MMA(1, 0, At, B0); PG8_MMA(1, 1, At, B1); PG8_BAR; PG8_SCHED;
	s_setprio 3
	s_waitcnt lgkmcnt(0)
	v_mfma_f32_16x16x32_bf16 v[126:129], v[160:163], v[192:195], v[126:129]
	v_mfma_f32_16x16x32_bf16 v[122:125], v[168:171], v[192:195], v[122:125]
	v_mfma_f32_16x16x32_bf16 v[118:121], v[160:163], v[200:203], v[118:121]
	v_mfma_f32_16x16x32_bf16 v[114:117], v[168:171], v[200:203], v[114:117]
	v_lshl_add_u64 v[152:153], s[42:43], 0, v[134:135]
	v_mfma_f32_16x16x32_bf16 v[106:109], v[160:163], v[208:211], v[106:109]
	v_mfma_f32_16x16x32_bf16 v[98:101], v[168:171], v[208:211], v[98:101]
	v_lshl_add_u64 v[224:225], s[42:43], 0, v[138:139]
	v_mfma_f32_16x16x32_bf16 v[78:81], v[160:163], v[216:219], v[78:81]
	v_mfma_f32_16x16x32_bf16 v[74:77], v[168:171], v[216:219], v[74:77]
	v_lshl_add_u64 v[230:231], s[44:45], 0, v[136:137]
	v_mfma_f32_16x16x32_bf16 v[126:129], v[164:167], v[196:199], v[126:129]
	v_mfma_f32_16x16x32_bf16 v[122:125], v[172:175], v[196:199], v[122:125]
	v_lshl_add_u64 v[226:227], s[44:45], 0, v[132:133]
	v_mfma_f32_16x16x32_bf16 v[118:121], v[164:167], v[204:207], v[118:121]
	v_mfma_f32_16x16x32_bf16 v[114:117], v[172:175], v[204:207], v[114:117]
	v_mfma_f32_16x16x32_bf16 v[106:109], v[164:167], v[212:215], v[106:109]
	v_mfma_f32_16x16x32_bf16 v[98:101], v[172:175], v[212:215], v[98:101]
	v_mfma_f32_16x16x32_bf16 v[78:81], v[164:167], v[220:223], v[78:81]
	v_mfma_f32_16x16x32_bf16 v[74:77], v[172:175], v[220:223], v[74:77]
	s_setprio 0
	s_setprio 3
	v_mfma_f32_16x16x32_bf16 v[110:113], v[176:179], v[192:195], v[110:113]
	v_mfma_f32_16x16x32_bf16 v[102:105], v[184:187], v[192:195], v[102:105]
	v_mfma_f32_16x16x32_bf16 v[94:97], v[176:179], v[200:203], v[94:97]
	v_mfma_f32_16x16x32_bf16 v[90:93], v[184:187], v[200:203], v[90:93]
	v_mfma_f32_16x16x32_bf16 v[86:89], v[176:179], v[208:211], v[86:89]
	v_mfma_f32_16x16x32_bf16 v[82:85], v[184:187], v[208:211], v[82:85]
	v_mfma_f32_16x16x32_bf16 v[70:73], v[176:179], v[216:219], v[70:73]
	v_mfma_f32_16x16x32_bf16 v[66:69], v[184:187], v[216:219], v[66:69]
	v_mfma_f32_16x16x32_bf16 v[110:113], v[180:183], v[196:199], v[110:113]
	v_mfma_f32_16x16x32_bf16 v[102:105], v[188:191], v[196:199], v[102:105]
	v_mfma_f32_16x16x32_bf16 v[94:97], v[180:183], v[204:207], v[94:97]
	v_mfma_f32_16x16x32_bf16 v[90:93], v[188:191], v[204:207], v[90:93]
	v_mfma_f32_16x16x32_bf16 v[86:89], v[180:183], v[212:215], v[86:89]
	v_mfma_f32_16x16x32_bf16 v[82:85], v[188:191], v[212:215], v[82:85]
	v_mfma_f32_16x16x32_bf16 v[70:73], v[180:183], v[220:223], v[70:73]
	v_mfma_f32_16x16x32_bf16 v[66:69], v[188:191], v[220:223], v[66:69]
	s_setprio 0
	s_barrier
	s_add_i32 s38, s60, s51
	s_mov_b32 m0, s38
	ds_read_b128 v[192:195], v159 offset:16384
	ds_read_b128 v[196:199], v159 offset:17408
	ds_read_b128 v[200:203], v159 offset:18432
	ds_read_b128 v[204:207], v159 offset:19456
	ds_read_b128 v[208:211], v159 offset:20480
	ds_read_b128 v[212:215], v159 offset:21504
	ds_read_b128 v[216:219], v159 offset:22528
	ds_read_b128 v[220:223], v159 offset:23552
	global_load_lds_dwordx4 v[152:153], off
	s_add_i32 m0, s38, 0x2000
	s_add_u32 s38, s42, 0xe0000
	s_addc_u32 s39, s43, 0
	s_add_i32 s70, s61, s51
	global_load_lds_dwordx4 v[224:225], off
	s_mov_b32 m0, s70
	s_nop 0
	global_load_lds_dwordx4 v134, s[38:39]
	s_add_i32 m0, s70, 0x2000
	s_nop 0
	global_load_lds_dwordx4 v138, s[38:39]
	s_mov_b32 m0, s37
	s_nop 0
	global_load_lds_dwordx4 v[226:227], off
	s_mov_b32 m0, s52
	s_nop 0
	global_load_lds_dwordx4 v[230:231], off
	s_waitcnt vmcnt(8)
	s_waitcnt lgkmcnt(0)
	s_barrier
	s_setprio 3
	s_waitcnt lgkmcnt(0)
	v_mfma_f32_16x16x32_bf16 v[62:65], v[160:163], v[192:195], v[62:65]
	v_mfma_f32_16x16x32_bf16 v[58:61], v[168:171], v[192:195], v[58:61]
	v_mfma_f32_16x16x32_bf16 v[50:53], v[160:163], v[200:203], v[50:53]
	v_mfma_f32_16x16x32_bf16 v[42:45], v[168:171], v[200:203], v[42:45]
	v_mfma_f32_16x16x32_bf16 v[34:37], v[160:163], v[208:211], v[34:37]
	v_mfma_f32_16x16x32_bf16 v[26:29], v[168:171], v[208:211], v[26:29]
	v_mfma_f32_16x16x32_bf16 v[18:21], v[160:163], v[216:219], v[18:21]
	v_mfma_f32_16x16x32_bf16 v[10:13], v[168:171], v[216:219], v[10:13]
	v_mfma_f32_16x16x32_bf16 v[62:65], v[164:167], v[196:199], v[62:65]
	v_mfma_f32_16x16x32_bf16 v[58:61], v[172:175], v[196:199], v[58:61]
	v_mfma_f32_16x16x32_bf16 v[50:53], v[164:167], v[204:207], v[50:53]
	v_mfma_f32_16x16x32_bf16 v[42:45], v[172:175], v[204:207], v[42:45]
	v_mfma_f32_16x16x32_bf16 v[34:37], v[164:167], v[212:215], v[34:37]
	v_mfma_f32_16x16x32_bf16 v[26:29], v[172:175], v[212:215], v[26:29]
	v_mfma_f32_16x16x32_bf16 v[18:21], v[164:167], v[220:223], v[18:21]
	v_mfma_f32_16x16x32_bf16 v[10:13], v[172:175], v[220:223], v[10:13]
	s_setprio 0
	s_setprio 3
	v_mfma_f32_16x16x32_bf16 v[54:57], v[176:179], v[192:195], v[54:57]
	v_mfma_f32_16x16x32_bf16 v[46:49], v[184:187], v[192:195], v[46:49]
	v_mfma_f32_16x16x32_bf16 v[38:41], v[176:179], v[200:203], v[38:41]
	v_mfma_f32_16x16x32_bf16 v[30:33], v[184:187], v[200:203], v[30:33]
	v_mfma_f32_16x16x32_bf16 v[22:25], v[176:179], v[208:211], v[22:25]
	v_mfma_f32_16x16x32_bf16 v[14:17], v[184:187], v[208:211], v[14:17]
	v_mfma_f32_16x16x32_bf16 v[6:9], v[176:179], v[216:219], v[6:9]
	v_mfma_f32_16x16x32_bf16 v[2:5], v[184:187], v[216:219], v[2:5]
	v_mfma_f32_16x16x32_bf16 v[54:57], v[180:183], v[196:199], v[54:57]
	v_mfma_f32_16x16x32_bf16 v[46:49], v[188:191], v[196:199], v[46:49]
	v_mfma_f32_16x16x32_bf16 v[38:41], v[180:183], v[204:207], v[38:41]
	v_mfma_f32_16x16x32_bf16 v[30:33], v[188:191], v[204:207], v[30:33]
	v_mfma_f32_16x16x32_bf16 v[22:25], v[180:183], v[212:215], v[22:25]
	v_mfma_f32_16x16x32_bf16 v[14:17], v[188:191], v[212:215], v[14:17]
	v_mfma_f32_16x16x32_bf16 v[6:9], v[180:183], v[220:223], v[6:9]
	v_mfma_f32_16x16x32_bf16 v[2:5], v[188:191], v[220:223], v[2:5]
	s_setprio 0
	s_barrier
; #define PG8_STAGE_A(b, h, ptr, NX) do { if constexpr (Sched::GATHER) { unsigned gs_[2]; gs_[0] = ((NX) && last_) ? gN[h][0] : gA[h][0]; gs_[1] = ((NX) && last_) ? gN[h][1] : gA[h][1]; PG8_STAGE(PG8_SA(b, h), ptr, gs_); } \
;         else PG8_STAGE(PG8_SA(b, h), (ptr) + ((h) ? hstep : (size_t)0), voffA); } while (0)
; #define PG8_STAGE(bufoff, gbase, voff) do { _Pragma("unroll") for (int _i = 0; _i < 2; ++_i) \
;         __builtin_amdgcn_global_load_lds((const unsigned*)((const char*)(gbase) + (voff)[_i]), (PG8_LAS unsigned*)(lds + (bufoff) + ldsw + _i * 8192), 16, 0, 0); } while (0)
; #define PG8_LDA(dst, b, h) do { _Pragma("unroll") for (int m = 0; m < 4; ++m) _Pragma("unroll") for (int k = 0; k < 2; ++k) dst[m][k] = *(const PG8_LAS bf16x8*)(lds + PG8_SA(b, h) + aoff + m * 2048 + k * 1024); } while (0)
; #define PG8_LDB(dst, b, h) do { _Pragma("unroll") for (int n = 0; n < 2; ++n) _Pragma("unroll") for (int k = 0; k < 2; ++k) dst[n][k] = *(const PG8_LAS bf16x8*)(lds + PG8_SB(b, h) + boff + n * 2048 + k * 1024); } while (0)
; #define PG8_MMA(ai, bj, At, Bt) do { __builtin_amdgcn_s_setprio(1); _Pragma("unroll") for (int m = 0; m < 4; ++m) _Pragma("unroll") for (int n = 0; n < 2; ++n) _Pragma("unroll") for (int k = 0; k < 2; ++k) \
;         acc[ai][bj][m][n] = __builtin_amdgcn_mfma_f32_16x16x32_bf16(Bt[n][k], At[m][k], acc[ai][bj][m][n], 0, 0, 0); __builtin_amdgcn_s_setprio(0); } while (0)
; #define PG8_WAIT_V(n) asm volatile("s_waitcnt vmcnt(" #n ")" ::: "memory")
; #define PG8_WAIT_L(n) asm volatile("s_waitcnt lgkmcnt(" #n ")" ::: "memory")
; #define PG8_BAR __builtin_amdgcn_s_barrier()
; #define PG8_SCHED __builtin_amdgcn_sched_barrier(0)
; template <class Epi, class Sched, bool ALIGN_EPI = false, bool SP2 = false>
; __device__ __forceinline__ void gemm_phase(PG8_LAS unsigned char* lds, const Gemm g, const Sched& S, const Epi& E, const bool skip_epi = false) {
;     ...
;             PG8_LDB(B0, 1, 0); PG8_LDB(B1, 1, 1); PG8_SCHED; PG8_LDA(At, 1, 0); PG8_STAGE_A(0, 1, a2, true);
;             PG8_WAIT_V(8); PG8_WAIT_L(0); PG8_BAR; PG8_MMA(0, 0, At, B0); PG8_MMA(0, 1, At, B1); PG8_BAR; PG8_SCHED;
;             PG8_LDA(At, 1, 1); PG8_STAGE(PG8_SB(1, 0), b3, voffB); PG8_STAGE(PG8_SB(1, 1), b3 + hstep, voffB); PG8_STAGE_A(1, 0, a3, true);
;             PG8_WAIT_V(8); PG8_WAIT_L(0); PG8_BAR; PG8_MMA(1, 0, At, B0); PG8_MMA(1, 1, At, B1); PG8_BAR; PG8_SCHED;
	s_add_i32 s70, 0, 0x18000
	v_add_u32_e32 v130, s70, v147
	s_add_i32 s71, 0, 0x1c000
	ds_read_b128 v[160:163], v130
	ds_read_b128 v[164:167], v130 offset:1024
	ds_read_b128 v[168:171], v130 offset:2048
	ds_read_b128 v[172:175], v130 offset:3072
	v_add_u32_e32 v130, s71, v147
	ds_read_b128 v[176:179], v130
	ds_read_b128 v[180:183], v130 offset:1024
	ds_read_b128 v[184:187], v130 offset:2048
	ds_read_b128 v[188:191], v130 offset:3072
	s_add_u32 s38, s44, 0xe0000
	s_addc_u32 s39, s45, 0
	s_mov_b32 m0, s53
	ds_read_b128 v[192:195], v159 offset:32768
	ds_read_b128 v[196:199], v159 offset:33792
	ds_read_b128 v[200:203], v159 offset:34816
	ds_read_b128 v[204:207], v159 offset:35840
	ds_read_b128 v[208:211], v159 offset:36864
	ds_read_b128 v[212:215], v159 offset:37888
	ds_read_b128 v[216:219], v159 offset:38912
	ds_read_b128 v[220:223], v159 offset:39936
	global_load_lds_dwordx4 v132, s[38:39]
	s_mov_b32 m0, s54
	s_nop 0
	global_load_lds_dwordx4 v136, s[38:39]
	s_waitcnt vmcnt(8)
	s_waitcnt lgkmcnt(0)
	s_barrier
	s_setprio 3
	s_waitcnt lgkmcnt(0)
	v_mfma_f32_16x16x32_bf16 v[126:129], v[160:163], v[192:195], v[126:129]
	v_mfma_f32_16x16x32_bf16 v[122:125], v[168:171], v[192:195], v[122:125]
	v_mfma_f32_16x16x32_bf16 v[118:121], v[160:163], v[200:203], v[118:121]
	v_mfma_f32_16x16x32_bf16 v[114:117], v[168:171], v[200:203], v[114:117]
	v_mfma_f32_16x16x32_bf16 v[106:109], v[160:163], v[208:211], v[106:109]
	v_mfma_f32_16x16x32_bf16 v[98:101], v[168:171], v[208:211], v[98:101]
	v_mfma_f32_16x16x32_bf16 v[78:81], v[160:163], v[216:219], v[78:81]
	v_mfma_f32_16x16x32_bf16 v[74:77], v[168:171], v[216:219], v[74:77]
	v_mfma_f32_16x16x32_bf16 v[126:129], v[164:167], v[196:199], v[126:129]
	v_mfma_f32_16x16x32_bf16 v[122:125], v[172:175], v[196:199], v[122:125]
	v_mfma_f32_16x16x32_bf16 v[118:121], v[164:167], v[204:207], v[118:121]
	v_mfma_f32_16x16x32_bf16 v[114:117], v[172:175], v[204:207], v[114:117]
	v_mfma_f32_16x16x32_bf16 v[106:109], v[164:167], v[212:215], v[106:109]
	v_mfma_f32_16x16x32_bf16 v[98:101], v[172:175], v[212:215], v[98:101]
	v_mfma_f32_16x16x32_bf16 v[78:81], v[164:167], v[220:223], v[78:81]
	v_mfma_f32_16x16x32_bf16 v[74:77], v[172:175], v[220:223], v[74:77]
	s_setprio 0
	s_setprio 3
	v_mfma_f32_16x16x32_bf16 v[110:113], v[176:179], v[192:195], v[110:113]
	v_mfma_f32_16x16x32_bf16 v[102:105], v[184:187], v[192:195], v[102:105]
	v_mfma_f32_16x16x32_bf16 v[94:97], v[176:179], v[200:203], v[94:97]
	v_mfma_f32_16x16x32_bf16 v[90:93], v[184:187], v[200:203], v[90:93]
	v_mfma_f32_16x16x32_bf16 v[86:89], v[176:179], v[208:211], v[86:89]
	v_mfma_f32_16x16x32_bf16 v[82:85], v[184:187], v[208:211], v[82:85]
	v_mfma_f32_16x16x32_bf16 v[70:73], v[176:179], v[216:219], v[70:73]
	v_mfma_f32_16x16x32_bf16 v[66:69], v[184:187], v[216:219], v[66:69]
	v_mfma_f32_16x16x32_bf16 v[110:113], v[180:183], v[196:199], v[110:113]
	v_mfma_f32_16x16x32_bf16 v[102:105], v[188:191], v[196:199], v[102:105]
	v_mfma_f32_16x16x32_bf16 v[94:97], v[180:183], v[204:207], v[94:97]
	v_mfma_f32_16x16x32_bf16 v[90:93], v[188:191], v[204:207], v[90:93]
	v_mfma_f32_16x16x32_bf16 v[86:89], v[180:183], v[212:215], v[86:89]
	v_mfma_f32_16x16x32_bf16 v[82:85], v[188:191], v[212:215], v[82:85]
	v_mfma_f32_16x16x32_bf16 v[70:73], v[180:183], v[220:223], v[70:73]
	v_mfma_f32_16x16x32_bf16 v[66:69], v[188:191], v[220:223], v[66:69]
	s_setprio 0
	s_barrier
	s_add_i32 s38, s70, s51
	s_add_i32 m0, s38, 0xffffff80
	ds_read_b128 v[192:195], v159 offset:49152
	ds_read_b128 v[196:199], v159 offset:50176
	ds_read_b128 v[200:203], v159 offset:51200
	ds_read_b128 v[204:207], v159 offset:52224
	ds_read_b128 v[208:211], v159 offset:53248
	ds_read_b128 v[212:215], v159 offset:54272
	ds_read_b128 v[216:219], v159 offset:55296
	ds_read_b128 v[220:223], v159 offset:56320
	global_load_lds_dwordx4 v[152:153], off offset:128
	s_add_i32 m0, s38, 0x1f80
	s_add_u32 s38, s42, 0xe0080
	s_addc_u32 s39, s43, 0
	s_add_i32 s42, s71, s51
	global_load_lds_dwordx4 v[224:225], off offset:128
	s_mov_b32 m0, s42
	s_nop 0
	global_load_lds_dwordx4 v134, s[38:39]
	s_add_i32 m0, s42, 0x2000
	s_nop 0
	global_load_lds_dwordx4 v138, s[38:39]
	s_add_i32 m0, s57, 0xffffff80
	s_nop 0
	global_load_lds_dwordx4 v[226:227], off offset:128
	s_add_i32 m0, s58, 0xffffff80
	s_nop 0
	global_load_lds_dwordx4 v[230:231], off offset:128
	s_waitcnt vmcnt(8)
	s_waitcnt lgkmcnt(0)
	s_barrier
	s_setprio 3
	s_waitcnt lgkmcnt(0)
	v_mfma_f32_16x16x32_bf16 v[62:65], v[160:163], v[192:195], v[62:65]
	v_mfma_f32_16x16x32_bf16 v[58:61], v[168:171], v[192:195], v[58:61]
	v_mfma_f32_16x16x32_bf16 v[50:53], v[160:163], v[200:203], v[50:53]
	v_mfma_f32_16x16x32_bf16 v[42:45], v[168:171], v[200:203], v[42:45]
	v_mfma_f32_16x16x32_bf16 v[34:37], v[160:163], v[208:211], v[34:37]
	v_mfma_f32_16x16x32_bf16 v[26:29], v[168:171], v[208:211], v[26:29]
	v_mfma_f32_16x16x32_bf16 v[18:21], v[160:163], v[216:219], v[18:21]
	v_mfma_f32_16x16x32_bf16 v[10:13], v[168:171], v[216:219], v[10:13]
	v_mfma_f32_16x16x32_bf16 v[62:65], v[164:167], v[196:199], v[62:65]
	v_mfma_f32_16x16x32_bf16 v[58:61], v[172:175], v[196:199], v[58:61]
	v_mfma_f32_16x16x32_bf16 v[50:53], v[164:167], v[204:207], v[50:53]
	v_mfma_f32_16x16x32_bf16 v[42:45], v[172:175], v[204:207], v[42:45]
	v_mfma_f32_16x16x32_bf16 v[34:37], v[164:167], v[212:215], v[34:37]
	v_mfma_f32_16x16x32_bf16 v[26:29], v[172:175], v[212:215], v[26:29]
	v_mfma_f32_16x16x32_bf16 v[18:21], v[164:167], v[220:223], v[18:21]
	v_mfma_f32_16x16x32_bf16 v[10:13], v[172:175], v[220:223], v[10:13]
	s_setprio 0
	s_setprio 3
	v_mfma_f32_16x16x32_bf16 v[54:57], v[176:179], v[192:195], v[54:57]
	v_mfma_f32_16x16x32_bf16 v[46:49], v[184:187], v[192:195], v[46:49]
	v_mfma_f32_16x16x32_bf16 v[38:41], v[176:179], v[200:203], v[38:41]
	v_mfma_f32_16x16x32_bf16 v[30:33], v[184:187], v[200:203], v[30:33]
	v_mfma_f32_16x16x32_bf16 v[22:25], v[176:179], v[208:211], v[22:25]
	v_mfma_f32_16x16x32_bf16 v[14:17], v[184:187], v[208:211], v[14:17]
	v_mfma_f32_16x16x32_bf16 v[6:9], v[176:179], v[216:219], v[6:9]
	v_mfma_f32_16x16x32_bf16 v[2:5], v[184:187], v[216:219], v[2:5]
	v_mfma_f32_16x16x32_bf16 v[54:57], v[180:183], v[196:199], v[54:57]
	v_mfma_f32_16x16x32_bf16 v[46:49], v[188:191], v[196:199], v[46:49]
	v_mfma_f32_16x16x32_bf16 v[38:41], v[180:183], v[204:207], v[38:41]
	v_mfma_f32_16x16x32_bf16 v[30:33], v[188:191], v[204:207], v[30:33]
	v_mfma_f32_16x16x32_bf16 v[22:25], v[180:183], v[212:215], v[22:25]
	v_mfma_f32_16x16x32_bf16 v[14:17], v[188:191], v[212:215], v[14:17]
	v_mfma_f32_16x16x32_bf16 v[6:9], v[180:183], v[220:223], v[6:9]
	v_mfma_f32_16x16x32_bf16 v[2:5], v[188:191], v[220:223], v[2:5]
	s_setprio 0
	s_barrier
	s_add_i32 s69, s69, 2
	s_add_u32 s67, s67, 0x100
	s_addc_u32 s68, s68, 0
	s_cmp_gt_u32 s69, 53
	s_mov_b64 s[38:39], s[40:41]
	s_cbranch_scc0 .LBB0_1823
	s_and_b64 vcc, exec, s[20:21]
	s_cbranch_vccz .LBB0_1826
	s_barrier

; #define PG8_STAGE_A(b, h, ptr, NX) do { if constexpr (Sched::GATHER) { unsigned gs_[2]; gs_[0] = ((NX) && last_) ? gN[h][0] : gA[h][0]; gs_[1] = ((NX) && last_) ? gN[h][1] : gA[h][1]; PG8_STAGE(PG8_SA(b, h), ptr, gs_); } \
;         else PG8_STAGE(PG8_SA(b, h), (ptr) + ((h) ? hstep : (size_t)0), voffA); } while (0)
; #define PG8_STAGE(bufoff, gbase, voff) do { _Pragma("unroll") for (int _i = 0; _i < 2; ++_i) \
;         __builtin_amdgcn_global_load_lds((const unsigned*)((const char*)(gbase) + (voff)[_i]), (PG8_LAS unsigned*)(lds + (bufoff) + ldsw + _i * 8192), 16, 0, 0); } while (0)
; #define PG8_LDA(dst, b, h) do { _Pragma("unroll") for (int m = 0; m < 4; ++m) _Pragma("unroll") for (int k = 0; k < 2; ++k) dst[m][k] = *(const PG8_LAS bf16x8*)(lds + PG8_SA(b, h) + aoff + m * 2048 + k * 1024); } while (0)
; #define PG8_LDB(dst, b, h) do { _Pragma("unroll") for (int n = 0; n < 2; ++n) _Pragma("unroll") for (int k = 0; k < 2; ++k) dst[n][k] = *(const PG8_LAS bf16x8*)(lds + PG8_SB(b, h) + boff + n * 2048 + k * 1024); } while (0)
; #define PG8_WAIT_V(n) asm volatile("s_waitcnt vmcnt(" #n ")" ::: "memory")
; #define PG8_WAIT_L(n) asm volatile("s_waitcnt lgkmcnt(" #n ")" ::: "memory")
; #define PG8_BAR __builtin_amdgcn_s_barrier()
; #define PG8_SCHED __builtin_amdgcn_sched_barrier(0)
; template <class Epi, class Sched, bool ALIGN_EPI = false, bool SP2 = false>
; __device__ __forceinline__ void gemm_phase(PG8_LAS unsigned char* lds, const Gemm g, const Sched& S, const Epi& E, const bool skip_epi = false) {
;     ...
;             const bool last = (t == nt - 2); last_ = last && has_next;
;             const char* a1 = cA + (size_t)(t + 1) * kstep;
;             const char* a2 = last ? nA : cA + (size_t)(t + 2) * kstep; const char* b2 = last ? nB : cB + (size_t)(t + 2) * kstep;
;             const char* a3 = a2 + kstep; const char* b3 = b2 + kstep;
;             if (last && has_next) S.a_ready(nxt);
;             if constexpr (SP2) {
;             PG8_LDB(B0, 0, 0); PG8_LDB(B1, 0, 1); PG8_SCHED; PG8_LDA(At, 0, 0); PG8_STAGE_A(1, 1, a1, false);
;             PG8_WAIT_V(8); PG8_WAIT_L(0); PG8_BAR; PG8_MMA(0, 0, At, B0); PG8_MMA(0, 1, At, B1); PG8_BAR; PG8_SCHED;
;             PG8_LDA(At, 0, 1); PG8_STAGE(PG8_SB(0, 0), b2, voffB); PG8_STAGE(PG8_SB(0, 1), b2 + hstep, voffB); PG8_STAGE_A(0, 0, a2, true);
.LBB0_1843:
	s_add_u32 s54, s30, 0x100
	s_addc_u32 s55, s31, 0
	s_mov_b32 s56, -2
	ds_read_b128 v[142:145], v150
	ds_read_b128 v[154:157], v150 offset:1024
	ds_read_b128 v[158:161], v150 offset:2048
	ds_read_b128 v[162:165], v150 offset:3072
	ds_read_b128 v[166:169], v151
	ds_read_b128 v[170:173], v151 offset:1024
	ds_read_b128 v[174:177], v151 offset:2048
	ds_read_b128 v[178:181], v151 offset:3072
	s_add_u32 s30, s28, 0x100
	s_addc_u32 s31, s29, 0
	s_cmp_eq_u32 s56, 10
	s_cselect_b32 s37, s7, s31
	s_cselect_b32 s36, s6, s30
	s_cselect_b32 s35, s25, s55
	s_cselect_b32 s34, s24, s54
	v_lshl_add_u64 v[214:215], s[28:29], 0, v[136:137]
	s_add_i32 m0, s38, 0xc000
	ds_read_b128 v[182:185], v152
	ds_read_b128 v[186:189], v152 offset:1024
	ds_read_b128 v[190:193], v152 offset:2048
	ds_read_b128 v[194:197], v152 offset:3072
	ds_read_b128 v[198:201], v152 offset:4096
	ds_read_b128 v[202:205], v152 offset:5120
	ds_read_b128 v[206:209], v152 offset:6144
	ds_read_b128 v[210:213], v152 offset:7168
	global_load_lds_dwordx4 v[214:215], off
	v_lshl_add_u64 v[214:215], s[28:29], 0, v[138:139]
	s_add_i32 m0, s38, 0xe000
	s_nop 0
	global_load_lds_dwordx4 v[214:215], off
	s_waitcnt vmcnt(8)
	s_waitcnt lgkmcnt(0)
	s_barrier
	s_setprio 3
	s_waitcnt lgkmcnt(0)
	v_mfma_f32_16x16x32_bf16 v[126:129], v[142:145], v[182:185], 0
	v_mfma_f32_16x16x32_bf16 v[122:125], v[158:161], v[182:185], 0
	v_mfma_f32_16x16x32_bf16 v[110:113], v[142:145], v[190:193], 0
	v_mfma_f32_16x16x32_bf16 v[106:109], v[158:161], v[190:193], 0
	v_lshl_add_u64 v[214:215], s[34:35], 0, v[132:133]
	v_mfma_f32_16x16x32_bf16 v[94:97], v[142:145], v[198:201], 0
	v_mfma_f32_16x16x32_bf16 v[90:93], v[158:161], v[198:201], 0
	v_lshl_add_u64 v[216:217], s[34:35], 0, v[134:135]
	v_mfma_f32_16x16x32_bf16 v[78:81], v[142:145], v[206:209], 0
	v_mfma_f32_16x16x32_bf16 v[74:77], v[158:161], v[206:209], 0
	v_lshl_add_u64 v[220:221], s[36:37], 0, v[134:135]
	v_mfma_f32_16x16x32_bf16 v[126:129], v[154:157], v[186:189], v[126:129]
	v_mfma_f32_16x16x32_bf16 v[122:125], v[162:165], v[186:189], v[122:125]
	v_lshl_add_u64 v[218:219], s[36:37], 0, v[132:133]
	v_mfma_f32_16x16x32_bf16 v[110:113], v[154:157], v[194:197], v[110:113]
	v_mfma_f32_16x16x32_bf16 v[106:109], v[162:165], v[194:197], v[106:109]
	v_mfma_f32_16x16x32_bf16 v[94:97], v[154:157], v[202:205], v[94:97]
	v_mfma_f32_16x16x32_bf16 v[90:93], v[162:165], v[202:205], v[90:93]
	v_mfma_f32_16x16x32_bf16 v[78:81], v[154:157], v[210:213], v[78:81]
	v_mfma_f32_16x16x32_bf16 v[74:77], v[162:165], v[210:213], v[74:77]
	s_setprio 0
	s_setprio 3
	v_mfma_f32_16x16x32_bf16 v[118:121], v[166:169], v[182:185], 0
	v_mfma_f32_16x16x32_bf16 v[114:117], v[174:177], v[182:185], 0
	v_mfma_f32_16x16x32_bf16 v[102:105], v[166:169], v[190:193], 0
	v_mfma_f32_16x16x32_bf16 v[98:101], v[174:177], v[190:193], 0
	v_mfma_f32_16x16x32_bf16 v[86:89], v[166:169], v[198:201], 0
	v_mfma_f32_16x16x32_bf16 v[82:85], v[174:177], v[198:201], 0
	v_mfma_f32_16x16x32_bf16 v[70:73], v[166:169], v[206:209], 0
	v_mfma_f32_16x16x32_bf16 v[66:69], v[174:177], v[206:209], 0
	v_mfma_f32_16x16x32_bf16 v[118:121], v[170:173], v[186:189], v[118:121]
	v_mfma_f32_16x16x32_bf16 v[114:117], v[178:181], v[186:189], v[114:117]
	v_mfma_f32_16x16x32_bf16 v[102:105], v[170:173], v[194:197], v[102:105]
	v_mfma_f32_16x16x32_bf16 v[98:101], v[178:181], v[194:197], v[98:101]
	v_mfma_f32_16x16x32_bf16 v[86:89], v[170:173], v[202:205], v[86:89]
	v_mfma_f32_16x16x32_bf16 v[82:85], v[178:181], v[202:205], v[82:85]
	v_mfma_f32_16x16x32_bf16 v[70:73], v[170:173], v[210:213], v[70:73]
	v_mfma_f32_16x16x32_bf16 v[66:69], v[178:181], v[210:213], v[66:69]
	s_setprio 0
	s_barrier
	s_add_i32 s28, s50, s3
	s_mov_b32 m0, s28
	ds_read_b128 v[182:185], v152 offset:16384
	ds_read_b128 v[186:189], v152 offset:17408
	ds_read_b128 v[190:193], v152 offset:18432
	ds_read_b128 v[194:197], v152 offset:19456
	ds_read_b128 v[198:201], v152 offset:20480
	ds_read_b128 v[202:205], v152 offset:21504
	ds_read_b128 v[206:209], v152 offset:22528
	ds_read_b128 v[210:213], v152 offset:23552
	global_load_lds_dwordx4 v[214:215], off
	s_add_i32 m0, s28, 0x2000
	s_add_u32 s28, s34, 0xe0000
	s_addc_u32 s29, s35, 0
	s_add_i32 s57, s51, s3
	global_load_lds_dwordx4 v[216:217], off
	s_mov_b32 m0, s57
	s_nop 0
	global_load_lds_dwordx4 v132, s[28:29]
	s_add_i32 m0, s57, 0x2000
	s_nop 0
	global_load_lds_dwordx4 v134, s[28:29]
	s_mov_b32 m0, s38
	s_nop 0
	global_load_lds_dwordx4 v[218:219], off
	s_mov_b32 m0, s39
	s_nop 0
	global_load_lds_dwordx4 v[220:221], off
	s_waitcnt vmcnt(8)
	s_waitcnt lgkmcnt(0)
	s_barrier
; #define PG8_STAGE_A(b, h, ptr, NX) do { if constexpr (Sched::GATHER) { unsigned gs_[2]; gs_[0] = ((NX) && last_) ? gN[h][0] : gA[h][0]; gs_[1] = ((NX) && last_) ? gN[h][1] : gA[h][1]; PG8_STAGE(PG8_SA(b, h), ptr, gs_); } \
;         else PG8_STAGE(PG8_SA(b, h), (ptr) + ((h) ? hstep : (size_t)0), voffA); } while (0)
; #define PG8_LDA(dst, b, h) do { _Pragma("unroll") for (int m = 0; m < 4; ++m) _Pragma("unroll") for (int k = 0; k < 2; ++k) dst[m][k] = *(const PG8_LAS bf16x8*)(lds + PG8_SA(b, h) + aoff + m * 2048 + k * 1024); } while (0)
; #define PG8_LDB(dst, b, h) do { _Pragma("unroll") for (int n = 0; n < 2; ++n) _Pragma("unroll") for (int k = 0; k < 2; ++k) dst[n][k] = *(const PG8_LAS bf16x8*)(lds + PG8_SB(b, h) + boff + n * 2048 + k * 1024); } while (0)
; #define PG8_MMA(ai, bj, At, Bt) do { __builtin_amdgcn_s_setprio(1); _Pragma("unroll") for (int m = 0; m < 4; ++m) _Pragma("unroll") for (int n = 0; n < 2; ++n) _Pragma("unroll") for (int k = 0; k < 2; ++k) \
;         acc[ai][bj][m][n] = __builtin_amdgcn_mfma_f32_16x16x32_bf16(Bt[n][k], At[m][k], acc[ai][bj][m][n], 0, 0, 0); __builtin_amdgcn_s_setprio(0); } while (0)
; #define PG8_WAIT_V(n) asm volatile("s_waitcnt vmcnt(" #n ")" ::: "memory")
; #define PG8_WAIT_L(n) asm volatile("s_waitcnt lgkmcnt(" #n ")" ::: "memory")
; #define PG8_BAR __builtin_amdgcn_s_barrier()
; #define PG8_SCHED __builtin_amdgcn_sched_barrier(0)
; template <class Epi, class Sched, bool ALIGN_EPI = false, bool SP2 = false>
; __device__ __forceinline__ void gemm_phase(PG8_LAS unsigned char* lds, const Gemm g, const Sched& S, const Epi& E, const bool skip_epi = false) {
;     ...
;             PG8_WAIT_V(8); PG8_WAIT_L(0); PG8_BAR; PG8_MMA(1, 0, At, B0); PG8_MMA(1, 1, At, B1); PG8_BAR; PG8_SCHED;
;             PG8_LDB(B0, 1, 0); PG8_LDB(B1, 1, 1); PG8_SCHED; PG8_LDA(At, 1, 0); PG8_STAGE_A(0, 1, a2, true);
;             PG8_WAIT_V(8); PG8_WAIT_L(0); PG8_BAR; PG8_MMA(0, 0, At, B0); PG8_MMA(0, 1, At, B1); PG8_BAR; PG8_SCHED;
	s_setprio 3
	s_waitcnt lgkmcnt(0)
	v_mfma_f32_16x16x32_bf16 v[62:65], v[142:145], v[182:185], 0
	v_mfma_f32_16x16x32_bf16 v[58:61], v[158:161], v[182:185], 0
	v_mfma_f32_16x16x32_bf16 v[46:49], v[142:145], v[190:193], 0
	v_mfma_f32_16x16x32_bf16 v[42:45], v[158:161], v[190:193], 0
	v_mfma_f32_16x16x32_bf16 v[30:33], v[142:145], v[198:201], 0
	v_mfma_f32_16x16x32_bf16 v[26:29], v[158:161], v[198:201], 0
	v_mfma_f32_16x16x32_bf16 v[14:17], v[142:145], v[206:209], 0
	v_mfma_f32_16x16x32_bf16 v[10:13], v[158:161], v[206:209], 0
	v_mfma_f32_16x16x32_bf16 v[62:65], v[154:157], v[186:189], v[62:65]
	v_mfma_f32_16x16x32_bf16 v[58:61], v[162:165], v[186:189], v[58:61]
	v_mfma_f32_16x16x32_bf16 v[46:49], v[154:157], v[194:197], v[46:49]
	v_mfma_f32_16x16x32_bf16 v[42:45], v[162:165], v[194:197], v[42:45]
	v_mfma_f32_16x16x32_bf16 v[30:33], v[154:157], v[202:205], v[30:33]
	v_mfma_f32_16x16x32_bf16 v[26:29], v[162:165], v[202:205], v[26:29]
	v_mfma_f32_16x16x32_bf16 v[14:17], v[154:157], v[210:213], v[14:17]
	v_mfma_f32_16x16x32_bf16 v[10:13], v[162:165], v[210:213], v[10:13]
	s_setprio 0
	s_setprio 3
	v_mfma_f32_16x16x32_bf16 v[54:57], v[166:169], v[182:185], 0
	v_mfma_f32_16x16x32_bf16 v[50:53], v[174:177], v[182:185], 0
	v_mfma_f32_16x16x32_bf16 v[38:41], v[166:169], v[190:193], 0
	v_mfma_f32_16x16x32_bf16 v[34:37], v[174:177], v[190:193], 0
	v_mfma_f32_16x16x32_bf16 v[22:25], v[166:169], v[198:201], 0
	v_mfma_f32_16x16x32_bf16 v[18:21], v[174:177], v[198:201], 0
	v_mfma_f32_16x16x32_bf16 v[6:9], v[166:169], v[206:209], 0
	v_mfma_f32_16x16x32_bf16 v[2:5], v[174:177], v[206:209], 0
	v_mfma_f32_16x16x32_bf16 v[54:57], v[170:173], v[186:189], v[54:57]
	v_mfma_f32_16x16x32_bf16 v[50:53], v[178:181], v[186:189], v[50:53]
	v_mfma_f32_16x16x32_bf16 v[38:41], v[170:173], v[194:197], v[38:41]
	v_mfma_f32_16x16x32_bf16 v[34:37], v[178:181], v[194:197], v[34:37]
	v_mfma_f32_16x16x32_bf16 v[22:25], v[170:173], v[202:205], v[22:25]
	v_mfma_f32_16x16x32_bf16 v[18:21], v[178:181], v[202:205], v[18:21]
	v_mfma_f32_16x16x32_bf16 v[6:9], v[170:173], v[210:213], v[6:9]
	v_mfma_f32_16x16x32_bf16 v[2:5], v[178:181], v[210:213], v[2:5]
	s_setprio 0
	s_barrier
	s_add_i32 s57, 0, 0x18000
	v_add_u32_e32 v130, s57, v146
	s_add_i32 s58, 0, 0x1c000
	ds_read_b128 v[142:145], v130
	ds_read_b128 v[154:157], v130 offset:1024
	ds_read_b128 v[158:161], v130 offset:2048
	ds_read_b128 v[162:165], v130 offset:3072
	v_add_u32_e32 v130, s58, v146
	ds_read_b128 v[166:169], v130
	ds_read_b128 v[170:173], v130 offset:1024
	ds_read_b128 v[174:177], v130 offset:2048
	ds_read_b128 v[178:181], v130 offset:3072
	s_add_u32 s28, s36, 0xe0000
	s_addc_u32 s29, s37, 0
	s_mov_b32 m0, s40
	ds_read_b128 v[182:185], v152 offset:32768
	ds_read_b128 v[186:189], v152 offset:33792
	ds_read_b128 v[190:193], v152 offset:34816
	ds_read_b128 v[194:197], v152 offset:35840
	ds_read_b128 v[198:201], v152 offset:36864
	ds_read_b128 v[202:205], v152 offset:37888
	ds_read_b128 v[206:209], v152 offset:38912
	ds_read_b128 v[210:213], v152 offset:39936
	global_load_lds_dwordx4 v132, s[28:29]
	s_mov_b32 m0, s41
	s_nop 0
	global_load_lds_dwordx4 v134, s[28:29]
	s_waitcnt vmcnt(8)
	s_waitcnt lgkmcnt(0)
	s_barrier
	s_setprio 3
	s_waitcnt lgkmcnt(0)
	v_mfma_f32_16x16x32_bf16 v[126:129], v[142:145], v[182:185], v[126:129]
	v_mfma_f32_16x16x32_bf16 v[122:125], v[158:161], v[182:185], v[122:125]
	v_mfma_f32_16x16x32_bf16 v[110:113], v[142:145], v[190:193], v[110:113]
	v_mfma_f32_16x16x32_bf16 v[106:109], v[158:161], v[190:193], v[106:109]
	v_mfma_f32_16x16x32_bf16 v[94:97], v[142:145], v[198:201], v[94:97]
	v_mfma_f32_16x16x32_bf16 v[90:93], v[158:161], v[198:201], v[90:93]
	v_mfma_f32_16x16x32_bf16 v[78:81], v[142:145], v[206:209], v[78:81]
	v_mfma_f32_16x16x32_bf16 v[74:77], v[158:161], v[206:209], v[74:77]
	v_mfma_f32_16x16x32_bf16 v[126:129], v[154:157], v[186:189], v[126:129]
	v_mfma_f32_16x16x32_bf16 v[122:125], v[162:165], v[186:189], v[122:125]
	v_mfma_f32_16x16x32_bf16 v[110:113], v[154:157], v[194:197], v[110:113]
	v_mfma_f32_16x16x32_bf16 v[106:109], v[162:165], v[194:197], v[106:109]
	v_mfma_f32_16x16x32_bf16 v[94:97], v[154:157], v[202:205], v[94:97]
	v_mfma_f32_16x16x32_bf16 v[90:93], v[162:165], v[202:205], v[90:93]
	v_mfma_f32_16x16x32_bf16 v[78:81], v[154:157], v[210:213], v[78:81]
	v_mfma_f32_16x16x32_bf16 v[74:77], v[162:165], v[210:213], v[74:77]
	s_setprio 0
	s_setprio 3
	v_mfma_f32_16x16x32_bf16 v[118:121], v[166:169], v[182:185], v[118:121]
	v_mfma_f32_16x16x32_bf16 v[114:117], v[174:177], v[182:185], v[114:117]
	v_mfma_f32_16x16x32_bf16 v[102:105], v[166:169], v[190:193], v[102:105]
	v_mfma_f32_16x16x32_bf16 v[98:101], v[174:177], v[190:193], v[98:101]
	v_mfma_f32_16x16x32_bf16 v[86:89], v[166:169], v[198:201], v[86:89]
	v_mfma_f32_16x16x32_bf16 v[82:85], v[174:177], v[198:201], v[82:85]
	v_mfma_f32_16x16x32_bf16 v[70:73], v[166:169], v[206:209], v[70:73]
	v_mfma_f32_16x16x32_bf16 v[66:69], v[174:177], v[206:209], v[66:69]
	v_mfma_f32_16x16x32_bf16 v[118:121], v[170:173], v[186:189], v[118:121]
	v_mfma_f32_16x16x32_bf16 v[114:117], v[178:181], v[186:189], v[114:117]
	v_mfma_f32_16x16x32_bf16 v[102:105], v[170:173], v[194:197], v[102:105]
	v_mfma_f32_16x16x32_bf16 v[98:101], v[178:181], v[194:197], v[98:101]
	v_mfma_f32_16x16x32_bf16 v[86:89], v[170:173], v[202:205], v[86:89]
	v_mfma_f32_16x16x32_bf16 v[82:85], v[178:181], v[202:205], v[82:85]
	v_mfma_f32_16x16x32_bf16 v[70:73], v[170:173], v[210:213], v[70:73]
	v_mfma_f32_16x16x32_bf16 v[66:69], v[178:181], v[210:213], v[66:69]
	s_setprio 0
	s_barrier
; #define PG8_STAGE_A(b, h, ptr, NX) do { if constexpr (Sched::GATHER) { unsigned gs_[2]; gs_[0] = ((NX) && last_) ? gN[h][0] : gA[h][0]; gs_[1] = ((NX) && last_) ? gN[h][1] : gA[h][1]; PG8_STAGE(PG8_SA(b, h), ptr, gs_); } \
;         else PG8_STAGE(PG8_SA(b, h), (ptr) + ((h) ? hstep : (size_t)0), voffA); } while (0)
; #define PG8_STAGE(bufoff, gbase, voff) do { _Pragma("unroll") for (int _i = 0; _i < 2; ++_i) \
;         __builtin_amdgcn_global_load_lds((const unsigned*)((const char*)(gbase) + (voff)[_i]), (PG8_LAS unsigned*)(lds + (bufoff) + ldsw + _i * 8192), 16, 0, 0); } while (0)
; #define PG8_LDA(dst, b, h) do { _Pragma("unroll") for (int m = 0; m < 4; ++m) _Pragma("unroll") for (int k = 0; k < 2; ++k) dst[m][k] = *(const PG8_LAS bf16x8*)(lds + PG8_SA(b, h) + aoff + m * 2048 + k * 1024); } while (0)
; #define PG8_MMA(ai, bj, At, Bt) do { __builtin_amdgcn_s_setprio(1); _Pragma("unroll") for (int m = 0; m < 4; ++m) _Pragma("unroll") for (int n = 0; n < 2; ++n) _Pragma("unroll") for (int k = 0; k < 2; ++k) \
;         acc[ai][bj][m][n] = __builtin_amdgcn_mfma_f32_16x16x32_bf16(Bt[n][k], At[m][k], acc[ai][bj][m][n], 0, 0, 0); __builtin_amdgcn_s_setprio(0); } while (0)
; #define PG8_WAIT_V(n) asm volatile("s_waitcnt vmcnt(" #n ")" ::: "memory")
; #define PG8_WAIT_L(n) asm volatile("s_waitcnt lgkmcnt(" #n ")" ::: "memory")
; #define PG8_BAR __builtin_amdgcn_s_barrier()
; #define PG8_SCHED __builtin_amdgcn_sched_barrier(0)
; template <class Epi, class Sched, bool ALIGN_EPI = false, bool SP2 = false>
; __device__ __forceinline__ void gemm_phase(PG8_LAS unsigned char* lds, const Gemm g, const Sched& S, const Epi& E, const bool skip_epi = false) {
;     ...
;             PG8_LDA(At, 1, 1); PG8_STAGE(PG8_SB(1, 0), b3, voffB); PG8_STAGE(PG8_SB(1, 1), b3 + hstep, voffB); PG8_STAGE_A(1, 0, a3, true);
;             PG8_WAIT_V(8); PG8_WAIT_L(0); PG8_BAR; PG8_MMA(1, 0, At, B0); PG8_MMA(1, 1, At, B1); PG8_BAR; PG8_SCHED;
	s_add_i32 s28, s57, s3
	s_add_i32 m0, s28, 0xffffff80
	ds_read_b128 v[182:185], v152 offset:49152
	ds_read_b128 v[186:189], v152 offset:50176
	ds_read_b128 v[190:193], v152 offset:51200
	ds_read_b128 v[194:197], v152 offset:52224
	ds_read_b128 v[198:201], v152 offset:53248
	ds_read_b128 v[202:205], v152 offset:54272
	ds_read_b128 v[206:209], v152 offset:55296
	ds_read_b128 v[210:213], v152 offset:56320
	global_load_lds_dwordx4 v[214:215], off offset:128
	s_add_i32 m0, s28, 0x1f80
	s_add_u32 s28, s34, 0xe0080
	s_addc_u32 s29, s35, 0
	s_add_i32 s34, s58, s3
	global_load_lds_dwordx4 v[216:217], off offset:128
	s_mov_b32 m0, s34
	s_nop 0
	global_load_lds_dwordx4 v132, s[28:29]
	s_add_i32 m0, s34, 0x2000
	s_nop 0
	global_load_lds_dwordx4 v134, s[28:29]
	s_add_i32 m0, s46, 0xffffff80
	s_nop 0
	global_load_lds_dwordx4 v[218:219], off offset:128
	s_add_i32 m0, s47, 0xffffff80
	s_nop 0
	global_load_lds_dwordx4 v[220:221], off offset:128
	s_waitcnt vmcnt(8)
	s_waitcnt lgkmcnt(0)
	s_barrier
	s_setprio 3
	s_waitcnt lgkmcnt(0)
	v_mfma_f32_16x16x32_bf16 v[62:65], v[142:145], v[182:185], v[62:65]
	v_mfma_f32_16x16x32_bf16 v[58:61], v[158:161], v[182:185], v[58:61]
	v_mfma_f32_16x16x32_bf16 v[46:49], v[142:145], v[190:193], v[46:49]
	v_mfma_f32_16x16x32_bf16 v[42:45], v[158:161], v[190:193], v[42:45]
	v_mfma_f32_16x16x32_bf16 v[30:33], v[142:145], v[198:201], v[30:33]
	v_mfma_f32_16x16x32_bf16 v[26:29], v[158:161], v[198:201], v[26:29]
	v_mfma_f32_16x16x32_bf16 v[14:17], v[142:145], v[206:209], v[14:17]
	v_mfma_f32_16x16x32_bf16 v[10:13], v[158:161], v[206:209], v[10:13]
	v_mfma_f32_16x16x32_bf16 v[62:65], v[154:157], v[186:189], v[62:65]
	v_mfma_f32_16x16x32_bf16 v[58:61], v[162:165], v[186:189], v[58:61]
	v_mfma_f32_16x16x32_bf16 v[46:49], v[154:157], v[194:197], v[46:49]
	v_mfma_f32_16x16x32_bf16 v[42:45], v[162:165], v[194:197], v[42:45]
	v_mfma_f32_16x16x32_bf16 v[30:33], v[154:157], v[202:205], v[30:33]
	v_mfma_f32_16x16x32_bf16 v[26:29], v[162:165], v[202:205], v[26:29]
	v_mfma_f32_16x16x32_bf16 v[14:17], v[154:157], v[210:213], v[14:17]
	v_mfma_f32_16x16x32_bf16 v[10:13], v[162:165], v[210:213], v[10:13]
	s_setprio 0
	s_setprio 3
	v_mfma_f32_16x16x32_bf16 v[54:57], v[166:169], v[182:185], v[54:57]
	v_mfma_f32_16x16x32_bf16 v[50:53], v[174:177], v[182:185], v[50:53]
	v_mfma_f32_16x16x32_bf16 v[38:41], v[166:169], v[190:193], v[38:41]
	v_mfma_f32_16x16x32_bf16 v[34:37], v[174:177], v[190:193], v[34:37]
	v_mfma_f32_16x16x32_bf16 v[22:25], v[166:169], v[198:201], v[22:25]
	v_mfma_f32_16x16x32_bf16 v[18:21], v[174:177], v[198:201], v[18:21]
	v_mfma_f32_16x16x32_bf16 v[6:9], v[166:169], v[206:209], v[6:9]
	v_mfma_f32_16x16x32_bf16 v[2:5], v[174:177], v[206:209], v[2:5]
	v_mfma_f32_16x16x32_bf16 v[54:57], v[170:173], v[186:189], v[54:57]
	v_mfma_f32_16x16x32_bf16 v[50:53], v[178:181], v[186:189], v[50:53]
	v_mfma_f32_16x16x32_bf16 v[38:41], v[170:173], v[194:197], v[38:41]
	v_mfma_f32_16x16x32_bf16 v[34:37], v[178:181], v[194:197], v[34:37]
	v_mfma_f32_16x16x32_bf16 v[22:25], v[170:173], v[202:205], v[22:25]
	v_mfma_f32_16x16x32_bf16 v[18:21], v[178:181], v[202:205], v[18:21]
	v_mfma_f32_16x16x32_bf16 v[6:9], v[170:173], v[210:213], v[6:9]
	v_mfma_f32_16x16x32_bf16 v[2:5], v[178:181], v[210:213], v[2:5]
	s_setprio 0
	s_barrier
	s_add_i32 s56, s56, 2
	s_add_u32 s54, s54, 0x100
	s_addc_u32 s55, s55, 0
	s_cmp_gt_u32 s56, 11
	s_mov_b64 s[28:29], s[30:31]
.LBB0_1844:
	ds_read_b128 v[142:145], v150
	ds_read_b128 v[154:157], v150 offset:1024
	ds_read_b128 v[158:161], v150 offset:2048
	ds_read_b128 v[162:165], v150 offset:3072
	ds_read_b128 v[166:169], v151
	ds_read_b128 v[170:173], v151 offset:1024
	ds_read_b128 v[174:177], v151 offset:2048
	ds_read_b128 v[178:181], v151 offset:3072
	s_add_u32 s30, s28, 0x100
	s_addc_u32 s31, s29, 0
	s_cmp_eq_u32 s56, 10
	s_cselect_b32 s37, s7, s31
	s_cselect_b32 s36, s6, s30
	s_cselect_b32 s35, s25, s55
	s_cselect_b32 s34, s24, s54
	v_lshl_add_u64 v[214:215], s[28:29], 0, v[136:137]
	s_add_i32 m0, s38, 0xc000
	ds_read_b128 v[182:185], v152
	ds_read_b128 v[186:189], v152 offset:1024
	ds_read_b128 v[190:193], v152 offset:2048
	ds_read_b128 v[194:197], v152 offset:3072
	ds_read_b128 v[198:201], v152 offset:4096
	ds_read_b128 v[202:205], v152 offset:5120
	ds_read_b128 v[206:209], v152 offset:6144
	ds_read_b128 v[210:213], v152 offset:7168
	global_load_lds_dwordx4 v[214:215], off
	v_lshl_add_u64 v[214:215], s[28:29], 0, v[138:139]
	s_add_i32 m0, s38, 0xe000
	s_nop 0
	global_load_lds_dwordx4 v[214:215], off
	s_waitcnt vmcnt(8)
	s_waitcnt lgkmcnt(0)
	s_barrier
; #define PG8_STAGE_A(b, h, ptr, NX) do { if constexpr (Sched::GATHER) { unsigned gs_[2]; gs_[0] = ((NX) && last_) ? gN[h][0] : gA[h][0]; gs_[1] = ((NX) && last_) ? gN[h][1] : gA[h][1]; PG8_STAGE(PG8_SA(b, h), ptr, gs_); } \
;         else PG8_STAGE(PG8_SA(b, h), (ptr) + ((h) ? hstep : (size_t)0), voffA); } while (0)
; #define PG8_STAGE(bufoff, gbase, voff) do { _Pragma("unroll") for (int _i = 0; _i < 2; ++_i) \
;         __builtin_amdgcn_global_load_lds((const unsigned*)((const char*)(gbase) + (voff)[_i]), (PG8_LAS unsigned*)(lds + (bufoff) + ldsw + _i * 8192), 16, 0, 0); } while (0)
; #define PG8_LDA(dst, b, h) do { _Pragma("unroll") for (int m = 0; m < 4; ++m) _Pragma("unroll") for (int k = 0; k < 2; ++k) dst[m][k] = *(const PG8_LAS bf16x8*)(lds + PG8_SA(b, h) + aoff + m * 2048 + k * 1024); } while (0)
; #define PG8_LDB(dst, b, h) do { _Pragma("unroll") for (int n = 0; n < 2; ++n) _Pragma("unroll") for (int k = 0; k < 2; ++k) dst[n][k] = *(const PG8_LAS bf16x8*)(lds + PG8_SB(b, h) + boff + n * 2048 + k * 1024); } while (0)
; #define PG8_MMA(ai, bj, At, Bt) do { __builtin_amdgcn_s_setprio(1); _Pragma("unroll") for (int m = 0; m < 4; ++m) _Pragma("unroll") for (int n = 0; n < 2; ++n) _Pragma("unroll") for (int k = 0; k < 2; ++k) \
;         acc[ai][bj][m][n] = __builtin_amdgcn_mfma_f32_16x16x32_bf16(Bt[n][k], At[m][k], acc[ai][bj][m][n], 0, 0, 0); __builtin_amdgcn_s_setprio(0); } while (0)
; #define PG8_WAIT_V(n) asm volatile("s_waitcnt vmcnt(" #n ")" ::: "memory")
; #define PG8_WAIT_L(n) asm volatile("s_waitcnt lgkmcnt(" #n ")" ::: "memory")
; #define PG8_BAR __builtin_amdgcn_s_barrier()
; #define PG8_SCHED __builtin_amdgcn_sched_barrier(0)
; template <class Epi, class Sched, bool ALIGN_EPI = false, bool SP2 = false>
; __device__ __forceinline__ void gemm_phase(PG8_LAS unsigned char* lds, const Gemm g, const Sched& S, const Epi& E, const bool skip_epi = false) {
;     ...
;             PG8_LDB(B0, 0, 0); PG8_LDB(B1, 0, 1); PG8_SCHED; PG8_LDA(At, 0, 0); PG8_STAGE_A(1, 1, a1, false);
;             PG8_WAIT_V(8); PG8_WAIT_L(0); PG8_BAR; PG8_MMA(0, 0, At, B0); PG8_MMA(0, 1, At, B1); PG8_BAR; PG8_SCHED;
;             PG8_LDA(At, 0, 1); PG8_STAGE(PG8_SB(0, 0), b2, voffB); PG8_STAGE(PG8_SB(0, 1), b2 + hstep, voffB); PG8_STAGE_A(0, 0, a2, true);
;             PG8_WAIT_V(8); PG8_WAIT_L(0); PG8_BAR; PG8_MMA(1, 0, At, B0); PG8_MMA(1, 1, At, B1); PG8_BAR; PG8_SCHED;
	s_setprio 3
	s_waitcnt lgkmcnt(0)
	v_mfma_f32_16x16x32_bf16 v[126:129], v[142:145], v[182:185], v[126:129]
	v_mfma_f32_16x16x32_bf16 v[122:125], v[158:161], v[182:185], v[122:125]
	v_mfma_f32_16x16x32_bf16 v[110:113], v[142:145], v[190:193], v[110:113]
	v_mfma_f32_16x16x32_bf16 v[106:109], v[158:161], v[190:193], v[106:109]
	v_lshl_add_u64 v[214:215], s[34:35], 0, v[132:133]
	v_mfma_f32_16x16x32_bf16 v[94:97], v[142:145], v[198:201], v[94:97]
	v_mfma_f32_16x16x32_bf16 v[90:93], v[158:161], v[198:201], v[90:93]
	v_lshl_add_u64 v[216:217], s[34:35], 0, v[134:135]
	v_mfma_f32_16x16x32_bf16 v[78:81], v[142:145], v[206:209], v[78:81]
	v_mfma_f32_16x16x32_bf16 v[74:77], v[158:161], v[206:209], v[74:77]
	v_lshl_add_u64 v[220:221], s[36:37], 0, v[134:135]
	v_mfma_f32_16x16x32_bf16 v[126:129], v[154:157], v[186:189], v[126:129]
	v_mfma_f32_16x16x32_bf16 v[122:125], v[162:165], v[186:189], v[122:125]
	v_lshl_add_u64 v[218:219], s[36:37], 0, v[132:133]
	v_mfma_f32_16x16x32_bf16 v[110:113], v[154:157], v[194:197], v[110:113]
	v_mfma_f32_16x16x32_bf16 v[106:109], v[162:165], v[194:197], v[106:109]
	v_mfma_f32_16x16x32_bf16 v[94:97], v[154:157], v[202:205], v[94:97]
	v_mfma_f32_16x16x32_bf16 v[90:93], v[162:165], v[202:205], v[90:93]
	v_mfma_f32_16x16x32_bf16 v[78:81], v[154:157], v[210:213], v[78:81]
	v_mfma_f32_16x16x32_bf16 v[74:77], v[162:165], v[210:213], v[74:77]
	s_setprio 0
	s_setprio 3
	v_mfma_f32_16x16x32_bf16 v[118:121], v[166:169], v[182:185], v[118:121]
	v_mfma_f32_16x16x32_bf16 v[114:117], v[174:177], v[182:185], v[114:117]
	v_mfma_f32_16x16x32_bf16 v[102:105], v[166:169], v[190:193], v[102:105]
	v_mfma_f32_16x16x32_bf16 v[98:101], v[174:177], v[190:193], v[98:101]
	v_mfma_f32_16x16x32_bf16 v[86:89], v[166:169], v[198:201], v[86:89]
	v_mfma_f32_16x16x32_bf16 v[82:85], v[174:177], v[198:201], v[82:85]
	v_mfma_f32_16x16x32_bf16 v[70:73], v[166:169], v[206:209], v[70:73]
	v_mfma_f32_16x16x32_bf16 v[66:69], v[174:177], v[206:209], v[66:69]
	v_mfma_f32_16x16x32_bf16 v[118:121], v[170:173], v[186:189], v[118:121]
	v_mfma_f32_16x16x32_bf16 v[114:117], v[178:181], v[186:189], v[114:117]
	v_mfma_f32_16x16x32_bf16 v[102:105], v[170:173], v[194:197], v[102:105]
	v_mfma_f32_16x16x32_bf16 v[98:101], v[178:181], v[194:197], v[98:101]
	v_mfma_f32_16x16x32_bf16 v[86:89], v[170:173], v[202:205], v[86:89]
	v_mfma_f32_16x16x32_bf16 v[82:85], v[178:181], v[202:205], v[82:85]
	v_mfma_f32_16x16x32_bf16 v[70:73], v[170:173], v[210:213], v[70:73]
	v_mfma_f32_16x16x32_bf16 v[66:69], v[178:181], v[210:213], v[66:69]
	s_setprio 0
	s_barrier
	s_add_i32 s28, s50, s3
	s_mov_b32 m0, s28
	ds_read_b128 v[182:185], v152 offset:16384
	ds_read_b128 v[186:189], v152 offset:17408
	ds_read_b128 v[190:193], v152 offset:18432
	ds_read_b128 v[194:197], v152 offset:19456
	ds_read_b128 v[198:201], v152 offset:20480
	ds_read_b128 v[202:205], v152 offset:21504
	ds_read_b128 v[206:209], v152 offset:22528
	ds_read_b128 v[210:213], v152 offset:23552
	global_load_lds_dwordx4 v[214:215], off
	s_add_i32 m0, s28, 0x2000
	s_add_u32 s28, s34, 0xe0000
	s_addc_u32 s29, s35, 0
	s_add_i32 s57, s51, s3
	global_load_lds_dwordx4 v[216:217], off
	s_mov_b32 m0, s57
	s_nop 0
	global_load_lds_dwordx4 v132, s[28:29]
	s_add_i32 m0, s57, 0x2000
	s_nop 0
	global_load_lds_dwordx4 v134, s[28:29]
	s_mov_b32 m0, s38
	s_nop 0
	global_load_lds_dwordx4 v[218:219], off
	s_mov_b32 m0, s39
	s_nop 0
	global_load_lds_dwordx4 v[220:221], off
	s_waitcnt vmcnt(8)
	s_waitcnt lgkmcnt(0)
	s_barrier
	s_setprio 3
	s_waitcnt lgkmcnt(0)
	v_mfma_f32_16x16x32_bf16 v[62:65], v[142:145], v[182:185], v[62:65]
	v_mfma_f32_16x16x32_bf16 v[58:61], v[158:161], v[182:185], v[58:61]
	v_mfma_f32_16x16x32_bf16 v[46:49], v[142:145], v[190:193], v[46:49]
	v_mfma_f32_16x16x32_bf16 v[42:45], v[158:161], v[190:193], v[42:45]
	v_mfma_f32_16x16x32_bf16 v[30:33], v[142:145], v[198:201], v[30:33]
	v_mfma_f32_16x16x32_bf16 v[26:29], v[158:161], v[198:201], v[26:29]
	v_mfma_f32_16x16x32_bf16 v[14:17], v[142:145], v[206:209], v[14:17]
	v_mfma_f32_16x16x32_bf16 v[10:13], v[158:161], v[206:209], v[10:13]
	v_mfma_f32_16x16x32_bf16 v[62:65], v[154:157], v[186:189], v[62:65]
	v_mfma_f32_16x16x32_bf16 v[58:61], v[162:165], v[186:189], v[58:61]
	v_mfma_f32_16x16x32_bf16 v[46:49], v[154:157], v[194:197], v[46:49]
	v_mfma_f32_16x16x32_bf16 v[42:45], v[162:165], v[194:197], v[42:45]
	v_mfma_f32_16x16x32_bf16 v[30:33], v[154:157], v[202:205], v[30:33]
	v_mfma_f32_16x16x32_bf16 v[26:29], v[162:165], v[202:205], v[26:29]
	v_mfma_f32_16x16x32_bf16 v[14:17], v[154:157], v[210:213], v[14:17]
	v_mfma_f32_16x16x32_bf16 v[10:13], v[162:165], v[210:213], v[10:13]
	s_setprio 0
	s_setprio 3
	v_mfma_f32_16x16x32_bf16 v[54:57], v[166:169], v[182:185], v[54:57]
	v_mfma_f32_16x16x32_bf16 v[50:53], v[174:177], v[182:185], v[50:53]
	v_mfma_f32_16x16x32_bf16 v[38:41], v[166:169], v[190:193], v[38:41]
	v_mfma_f32_16x16x32_bf16 v[34:37], v[174:177], v[190:193], v[34:37]
	v_mfma_f32_16x16x32_bf16 v[22:25], v[166:169], v[198:201], v[22:25]
	v_mfma_f32_16x16x32_bf16 v[18:21], v[174:177], v[198:201], v[18:21]
	v_mfma_f32_16x16x32_bf16 v[6:9], v[166:169], v[206:209], v[6:9]
	v_mfma_f32_16x16x32_bf16 v[2:5], v[174:177], v[206:209], v[2:5]
	v_mfma_f32_16x16x32_bf16 v[54:57], v[170:173], v[186:189], v[54:57]
	v_mfma_f32_16x16x32_bf16 v[50:53], v[178:181], v[186:189], v[50:53]
	v_mfma_f32_16x16x32_bf16 v[38:41], v[170:173], v[194:197], v[38:41]
	v_mfma_f32_16x16x32_bf16 v[34:37], v[178:181], v[194:197], v[34:37]
	v_mfma_f32_16x16x32_bf16 v[22:25], v[170:173], v[202:205], v[22:25]
	v_mfma_f32_16x16x32_bf16 v[18:21], v[178:181], v[202:205], v[18:21]
	v_mfma_f32_16x16x32_bf16 v[6:9], v[170:173], v[210:213], v[6:9]
	v_mfma_f32_16x16x32_bf16 v[2:5], v[178:181], v[210:213], v[2:5]
	s_setprio 0
	s_barrier
; #define PG8_STAGE_A(b, h, ptr, NX) do { if constexpr (Sched::GATHER) { unsigned gs_[2]; gs_[0] = ((NX) && last_) ? gN[h][0] : gA[h][0]; gs_[1] = ((NX) && last_) ? gN[h][1] : gA[h][1]; PG8_STAGE(PG8_SA(b, h), ptr, gs_); } \
;         else PG8_STAGE(PG8_SA(b, h), (ptr) + ((h) ? hstep : (size_t)0), voffA); } while (0)
; #define PG8_STAGE(bufoff, gbase, voff) do { _Pragma("unroll") for (int _i = 0; _i < 2; ++_i) \
;         __builtin_amdgcn_global_load_lds((const unsigned*)((const char*)(gbase) + (voff)[_i]), (PG8_LAS unsigned*)(lds + (bufoff) + ldsw + _i * 8192), 16, 0, 0); } while (0)
; #define PG8_LDA(dst, b, h) do { _Pragma("unroll") for (int m = 0; m < 4; ++m) _Pragma("unroll") for (int k = 0; k < 2; ++k) dst[m][k] = *(const PG8_LAS bf16x8*)(lds + PG8_SA(b, h) + aoff + m * 2048 + k * 1024); } while (0)
; #define PG8_LDB(dst, b, h) do { _Pragma("unroll") for (int n = 0; n < 2; ++n) _Pragma("unroll") for (int k = 0; k < 2; ++k) dst[n][k] = *(const PG8_LAS bf16x8*)(lds + PG8_SB(b, h) + boff + n * 2048 + k * 1024); } while (0)
; #define PG8_MMA(ai, bj, At, Bt) do { __builtin_amdgcn_s_setprio(1); _Pragma("unroll") for (int m = 0; m < 4; ++m) _Pragma("unroll") for (int n = 0; n < 2; ++n) _Pragma("unroll") for (int k = 0; k < 2; ++k) \
;         acc[ai][bj][m][n] = __builtin_amdgcn_mfma_f32_16x16x32_bf16(Bt[n][k], At[m][k], acc[ai][bj][m][n], 0, 0, 0); __builtin_amdgcn_s_setprio(0); } while (0)
; #define PG8_WAIT_V(n) asm volatile("s_waitcnt vmcnt(" #n ")" ::: "memory")
; #define PG8_WAIT_L(n) asm volatile("s_waitcnt lgkmcnt(" #n ")" ::: "memory")
; #define PG8_BAR __builtin_amdgcn_s_barrier()
; #define PG8_SCHED __builtin_amdgcn_sched_barrier(0)
; template <class Epi, class Sched, bool ALIGN_EPI = false, bool SP2 = false>
; __device__ __forceinline__ void gemm_phase(PG8_LAS unsigned char* lds, const Gemm g, const Sched& S, const Epi& E, const bool skip_epi = false) {
;     ...
;             PG8_LDB(B0, 1, 0); PG8_LDB(B1, 1, 1); PG8_SCHED; PG8_LDA(At, 1, 0); PG8_STAGE_A(0, 1, a2, true);
;             PG8_WAIT_V(8); PG8_WAIT_L(0); PG8_BAR; PG8_MMA(0, 0, At, B0); PG8_MMA(0, 1, At, B1); PG8_BAR; PG8_SCHED;
;             PG8_LDA(At, 1, 1); PG8_STAGE(PG8_SB(1, 0), b3, voffB); PG8_STAGE(PG8_SB(1, 1), b3 + hstep, voffB); PG8_STAGE_A(1, 0, a3, true);
;             PG8_WAIT_V(8); PG8_WAIT_L(0); PG8_BAR; PG8_MMA(1, 0, At, B0); PG8_MMA(1, 1, At, B1); PG8_BAR; PG8_SCHED;
	s_add_i32 s57, 0, 0x18000
	v_add_u32_e32 v130, s57, v146
	s_add_i32 s58, 0, 0x1c000
	ds_read_b128 v[142:145], v130
	ds_read_b128 v[154:157], v130 offset:1024
	ds_read_b128 v[158:161], v130 offset:2048
	ds_read_b128 v[162:165], v130 offset:3072
	v_add_u32_e32 v130, s58, v146
	ds_read_b128 v[166:169], v130
	ds_read_b128 v[170:173], v130 offset:1024
	ds_read_b128 v[174:177], v130 offset:2048
	ds_read_b128 v[178:181], v130 offset:3072
	s_add_u32 s28, s36, 0xe0000
	s_addc_u32 s29, s37, 0
	s_mov_b32 m0, s40
	ds_read_b128 v[182:185], v152 offset:32768
	ds_read_b128 v[186:189], v152 offset:33792
	ds_read_b128 v[190:193], v152 offset:34816
	ds_read_b128 v[194:197], v152 offset:35840
	ds_read_b128 v[198:201], v152 offset:36864
	ds_read_b128 v[202:205], v152 offset:37888
	ds_read_b128 v[206:209], v152 offset:38912
	ds_read_b128 v[210:213], v152 offset:39936
	global_load_lds_dwordx4 v132, s[28:29]
	s_mov_b32 m0, s41
	s_nop 0
	global_load_lds_dwordx4 v134, s[28:29]
	s_waitcnt vmcnt(8)
	s_waitcnt lgkmcnt(0)
	s_barrier
	s_setprio 3
	s_waitcnt lgkmcnt(0)
	v_mfma_f32_16x16x32_bf16 v[126:129], v[142:145], v[182:185], v[126:129]
	v_mfma_f32_16x16x32_bf16 v[122:125], v[158:161], v[182:185], v[122:125]
	v_mfma_f32_16x16x32_bf16 v[110:113], v[142:145], v[190:193], v[110:113]
	v_mfma_f32_16x16x32_bf16 v[106:109], v[158:161], v[190:193], v[106:109]
	v_mfma_f32_16x16x32_bf16 v[94:97], v[142:145], v[198:201], v[94:97]
	v_mfma_f32_16x16x32_bf16 v[90:93], v[158:161], v[198:201], v[90:93]
	v_mfma_f32_16x16x32_bf16 v[78:81], v[142:145], v[206:209], v[78:81]
	v_mfma_f32_16x16x32_bf16 v[74:77], v[158:161], v[206:209], v[74:77]
	v_mfma_f32_16x16x32_bf16 v[126:129], v[154:157], v[186:189], v[126:129]
	v_mfma_f32_16x16x32_bf16 v[122:125], v[162:165], v[186:189], v[122:125]
	v_mfma_f32_16x16x32_bf16 v[110:113], v[154:157], v[194:197], v[110:113]
	v_mfma_f32_16x16x32_bf16 v[106:109], v[162:165], v[194:197], v[106:109]
	v_mfma_f32_16x16x32_bf16 v[94:97], v[154:157], v[202:205], v[94:97]
	v_mfma_f32_16x16x32_bf16 v[90:93], v[162:165], v[202:205], v[90:93]
	v_mfma_f32_16x16x32_bf16 v[78:81], v[154:157], v[210:213], v[78:81]
	v_mfma_f32_16x16x32_bf16 v[74:77], v[162:165], v[210:213], v[74:77]
	s_setprio 0
	s_setprio 3
	v_mfma_f32_16x16x32_bf16 v[118:121], v[166:169], v[182:185], v[118:121]
	v_mfma_f32_16x16x32_bf16 v[114:117], v[174:177], v[182:185], v[114:117]
	v_mfma_f32_16x16x32_bf16 v[102:105], v[166:169], v[190:193], v[102:105]
	v_mfma_f32_16x16x32_bf16 v[98:101], v[174:177], v[190:193], v[98:101]
	v_mfma_f32_16x16x32_bf16 v[86:89], v[166:169], v[198:201], v[86:89]
	v_mfma_f32_16x16x32_bf16 v[82:85], v[174:177], v[198:201], v[82:85]
	v_mfma_f32_16x16x32_bf16 v[70:73], v[166:169], v[206:209], v[70:73]
	v_mfma_f32_16x16x32_bf16 v[66:69], v[174:177], v[206:209], v[66:69]
	v_mfma_f32_16x16x32_bf16 v[118:121], v[170:173], v[186:189], v[118:121]
	v_mfma_f32_16x16x32_bf16 v[114:117], v[178:181], v[186:189], v[114:117]
	v_mfma_f32_16x16x32_bf16 v[102:105], v[170:173], v[194:197], v[102:105]
	v_mfma_f32_16x16x32_bf16 v[98:101], v[178:181], v[194:197], v[98:101]
	v_mfma_f32_16x16x32_bf16 v[86:89], v[170:173], v[202:205], v[86:89]
	v_mfma_f32_16x16x32_bf16 v[82:85], v[178:181], v[202:205], v[82:85]
	v_mfma_f32_16x16x32_bf16 v[70:73], v[170:173], v[210:213], v[70:73]
	v_mfma_f32_16x16x32_bf16 v[66:69], v[178:181], v[210:213], v[66:69]
	s_setprio 0
	s_barrier
	s_add_i32 s28, s57, s3
	s_add_i32 m0, s28, 0xffffff80
	ds_read_b128 v[182:185], v152 offset:49152
	ds_read_b128 v[186:189], v152 offset:50176
	ds_read_b128 v[190:193], v152 offset:51200
	ds_read_b128 v[194:197], v152 offset:52224
	ds_read_b128 v[198:201], v152 offset:53248
	ds_read_b128 v[202:205], v152 offset:54272
	ds_read_b128 v[206:209], v152 offset:55296
	ds_read_b128 v[210:213], v152 offset:56320
	global_load_lds_dwordx4 v[214:215], off offset:128
	s_add_i32 m0, s28, 0x1f80
	s_add_u32 s28, s34, 0xe0080
	s_addc_u32 s29, s35, 0
	s_add_i32 s34, s58, s3
	global_load_lds_dwordx4 v[216:217], off offset:128
	s_mov_b32 m0, s34
	s_nop 0
	global_load_lds_dwordx4 v132, s[28:29]
	s_add_i32 m0, s34, 0x2000
	s_nop 0
	global_load_lds_dwordx4 v134, s[28:29]
	s_add_i32 m0, s46, 0xffffff80
	s_nop 0
	global_load_lds_dwordx4 v[218:219], off offset:128
	s_add_i32 m0, s47, 0xffffff80
	s_nop 0
	global_load_lds_dwordx4 v[220:221], off offset:128
	s_waitcnt vmcnt(8)
	s_waitcnt lgkmcnt(0)
	s_barrier
	s_setprio 3
	s_waitcnt lgkmcnt(0)
	v_mfma_f32_16x16x32_bf16 v[62:65], v[142:145], v[182:185], v[62:65]
	v_mfma_f32_16x16x32_bf16 v[58:61], v[158:161], v[182:185], v[58:61]
	v_mfma_f32_16x16x32_bf16 v[46:49], v[142:145], v[190:193], v[46:49]
	v_mfma_f32_16x16x32_bf16 v[42:45], v[158:161], v[190:193], v[42:45]
	v_mfma_f32_16x16x32_bf16 v[30:33], v[142:145], v[198:201], v[30:33]
	v_mfma_f32_16x16x32_bf16 v[26:29], v[158:161], v[198:201], v[26:29]
	v_mfma_f32_16x16x32_bf16 v[14:17], v[142:145], v[206:209], v[14:17]
	v_mfma_f32_16x16x32_bf16 v[10:13], v[158:161], v[206:209], v[10:13]
	v_mfma_f32_16x16x32_bf16 v[62:65], v[154:157], v[186:189], v[62:65]
	v_mfma_f32_16x16x32_bf16 v[58:61], v[162:165], v[186:189], v[58:61]
	v_mfma_f32_16x16x32_bf16 v[46:49], v[154:157], v[194:197], v[46:49]
	v_mfma_f32_16x16x32_bf16 v[42:45], v[162:165], v[194:197], v[42:45]
	v_mfma_f32_16x16x32_bf16 v[30:33], v[154:157], v[202:205], v[30:33]
	v_mfma_f32_16x16x32_bf16 v[26:29], v[162:165], v[202:205], v[26:29]
	v_mfma_f32_16x16x32_bf16 v[14:17], v[154:157], v[210:213], v[14:17]
	v_mfma_f32_16x16x32_bf16 v[10:13], v[162:165], v[210:213], v[10:13]
	s_setprio 0
	s_setprio 3
	v_mfma_f32_16x16x32_bf16 v[54:57], v[166:169], v[182:185], v[54:57]
	v_mfma_f32_16x16x32_bf16 v[50:53], v[174:177], v[182:185], v[50:53]
	v_mfma_f32_16x16x32_bf16 v[38:41], v[166:169], v[190:193], v[38:41]
	v_mfma_f32_16x16x32_bf16 v[34:37], v[174:177], v[190:193], v[34:37]
	v_mfma_f32_16x16x32_bf16 v[22:25], v[166:169], v[198:201], v[22:25]
	v_mfma_f32_16x16x32_bf16 v[18:21], v[174:177], v[198:201], v[18:21]
	v_mfma_f32_16x16x32_bf16 v[6:9], v[166:169], v[206:209], v[6:9]
	v_mfma_f32_16x16x32_bf16 v[2:5], v[174:177], v[206:209], v[2:5]
	v_mfma_f32_16x16x32_bf16 v[54:57], v[170:173], v[186:189], v[54:57]
	v_mfma_f32_16x16x32_bf16 v[50:53], v[178:181], v[186:189], v[50:53]
	v_mfma_f32_16x16x32_bf16 v[38:41], v[170:173], v[194:197], v[38:41]
	v_mfma_f32_16x16x32_bf16 v[34:37], v[178:181], v[194:197], v[34:37]
	v_mfma_f32_16x16x32_bf16 v[22:25], v[170:173], v[202:205], v[22:25]
	v_mfma_f32_16x16x32_bf16 v[18:21], v[178:181], v[202:205], v[18:21]
	v_mfma_f32_16x16x32_bf16 v[6:9], v[170:173], v[210:213], v[6:9]
	v_mfma_f32_16x16x32_bf16 v[2:5], v[178:181], v[210:213], v[2:5]
	s_setprio 0
	s_barrier
	s_add_i32 s56, s56, 2
	s_add_u32 s54, s54, 0x100
	s_addc_u32 s55, s55, 0
	s_cmp_gt_u32 s56, 11
	s_mov_b64 s[28:29], s[30:31]
	s_cbranch_scc0 .LBB0_1844
	s_and_b64 vcc, exec, s[20:21]
	s_cbranch_vccz .LBB0_1847
	s_barrier
